# v56 + cache policy: in-phase weight conversion (f32 loads, bf16 stores) marked nt so the streaming traffic does not displace GEMM tiles in L2
# speedup vs baseline: 1.0164x; 1.0164x over previous
; #define GAS __attribute__((address_space(1)))
; #define LAS __attribute__((address_space(3)))
; #define LDS_WAIT() asm volatile("s_waitcnt lgkmcnt(0)" ::: "memory")
; __device__ __forceinline__ unsigned pk2(float lo, float hi) { unsigned r; asm("v_cvt_pk_bf16_f32 %0, %1, %2" : "=v"(r) : "v"(lo), "v"(hi)); return r; }
; __device__ __forceinline__ void transpose_item(const float* W, int K, int N, bf16* WT, int drow0, int kb, int n0, LAS float* scr, int lane) {
;     const int k0 = 64 * kb; const int c4 = 4 * (lane & 7); const bool ok = (n0 + c4) < N;
;     f32x4 v[8];
; #pragma unroll
;     for (int i = 0; i < 8; ++i) { const int kk = 8 * i + (lane >> 3); v[i] = ok ? *(const f32x4*)(W + (size_t)(k0 + kk) * N + n0 + c4) : (f32x4){0.f, 0.f, 0.f, 0.f}; }
; #pragma unroll
;     for (int i = 0; i < 8; ++i) { const int kk = 8 * i + (lane >> 3); LAS float* d = scr + kk * 33 + c4; d[0] = v[i][0]; d[1] = v[i][1]; d[2] = v[i][2]; d[3] = v[i][3]; }
;     LDS_WAIT(); asm volatile("" ::: "memory");
;     const int c = lane & 7;
; #pragma unroll
;     for (int j = 0; j < 4; ++j) { const int n = (lane >> 3) + 8 * j; const LAS float* s = scr + (8 * c) * 33 + n;
;         v4u o; o.x = pk2(s[0 * 33], s[1 * 33]); o.y = pk2(s[2 * 33], s[3 * 33]); o.z = pk2(s[4 * 33], s[5 * 33]); o.w = pk2(s[6 * 33], s[7 * 33]);
;         *(GAS v4u*)(WT + (size_t)(drow0 + n) * K + k0 + 8 * c) = o; }
;     LDS_WAIT(); asm volatile("" ::: "memory");
; }
; __device__ __forceinline__ void convert_item(const In& I, unsigned char* ws, int it, LAS float* scr, int lane) {
;     ...
;     { const int jk = r >> 3; r &= 7; const int kb = r >> 1, nb = r & 1;
;         transpose_item(I.nsa_w2 + (size_t)jk * 256 * 64, 256, 64, W2t + (size_t)jk * 64 * 256, 32 * nb, kb, 32 * nb, scr, lane); }
.LBB0_167:
	s_add_i32 s45, s40, 0xa800
	s_cmp_gt_i32 s45, 0x83ff
	s_mov_b64 s[2:3], -1
	s_cbranch_scc0 .LBB0_221
	s_cmpk_gt_u32 s45, 0x8eff
	s_cbranch_scc0 .LBB0_202
	s_cmpk_gt_u32 s45, 0x92ff
	s_cbranch_scc0 .LBB0_199
	s_cmpk_gt_u32 s45, 0x9fff
	s_cbranch_scc0 .LBB0_180
	s_cmpk_gt_u32 s45, 0xa3ff
	s_cbranch_scc0 .LBB0_177
	s_cmpk_gt_u32 s45, 0xa7ff
	s_cbranch_scc0 .LBB0_174
	s_lshr_b32 s68, s40, 3
	v_readlane_b32 s48, v253, 16
	s_lshl_b64 s[2:3], s[68:69], 16
	v_readlane_b32 s52, v253, 20
	v_readlane_b32 s53, v253, 21
	s_add_u32 s6, s52, s2
	s_addc_u32 s7, s53, s3
	s_lshl_b64 s[2:3], s[68:69], 15
	s_add_u32 s8, s35, s2
	s_addc_u32 s3, s39, s3
	s_and_b32 s2, s42, 32
	s_and_b32 s9, s42, 0xc0
	s_lshl_b32 s10, s2, 2
	s_add_u32 s6, s6, s10
	v_or_b32_e32 v6, s9, v39
	s_addc_u32 s7, s7, 0
	v_lshlrev_b32_e32 v2, 2, v36
	v_lshl_add_u64 v[4:5], s[6:7], 0, v[2:3]
	v_lshlrev_b32_e32 v2, 8, v6
	v_lshl_add_u64 v[28:29], v[4:5], 0, v[2:3]
	global_load_dwordx4 v[4:7], v[28:29], off nt
	global_load_dwordx4 v[8:11], v[28:29], off offset:2048 nt
	v_add_co_u32_e32 v16, vcc, s84, v28
	s_movk_i32 s6, 0x3000
	s_nop 0
	v_addc_co_u32_e32 v17, vcc, 0, v29, vcc
	v_add_co_u32_e32 v24, vcc, s74, v28
	v_add_u32_e32 v2, v44, v45
	s_nop 0
	v_addc_co_u32_e32 v25, vcc, 0, v29, vcc
	global_load_dwordx4 v[12:15], v[24:25], off offset:-4096 nt
	s_nop 0
	global_load_dwordx4 v[16:19], v[16:17], off offset:2048 nt
	s_nop 0
	global_load_dwordx4 v[20:23], v[24:25], off nt
	s_nop 0
	global_load_dwordx4 v[24:27], v[24:25], off offset:2048 nt
	v_add_co_u32_e32 v32, vcc, s6, v28
	s_lshl_b32 s6, s9, 1
	s_nop 0
	v_addc_co_u32_e32 v33, vcc, 0, v29, vcc
	global_load_dwordx4 v[28:31], v[32:33], off nt
	s_nop 0
	global_load_dwordx4 v[32:35], v[32:33], off offset:2048 nt
	s_add_u32 s6, s8, s6
	s_addc_u32 s7, s3, 0
	v_readlane_b32 s49, v253, 17
	v_readlane_b32 s50, v253, 18
	v_readlane_b32 s51, v253, 19
	v_readlane_b32 s54, v253, 22
	v_readlane_b32 s55, v253, 23
	v_readlane_b32 s56, v253, 24
	v_readlane_b32 s57, v253, 25
	v_readlane_b32 s58, v253, 26
	v_readlane_b32 s59, v253, 27
	v_readlane_b32 s60, v253, 28
	v_readlane_b32 s61, v253, 29
	v_readlane_b32 s62, v253, 30
	v_readlane_b32 s63, v253, 31
	s_waitcnt vmcnt(0)
	ds_write2_b32 v2, v4, v5 offset1:1
	ds_write2_b32 v2, v6, v7 offset0:2 offset1:3
	v_add_u32_e32 v4, 0x420, v2
	ds_write2_b32 v4, v8, v9 offset1:1
	v_add_u32_e32 v4, 0x428, v2
	ds_write2_b32 v4, v10, v11 offset1:1
	v_add_u32_e32 v4, 0x840, v2
	ds_write2_b32 v4, v12, v13 offset1:1
	v_add_u32_e32 v4, 0x848, v2
	ds_write2_b32 v4, v14, v15 offset1:1
	v_add_u32_e32 v4, 0xc60, v2
	ds_write2_b32 v4, v16, v17 offset1:1
	v_add_u32_e32 v4, 0xc68, v2
	ds_write2_b32 v4, v18, v19 offset1:1
	v_add_u32_e32 v4, 0x1080, v2
	ds_write2_b32 v4, v20, v21 offset1:1
	v_add_u32_e32 v4, 0x1088, v2
	ds_write2_b32 v4, v22, v23 offset1:1
	v_add_u32_e32 v4, 0x14a0, v2
	ds_write2_b32 v4, v24, v25 offset1:1
	v_add_u32_e32 v4, 0x14a8, v2
	ds_write2_b32 v4, v26, v27 offset1:1
	v_add_u32_e32 v4, 0x18c0, v2
	ds_write2_b32 v4, v28, v29 offset1:1
	v_add_u32_e32 v4, 0x18c8, v2
	ds_write2_b32 v4, v30, v31 offset1:1
	v_add_u32_e32 v4, 0x1ce0, v2
	v_add_u32_e32 v2, 0x1ce8, v2
	ds_write2_b32 v4, v32, v33 offset1:1
	ds_write2_b32 v2, v34, v35 offset1:1
	s_waitcnt lgkmcnt(0)
	ds_read2_b32 v[10:11], v49 offset0:33 offset1:41
	ds_read2_b32 v[12:13], v49 offset1:8
	v_lshlrev_b32_e32 v2, 1, v38
	ds_read2_b32 v[14:15], v49 offset0:66 offset1:74
	ds_read2_b32 v[16:17], v49 offset0:99 offset1:107
	ds_read2_b32 v[18:19], v49 offset0:132 offset1:140
	ds_read2_b32 v[20:21], v49 offset0:165 offset1:173
	ds_read2_b32 v[22:23], v49 offset0:198 offset1:206
	ds_read2_b32 v[24:25], v49 offset0:231 offset1:239
	v_lshl_add_u64 v[4:5], s[6:7], 0, v[2:3]
	v_or_b32_e32 v2, s2, v39
	v_lshlrev_b32_e32 v2, 9, v2
	v_lshl_add_u64 v[26:27], v[4:5], 0, v[2:3]
	v_or_b32_e32 v2, s2, v46
	s_waitcnt lgkmcnt(0)
	v_cvt_pk_bf16_f32 v6, v12, v10
	v_lshlrev_b32_e32 v2, 9, v2
	v_cvt_pk_bf16_f32 v7, v14, v16
	v_cvt_pk_bf16_f32 v8, v18, v20
	v_cvt_pk_bf16_f32 v9, v22, v24
	global_store_dwordx4 v[26:27], v[6:9], off sc1 nt
	s_nop 1
	v_cvt_pk_bf16_f32 v6, v13, v11
	v_lshl_add_u64 v[10:11], v[4:5], 0, v[2:3]
	v_cvt_pk_bf16_f32 v7, v15, v17
	v_cvt_pk_bf16_f32 v8, v19, v21
	v_cvt_pk_bf16_f32 v9, v23, v25
	global_store_dwordx4 v[10:11], v[6:9], off sc1 nt
	ds_read2_b32 v[10:11], v49 offset0:16 offset1:24
	ds_read2_b32 v[12:13], v49 offset0:49 offset1:57
	ds_read2_b32 v[14:15], v49 offset0:82 offset1:90
	ds_read2_b32 v[16:17], v49 offset0:115 offset1:123
	ds_read2_b32 v[18:19], v49 offset0:148 offset1:156
	ds_read2_b32 v[20:21], v49 offset0:181 offset1:189
	ds_read2_b32 v[22:23], v49 offset0:214 offset1:222
	ds_read2_b32 v[24:25], v49 offset0:247 offset1:255
	v_or_b32_e32 v2, s2, v47
	v_lshlrev_b32_e32 v2, 9, v2
	v_lshl_add_u64 v[26:27], v[4:5], 0, v[2:3]
	v_or_b32_e32 v2, s2, v48
	v_lshlrev_b32_e32 v2, 9, v2
	s_waitcnt lgkmcnt(6)
	v_cvt_pk_bf16_f32 v6, v10, v12
	s_waitcnt lgkmcnt(4)
	v_cvt_pk_bf16_f32 v7, v14, v16
	s_waitcnt lgkmcnt(2)
	v_cvt_pk_bf16_f32 v8, v18, v20
	s_waitcnt lgkmcnt(0)
	v_cvt_pk_bf16_f32 v9, v22, v24
	v_lshl_add_u64 v[4:5], v[4:5], 0, v[2:3]
	global_store_dwordx4 v[26:27], v[6:9], off sc1 nt
	s_mov_b64 s[2:3], 0
	s_nop 0
	v_cvt_pk_bf16_f32 v6, v11, v13
	v_cvt_pk_bf16_f32 v7, v15, v17
	v_cvt_pk_bf16_f32 v8, v19, v21
	v_cvt_pk_bf16_f32 v9, v23, v25
	global_store_dwordx4 v[4:5], v[6:9], off sc1 nt
	s_waitcnt lgkmcnt(0)
; #define GAS __attribute__((address_space(1)))
; #define LAS __attribute__((address_space(3)))
; #define LDS_WAIT() asm volatile("s_waitcnt lgkmcnt(0)" ::: "memory")
; __device__ __forceinline__ unsigned pk2(float lo, float hi) { unsigned r; asm("v_cvt_pk_bf16_f32 %0, %1, %2" : "=v"(r) : "v"(lo), "v"(hi)); return r; }
; __device__ __forceinline__ void transpose_item(const float* W, int K, int N, bf16* WT, int drow0, int kb, int n0, LAS float* scr, int lane) {
;     const int k0 = 64 * kb; const int c4 = 4 * (lane & 7); const bool ok = (n0 + c4) < N;
;     f32x4 v[8];
; #pragma unroll
;     for (int i = 0; i < 8; ++i) { const int kk = 8 * i + (lane >> 3); v[i] = ok ? *(const f32x4*)(W + (size_t)(k0 + kk) * N + n0 + c4) : (f32x4){0.f, 0.f, 0.f, 0.f}; }
; #pragma unroll
;     for (int i = 0; i < 8; ++i) { const int kk = 8 * i + (lane >> 3); LAS float* d = scr + kk * 33 + c4; d[0] = v[i][0]; d[1] = v[i][1]; d[2] = v[i][2]; d[3] = v[i][3]; }
;     LDS_WAIT(); asm volatile("" ::: "memory");
;     const int c = lane & 7;
; #pragma unroll
;     for (int j = 0; j < 4; ++j) { const int n = (lane >> 3) + 8 * j; const LAS float* s = scr + (8 * c) * 33 + n;
;         v4u o; o.x = pk2(s[0 * 33], s[1 * 33]); o.y = pk2(s[2 * 33], s[3 * 33]); o.z = pk2(s[4 * 33], s[5 * 33]); o.w = pk2(s[6 * 33], s[7 * 33]);
;         *(GAS v4u*)(WT + (size_t)(drow0 + n) * K + k0 + 8 * c) = o; }
;     LDS_WAIT(); asm volatile("" ::: "memory");
; }
; __device__ __forceinline__ void convert_item(const In& I, unsigned char* ws, int it, LAS float* scr, int lane) {
;     ...
;     if (r < 4 * I_W1) { const int jk = r / I_W1; r -= jk * I_W1; const int kb = r / 8, nb = r % 8;
;         transpose_item(I.nsa_w1 + (size_t)jk * 2048 * 256, 2048, 256, W1t + (size_t)jk * 256 * 2048, 32 * nb, kb, 32 * nb, scr, lane); return; }
.LBB0_174:
	s_andn2_b64 vcc, exec, s[2:3]
	s_cbranch_vccnz .LBB0_176
	s_add_i32 s2, s40, 0x400
	s_lshr_b32 s68, s2, 8
	s_lshl_b64 s[2:3], s[68:69], 21
	v_readlane_b32 s48, v253, 16
	v_readlane_b32 s49, v253, 17
	s_add_u32 s6, s48, s2
	s_addc_u32 s7, s49, s3
	s_lshl_b64 s[2:3], s[68:69], 20
	s_add_u32 s8, s33, s2
	s_addc_u32 s3, s34, s3
	s_and_b32 s2, s42, 0xe0
	s_and_b32 s9, s41, 0x7c0
	s_lshl_b32 s10, s2, 2
	s_add_u32 s6, s6, s10
	v_or_b32_e32 v6, s9, v39
	s_addc_u32 s7, s7, 0
	v_lshlrev_b32_e32 v2, 2, v36
	v_lshl_add_u64 v[4:5], s[6:7], 0, v[2:3]
	v_lshlrev_b32_e32 v2, 10, v6
	v_lshl_add_u64 v[32:33], v[4:5], 0, v[2:3]
	v_add_co_u32_e32 v8, vcc, s74, v32
	global_load_dwordx4 v[4:7], v[32:33], off nt
	s_nop 0
	v_addc_co_u32_e32 v9, vcc, 0, v33, vcc
	s_movk_i32 s6, 0x4000
	global_load_dwordx4 v[8:11], v[8:9], off nt
	v_add_co_u32_e32 v12, vcc, s6, v32
	s_movk_i32 s6, 0x6000
	s_nop 0
	v_addc_co_u32_e32 v13, vcc, 0, v33, vcc
	global_load_dwordx4 v[12:15], v[12:13], off nt
	v_add_co_u32_e32 v16, vcc, s6, v32
	s_mov_b32 s6, 0xa000
	s_nop 0
	v_addc_co_u32_e32 v17, vcc, 0, v33, vcc
	global_load_dwordx4 v[16:19], v[16:17], off nt
	v_add_co_u32_e32 v20, vcc, s81, v32
	v_add_u32_e32 v2, v44, v45
	s_nop 0
	v_addc_co_u32_e32 v21, vcc, 0, v33, vcc
	global_load_dwordx4 v[20:23], v[20:21], off nt
	v_add_co_u32_e32 v24, vcc, s6, v32
	s_mov_b32 s6, 0xc000
	s_nop 0
	v_addc_co_u32_e32 v25, vcc, 0, v33, vcc
	global_load_dwordx4 v[24:27], v[24:25], off nt
	v_add_co_u32_e32 v28, vcc, s6, v32
	s_mov_b32 s6, 0xe000
	s_nop 0
	v_addc_co_u32_e32 v29, vcc, 0, v33, vcc
	global_load_dwordx4 v[28:31], v[28:29], off nt
	v_add_co_u32_e32 v32, vcc, s6, v32
	s_lshl_b32 s6, s9, 1
	s_nop 0
	v_addc_co_u32_e32 v33, vcc, 0, v33, vcc
	global_load_dwordx4 v[32:35], v[32:33], off nt
	s_add_u32 s6, s8, s6
	s_addc_u32 s7, s3, 0
	v_readlane_b32 s50, v253, 18
	v_readlane_b32 s51, v253, 19
	v_readlane_b32 s52, v253, 20
	v_readlane_b32 s53, v253, 21
	v_readlane_b32 s54, v253, 22
	v_readlane_b32 s55, v253, 23
	v_readlane_b32 s56, v253, 24
	v_readlane_b32 s57, v253, 25
	v_readlane_b32 s58, v253, 26
	v_readlane_b32 s59, v253, 27
	v_readlane_b32 s60, v253, 28
	v_readlane_b32 s61, v253, 29
	v_readlane_b32 s62, v253, 30
	v_readlane_b32 s63, v253, 31
	s_waitcnt vmcnt(0)
	ds_write2_b32 v2, v4, v5 offset1:1
	ds_write2_b32 v2, v6, v7 offset0:2 offset1:3
	v_add_u32_e32 v4, 0x420, v2
	ds_write2_b32 v4, v8, v9 offset1:1
	v_add_u32_e32 v4, 0x428, v2
	ds_write2_b32 v4, v10, v11 offset1:1
	v_add_u32_e32 v4, 0x840, v2
	ds_write2_b32 v4, v12, v13 offset1:1
	v_add_u32_e32 v4, 0x848, v2
	ds_write2_b32 v4, v14, v15 offset1:1
	v_add_u32_e32 v4, 0xc60, v2
	ds_write2_b32 v4, v16, v17 offset1:1
	v_add_u32_e32 v4, 0xc68, v2
	ds_write2_b32 v4, v18, v19 offset1:1
	v_add_u32_e32 v4, 0x1080, v2
	ds_write2_b32 v4, v20, v21 offset1:1
	v_add_u32_e32 v4, 0x1088, v2
	ds_write2_b32 v4, v22, v23 offset1:1
	v_add_u32_e32 v4, 0x14a0, v2
	ds_write2_b32 v4, v24, v25 offset1:1
	v_add_u32_e32 v4, 0x14a8, v2
	ds_write2_b32 v4, v26, v27 offset1:1
	v_add_u32_e32 v4, 0x18c0, v2
	ds_write2_b32 v4, v28, v29 offset1:1
	v_add_u32_e32 v4, 0x18c8, v2
	ds_write2_b32 v4, v30, v31 offset1:1
	v_add_u32_e32 v4, 0x1ce0, v2
	v_add_u32_e32 v2, 0x1ce8, v2
	ds_write2_b32 v4, v32, v33 offset1:1
	ds_write2_b32 v2, v34, v35 offset1:1
	s_waitcnt lgkmcnt(0)
	ds_read2_b32 v[10:11], v49 offset0:33 offset1:41
	ds_read2_b32 v[12:13], v49 offset1:8
	v_lshlrev_b32_e32 v2, 1, v38
	ds_read2_b32 v[14:15], v49 offset0:66 offset1:74
	ds_read2_b32 v[16:17], v49 offset0:99 offset1:107
	ds_read2_b32 v[18:19], v49 offset0:132 offset1:140
	ds_read2_b32 v[20:21], v49 offset0:165 offset1:173
	ds_read2_b32 v[22:23], v49 offset0:198 offset1:206
	ds_read2_b32 v[24:25], v49 offset0:231 offset1:239
	v_lshl_add_u64 v[8:9], s[6:7], 0, v[2:3]
	v_or_b32_e32 v2, s2, v39
	v_lshlrev_b32_e32 v2, 12, v2
	v_lshl_add_u64 v[26:27], v[8:9], 0, v[2:3]
	v_or_b32_e32 v2, s2, v46
	s_waitcnt lgkmcnt(0)
	v_cvt_pk_bf16_f32 v4, v12, v10
	v_lshlrev_b32_e32 v2, 12, v2
	v_cvt_pk_bf16_f32 v5, v14, v16
	v_cvt_pk_bf16_f32 v6, v18, v20
	v_cvt_pk_bf16_f32 v7, v22, v24
	global_store_dwordx4 v[26:27], v[4:7], off sc1 nt
	s_nop 1
	v_cvt_pk_bf16_f32 v4, v13, v11
	v_lshl_add_u64 v[10:11], v[8:9], 0, v[2:3]
	v_cvt_pk_bf16_f32 v5, v15, v17
	v_cvt_pk_bf16_f32 v6, v19, v21
	v_cvt_pk_bf16_f32 v7, v23, v25
	global_store_dwordx4 v[10:11], v[4:7], off sc1 nt
	ds_read2_b32 v[10:11], v49 offset0:16 offset1:24
	ds_read2_b32 v[12:13], v49 offset0:49 offset1:57
	ds_read2_b32 v[14:15], v49 offset0:82 offset1:90
	ds_read2_b32 v[16:17], v49 offset0:115 offset1:123
	ds_read2_b32 v[18:19], v49 offset0:148 offset1:156
	ds_read2_b32 v[20:21], v49 offset0:181 offset1:189
	ds_read2_b32 v[22:23], v49 offset0:214 offset1:222
	ds_read2_b32 v[24:25], v49 offset0:247 offset1:255
	v_or_b32_e32 v2, s2, v47
	v_lshlrev_b32_e32 v2, 12, v2
	v_lshl_add_u64 v[26:27], v[8:9], 0, v[2:3]
	v_or_b32_e32 v2, s2, v48
	v_lshlrev_b32_e32 v2, 12, v2
	s_waitcnt lgkmcnt(6)
	v_cvt_pk_bf16_f32 v4, v10, v12
	s_waitcnt lgkmcnt(4)
	v_cvt_pk_bf16_f32 v5, v14, v16
	s_waitcnt lgkmcnt(2)
	v_cvt_pk_bf16_f32 v6, v18, v20
	s_waitcnt lgkmcnt(0)
	v_cvt_pk_bf16_f32 v7, v22, v24
	v_lshl_add_u64 v[8:9], v[8:9], 0, v[2:3]
	global_store_dwordx4 v[26:27], v[4:7], off sc1 nt
	s_nop 1
	v_cvt_pk_bf16_f32 v4, v11, v13
	v_cvt_pk_bf16_f32 v5, v15, v17
	v_cvt_pk_bf16_f32 v6, v19, v21
	v_cvt_pk_bf16_f32 v7, v23, v25
	global_store_dwordx4 v[8:9], v[4:7], off sc1 nt
	s_waitcnt lgkmcnt(0)

; #define GAS __attribute__((address_space(1)))
; #define LAS __attribute__((address_space(3)))
; #define LDS_WAIT() asm volatile("s_waitcnt lgkmcnt(0)" ::: "memory")
; __device__ __forceinline__ unsigned pk2(float lo, float hi) { unsigned r; asm("v_cvt_pk_bf16_f32 %0, %1, %2" : "=v"(r) : "v"(lo), "v"(hi)); return r; }
; __device__ __forceinline__ void transpose_item(const float* W, int K, int N, bf16* WT, int drow0, int kb, int n0, LAS float* scr, int lane) {
;     const int k0 = 64 * kb; const int c4 = 4 * (lane & 7); const bool ok = (n0 + c4) < N;
;     f32x4 v[8];
; #pragma unroll
;     for (int i = 0; i < 8; ++i) { const int kk = 8 * i + (lane >> 3); v[i] = ok ? *(const f32x4*)(W + (size_t)(k0 + kk) * N + n0 + c4) : (f32x4){0.f, 0.f, 0.f, 0.f}; }
; #pragma unroll
;     for (int i = 0; i < 8; ++i) { const int kk = 8 * i + (lane >> 3); LAS float* d = scr + kk * 33 + c4; d[0] = v[i][0]; d[1] = v[i][1]; d[2] = v[i][2]; d[3] = v[i][3]; }
;     LDS_WAIT(); asm volatile("" ::: "memory");
;     const int c = lane & 7;
; #pragma unroll
;     for (int j = 0; j < 4; ++j) { const int n = (lane >> 3) + 8 * j; const LAS float* s = scr + (8 * c) * 33 + n;
;         v4u o; o.x = pk2(s[0 * 33], s[1 * 33]); o.y = pk2(s[2 * 33], s[3 * 33]); o.z = pk2(s[4 * 33], s[5 * 33]); o.w = pk2(s[6 * 33], s[7 * 33]);
;         *(GAS v4u*)(WT + (size_t)(drow0 + n) * K + k0 + 8 * c) = o; }
;     LDS_WAIT(); asm volatile("" ::: "memory");
; }
; __device__ __forceinline__ void convert_item(const In& I, unsigned char* ws, int it, LAS float* scr, int lane) {
;     ...
;     if (r < 2 * I_SQ) { const int j = r / I_SQ; r -= j * I_SQ; const int kb = r / 32, nb = r % 32;
;         transpose_item(I.fox_w_out + (size_t)j * D * D, D, D, Wfout + (size_t)j * D * D, 32 * nb, kb, 32 * nb, scr, lane); return; }
.LBB0_177:
	s_andn2_b64 vcc, exec, s[2:3]
	s_cbranch_vccnz .LBB0_179
	s_add_i32 s2, s40, 0x800
	s_lshr_b32 s68, s2, 9
	v_readlane_b32 s48, v253, 16
	s_lshl_b64 s[2:3], s[68:69], 22
	v_readlane_b32 s60, v253, 28
	v_readlane_b32 s61, v253, 29
	s_add_u32 s6, s60, s2
	s_addc_u32 s7, s61, s3
	s_lshl_b64 s[2:3], s[68:69], 21
	s_add_u32 s8, s27, s2
	s_addc_u32 s3, s31, s3
	s_and_b32 s2, s42, 0x3e0
	s_add_i32 s9, s43, s44
	s_and_b32 s9, s9, 0x3c0
	s_lshl_b32 s10, s2, 2
	s_add_u32 s6, s6, s10
	v_or_b32_e32 v6, s9, v39
	s_addc_u32 s7, s7, 0
	v_lshlrev_b32_e32 v2, 2, v36
	v_lshl_add_u64 v[4:5], s[6:7], 0, v[2:3]
	v_lshlrev_b32_e32 v2, 12, v6
	v_lshl_add_u64 v[32:33], v[4:5], 0, v[2:3]
	v_add_co_u32_e32 v8, vcc, s81, v32
	global_load_dwordx4 v[4:7], v[32:33], off nt
	s_nop 0
	v_addc_co_u32_e32 v9, vcc, 0, v33, vcc
	global_load_dwordx4 v[8:11], v[8:9], off nt
	v_add_co_u32_e32 v12, vcc, s79, v32
	v_add_u32_e32 v2, v44, v45
	s_nop 0
	v_addc_co_u32_e32 v13, vcc, 0, v33, vcc
	global_load_dwordx4 v[12:15], v[12:13], off nt
	v_add_co_u32_e32 v16, vcc, s80, v32
	s_lshl_b32 s6, s9, 1
	s_nop 0
	v_addc_co_u32_e32 v17, vcc, 0, v33, vcc
	global_load_dwordx4 v[16:19], v[16:17], off nt
	v_add_co_u32_e32 v20, vcc, s85, v32
	s_add_u32 s6, s8, s6
	s_nop 0
	v_addc_co_u32_e32 v21, vcc, 0, v33, vcc
	global_load_dwordx4 v[20:23], v[20:21], off nt
	v_add_co_u32_e32 v24, vcc, s86, v32
	s_addc_u32 s7, s3, 0
	s_nop 0
	v_addc_co_u32_e32 v25, vcc, 0, v33, vcc
	global_load_dwordx4 v[24:27], v[24:25], off nt
	v_add_co_u32_e32 v28, vcc, s87, v32
	v_readlane_b32 s49, v253, 17
	s_nop 0
	v_addc_co_u32_e32 v29, vcc, 0, v33, vcc
	global_load_dwordx4 v[28:31], v[28:29], off nt
	v_add_co_u32_e32 v32, vcc, s89, v32
	v_readlane_b32 s50, v253, 18
	s_nop 0
	v_addc_co_u32_e32 v33, vcc, 0, v33, vcc
	global_load_dwordx4 v[32:35], v[32:33], off nt
	v_readlane_b32 s51, v253, 19
	v_readlane_b32 s52, v253, 20
	v_readlane_b32 s53, v253, 21
	v_readlane_b32 s54, v253, 22
	v_readlane_b32 s55, v253, 23
	v_readlane_b32 s56, v253, 24
	v_readlane_b32 s57, v253, 25
	v_readlane_b32 s58, v253, 26
	v_readlane_b32 s59, v253, 27
	v_readlane_b32 s62, v253, 30
	v_readlane_b32 s63, v253, 31
	s_waitcnt vmcnt(0)
	ds_write2_b32 v2, v4, v5 offset1:1
	ds_write2_b32 v2, v6, v7 offset0:2 offset1:3
	v_add_u32_e32 v4, 0x420, v2
	ds_write2_b32 v4, v8, v9 offset1:1
	v_add_u32_e32 v4, 0x428, v2
	ds_write2_b32 v4, v10, v11 offset1:1
	v_add_u32_e32 v4, 0x840, v2
	ds_write2_b32 v4, v12, v13 offset1:1
	v_add_u32_e32 v4, 0x848, v2
	ds_write2_b32 v4, v14, v15 offset1:1
	v_add_u32_e32 v4, 0xc60, v2
	ds_write2_b32 v4, v16, v17 offset1:1
	v_add_u32_e32 v4, 0xc68, v2
	ds_write2_b32 v4, v18, v19 offset1:1
	v_add_u32_e32 v4, 0x1080, v2
	ds_write2_b32 v4, v20, v21 offset1:1
	v_add_u32_e32 v4, 0x1088, v2
	ds_write2_b32 v4, v22, v23 offset1:1
	v_add_u32_e32 v4, 0x14a0, v2
	ds_write2_b32 v4, v24, v25 offset1:1
	v_add_u32_e32 v4, 0x14a8, v2
	ds_write2_b32 v4, v26, v27 offset1:1
	v_add_u32_e32 v4, 0x18c0, v2
	ds_write2_b32 v4, v28, v29 offset1:1
	v_add_u32_e32 v4, 0x18c8, v2
	ds_write2_b32 v4, v30, v31 offset1:1
	v_add_u32_e32 v4, 0x1ce0, v2
	v_add_u32_e32 v2, 0x1ce8, v2
	ds_write2_b32 v4, v32, v33 offset1:1
	ds_write2_b32 v2, v34, v35 offset1:1
	s_waitcnt lgkmcnt(0)
	ds_read2_b32 v[10:11], v49 offset0:33 offset1:41
	ds_read2_b32 v[12:13], v49 offset1:8
	v_lshlrev_b32_e32 v2, 1, v38
	ds_read2_b32 v[14:15], v49 offset0:66 offset1:74
	ds_read2_b32 v[16:17], v49 offset0:99 offset1:107
	ds_read2_b32 v[18:19], v49 offset0:132 offset1:140
	ds_read2_b32 v[20:21], v49 offset0:165 offset1:173
	ds_read2_b32 v[22:23], v49 offset0:198 offset1:206
	ds_read2_b32 v[24:25], v49 offset0:231 offset1:239
	v_lshl_add_u64 v[8:9], s[6:7], 0, v[2:3]
	v_or_b32_e32 v2, s2, v39
	v_lshlrev_b32_e32 v2, 11, v2
	v_lshl_add_u64 v[26:27], v[8:9], 0, v[2:3]
	v_or_b32_e32 v2, s2, v46
	s_waitcnt lgkmcnt(0)
	v_cvt_pk_bf16_f32 v4, v12, v10
	v_lshlrev_b32_e32 v2, 11, v2
	v_cvt_pk_bf16_f32 v5, v14, v16
	v_cvt_pk_bf16_f32 v6, v18, v20
	v_cvt_pk_bf16_f32 v7, v22, v24
	global_store_dwordx4 v[26:27], v[4:7], off sc1 nt
	s_nop 1
	v_cvt_pk_bf16_f32 v4, v13, v11
	v_lshl_add_u64 v[10:11], v[8:9], 0, v[2:3]
	v_cvt_pk_bf16_f32 v5, v15, v17
	v_cvt_pk_bf16_f32 v6, v19, v21
	v_cvt_pk_bf16_f32 v7, v23, v25
	global_store_dwordx4 v[10:11], v[4:7], off sc1 nt
	ds_read2_b32 v[10:11], v49 offset0:16 offset1:24
	ds_read2_b32 v[12:13], v49 offset0:49 offset1:57
	ds_read2_b32 v[14:15], v49 offset0:82 offset1:90
	ds_read2_b32 v[16:17], v49 offset0:115 offset1:123
	ds_read2_b32 v[18:19], v49 offset0:148 offset1:156
	ds_read2_b32 v[20:21], v49 offset0:181 offset1:189
	ds_read2_b32 v[22:23], v49 offset0:214 offset1:222
	ds_read2_b32 v[24:25], v49 offset0:247 offset1:255
	v_or_b32_e32 v2, s2, v47
	v_lshlrev_b32_e32 v2, 11, v2
	v_lshl_add_u64 v[26:27], v[8:9], 0, v[2:3]
	v_or_b32_e32 v2, s2, v48
	v_lshlrev_b32_e32 v2, 11, v2
	s_waitcnt lgkmcnt(6)
	v_cvt_pk_bf16_f32 v4, v10, v12
	s_waitcnt lgkmcnt(4)
	v_cvt_pk_bf16_f32 v5, v14, v16
	s_waitcnt lgkmcnt(2)
	v_cvt_pk_bf16_f32 v6, v18, v20
	s_waitcnt lgkmcnt(0)
	v_cvt_pk_bf16_f32 v7, v22, v24
	v_lshl_add_u64 v[8:9], v[8:9], 0, v[2:3]
	global_store_dwordx4 v[26:27], v[4:7], off sc1 nt
	s_nop 1
	v_cvt_pk_bf16_f32 v4, v11, v13
	v_cvt_pk_bf16_f32 v5, v15, v17
	v_cvt_pk_bf16_f32 v6, v19, v21
	v_cvt_pk_bf16_f32 v7, v23, v25
	global_store_dwordx4 v[8:9], v[4:7], off sc1 nt
	s_waitcnt lgkmcnt(0)

; #define LAS __attribute__((address_space(3)))
; __device__ __forceinline__ void transpose_item(const float* W, int K, int N, bf16* WT, int drow0, int kb, int n0, LAS float* scr, int lane) {
;     const int k0 = 64 * kb; const int c4 = 4 * (lane & 7); const bool ok = (n0 + c4) < N;
;     f32x4 v[8];
; #pragma unroll
;     for (int i = 0; i < 8; ++i) { const int kk = 8 * i + (lane >> 3); v[i] = ok ? *(const f32x4*)(W + (size_t)(k0 + kk) * N + n0 + c4) : (f32x4){0.f, 0.f, 0.f, 0.f}; }
; #pragma unroll
;     for (int i = 0; i < 8; ++i) { const int kk = 8 * i + (lane >> 3); LAS float* d = scr + kk * 33 + c4; d[0] = v[i][0]; d[1] = v[i][1]; d[2] = v[i][2]; d[3] = v[i][3]; }
; __device__ __forceinline__ void convert_item(const In& I, unsigned char* ws, int it, LAS float* scr, int lane) {
;     ...
;     if (r < 2 * I_FIN) { const int j = r / I_FIN; r -= j * I_FIN; const int kb = r / 104, nb = r % 104;
;         transpose_item(I.fox_w_in + (size_t)j * D * FOX_IN, D, FOX_IN, Wfin + (size_t)j * FOX_IN_PAD * D, 32 * nb, kb, 32 * nb, scr, lane); return; }
.LBB0_180:
	s_andn2_b64 vcc, exec, s[2:3]
	s_cbranch_vccnz .LBB0_198
	s_add_i32 s6, s40, 0x1500
	s_cmpk_gt_u32 s6, 0x67f
	s_cselect_b64 s[10:11], -1, 0
	s_and_b64 s[2:3], s[10:11], exec
	s_cselect_b32 s2, 0xf980, 0
	s_cselect_b32 s3, 0xc10000, 0
	s_add_i32 s6, s6, s2
	s_sext_i32_i16 s2, s6
	s_mulk_i32 s2, 0x4ec5
	s_lshr_b32 s7, s2, 31
	s_ashr_i32 s2, s2, 21
	s_add_i32 s2, s2, s7
	s_mul_i32 s7, s2, 0x68
	v_readlane_b32 s48, v253, 16
	s_sub_i32 s6, s6, s7
	v_readlane_b32 s56, v253, 24
	s_sext_i32_i16 s6, s6
	v_readlane_b32 s57, v253, 25
	s_add_u32 s9, s56, s3
	s_addc_u32 s46, s57, 0
	s_lshl_b32 s6, s6, 5
	s_ashr_i32 s7, s6, 31
	s_lshl_b32 s8, s2, 6
	s_lshl_b64 s[12:13], s[6:7], 2
	v_or_b32_e32 v2, s6, v36
	s_movk_i32 s2, 0xc10
	v_or_b32_e32 v5, s8, v39
	s_add_u32 s12, s9, s12
	v_cmp_gt_i32_e64 s[2:3], s2, v2
	s_addc_u32 s13, s46, s13
	v_lshlrev_b32_e32 v2, 2, v36
	v_mul_i32_i24_e32 v42, 0x3040, v5
	v_lshl_add_u64 v[40:41], s[12:13], 0, v[2:3]
	v_mov_b32_e32 v4, 0
	v_ashrrev_i32_e32 v43, 31, v42
	v_mov_b32_e32 v8, 0
	v_mov_b32_e32 v9, 0
	v_mov_b32_e32 v10, 0
	v_mov_b32_e32 v11, 0
	v_readlane_b32 s49, v253, 17
	v_readlane_b32 s50, v253, 18
	v_readlane_b32 s51, v253, 19
	v_readlane_b32 s52, v253, 20
	v_readlane_b32 s53, v253, 21
	v_readlane_b32 s54, v253, 22
	v_readlane_b32 s55, v253, 23
	v_readlane_b32 s58, v253, 26
	v_readlane_b32 s59, v253, 27
	v_readlane_b32 s60, v253, 28
	v_readlane_b32 s61, v253, 29
	v_readlane_b32 s62, v253, 30
	v_readlane_b32 s63, v253, 31
	s_and_saveexec_b64 s[12:13], s[2:3]
	s_cbranch_execz .LBB0_183
	v_lshl_add_u64 v[6:7], v[40:41], 0, v[42:43]
	global_load_dwordx4 v[8:11], v[6:7], off nt
.LBB0_183:
	s_or_b64 exec, exec, s[12:13]
	v_mov_b32_e32 v5, 0
	v_mov_b32_e32 v6, 0
	v_mov_b32_e32 v7, 0
	s_and_saveexec_b64 s[12:13], s[2:3]
	s_cbranch_execz .LBB0_185
	v_lshl_add_u64 v[4:5], v[40:41], 0, v[42:43]
	v_add_co_u32_e32 v4, vcc, 0x18000, v4
	s_nop 1
	v_addc_co_u32_e32 v5, vcc, 0, v5, vcc
	global_load_dwordx4 v[4:7], v[4:5], off offset:512 nt
.LBB0_185:
	s_or_b64 exec, exec, s[12:13]
	v_mov_b32_e32 v12, 0
	v_mov_b32_e32 v16, 0
	v_mov_b32_e32 v17, 0
	v_mov_b32_e32 v18, 0
	v_mov_b32_e32 v19, 0
	s_and_saveexec_b64 s[12:13], s[2:3]
	s_cbranch_execz .LBB0_187
	v_lshl_add_u64 v[14:15], v[40:41], 0, v[42:43]
	v_add_co_u32_e32 v14, vcc, 0x30000, v14
	s_nop 1
	v_addc_co_u32_e32 v15, vcc, 0, v15, vcc
	global_load_dwordx4 v[16:19], v[14:15], off offset:1024 nt
.LBB0_187:
	s_or_b64 exec, exec, s[12:13]
	v_mov_b32_e32 v13, 0
	v_mov_b32_e32 v14, 0
	v_mov_b32_e32 v15, 0
	s_and_saveexec_b64 s[12:13], s[2:3]
	s_cbranch_execz .LBB0_189
	v_lshl_add_u64 v[12:13], v[40:41], 0, v[42:43]
	v_add_co_u32_e32 v12, vcc, 0x48000, v12
	s_nop 1
	v_addc_co_u32_e32 v13, vcc, 0, v13, vcc
	global_load_dwordx4 v[12:15], v[12:13], off offset:1536 nt
.LBB0_189:
	s_or_b64 exec, exec, s[12:13]
	v_mov_b32_e32 v20, 0
	v_mov_b32_e32 v24, 0
	v_mov_b32_e32 v25, 0
	v_mov_b32_e32 v26, 0
	v_mov_b32_e32 v27, 0
	s_and_saveexec_b64 s[12:13], s[2:3]
	s_cbranch_execz .LBB0_191
	v_lshl_add_u64 v[22:23], v[40:41], 0, v[42:43]
	v_add_co_u32_e32 v22, vcc, 0x60000, v22
	s_nop 1
	v_addc_co_u32_e32 v23, vcc, 0, v23, vcc
	global_load_dwordx4 v[24:27], v[22:23], off offset:2048 nt
.LBB0_191:
	s_or_b64 exec, exec, s[12:13]
	v_mov_b32_e32 v21, 0
	v_mov_b32_e32 v22, 0
	v_mov_b32_e32 v23, 0
	s_and_saveexec_b64 s[12:13], s[2:3]
	s_cbranch_execz .LBB0_193
	v_lshl_add_u64 v[20:21], v[40:41], 0, v[42:43]
	v_add_co_u32_e32 v20, vcc, 0x78000, v20
	s_nop 1
	v_addc_co_u32_e32 v21, vcc, 0, v21, vcc
	global_load_dwordx4 v[20:23], v[20:21], off offset:2560 nt
.LBB0_193:
	s_or_b64 exec, exec, s[12:13]
	v_mov_b32_e32 v28, 0
	v_mov_b32_e32 v32, 0
	v_mov_b32_e32 v33, 0
	v_mov_b32_e32 v34, 0
	v_mov_b32_e32 v35, 0
	s_and_saveexec_b64 s[12:13], s[2:3]
	s_cbranch_execz .LBB0_195
	v_lshl_add_u64 v[30:31], v[40:41], 0, v[42:43]
	v_add_co_u32_e32 v30, vcc, 0x90000, v30
	s_nop 1
	v_addc_co_u32_e32 v31, vcc, 0, v31, vcc
	global_load_dwordx4 v[32:35], v[30:31], off offset:3072 nt
; #define GAS __attribute__((address_space(1)))
; #define LAS __attribute__((address_space(3)))
; #define LDS_WAIT() asm volatile("s_waitcnt lgkmcnt(0)" ::: "memory")
; __device__ __forceinline__ unsigned pk2(float lo, float hi) { unsigned r; asm("v_cvt_pk_bf16_f32 %0, %1, %2" : "=v"(r) : "v"(lo), "v"(hi)); return r; }
; __device__ __forceinline__ void transpose_item(const float* W, int K, int N, bf16* WT, int drow0, int kb, int n0, LAS float* scr, int lane) {
;     const int k0 = 64 * kb; const int c4 = 4 * (lane & 7); const bool ok = (n0 + c4) < N;
;     f32x4 v[8];
; #pragma unroll
;     for (int i = 0; i < 8; ++i) { const int kk = 8 * i + (lane >> 3); v[i] = ok ? *(const f32x4*)(W + (size_t)(k0 + kk) * N + n0 + c4) : (f32x4){0.f, 0.f, 0.f, 0.f}; }
; #pragma unroll
;     for (int i = 0; i < 8; ++i) { const int kk = 8 * i + (lane >> 3); LAS float* d = scr + kk * 33 + c4; d[0] = v[i][0]; d[1] = v[i][1]; d[2] = v[i][2]; d[3] = v[i][3]; }
;     LDS_WAIT(); asm volatile("" ::: "memory");
;     const int c = lane & 7;
; #pragma unroll
;     for (int j = 0; j < 4; ++j) { const int n = (lane >> 3) + 8 * j; const LAS float* s = scr + (8 * c) * 33 + n;
;         v4u o; o.x = pk2(s[0 * 33], s[1 * 33]); o.y = pk2(s[2 * 33], s[3 * 33]); o.z = pk2(s[4 * 33], s[5 * 33]); o.w = pk2(s[6 * 33], s[7 * 33]);
;         *(GAS v4u*)(WT + (size_t)(drow0 + n) * K + k0 + 8 * c) = o; }
;     LDS_WAIT(); asm volatile("" ::: "memory");
; }
.LBB0_195:
	s_or_b64 exec, exec, s[12:13]
	v_mov_b32_e32 v29, 0
	v_mov_b32_e32 v30, 0
	v_mov_b32_e32 v31, 0
	s_and_saveexec_b64 s[12:13], s[2:3]
	s_cbranch_execz .LBB0_197
	v_lshl_add_u64 v[28:29], v[40:41], 0, v[42:43]
	v_add_co_u32_e32 v28, vcc, 0xa8000, v28
	s_nop 1
	v_addc_co_u32_e32 v29, vcc, 0, v29, vcc
	global_load_dwordx4 v[28:31], v[28:29], off offset:3584 nt
.LBB0_197:
	s_or_b64 exec, exec, s[12:13]
	v_add_u32_e32 v2, v44, v45
	s_waitcnt vmcnt(0)
	ds_write2_b32 v2, v8, v9 offset1:1
	ds_write2_b32 v2, v10, v11 offset0:2 offset1:3
	v_add_u32_e32 v8, 0x420, v2
	ds_write2_b32 v8, v4, v5 offset1:1
	v_add_u32_e32 v4, 0x428, v2
	ds_write2_b32 v4, v6, v7 offset1:1
	v_add_u32_e32 v4, 0x840, v2
	ds_write2_b32 v4, v16, v17 offset1:1
	v_add_u32_e32 v4, 0x848, v2
	ds_write2_b32 v4, v18, v19 offset1:1
	v_add_u32_e32 v4, 0xc60, v2
	ds_write2_b32 v4, v12, v13 offset1:1
	v_add_u32_e32 v4, 0xc68, v2
	ds_write2_b32 v4, v14, v15 offset1:1
	v_add_u32_e32 v4, 0x1080, v2
	ds_write2_b32 v4, v24, v25 offset1:1
	v_add_u32_e32 v4, 0x1088, v2
	ds_write2_b32 v4, v26, v27 offset1:1
	v_add_u32_e32 v4, 0x14a0, v2
	ds_write2_b32 v4, v20, v21 offset1:1
	v_add_u32_e32 v4, 0x14a8, v2
	ds_write2_b32 v4, v22, v23 offset1:1
	v_add_u32_e32 v4, 0x18c0, v2
	ds_write2_b32 v4, v32, v33 offset1:1
	v_add_u32_e32 v4, 0x18c8, v2
	s_and_b64 s[2:3], s[10:11], exec
	ds_write2_b32 v4, v34, v35 offset1:1
	v_add_u32_e32 v4, 0x1ce0, v2
	v_add_u32_e32 v2, 0x1ce8, v2
	s_cselect_b32 s2, 0x680000, 0
	ds_write2_b32 v4, v28, v29 offset1:1
	ds_write2_b32 v2, v30, v31 offset1:1
	s_add_u32 s7, s25, s2
	s_waitcnt lgkmcnt(0)
	s_addc_u32 s10, s26, 0
	s_ashr_i32 s9, s8, 31
	s_lshl_b64 s[2:3], s[8:9], 1
	ds_read2_b32 v[8:9], v49 offset0:33 offset1:41
	ds_read2_b32 v[10:11], v49 offset1:8
	ds_read2_b32 v[12:13], v49 offset0:66 offset1:74
	ds_read2_b32 v[14:15], v49 offset0:99 offset1:107
	ds_read2_b32 v[16:17], v49 offset0:132 offset1:140
	ds_read2_b32 v[18:19], v49 offset0:165 offset1:173
	ds_read2_b32 v[20:21], v49 offset0:198 offset1:206
	ds_read2_b32 v[22:23], v49 offset0:231 offset1:239
	s_add_u32 s2, s7, s2
	v_or_b32_e32 v26, s6, v39
	s_addc_u32 s3, s10, s3
	v_lshlrev_b32_e32 v2, 1, v38
	v_ashrrev_i32_e32 v27, 31, v26
	v_lshl_add_u64 v[24:25], s[2:3], 0, v[2:3]
	v_lshlrev_b64 v[26:27], 11, v[26:27]
	s_waitcnt lgkmcnt(0)
	v_cvt_pk_bf16_f32 v4, v10, v8
	v_lshl_add_u64 v[26:27], v[24:25], 0, v[26:27]
	v_or_b32_e32 v8, s6, v46
	v_cvt_pk_bf16_f32 v5, v12, v14
	v_cvt_pk_bf16_f32 v6, v16, v18
	v_cvt_pk_bf16_f32 v7, v20, v22
	global_store_dwordx4 v[26:27], v[4:7], off sc1 nt
	s_nop 1
	v_cvt_pk_bf16_f32 v4, v11, v9
	v_ashrrev_i32_e32 v9, 31, v8
	v_lshlrev_b64 v[8:9], 11, v[8:9]
	v_cvt_pk_bf16_f32 v5, v13, v15
	v_cvt_pk_bf16_f32 v6, v17, v19
	v_cvt_pk_bf16_f32 v7, v21, v23
	v_lshl_add_u64 v[8:9], v[24:25], 0, v[8:9]
	ds_read2_b32 v[10:11], v49 offset0:16 offset1:24
	ds_read2_b32 v[12:13], v49 offset0:49 offset1:57
	ds_read2_b32 v[14:15], v49 offset0:82 offset1:90
	ds_read2_b32 v[16:17], v49 offset0:115 offset1:123
	ds_read2_b32 v[18:19], v49 offset0:148 offset1:156
	ds_read2_b32 v[20:21], v49 offset0:181 offset1:189
	ds_read2_b32 v[22:23], v49 offset0:214 offset1:222
	ds_read2_b32 v[26:27], v49 offset0:247 offset1:255
	global_store_dwordx4 v[8:9], v[4:7], off sc1 nt
	v_or_b32_e32 v8, s6, v47
	v_ashrrev_i32_e32 v9, 31, v8
	v_lshlrev_b64 v[8:9], 11, v[8:9]
	v_lshl_add_u64 v[8:9], v[24:25], 0, v[8:9]
	s_waitcnt lgkmcnt(6)
	v_cvt_pk_bf16_f32 v4, v10, v12
	s_waitcnt lgkmcnt(4)
	v_cvt_pk_bf16_f32 v5, v14, v16
	s_waitcnt lgkmcnt(2)
	v_cvt_pk_bf16_f32 v6, v18, v20
	s_waitcnt lgkmcnt(0)
	v_cvt_pk_bf16_f32 v7, v22, v26
	global_store_dwordx4 v[8:9], v[4:7], off sc1 nt
	v_or_b32_e32 v8, s6, v48
	v_ashrrev_i32_e32 v9, 31, v8
	v_lshlrev_b64 v[8:9], 11, v[8:9]
	v_lshl_add_u64 v[8:9], v[24:25], 0, v[8:9]
	v_cvt_pk_bf16_f32 v4, v11, v13
	v_cvt_pk_bf16_f32 v5, v15, v17
	v_cvt_pk_bf16_f32 v6, v19, v21
	v_cvt_pk_bf16_f32 v7, v23, v27
	global_store_dwordx4 v[8:9], v[4:7], off sc1 nt
	s_waitcnt lgkmcnt(0)

; #define GAS __attribute__((address_space(1)))
; #define LAS __attribute__((address_space(3)))
; #define LDS_WAIT() asm volatile("s_waitcnt lgkmcnt(0)" ::: "memory")
; __device__ __forceinline__ unsigned pk2(float lo, float hi) { unsigned r; asm("v_cvt_pk_bf16_f32 %0, %1, %2" : "=v"(r) : "v"(lo), "v"(hi)); return r; }
; __device__ __forceinline__ void transpose_item(const float* W, int K, int N, bf16* WT, int drow0, int kb, int n0, LAS float* scr, int lane) {
;     const int k0 = 64 * kb; const int c4 = 4 * (lane & 7); const bool ok = (n0 + c4) < N;
;     f32x4 v[8];
; #pragma unroll
;     for (int i = 0; i < 8; ++i) { const int kk = 8 * i + (lane >> 3); v[i] = ok ? *(const f32x4*)(W + (size_t)(k0 + kk) * N + n0 + c4) : (f32x4){0.f, 0.f, 0.f, 0.f}; }
; #pragma unroll
;     for (int i = 0; i < 8; ++i) { const int kk = 8 * i + (lane >> 3); LAS float* d = scr + kk * 33 + c4; d[0] = v[i][0]; d[1] = v[i][1]; d[2] = v[i][2]; d[3] = v[i][3]; }
;     LDS_WAIT(); asm volatile("" ::: "memory");
;     const int c = lane & 7;
; #pragma unroll
;     for (int j = 0; j < 4; ++j) { const int n = (lane >> 3) + 8 * j; const LAS float* s = scr + (8 * c) * 33 + n;
;         v4u o; o.x = pk2(s[0 * 33], s[1 * 33]); o.y = pk2(s[2 * 33], s[3 * 33]); o.z = pk2(s[4 * 33], s[5 * 33]); o.w = pk2(s[6 * 33], s[7 * 33]);
;         *(GAS v4u*)(WT + (size_t)(drow0 + n) * K + k0 + 8 * c) = o; }
;     LDS_WAIT(); asm volatile("" ::: "memory");
; }
; __device__ __forceinline__ void convert_item(const In& I, unsigned char* ws, int it, LAS float* scr, int lane) {
;     ...
;     if (r < 2 * I_SQ) { const int j = r / I_SQ; r -= j * I_SQ; const int kb = r / 32, nb = r % 32;
;         transpose_item(I.nsa_w_out + (size_t)j * D * D, D, D, Wnout + (size_t)j * D * D, 32 * nb, kb, 32 * nb, scr, lane); return; }
.LBB0_199:
	s_andn2_b64 vcc, exec, s[2:3]
	s_cbranch_vccnz .LBB0_201
	s_add_i32 s2, s40, 0x1900
	s_lshr_b32 s68, s2, 9
	v_readlane_b32 s48, v253, 16
	s_lshl_b64 s[2:3], s[68:69], 22
	v_readlane_b32 s54, v253, 22
	v_readlane_b32 s55, v253, 23
	s_add_u32 s6, s54, s2
	s_addc_u32 s7, s55, s3
	s_lshl_b64 s[2:3], s[68:69], 21
	s_add_u32 s8, s23, s2
	s_addc_u32 s3, s24, s3
	s_add_i32 s9, s43, s44
	s_and_b32 s2, s42, 0x3e0
	s_add_i32 s9, s9, 0xfffee200
	s_and_b32 s9, s9, 0x3c0
	s_lshl_b32 s10, s2, 2
	s_add_u32 s6, s6, s10
	v_or_b32_e32 v6, s9, v39
	s_addc_u32 s7, s7, 0
	v_lshlrev_b32_e32 v2, 2, v36
	v_lshl_add_u64 v[4:5], s[6:7], 0, v[2:3]
	v_lshlrev_b32_e32 v2, 12, v6
	v_lshl_add_u64 v[32:33], v[4:5], 0, v[2:3]
	v_add_co_u32_e32 v8, vcc, s81, v32
	global_load_dwordx4 v[4:7], v[32:33], off nt
	s_nop 0
	v_addc_co_u32_e32 v9, vcc, 0, v33, vcc
	global_load_dwordx4 v[8:11], v[8:9], off nt
	v_add_co_u32_e32 v12, vcc, s79, v32
	v_add_u32_e32 v2, v44, v45
	s_nop 0
	v_addc_co_u32_e32 v13, vcc, 0, v33, vcc
	global_load_dwordx4 v[12:15], v[12:13], off nt
	v_add_co_u32_e32 v16, vcc, s80, v32
	s_lshl_b32 s6, s9, 1
	s_nop 0
	v_addc_co_u32_e32 v17, vcc, 0, v33, vcc
	global_load_dwordx4 v[16:19], v[16:17], off nt
	v_add_co_u32_e32 v20, vcc, s85, v32
	s_add_u32 s6, s8, s6
	s_nop 0
	v_addc_co_u32_e32 v21, vcc, 0, v33, vcc
	global_load_dwordx4 v[20:23], v[20:21], off nt
	v_add_co_u32_e32 v24, vcc, s86, v32
	s_addc_u32 s7, s3, 0
	s_nop 0
	v_addc_co_u32_e32 v25, vcc, 0, v33, vcc
	global_load_dwordx4 v[24:27], v[24:25], off nt
	v_add_co_u32_e32 v28, vcc, s87, v32
	v_readlane_b32 s49, v253, 17
	s_nop 0
	v_addc_co_u32_e32 v29, vcc, 0, v33, vcc
	global_load_dwordx4 v[28:31], v[28:29], off nt
	v_add_co_u32_e32 v32, vcc, s89, v32
	v_readlane_b32 s50, v253, 18
	s_nop 0
	v_addc_co_u32_e32 v33, vcc, 0, v33, vcc
	global_load_dwordx4 v[32:35], v[32:33], off nt
	v_readlane_b32 s51, v253, 19
	v_readlane_b32 s52, v253, 20
	v_readlane_b32 s53, v253, 21
	v_readlane_b32 s56, v253, 24
	v_readlane_b32 s57, v253, 25
	v_readlane_b32 s58, v253, 26
	v_readlane_b32 s59, v253, 27
	v_readlane_b32 s60, v253, 28
	v_readlane_b32 s61, v253, 29
	v_readlane_b32 s62, v253, 30
	v_readlane_b32 s63, v253, 31
	s_waitcnt vmcnt(0)
	ds_write2_b32 v2, v4, v5 offset1:1
	ds_write2_b32 v2, v6, v7 offset0:2 offset1:3
	v_add_u32_e32 v4, 0x420, v2
	ds_write2_b32 v4, v8, v9 offset1:1
	v_add_u32_e32 v4, 0x428, v2
	ds_write2_b32 v4, v10, v11 offset1:1
	v_add_u32_e32 v4, 0x840, v2
	ds_write2_b32 v4, v12, v13 offset1:1
	v_add_u32_e32 v4, 0x848, v2
	ds_write2_b32 v4, v14, v15 offset1:1
	v_add_u32_e32 v4, 0xc60, v2
	ds_write2_b32 v4, v16, v17 offset1:1
	v_add_u32_e32 v4, 0xc68, v2
	ds_write2_b32 v4, v18, v19 offset1:1
	v_add_u32_e32 v4, 0x1080, v2
	ds_write2_b32 v4, v20, v21 offset1:1
	v_add_u32_e32 v4, 0x1088, v2
	ds_write2_b32 v4, v22, v23 offset1:1
	v_add_u32_e32 v4, 0x14a0, v2
	ds_write2_b32 v4, v24, v25 offset1:1
	v_add_u32_e32 v4, 0x14a8, v2
	ds_write2_b32 v4, v26, v27 offset1:1
	v_add_u32_e32 v4, 0x18c0, v2
	ds_write2_b32 v4, v28, v29 offset1:1
	v_add_u32_e32 v4, 0x18c8, v2
	ds_write2_b32 v4, v30, v31 offset1:1
	v_add_u32_e32 v4, 0x1ce0, v2
	v_add_u32_e32 v2, 0x1ce8, v2
	ds_write2_b32 v4, v32, v33 offset1:1
	ds_write2_b32 v2, v34, v35 offset1:1
	s_waitcnt lgkmcnt(0)
	ds_read2_b32 v[10:11], v49 offset0:33 offset1:41
	ds_read2_b32 v[12:13], v49 offset1:8
	v_lshlrev_b32_e32 v2, 1, v38
	ds_read2_b32 v[14:15], v49 offset0:66 offset1:74
	ds_read2_b32 v[16:17], v49 offset0:99 offset1:107
	ds_read2_b32 v[18:19], v49 offset0:132 offset1:140
	ds_read2_b32 v[20:21], v49 offset0:165 offset1:173
	ds_read2_b32 v[22:23], v49 offset0:198 offset1:206
	ds_read2_b32 v[24:25], v49 offset0:231 offset1:239
	v_lshl_add_u64 v[8:9], s[6:7], 0, v[2:3]
	v_or_b32_e32 v2, s2, v39
	v_lshlrev_b32_e32 v2, 11, v2
	v_lshl_add_u64 v[26:27], v[8:9], 0, v[2:3]
	v_or_b32_e32 v2, s2, v46
	s_waitcnt lgkmcnt(0)
	v_cvt_pk_bf16_f32 v4, v12, v10
	v_lshlrev_b32_e32 v2, 11, v2
	v_cvt_pk_bf16_f32 v5, v14, v16
	v_cvt_pk_bf16_f32 v6, v18, v20
	v_cvt_pk_bf16_f32 v7, v22, v24
	global_store_dwordx4 v[26:27], v[4:7], off sc1 nt
	s_nop 1
	v_cvt_pk_bf16_f32 v4, v13, v11
	v_lshl_add_u64 v[10:11], v[8:9], 0, v[2:3]
	v_cvt_pk_bf16_f32 v5, v15, v17
	v_cvt_pk_bf16_f32 v6, v19, v21
	v_cvt_pk_bf16_f32 v7, v23, v25
	global_store_dwordx4 v[10:11], v[4:7], off sc1 nt
	ds_read2_b32 v[10:11], v49 offset0:16 offset1:24
	ds_read2_b32 v[12:13], v49 offset0:49 offset1:57
	ds_read2_b32 v[14:15], v49 offset0:82 offset1:90
	ds_read2_b32 v[16:17], v49 offset0:115 offset1:123
	ds_read2_b32 v[18:19], v49 offset0:148 offset1:156
	ds_read2_b32 v[20:21], v49 offset0:181 offset1:189
	ds_read2_b32 v[22:23], v49 offset0:214 offset1:222
	ds_read2_b32 v[24:25], v49 offset0:247 offset1:255
	v_or_b32_e32 v2, s2, v47
	v_lshlrev_b32_e32 v2, 11, v2
	v_lshl_add_u64 v[26:27], v[8:9], 0, v[2:3]
	v_or_b32_e32 v2, s2, v48
	v_lshlrev_b32_e32 v2, 11, v2
	s_waitcnt lgkmcnt(6)
	v_cvt_pk_bf16_f32 v4, v10, v12
	s_waitcnt lgkmcnt(4)
	v_cvt_pk_bf16_f32 v5, v14, v16
	s_waitcnt lgkmcnt(2)
	v_cvt_pk_bf16_f32 v6, v18, v20
	s_waitcnt lgkmcnt(0)
	v_cvt_pk_bf16_f32 v7, v22, v24
	v_lshl_add_u64 v[8:9], v[8:9], 0, v[2:3]
	global_store_dwordx4 v[26:27], v[4:7], off sc1 nt
	s_nop 1
	v_cvt_pk_bf16_f32 v4, v11, v13
	v_cvt_pk_bf16_f32 v5, v15, v17
	v_cvt_pk_bf16_f32 v6, v19, v21
	v_cvt_pk_bf16_f32 v7, v23, v25
	global_store_dwordx4 v[8:9], v[4:7], off sc1 nt
	s_waitcnt lgkmcnt(0)

; #define LAS __attribute__((address_space(3)))
; __device__ __forceinline__ void transpose_item(const float* W, int K, int N, bf16* WT, int drow0, int kb, int n0, LAS float* scr, int lane) {
;     const int k0 = 64 * kb; const int c4 = 4 * (lane & 7); const bool ok = (n0 + c4) < N;
;     f32x4 v[8];
; #pragma unroll
;     for (int i = 0; i < 8; ++i) { const int kk = 8 * i + (lane >> 3); v[i] = ok ? *(const f32x4*)(W + (size_t)(k0 + kk) * N + n0 + c4) : (f32x4){0.f, 0.f, 0.f, 0.f}; }
; __device__ __forceinline__ void convert_item(const In& I, unsigned char* ws, int it, LAS float* scr, int lane) {
;     ...
;     if (r < 2 * I_NIN) { const int j = r / I_NIN; r -= j * I_NIN; const int kb = r / 88, nb = r % 88;
;         transpose_item(I.nsa_w_in + (size_t)j * D * NSA_IN, D, NSA_IN, Wnin + (size_t)j * NSA_IN_PAD * D, 32 * nb, kb, 32 * nb, scr, lane); return; }
.LBB0_202:
	s_andn2_b64 vcc, exec, s[2:3]
	s_cbranch_vccnz .LBB0_220
	s_add_i32 s6, s40, 0x2400
	s_cmpk_gt_u32 s6, 0x57f
	s_cselect_b64 s[10:11], -1, 0
	s_and_b64 s[2:3], s[10:11], exec
	s_cselect_b32 s2, 0xfa80, 0
	s_cselect_b32 s3, 0xa30000, 0
	s_add_i32 s6, s6, s2
	s_sext_i32_i16 s2, s6
	s_mulk_i32 s2, 0xba3
	s_lshr_b32 s7, s2, 31
	s_ashr_i32 s2, s2, 18
	v_readlane_b32 s48, v253, 0
	s_add_i32 s2, s2, s7
	v_readlane_b32 s49, v253, 1
	v_readlane_b32 s50, v253, 2
	v_readlane_b32 s51, v253, 3
	v_readlane_b32 s52, v253, 4
	v_readlane_b32 s53, v253, 5
	s_mul_i32 s7, s2, 0x58
	v_readlane_b32 s54, v253, 6
	v_readlane_b32 s55, v253, 7
	v_readlane_b32 s56, v253, 8
	v_readlane_b32 s57, v253, 9
	v_readlane_b32 s60, v253, 12
	v_readlane_b32 s61, v253, 13
	s_mov_b64 s[48:49], s[52:53]
	s_sub_i32 s6, s6, s7
	s_mov_b64 s[50:51], s[54:55]
	s_mov_b64 s[52:53], s[56:57]
	s_mov_b64 s[56:57], s[60:61]
	s_sext_i32_i16 s6, s6
	s_add_u32 s9, s56, s3
	s_addc_u32 s46, s57, 0
	s_lshl_b32 s6, s6, 5
	s_ashr_i32 s7, s6, 31
	s_lshl_b32 s8, s2, 6
	s_lshl_b64 s[12:13], s[6:7], 2
	v_or_b32_e32 v2, s6, v36
	s_movk_i32 s2, 0xa30
	s_add_u32 s12, s9, s12
	v_cmp_gt_i32_e64 s[2:3], s2, v2
	s_addc_u32 s13, s46, s13
	v_lshlrev_b32_e32 v2, 2, v36
	v_or_b32_e32 v42, s8, v39
	v_lshl_add_u64 v[40:41], s[12:13], 0, v[2:3]
	v_mov_b32_e32 v8, 0
	v_mov_b32_e32 v4, 0
	v_mov_b32_e32 v5, 0
	v_mov_b32_e32 v6, 0
	v_mov_b32_e32 v7, 0
	v_readlane_b32 s58, v253, 10
	v_readlane_b32 s59, v253, 11
	v_readlane_b32 s62, v253, 14
	v_readlane_b32 s63, v253, 15
	s_and_saveexec_b64 s[12:13], s[2:3]
	s_cbranch_execz .LBB0_205
	v_mul_i32_i24_e32 v4, 0x28c0, v42
	v_ashrrev_i32_e32 v5, 31, v4
	v_lshl_add_u64 v[4:5], v[40:41], 0, v[4:5]
	global_load_dwordx4 v[4:7], v[4:5], off nt
.LBB0_205:
	s_or_b64 exec, exec, s[12:13]
	v_mov_b32_e32 v9, 0
	v_mov_b32_e32 v10, 0
	v_mov_b32_e32 v11, 0
	s_and_saveexec_b64 s[12:13], s[2:3]
	s_cbranch_execz .LBB0_207
	v_mul_i32_i24_e32 v8, 0x28c0, v42
	v_ashrrev_i32_e32 v9, 31, v8
	v_lshl_add_u64 v[8:9], v[40:41], 0, v[8:9]
	v_add_co_u32_e32 v8, vcc, 0x14000, v8
	s_nop 1
	v_addc_co_u32_e32 v9, vcc, 0, v9, vcc
	global_load_dwordx4 v[8:11], v[8:9], off offset:1536 nt
.LBB0_207:
	s_or_b64 exec, exec, s[12:13]
	v_mov_b32_e32 v12, 0
	v_mov_b32_e32 v16, 0
	v_mov_b32_e32 v17, 0
	v_mov_b32_e32 v18, 0
	v_mov_b32_e32 v19, 0
	s_and_saveexec_b64 s[12:13], s[2:3]
	s_cbranch_execz .LBB0_209
	v_mul_i32_i24_e32 v14, 0x28c0, v42
	v_ashrrev_i32_e32 v15, 31, v14
	v_lshl_add_u64 v[14:15], v[40:41], 0, v[14:15]
	v_add_co_u32_e32 v14, vcc, 0x28000, v14
	s_nop 1
	v_addc_co_u32_e32 v15, vcc, 0, v15, vcc
	global_load_dwordx4 v[16:19], v[14:15], off offset:3072 nt
.LBB0_209:
	s_or_b64 exec, exec, s[12:13]
	v_mov_b32_e32 v13, 0
	v_mov_b32_e32 v14, 0
	v_mov_b32_e32 v15, 0
	s_and_saveexec_b64 s[12:13], s[2:3]
	s_cbranch_execz .LBB0_211
	v_mul_i32_i24_e32 v12, 0x28c0, v42
	v_ashrrev_i32_e32 v13, 31, v12
	v_lshl_add_u64 v[12:13], v[40:41], 0, v[12:13]
	v_add_co_u32_e32 v12, vcc, 0x3d000, v12
	s_nop 1
	v_addc_co_u32_e32 v13, vcc, 0, v13, vcc
	global_load_dwordx4 v[12:15], v[12:13], off offset:512 nt
.LBB0_211:
	s_or_b64 exec, exec, s[12:13]
	v_mov_b32_e32 v20, 0
	v_mov_b32_e32 v24, 0
	v_mov_b32_e32 v25, 0
	v_mov_b32_e32 v26, 0
	v_mov_b32_e32 v27, 0
	s_and_saveexec_b64 s[12:13], s[2:3]
	s_cbranch_execz .LBB0_213
	v_mul_i32_i24_e32 v22, 0x28c0, v42
	v_ashrrev_i32_e32 v23, 31, v22
	v_lshl_add_u64 v[22:23], v[40:41], 0, v[22:23]
	v_add_co_u32_e32 v22, vcc, 0x51000, v22
	s_nop 1
	v_addc_co_u32_e32 v23, vcc, 0, v23, vcc
	global_load_dwordx4 v[24:27], v[22:23], off offset:2048 nt
.LBB0_213:
	s_or_b64 exec, exec, s[12:13]
	v_mov_b32_e32 v21, 0
	v_mov_b32_e32 v22, 0
	v_mov_b32_e32 v23, 0
	s_and_saveexec_b64 s[12:13], s[2:3]
	s_cbranch_execz .LBB0_215
	v_mul_i32_i24_e32 v20, 0x28c0, v42
	v_ashrrev_i32_e32 v21, 31, v20
	v_lshl_add_u64 v[20:21], v[40:41], 0, v[20:21]
	v_add_co_u32_e32 v20, vcc, 0x65000, v20
	s_nop 1
	v_addc_co_u32_e32 v21, vcc, 0, v21, vcc
	global_load_dwordx4 v[20:23], v[20:21], off offset:3584 nt
.LBB0_215:
	s_or_b64 exec, exec, s[12:13]
	v_mov_b32_e32 v28, 0
	v_mov_b32_e32 v32, 0
	v_mov_b32_e32 v33, 0
	v_mov_b32_e32 v34, 0
	v_mov_b32_e32 v35, 0
	s_and_saveexec_b64 s[12:13], s[2:3]
	s_cbranch_execz .LBB0_217
	v_mul_i32_i24_e32 v30, 0x28c0, v42
	v_ashrrev_i32_e32 v31, 31, v30
	v_lshl_add_u64 v[30:31], v[40:41], 0, v[30:31]
	v_add_co_u32_e32 v30, vcc, 0x7a000, v30
	s_nop 1
	v_addc_co_u32_e32 v31, vcc, 0, v31, vcc
	global_load_dwordx4 v[32:35], v[30:31], off offset:1024 nt
; #define GAS __attribute__((address_space(1)))
; #define LAS __attribute__((address_space(3)))
; #define LDS_WAIT() asm volatile("s_waitcnt lgkmcnt(0)" ::: "memory")
; __device__ __forceinline__ unsigned pk2(float lo, float hi) { unsigned r; asm("v_cvt_pk_bf16_f32 %0, %1, %2" : "=v"(r) : "v"(lo), "v"(hi)); return r; }
; __device__ __forceinline__ void transpose_item(const float* W, int K, int N, bf16* WT, int drow0, int kb, int n0, LAS float* scr, int lane) {
;     const int k0 = 64 * kb; const int c4 = 4 * (lane & 7); const bool ok = (n0 + c4) < N;
;     f32x4 v[8];
; #pragma unroll
;     for (int i = 0; i < 8; ++i) { const int kk = 8 * i + (lane >> 3); v[i] = ok ? *(const f32x4*)(W + (size_t)(k0 + kk) * N + n0 + c4) : (f32x4){0.f, 0.f, 0.f, 0.f}; }
; #pragma unroll
;     for (int i = 0; i < 8; ++i) { const int kk = 8 * i + (lane >> 3); LAS float* d = scr + kk * 33 + c4; d[0] = v[i][0]; d[1] = v[i][1]; d[2] = v[i][2]; d[3] = v[i][3]; }
;     LDS_WAIT(); asm volatile("" ::: "memory");
;     const int c = lane & 7;
; #pragma unroll
;     for (int j = 0; j < 4; ++j) { const int n = (lane >> 3) + 8 * j; const LAS float* s = scr + (8 * c) * 33 + n;
;         v4u o; o.x = pk2(s[0 * 33], s[1 * 33]); o.y = pk2(s[2 * 33], s[3 * 33]); o.z = pk2(s[4 * 33], s[5 * 33]); o.w = pk2(s[6 * 33], s[7 * 33]);
;         *(GAS v4u*)(WT + (size_t)(drow0 + n) * K + k0 + 8 * c) = o; }
;     LDS_WAIT(); asm volatile("" ::: "memory");
; }
.LBB0_217:
	s_or_b64 exec, exec, s[12:13]
	v_mov_b32_e32 v29, 0
	v_mov_b32_e32 v30, 0
	v_mov_b32_e32 v31, 0
	s_and_saveexec_b64 s[12:13], s[2:3]
	s_cbranch_execz .LBB0_219
	v_mul_i32_i24_e32 v28, 0x28c0, v42
	v_ashrrev_i32_e32 v29, 31, v28
	v_lshl_add_u64 v[28:29], v[40:41], 0, v[28:29]
	v_add_co_u32_e32 v28, vcc, 0x8e000, v28
	s_nop 1
	v_addc_co_u32_e32 v29, vcc, 0, v29, vcc
	global_load_dwordx4 v[28:31], v[28:29], off offset:2560 nt
.LBB0_219:
	s_or_b64 exec, exec, s[12:13]
	v_add_u32_e32 v2, v44, v45
	s_waitcnt vmcnt(0)
	ds_write2_b32 v2, v4, v5 offset1:1
	ds_write2_b32 v2, v6, v7 offset0:2 offset1:3
	v_add_u32_e32 v4, 0x420, v2
	ds_write2_b32 v4, v8, v9 offset1:1
	v_add_u32_e32 v4, 0x428, v2
	ds_write2_b32 v4, v10, v11 offset1:1
	v_add_u32_e32 v4, 0x840, v2
	ds_write2_b32 v4, v16, v17 offset1:1
	v_add_u32_e32 v4, 0x848, v2
	ds_write2_b32 v4, v18, v19 offset1:1
	v_add_u32_e32 v4, 0xc60, v2
	ds_write2_b32 v4, v12, v13 offset1:1
	v_add_u32_e32 v4, 0xc68, v2
	ds_write2_b32 v4, v14, v15 offset1:1
	v_add_u32_e32 v4, 0x1080, v2
	ds_write2_b32 v4, v24, v25 offset1:1
	v_add_u32_e32 v4, 0x1088, v2
	ds_write2_b32 v4, v26, v27 offset1:1
	v_add_u32_e32 v4, 0x14a0, v2
	ds_write2_b32 v4, v20, v21 offset1:1
	v_add_u32_e32 v4, 0x14a8, v2
	ds_write2_b32 v4, v22, v23 offset1:1
	v_add_u32_e32 v4, 0x18c0, v2
	ds_write2_b32 v4, v32, v33 offset1:1
	v_add_u32_e32 v4, 0x18c8, v2
	s_and_b64 s[2:3], s[10:11], exec
	ds_write2_b32 v4, v34, v35 offset1:1
	v_add_u32_e32 v4, 0x1ce0, v2
	v_add_u32_e32 v2, 0x1ce8, v2
	s_cselect_b32 s2, 0x580000, 0
	ds_write2_b32 v4, v28, v29 offset1:1
	ds_write2_b32 v2, v30, v31 offset1:1
	s_add_u32 s7, s21, s2
	s_waitcnt lgkmcnt(0)
	s_addc_u32 s10, s22, 0
	s_ashr_i32 s9, s8, 31
	s_lshl_b64 s[2:3], s[8:9], 1
	ds_read2_b32 v[8:9], v49 offset0:33 offset1:41
	ds_read2_b32 v[10:11], v49 offset1:8
	ds_read2_b32 v[12:13], v49 offset0:66 offset1:74
	ds_read2_b32 v[14:15], v49 offset0:99 offset1:107
	ds_read2_b32 v[16:17], v49 offset0:132 offset1:140
	ds_read2_b32 v[18:19], v49 offset0:165 offset1:173
	ds_read2_b32 v[20:21], v49 offset0:198 offset1:206
	ds_read2_b32 v[22:23], v49 offset0:231 offset1:239
	s_add_u32 s2, s7, s2
	v_or_b32_e32 v26, s6, v39
	s_addc_u32 s3, s10, s3
	v_lshlrev_b32_e32 v2, 1, v38
	v_ashrrev_i32_e32 v27, 31, v26
	v_lshl_add_u64 v[24:25], s[2:3], 0, v[2:3]
	v_lshlrev_b64 v[26:27], 11, v[26:27]
	s_waitcnt lgkmcnt(0)
	v_cvt_pk_bf16_f32 v4, v10, v8
	v_lshl_add_u64 v[26:27], v[24:25], 0, v[26:27]
	v_or_b32_e32 v8, s6, v46
	v_cvt_pk_bf16_f32 v5, v12, v14
	v_cvt_pk_bf16_f32 v6, v16, v18
	v_cvt_pk_bf16_f32 v7, v20, v22
	global_store_dwordx4 v[26:27], v[4:7], off sc1 nt
	s_nop 1
	v_cvt_pk_bf16_f32 v4, v11, v9
	v_ashrrev_i32_e32 v9, 31, v8
	v_lshlrev_b64 v[8:9], 11, v[8:9]
	v_cvt_pk_bf16_f32 v5, v13, v15
	v_cvt_pk_bf16_f32 v6, v17, v19
	v_cvt_pk_bf16_f32 v7, v21, v23
	v_lshl_add_u64 v[8:9], v[24:25], 0, v[8:9]
	ds_read2_b32 v[10:11], v49 offset0:16 offset1:24
	ds_read2_b32 v[12:13], v49 offset0:49 offset1:57
	ds_read2_b32 v[14:15], v49 offset0:82 offset1:90
	ds_read2_b32 v[16:17], v49 offset0:115 offset1:123
	ds_read2_b32 v[18:19], v49 offset0:148 offset1:156
	ds_read2_b32 v[20:21], v49 offset0:181 offset1:189
	ds_read2_b32 v[22:23], v49 offset0:214 offset1:222
	ds_read2_b32 v[26:27], v49 offset0:247 offset1:255
	global_store_dwordx4 v[8:9], v[4:7], off sc1 nt
	v_or_b32_e32 v8, s6, v47
	v_ashrrev_i32_e32 v9, 31, v8
	v_lshlrev_b64 v[8:9], 11, v[8:9]
	v_lshl_add_u64 v[8:9], v[24:25], 0, v[8:9]
	s_waitcnt lgkmcnt(6)
	v_cvt_pk_bf16_f32 v4, v10, v12
	s_waitcnt lgkmcnt(4)
	v_cvt_pk_bf16_f32 v5, v14, v16
	s_waitcnt lgkmcnt(2)
	v_cvt_pk_bf16_f32 v6, v18, v20
	s_waitcnt lgkmcnt(0)
	v_cvt_pk_bf16_f32 v7, v22, v26
	global_store_dwordx4 v[8:9], v[4:7], off sc1 nt
	v_or_b32_e32 v8, s6, v48
	v_ashrrev_i32_e32 v9, 31, v8
	v_lshlrev_b64 v[8:9], 11, v[8:9]
	v_lshl_add_u64 v[8:9], v[24:25], 0, v[8:9]
	v_cvt_pk_bf16_f32 v4, v11, v13
	v_cvt_pk_bf16_f32 v5, v15, v17
	v_cvt_pk_bf16_f32 v6, v19, v21
	v_cvt_pk_bf16_f32 v7, v23, v27
	global_store_dwordx4 v[8:9], v[4:7], off sc1 nt
	s_waitcnt lgkmcnt(0)

; #define GAS __attribute__((address_space(1)))
; #define LAS __attribute__((address_space(3)))
; #define LDS_WAIT() asm volatile("s_waitcnt lgkmcnt(0)" ::: "memory")
; __device__ __forceinline__ unsigned pk2(float lo, float hi) { unsigned r; asm("v_cvt_pk_bf16_f32 %0, %1, %2" : "=v"(r) : "v"(lo), "v"(hi)); return r; }
; __device__ __forceinline__ void transpose_item(const float* W, int K, int N, bf16* WT, int drow0, int kb, int n0, LAS float* scr, int lane) {
;     const int k0 = 64 * kb; const int c4 = 4 * (lane & 7); const bool ok = (n0 + c4) < N;
;     f32x4 v[8];
; #pragma unroll
;     for (int i = 0; i < 8; ++i) { const int kk = 8 * i + (lane >> 3); v[i] = ok ? *(const f32x4*)(W + (size_t)(k0 + kk) * N + n0 + c4) : (f32x4){0.f, 0.f, 0.f, 0.f}; }
; #pragma unroll
;     for (int i = 0; i < 8; ++i) { const int kk = 8 * i + (lane >> 3); LAS float* d = scr + kk * 33 + c4; d[0] = v[i][0]; d[1] = v[i][1]; d[2] = v[i][2]; d[3] = v[i][3]; }
;     LDS_WAIT(); asm volatile("" ::: "memory");
;     const int c = lane & 7;
; #pragma unroll
;     for (int j = 0; j < 4; ++j) { const int n = (lane >> 3) + 8 * j; const LAS float* s = scr + (8 * c) * 33 + n;
;         v4u o; o.x = pk2(s[0 * 33], s[1 * 33]); o.y = pk2(s[2 * 33], s[3 * 33]); o.z = pk2(s[4 * 33], s[5 * 33]); o.w = pk2(s[6 * 33], s[7 * 33]);
;         *(GAS v4u*)(WT + (size_t)(drow0 + n) * K + k0 + 8 * c) = o; }
;     LDS_WAIT(); asm volatile("" ::: "memory");
; }
; __device__ __forceinline__ void convert_item(const In& I, unsigned char* ws, int it, LAS float* scr, int lane) {
;     ...
;     if (r < T0) { const int f = r / I_FFN; r -= f * I_FFN;
;     ...
;         else { r -= 2 * I_G; const int kb = r / 32, nb = r % 32; transpose_item(I.w_down + (size_t)f * FF * D, FF, D, Wd + (size_t)f * D * FF, 32 * nb, kb, 32 * nb, scr, lane); }
.LBB0_221:
	s_andn2_b64 vcc, exec, s[2:3]
	s_cbranch_vccnz .LBB0_166
	s_mul_hi_i32 s2, s45, 0x3e0f83e1
	s_lshr_b32 s3, s2, 31
	s_ashr_i32 s6, s2, 10
	s_add_i32 s6, s6, s3
	s_mul_i32 s2, s6, 0xffffef80
	s_add_i32 s7, s40, s2
	s_add_i32 s7, s7, 0xa800
	s_cmpk_gt_i32 s7, 0xaff
	s_mov_b64 s[2:3], -1
	s_cbranch_scc0 .LBB0_224
	v_readlane_b32 s48, v253, 0
	v_readlane_b32 s49, v253, 1
	v_readlane_b32 s50, v253, 2
	v_readlane_b32 s51, v253, 3
	v_readlane_b32 s52, v253, 4
	v_readlane_b32 s53, v253, 5
	v_readlane_b32 s54, v253, 6
	v_readlane_b32 s55, v253, 7
	v_readlane_b32 s56, v253, 8
	v_readlane_b32 s57, v253, 9
	s_mov_b64 s[48:49], s[52:53]
	s_mul_i32 s3, s6, 0xb00000
	s_mov_b64 s[50:51], s[54:55]
	s_mov_b64 s[52:53], s[56:57]
	s_mul_hi_i32 s2, s6, 0xb00000
	s_add_u32 s9, s52, s3
	s_addc_u32 s11, s53, s2
	s_mul_i32 s3, s6, 0x580000
	s_mul_hi_i32 s2, s6, 0x580000
	s_add_u32 s3, s19, s3
	s_addc_u32 s8, s20, s2
	s_mul_i32 s10, s6, 0xffffdf00
	s_add_i32 s12, s43, s44
	s_add_i32 s10, s12, s10
	s_and_b32 s2, s42, 0x3e0
	s_andn2_b32 s10, s10, 63
	s_add_i32 s68, s10, 0xffffea00
	s_lshl_b32 s10, s2, 2
	v_or_b32_e32 v32, s68, v39
	s_add_u32 s10, s9, s10
	s_addc_u32 s11, s11, 0
	v_lshlrev_b32_e32 v2, 2, v36
	v_ashrrev_i32_e32 v33, 31, v32
	v_or_b32_e32 v8, 8, v32
	v_lshl_add_u64 v[34:35], s[10:11], 0, v[2:3]
	v_lshlrev_b64 v[4:5], 12, v[32:33]
	v_ashrrev_i32_e32 v9, 31, v8
	v_lshl_add_u64 v[4:5], v[34:35], 0, v[4:5]
	v_lshlrev_b64 v[8:9], 12, v[8:9]
	v_or_b32_e32 v12, 16, v32
	global_load_dwordx4 v[4:7], v[4:5], off nt
	v_lshl_add_u64 v[8:9], v[34:35], 0, v[8:9]
	v_ashrrev_i32_e32 v13, 31, v12
	global_load_dwordx4 v[8:11], v[8:9], off nt
	v_lshlrev_b64 v[12:13], 12, v[12:13]
	v_or_b32_e32 v16, 24, v32
	v_lshl_add_u64 v[12:13], v[34:35], 0, v[12:13]
	v_ashrrev_i32_e32 v17, 31, v16
	global_load_dwordx4 v[12:15], v[12:13], off nt
	v_lshlrev_b64 v[16:17], 12, v[16:17]
	v_or_b32_e32 v20, 32, v32
	v_lshl_add_u64 v[16:17], v[34:35], 0, v[16:17]
	v_ashrrev_i32_e32 v21, 31, v20
	global_load_dwordx4 v[16:19], v[16:17], off nt
	v_lshlrev_b64 v[20:21], 12, v[20:21]
	v_or_b32_e32 v24, 40, v32
	v_lshl_add_u64 v[20:21], v[34:35], 0, v[20:21]
	v_ashrrev_i32_e32 v25, 31, v24
	global_load_dwordx4 v[20:23], v[20:21], off nt
	v_lshlrev_b64 v[24:25], 12, v[24:25]
	v_or_b32_e32 v28, 48, v32
	v_lshl_add_u64 v[24:25], v[34:35], 0, v[24:25]
	v_ashrrev_i32_e32 v29, 31, v28
	global_load_dwordx4 v[24:27], v[24:25], off nt
	v_lshlrev_b64 v[28:29], 12, v[28:29]
	v_or_b32_e32 v32, 56, v32
	v_lshl_add_u64 v[28:29], v[34:35], 0, v[28:29]
	v_ashrrev_i32_e32 v33, 31, v32
	global_load_dwordx4 v[28:31], v[28:29], off nt
	v_lshlrev_b64 v[32:33], 12, v[32:33]
	v_lshl_add_u64 v[32:33], v[34:35], 0, v[32:33]
	global_load_dwordx4 v[32:35], v[32:33], off nt
	v_add_u32_e32 v2, v44, v45
	s_lshl_b64 s[10:11], s[68:69], 1
	s_add_u32 s10, s3, s10
	s_addc_u32 s11, s8, s11
	v_readlane_b32 s58, v253, 10
	v_readlane_b32 s59, v253, 11
	v_readlane_b32 s60, v253, 12
	v_readlane_b32 s61, v253, 13
	v_readlane_b32 s62, v253, 14
	v_readlane_b32 s63, v253, 15
	s_waitcnt vmcnt(0)
	ds_write2_b32 v2, v4, v5 offset1:1
	ds_write2_b32 v2, v6, v7 offset0:2 offset1:3
	v_add_u32_e32 v4, 0x420, v2
	ds_write2_b32 v4, v8, v9 offset1:1
	v_add_u32_e32 v4, 0x428, v2
	ds_write2_b32 v4, v10, v11 offset1:1
	v_add_u32_e32 v4, 0x840, v2
	ds_write2_b32 v4, v12, v13 offset1:1
	v_add_u32_e32 v4, 0x848, v2
	ds_write2_b32 v4, v14, v15 offset1:1
	v_add_u32_e32 v4, 0xc60, v2
	ds_write2_b32 v4, v16, v17 offset1:1
	v_add_u32_e32 v4, 0xc68, v2
	ds_write2_b32 v4, v18, v19 offset1:1
	v_add_u32_e32 v4, 0x1080, v2
	ds_write2_b32 v4, v20, v21 offset1:1
	v_add_u32_e32 v4, 0x1088, v2
	ds_write2_b32 v4, v22, v23 offset1:1
	v_add_u32_e32 v4, 0x14a0, v2
	ds_write2_b32 v4, v24, v25 offset1:1
	v_add_u32_e32 v4, 0x14a8, v2
	ds_write2_b32 v4, v26, v27 offset1:1
	v_add_u32_e32 v4, 0x18c0, v2
	ds_write2_b32 v4, v28, v29 offset1:1
	v_add_u32_e32 v4, 0x18c8, v2
	ds_write2_b32 v4, v30, v31 offset1:1
	v_add_u32_e32 v4, 0x1ce0, v2
	v_add_u32_e32 v2, 0x1ce8, v2
	ds_write2_b32 v4, v32, v33 offset1:1
	ds_write2_b32 v2, v34, v35 offset1:1
	s_waitcnt lgkmcnt(0)
	ds_read2_b32 v[10:11], v49 offset0:33 offset1:41
	ds_read2_b32 v[12:13], v49 offset1:8
	v_lshlrev_b32_e32 v2, 1, v38
	ds_read2_b32 v[14:15], v49 offset0:66 offset1:74
	ds_read2_b32 v[16:17], v49 offset0:99 offset1:107
	ds_read2_b32 v[18:19], v49 offset0:132 offset1:140
	ds_read2_b32 v[20:21], v49 offset0:165 offset1:173
	ds_read2_b32 v[22:23], v49 offset0:198 offset1:206
	ds_read2_b32 v[24:25], v49 offset0:231 offset1:239
	v_lshl_add_u64 v[8:9], s[10:11], 0, v[2:3]
	v_or_b32_e32 v2, s2, v39
	v_mul_u32_u24_e32 v2, 0x1600, v2
	v_lshl_add_u64 v[26:27], v[8:9], 0, v[2:3]
	v_or_b32_e32 v2, s2, v46
	s_waitcnt lgkmcnt(0)
	v_cvt_pk_bf16_f32 v4, v12, v10
	v_mul_u32_u24_e32 v2, 0x1600, v2
	v_cvt_pk_bf16_f32 v5, v14, v16
	v_cvt_pk_bf16_f32 v6, v18, v20
	v_cvt_pk_bf16_f32 v7, v22, v24
	global_store_dwordx4 v[26:27], v[4:7], off sc1 nt
	s_nop 1
	v_cvt_pk_bf16_f32 v4, v13, v11
	v_lshl_add_u64 v[10:11], v[8:9], 0, v[2:3]
	v_cvt_pk_bf16_f32 v5, v15, v17
	v_cvt_pk_bf16_f32 v6, v19, v21
	v_cvt_pk_bf16_f32 v7, v23, v25
	global_store_dwordx4 v[10:11], v[4:7], off sc1 nt
	ds_read2_b32 v[10:11], v49 offset0:16 offset1:24
	ds_read2_b32 v[12:13], v49 offset0:49 offset1:57
	ds_read2_b32 v[14:15], v49 offset0:82 offset1:90
	ds_read2_b32 v[16:17], v49 offset0:115 offset1:123
	ds_read2_b32 v[18:19], v49 offset0:148 offset1:156
	ds_read2_b32 v[20:21], v49 offset0:181 offset1:189
	ds_read2_b32 v[22:23], v49 offset0:214 offset1:222
	ds_read2_b32 v[24:25], v49 offset0:247 offset1:255
	v_or_b32_e32 v2, s2, v47
	v_mul_u32_u24_e32 v2, 0x1600, v2
	v_lshl_add_u64 v[26:27], v[8:9], 0, v[2:3]
	v_or_b32_e32 v2, s2, v48
	v_mul_u32_u24_e32 v2, 0x1600, v2
	s_waitcnt lgkmcnt(6)
	v_cvt_pk_bf16_f32 v4, v10, v12
	s_waitcnt lgkmcnt(4)
	v_cvt_pk_bf16_f32 v5, v14, v16
	s_waitcnt lgkmcnt(2)
	v_cvt_pk_bf16_f32 v6, v18, v20
	s_waitcnt lgkmcnt(0)
	v_cvt_pk_bf16_f32 v7, v22, v24
	v_lshl_add_u64 v[8:9], v[8:9], 0, v[2:3]
	global_store_dwordx4 v[26:27], v[4:7], off sc1 nt
	s_mov_b64 s[2:3], 0
	s_nop 0
	v_cvt_pk_bf16_f32 v4, v11, v13
	v_cvt_pk_bf16_f32 v5, v15, v17
	v_cvt_pk_bf16_f32 v6, v19, v21
	v_cvt_pk_bf16_f32 v7, v23, v25
	global_store_dwordx4 v[8:9], v[4:7], off sc1 nt
	s_waitcnt lgkmcnt(0)
; #define GAS __attribute__((address_space(1)))
; #define LAS __attribute__((address_space(3)))
; #define LDS_WAIT() asm volatile("s_waitcnt lgkmcnt(0)" ::: "memory")
; __device__ __forceinline__ unsigned pk2(float lo, float hi) { unsigned r; asm("v_cvt_pk_bf16_f32 %0, %1, %2" : "=v"(r) : "v"(lo), "v"(hi)); return r; }
; __device__ __forceinline__ void transpose_item(const float* W, int K, int N, bf16* WT, int drow0, int kb, int n0, LAS float* scr, int lane) {
;     const int k0 = 64 * kb; const int c4 = 4 * (lane & 7); const bool ok = (n0 + c4) < N;
;     f32x4 v[8];
; #pragma unroll
;     for (int i = 0; i < 8; ++i) { const int kk = 8 * i + (lane >> 3); v[i] = ok ? *(const f32x4*)(W + (size_t)(k0 + kk) * N + n0 + c4) : (f32x4){0.f, 0.f, 0.f, 0.f}; }
; #pragma unroll
;     for (int i = 0; i < 8; ++i) { const int kk = 8 * i + (lane >> 3); LAS float* d = scr + kk * 33 + c4; d[0] = v[i][0]; d[1] = v[i][1]; d[2] = v[i][2]; d[3] = v[i][3]; }
;     LDS_WAIT(); asm volatile("" ::: "memory");
;     const int c = lane & 7;
; #pragma unroll
;     for (int j = 0; j < 4; ++j) { const int n = (lane >> 3) + 8 * j; const LAS float* s = scr + (8 * c) * 33 + n;
;         v4u o; o.x = pk2(s[0 * 33], s[1 * 33]); o.y = pk2(s[2 * 33], s[3 * 33]); o.z = pk2(s[4 * 33], s[5 * 33]); o.w = pk2(s[6 * 33], s[7 * 33]);
;         *(GAS v4u*)(WT + (size_t)(drow0 + n) * K + k0 + 8 * c) = o; }
;     LDS_WAIT(); asm volatile("" ::: "memory");
; }
; __device__ __forceinline__ void convert_item(const In& I, unsigned char* ws, int it, LAS float* scr, int lane) {
;     ...
;         if (r < 2 * I_G) { const int up = r >= I_G; r -= up * I_G; const int kb = r / 88, nb = r % 88;
;             transpose_item((up ? I.w_up : I.w_gate) + (size_t)f * D * FF, D, FF, Wgu + (size_t)f * NGU * D, 256 * (nb >> 2) + 32 * (nb & 3) + 128 * up, kb, 32 * nb, scr, lane); }
.LBB0_224:
	s_andn2_b64 vcc, exec, s[2:3]
	s_cbranch_vccnz .LBB0_166
	v_readlane_b32 s48, v253, 0
	v_readlane_b32 s49, v253, 1
	v_readlane_b32 s50, v253, 2
	v_readlane_b32 s51, v253, 3
	v_readlane_b32 s52, v253, 4
	v_readlane_b32 s53, v253, 5
	s_cmpk_gt_i32 s7, 0x57f
	v_readlane_b32 s54, v253, 6
	v_readlane_b32 s55, v253, 7
	v_readlane_b32 s56, v253, 8
	v_readlane_b32 s57, v253, 9
	s_mov_b64 s[48:49], s[52:53]
	s_cselect_b32 s2, 0xfffffa80, 0
	s_mul_i32 s3, s6, 0x1080
	s_mov_b64 s[50:51], s[54:55]
	s_cselect_b32 s7, 0x80, 0
	s_cselect_b32 s8, s50, s48
	s_cselect_b32 s9, s51, s49
	s_sub_i32 s2, s2, s3
	s_add_i32 s2, s40, s2
	s_add_i32 s2, s2, 0xa800
	s_mul_hi_i32 s3, s2, 0x2e8ba2e9
	s_lshr_b32 s10, s3, 31
	s_ashr_i32 s3, s3, 4
	s_add_i32 s3, s3, s10
	s_mul_i32 s10, s3, 0x58
	s_sub_i32 s2, s2, s10
	s_mul_hi_i32 s10, s6, 0xb00000
	s_mul_i32 s6, s6, 0xb00000
	s_add_u32 s11, s8, s6
	s_addc_u32 s12, s9, s10
	s_add_u32 s13, s28, s6
	s_addc_u32 s10, s29, s10
	s_lshl_b32 s8, s2, 5
	s_lshl_b32 s6, s2, 6
	s_and_b32 s2, s8, 0x60
	s_and_b32 s6, s6, 0xffffff00
	s_or_b32 s2, s2, s7
	s_ashr_i32 s9, s8, 31
	s_or_b32 s6, s2, s6
	s_lshl_b32 s2, s3, 6
	s_lshl_b64 s[8:9], s[8:9], 2
	s_add_u32 s8, s11, s8
	s_addc_u32 s9, s12, s9
	v_lshlrev_b32_e32 v2, 2, v36
	v_or_b32_e32 v34, s2, v39
	v_lshl_add_u64 v[32:33], s[8:9], 0, v[2:3]
	s_movk_i32 s3, 0x2c00
	v_mad_i64_i32 v[4:5], s[8:9], v34, s3, v[32:33]
	v_or_b32_e32 v2, 8, v34
	global_load_dwordx4 v[4:7], v[4:5], off nt
	v_mad_i64_i32 v[8:9], s[8:9], v2, s3, v[32:33]
	global_load_dwordx4 v[8:11], v[8:9], off nt
	v_or_b32_e32 v2, 16, v34
	v_mad_i64_i32 v[12:13], s[8:9], v2, s3, v[32:33]
	global_load_dwordx4 v[12:15], v[12:13], off nt
	v_or_b32_e32 v2, 24, v34
	v_mad_i64_i32 v[16:17], s[8:9], v2, s3, v[32:33]
	global_load_dwordx4 v[16:19], v[16:17], off nt
	v_or_b32_e32 v2, 32, v34
	v_mad_i64_i32 v[20:21], s[8:9], v2, s3, v[32:33]
	global_load_dwordx4 v[20:23], v[20:21], off nt
	v_or_b32_e32 v2, 40, v34
	v_mad_i64_i32 v[24:25], s[8:9], v2, s3, v[32:33]
	global_load_dwordx4 v[24:27], v[24:25], off nt
	v_or_b32_e32 v2, 48, v34
	v_mad_i64_i32 v[28:29], s[8:9], v2, s3, v[32:33]
	global_load_dwordx4 v[28:31], v[28:29], off nt
	v_or_b32_e32 v2, 56, v34
	v_mad_i64_i32 v[32:33], s[8:9], v2, s3, v[32:33]
	global_load_dwordx4 v[32:35], v[32:33], off nt
	v_add_u32_e32 v2, v44, v45
	s_ashr_i32 s3, s2, 31
	s_lshl_b64 s[2:3], s[2:3], 1
	s_add_u32 s2, s13, s2
	s_addc_u32 s3, s10, s3
	v_readlane_b32 s58, v253, 10
	v_readlane_b32 s59, v253, 11
	v_readlane_b32 s60, v253, 12
	v_readlane_b32 s61, v253, 13
	v_readlane_b32 s62, v253, 14
	v_readlane_b32 s63, v253, 15
	s_mov_b64 s[52:53], s[56:57]
	s_waitcnt vmcnt(0)
	ds_write2_b32 v2, v4, v5 offset1:1
	ds_write2_b32 v2, v6, v7 offset0:2 offset1:3
	v_add_u32_e32 v4, 0x420, v2
	ds_write2_b32 v4, v8, v9 offset1:1
	v_add_u32_e32 v4, 0x428, v2
	ds_write2_b32 v4, v10, v11 offset1:1
	v_add_u32_e32 v4, 0x840, v2
	ds_write2_b32 v4, v12, v13 offset1:1
	v_add_u32_e32 v4, 0x848, v2
	ds_write2_b32 v4, v14, v15 offset1:1
	v_add_u32_e32 v4, 0xc60, v2
	ds_write2_b32 v4, v16, v17 offset1:1
	v_add_u32_e32 v4, 0xc68, v2
	ds_write2_b32 v4, v18, v19 offset1:1
	v_add_u32_e32 v4, 0x1080, v2
	ds_write2_b32 v4, v20, v21 offset1:1
	v_add_u32_e32 v4, 0x1088, v2
	ds_write2_b32 v4, v22, v23 offset1:1
	v_add_u32_e32 v4, 0x14a0, v2
	ds_write2_b32 v4, v24, v25 offset1:1
	v_add_u32_e32 v4, 0x14a8, v2
	ds_write2_b32 v4, v26, v27 offset1:1
	v_add_u32_e32 v4, 0x18c0, v2
	ds_write2_b32 v4, v28, v29 offset1:1
	v_add_u32_e32 v4, 0x18c8, v2
	ds_write2_b32 v4, v30, v31 offset1:1
	v_add_u32_e32 v4, 0x1ce0, v2
	v_add_u32_e32 v2, 0x1ce8, v2
	ds_write2_b32 v4, v32, v33 offset1:1
	ds_write2_b32 v2, v34, v35 offset1:1
	s_waitcnt lgkmcnt(0)
	ds_read2_b32 v[10:11], v49 offset0:33 offset1:41
	ds_read2_b32 v[12:13], v49 offset1:8
	ds_read2_b32 v[14:15], v49 offset0:66 offset1:74
	ds_read2_b32 v[16:17], v49 offset0:99 offset1:107
	ds_read2_b32 v[18:19], v49 offset0:132 offset1:140
	ds_read2_b32 v[20:21], v49 offset0:165 offset1:173
	ds_read2_b32 v[22:23], v49 offset0:198 offset1:206
	ds_read2_b32 v[24:25], v49 offset0:231 offset1:239
	v_or_b32_e32 v26, s6, v39
	v_lshlrev_b32_e32 v2, 1, v38
	v_ashrrev_i32_e32 v27, 31, v26
	v_lshl_add_u64 v[8:9], s[2:3], 0, v[2:3]
	v_lshlrev_b64 v[26:27], 11, v[26:27]
	s_waitcnt lgkmcnt(0)
	v_cvt_pk_bf16_f32 v4, v12, v10
	v_lshl_add_u64 v[26:27], v[8:9], 0, v[26:27]
	v_or_b32_e32 v10, s6, v46
	v_cvt_pk_bf16_f32 v5, v14, v16
	v_cvt_pk_bf16_f32 v6, v18, v20
	v_cvt_pk_bf16_f32 v7, v22, v24
	global_store_dwordx4 v[26:27], v[4:7], off sc1 nt
	v_or_b32_e32 v26, s6, v47
	v_ashrrev_i32_e32 v27, 31, v26
	v_cvt_pk_bf16_f32 v4, v13, v11
	v_ashrrev_i32_e32 v11, 31, v10
	v_lshlrev_b64 v[10:11], 11, v[10:11]
	v_lshl_add_u64 v[10:11], v[8:9], 0, v[10:11]
	v_cvt_pk_bf16_f32 v5, v15, v17
	v_cvt_pk_bf16_f32 v6, v19, v21
	v_cvt_pk_bf16_f32 v7, v23, v25
	global_store_dwordx4 v[10:11], v[4:7], off sc1 nt
	ds_read2_b32 v[10:11], v49 offset0:16 offset1:24
	ds_read2_b32 v[12:13], v49 offset0:49 offset1:57
	ds_read2_b32 v[14:15], v49 offset0:82 offset1:90
	ds_read2_b32 v[16:17], v49 offset0:115 offset1:123
	ds_read2_b32 v[18:19], v49 offset0:148 offset1:156
	ds_read2_b32 v[20:21], v49 offset0:181 offset1:189
	ds_read2_b32 v[22:23], v49 offset0:214 offset1:222
	ds_read2_b32 v[24:25], v49 offset0:247 offset1:255
	v_lshlrev_b64 v[26:27], 11, v[26:27]
	s_waitcnt lgkmcnt(6)
	v_cvt_pk_bf16_f32 v4, v10, v12
	v_lshl_add_u64 v[26:27], v[8:9], 0, v[26:27]
	v_or_b32_e32 v10, s6, v48
	s_waitcnt lgkmcnt(4)
	v_cvt_pk_bf16_f32 v5, v14, v16
	s_waitcnt lgkmcnt(2)
	v_cvt_pk_bf16_f32 v6, v18, v20
	s_waitcnt lgkmcnt(0)
	v_cvt_pk_bf16_f32 v7, v22, v24
	global_store_dwordx4 v[26:27], v[4:7], off sc1 nt
	s_nop 1
	v_cvt_pk_bf16_f32 v4, v11, v13
	v_ashrrev_i32_e32 v11, 31, v10
	v_lshlrev_b64 v[10:11], 11, v[10:11]
	v_lshl_add_u64 v[8:9], v[8:9], 0, v[10:11]
	v_cvt_pk_bf16_f32 v5, v15, v17
	v_cvt_pk_bf16_f32 v6, v19, v21
	v_cvt_pk_bf16_f32 v7, v23, v25
	global_store_dwordx4 v[8:9], v[4:7], off sc1 nt
	s_waitcnt lgkmcnt(0)
	s_branch .LBB0_166

; #define GAS __attribute__((address_space(1)))
; #define LAS __attribute__((address_space(3)))
; #define LDS_WAIT() asm volatile("s_waitcnt lgkmcnt(0)" ::: "memory")
; __device__ __forceinline__ unsigned pk2(float lo, float hi) { unsigned r; asm("v_cvt_pk_bf16_f32 %0, %1, %2" : "=v"(r) : "v"(lo), "v"(hi)); return r; }
; __device__ __forceinline__ void transpose_item(const float* W, int K, int N, bf16* WT, int drow0, int kb, int n0, LAS float* scr, int lane) {
;     const int k0 = 64 * kb; const int c4 = 4 * (lane & 7); const bool ok = (n0 + c4) < N;
;     f32x4 v[8];
; #pragma unroll
;     for (int i = 0; i < 8; ++i) { const int kk = 8 * i + (lane >> 3); v[i] = ok ? *(const f32x4*)(W + (size_t)(k0 + kk) * N + n0 + c4) : (f32x4){0.f, 0.f, 0.f, 0.f}; }
; #pragma unroll
;     for (int i = 0; i < 8; ++i) { const int kk = 8 * i + (lane >> 3); LAS float* d = scr + kk * 33 + c4; d[0] = v[i][0]; d[1] = v[i][1]; d[2] = v[i][2]; d[3] = v[i][3]; }
;     LDS_WAIT(); asm volatile("" ::: "memory");
;     const int c = lane & 7;
; #pragma unroll
;     for (int j = 0; j < 4; ++j) { const int n = (lane >> 3) + 8 * j; const LAS float* s = scr + (8 * c) * 33 + n;
;         v4u o; o.x = pk2(s[0 * 33], s[1 * 33]); o.y = pk2(s[2 * 33], s[3 * 33]); o.z = pk2(s[4 * 33], s[5 * 33]); o.w = pk2(s[6 * 33], s[7 * 33]);
;         *(GAS v4u*)(WT + (size_t)(drow0 + n) * K + k0 + 8 * c) = o; }
;     LDS_WAIT(); asm volatile("" ::: "memory");
; }
; __device__ __forceinline__ void convert_item(const In& I, unsigned char* ws, int it, LAS float* scr, int lane) {
;     ...
;     { const int jk = r >> 3; r &= 7; const int kb = r >> 1, nb = r & 1;
;         transpose_item(I.nsa_w2 + (size_t)jk * 256 * 64, 256, 64, W2t + (size_t)jk * 64 * 256, 32 * nb, kb, 32 * nb, scr, lane); }
.LBB0_229:
	s_add_i32 s44, s40, 0xa800
	s_cmp_gt_i32 s44, 0x83ff
	s_mov_b64 s[2:3], -1
	s_cbranch_scc0 .LBB0_283
	s_cmpk_gt_u32 s44, 0x8eff
	s_cbranch_scc0 .LBB0_264
	s_cmpk_gt_u32 s44, 0x92ff
	s_cbranch_scc0 .LBB0_261
	s_cmpk_gt_u32 s44, 0x9fff
	s_cbranch_scc0 .LBB0_242
	s_cmpk_gt_u32 s44, 0xa3ff
	s_cbranch_scc0 .LBB0_239
	s_cmpk_gt_u32 s44, 0xa7ff
	s_cbranch_scc0 .LBB0_236
	s_lshr_b32 s68, s40, 3
	v_readlane_b32 s48, v253, 16
	s_lshl_b64 s[2:3], s[68:69], 16
	v_readlane_b32 s52, v253, 20
	v_readlane_b32 s53, v253, 21
	s_add_u32 s6, s52, s2
	s_addc_u32 s7, s53, s3
	s_lshl_b64 s[2:3], s[68:69], 15
	s_add_u32 s8, s35, s2
	s_addc_u32 s3, s39, s3
	s_and_b32 s2, s42, 32
	s_and_b32 s9, s42, 0xc0
	s_lshl_b32 s10, s2, 2
	s_add_u32 s6, s6, s10
	v_or_b32_e32 v6, s9, v39
	s_addc_u32 s7, s7, 0
	v_lshlrev_b32_e32 v2, 2, v36
	v_lshl_add_u64 v[4:5], s[6:7], 0, v[2:3]
	v_lshlrev_b32_e32 v2, 8, v6
	v_lshl_add_u64 v[28:29], v[4:5], 0, v[2:3]
	global_load_dwordx4 v[4:7], v[28:29], off nt
	global_load_dwordx4 v[8:11], v[28:29], off offset:2048 nt
	v_add_co_u32_e32 v16, vcc, s84, v28
	s_movk_i32 s6, 0x3000
	s_nop 0
	v_addc_co_u32_e32 v17, vcc, 0, v29, vcc
	v_add_co_u32_e32 v24, vcc, s74, v28
	v_add_u32_e32 v2, v44, v45
	s_nop 0
	v_addc_co_u32_e32 v25, vcc, 0, v29, vcc
	global_load_dwordx4 v[12:15], v[24:25], off offset:-4096 nt
	s_nop 0
	global_load_dwordx4 v[16:19], v[16:17], off offset:2048 nt
	s_nop 0
	global_load_dwordx4 v[20:23], v[24:25], off nt
	s_nop 0
	global_load_dwordx4 v[24:27], v[24:25], off offset:2048 nt
	v_add_co_u32_e32 v32, vcc, s6, v28
	s_lshl_b32 s6, s9, 1
	s_nop 0
	v_addc_co_u32_e32 v33, vcc, 0, v29, vcc
	global_load_dwordx4 v[28:31], v[32:33], off nt
	s_nop 0
	global_load_dwordx4 v[32:35], v[32:33], off offset:2048 nt
	s_add_u32 s6, s8, s6
	s_addc_u32 s7, s3, 0
	v_readlane_b32 s49, v253, 17
	v_readlane_b32 s50, v253, 18
	v_readlane_b32 s51, v253, 19
	v_readlane_b32 s54, v253, 22
	v_readlane_b32 s55, v253, 23
	v_readlane_b32 s56, v253, 24
	v_readlane_b32 s57, v253, 25
	v_readlane_b32 s58, v253, 26
	v_readlane_b32 s59, v253, 27
	v_readlane_b32 s60, v253, 28
	v_readlane_b32 s61, v253, 29
	v_readlane_b32 s62, v253, 30
	v_readlane_b32 s63, v253, 31
	s_waitcnt vmcnt(0)
	ds_write2_b32 v2, v4, v5 offset1:1
	ds_write2_b32 v2, v6, v7 offset0:2 offset1:3
	v_add_u32_e32 v4, 0x420, v2
	ds_write2_b32 v4, v8, v9 offset1:1
	v_add_u32_e32 v4, 0x428, v2
	ds_write2_b32 v4, v10, v11 offset1:1
	v_add_u32_e32 v4, 0x840, v2
	ds_write2_b32 v4, v12, v13 offset1:1
	v_add_u32_e32 v4, 0x848, v2
	ds_write2_b32 v4, v14, v15 offset1:1
	v_add_u32_e32 v4, 0xc60, v2
	ds_write2_b32 v4, v16, v17 offset1:1
	v_add_u32_e32 v4, 0xc68, v2
	ds_write2_b32 v4, v18, v19 offset1:1
	v_add_u32_e32 v4, 0x1080, v2
	ds_write2_b32 v4, v20, v21 offset1:1
	v_add_u32_e32 v4, 0x1088, v2
	ds_write2_b32 v4, v22, v23 offset1:1
	v_add_u32_e32 v4, 0x14a0, v2
	ds_write2_b32 v4, v24, v25 offset1:1
	v_add_u32_e32 v4, 0x14a8, v2
	ds_write2_b32 v4, v26, v27 offset1:1
	v_add_u32_e32 v4, 0x18c0, v2
	ds_write2_b32 v4, v28, v29 offset1:1
	v_add_u32_e32 v4, 0x18c8, v2
	ds_write2_b32 v4, v30, v31 offset1:1
	v_add_u32_e32 v4, 0x1ce0, v2
	v_add_u32_e32 v2, 0x1ce8, v2
	ds_write2_b32 v4, v32, v33 offset1:1
	ds_write2_b32 v2, v34, v35 offset1:1
	s_waitcnt lgkmcnt(0)
	ds_read2_b32 v[10:11], v49 offset0:33 offset1:41
	ds_read2_b32 v[12:13], v49 offset1:8
	v_lshlrev_b32_e32 v2, 1, v38
	ds_read2_b32 v[14:15], v49 offset0:66 offset1:74
	ds_read2_b32 v[16:17], v49 offset0:99 offset1:107
	ds_read2_b32 v[18:19], v49 offset0:132 offset1:140
	ds_read2_b32 v[20:21], v49 offset0:165 offset1:173
	ds_read2_b32 v[22:23], v49 offset0:198 offset1:206
	ds_read2_b32 v[24:25], v49 offset0:231 offset1:239
	v_lshl_add_u64 v[4:5], s[6:7], 0, v[2:3]
	v_or_b32_e32 v2, s2, v39
	v_lshlrev_b32_e32 v2, 9, v2
	v_lshl_add_u64 v[26:27], v[4:5], 0, v[2:3]
	v_or_b32_e32 v2, s2, v46
	s_waitcnt lgkmcnt(0)
	v_cvt_pk_bf16_f32 v6, v12, v10
	v_lshlrev_b32_e32 v2, 9, v2
	v_cvt_pk_bf16_f32 v7, v14, v16
	v_cvt_pk_bf16_f32 v8, v18, v20
	v_cvt_pk_bf16_f32 v9, v22, v24
	global_store_dwordx4 v[26:27], v[6:9], off sc1 nt
	s_nop 1
	v_cvt_pk_bf16_f32 v6, v13, v11
	v_lshl_add_u64 v[10:11], v[4:5], 0, v[2:3]
	v_cvt_pk_bf16_f32 v7, v15, v17
	v_cvt_pk_bf16_f32 v8, v19, v21
	v_cvt_pk_bf16_f32 v9, v23, v25
	global_store_dwordx4 v[10:11], v[6:9], off sc1 nt
	ds_read2_b32 v[10:11], v49 offset0:16 offset1:24
	ds_read2_b32 v[12:13], v49 offset0:49 offset1:57
	ds_read2_b32 v[14:15], v49 offset0:82 offset1:90
	ds_read2_b32 v[16:17], v49 offset0:115 offset1:123
	ds_read2_b32 v[18:19], v49 offset0:148 offset1:156
	ds_read2_b32 v[20:21], v49 offset0:181 offset1:189
	ds_read2_b32 v[22:23], v49 offset0:214 offset1:222
	ds_read2_b32 v[24:25], v49 offset0:247 offset1:255
	v_or_b32_e32 v2, s2, v47
	v_lshlrev_b32_e32 v2, 9, v2
	v_lshl_add_u64 v[26:27], v[4:5], 0, v[2:3]
	v_or_b32_e32 v2, s2, v48
	v_lshlrev_b32_e32 v2, 9, v2
	s_waitcnt lgkmcnt(6)
	v_cvt_pk_bf16_f32 v6, v10, v12
	s_waitcnt lgkmcnt(4)
	v_cvt_pk_bf16_f32 v7, v14, v16
	s_waitcnt lgkmcnt(2)
	v_cvt_pk_bf16_f32 v8, v18, v20
	s_waitcnt lgkmcnt(0)
	v_cvt_pk_bf16_f32 v9, v22, v24
	v_lshl_add_u64 v[4:5], v[4:5], 0, v[2:3]
	global_store_dwordx4 v[26:27], v[6:9], off sc1 nt
	s_mov_b64 s[2:3], 0
	s_nop 0
	v_cvt_pk_bf16_f32 v6, v11, v13
	v_cvt_pk_bf16_f32 v7, v15, v17
	v_cvt_pk_bf16_f32 v8, v19, v21
	v_cvt_pk_bf16_f32 v9, v23, v25
	global_store_dwordx4 v[4:5], v[6:9], off sc1 nt
	s_waitcnt lgkmcnt(0)

; #define GAS __attribute__((address_space(1)))
; #define LAS __attribute__((address_space(3)))
; #define LDS_WAIT() asm volatile("s_waitcnt lgkmcnt(0)" ::: "memory")
; __device__ __forceinline__ unsigned pk2(float lo, float hi) { unsigned r; asm("v_cvt_pk_bf16_f32 %0, %1, %2" : "=v"(r) : "v"(lo), "v"(hi)); return r; }
; __device__ __forceinline__ void transpose_item(const float* W, int K, int N, bf16* WT, int drow0, int kb, int n0, LAS float* scr, int lane) {
;     const int k0 = 64 * kb; const int c4 = 4 * (lane & 7); const bool ok = (n0 + c4) < N;
;     f32x4 v[8];
; #pragma unroll
;     for (int i = 0; i < 8; ++i) { const int kk = 8 * i + (lane >> 3); v[i] = ok ? *(const f32x4*)(W + (size_t)(k0 + kk) * N + n0 + c4) : (f32x4){0.f, 0.f, 0.f, 0.f}; }
; #pragma unroll
;     for (int i = 0; i < 8; ++i) { const int kk = 8 * i + (lane >> 3); LAS float* d = scr + kk * 33 + c4; d[0] = v[i][0]; d[1] = v[i][1]; d[2] = v[i][2]; d[3] = v[i][3]; }
;     LDS_WAIT(); asm volatile("" ::: "memory");
;     const int c = lane & 7;
; #pragma unroll
;     for (int j = 0; j < 4; ++j) { const int n = (lane >> 3) + 8 * j; const LAS float* s = scr + (8 * c) * 33 + n;
;         v4u o; o.x = pk2(s[0 * 33], s[1 * 33]); o.y = pk2(s[2 * 33], s[3 * 33]); o.z = pk2(s[4 * 33], s[5 * 33]); o.w = pk2(s[6 * 33], s[7 * 33]);
;         *(GAS v4u*)(WT + (size_t)(drow0 + n) * K + k0 + 8 * c) = o; }
;     LDS_WAIT(); asm volatile("" ::: "memory");
; }
; __device__ __forceinline__ void convert_item(const In& I, unsigned char* ws, int it, LAS float* scr, int lane) {
;     ...
;     if (r < 2 * I_SQ) { const int j = r / I_SQ; r -= j * I_SQ; const int kb = r / 32, nb = r % 32;
;         transpose_item(I.fox_w_out + (size_t)j * D * D, D, D, Wfout + (size_t)j * D * D, 32 * nb, kb, 32 * nb, scr, lane); return; }
.LBB0_239:
	s_andn2_b64 vcc, exec, s[2:3]
	s_cbranch_vccnz .LBB0_241
	s_add_i32 s2, s40, 0x800
	s_lshr_b32 s68, s2, 9
	v_readlane_b32 s48, v253, 16
	s_lshl_b64 s[2:3], s[68:69], 22
	v_readlane_b32 s60, v253, 28
	v_readlane_b32 s61, v253, 29
	s_add_u32 s6, s60, s2
	s_addc_u32 s7, s61, s3
	s_lshl_b64 s[2:3], s[68:69], 21
	s_add_u32 s8, s27, s2
	s_addc_u32 s3, s31, s3
	s_and_b32 s2, s42, 0x3e0
	s_add_i32 s9, s43, 0x13800
	s_and_b32 s9, s9, 0x3c0
	s_lshl_b32 s10, s2, 2
	s_add_u32 s6, s6, s10
	v_or_b32_e32 v6, s9, v39
	s_addc_u32 s7, s7, 0
	v_lshlrev_b32_e32 v2, 2, v36
	v_lshl_add_u64 v[4:5], s[6:7], 0, v[2:3]
	v_lshlrev_b32_e32 v2, 12, v6
	v_lshl_add_u64 v[32:33], v[4:5], 0, v[2:3]
	v_add_co_u32_e32 v8, vcc, s81, v32
	global_load_dwordx4 v[4:7], v[32:33], off nt
	s_nop 0
	v_addc_co_u32_e32 v9, vcc, 0, v33, vcc
	global_load_dwordx4 v[8:11], v[8:9], off nt
	v_add_co_u32_e32 v12, vcc, s79, v32
	v_add_u32_e32 v2, v44, v45
	s_nop 0
	v_addc_co_u32_e32 v13, vcc, 0, v33, vcc
	global_load_dwordx4 v[12:15], v[12:13], off nt
	v_add_co_u32_e32 v16, vcc, s80, v32
	s_lshl_b32 s6, s9, 1
	s_nop 0
	v_addc_co_u32_e32 v17, vcc, 0, v33, vcc
	global_load_dwordx4 v[16:19], v[16:17], off nt
	v_add_co_u32_e32 v20, vcc, s85, v32
	s_add_u32 s6, s8, s6
	s_nop 0
	v_addc_co_u32_e32 v21, vcc, 0, v33, vcc
	global_load_dwordx4 v[20:23], v[20:21], off nt
	v_add_co_u32_e32 v24, vcc, s86, v32
	s_addc_u32 s7, s3, 0
	s_nop 0
	v_addc_co_u32_e32 v25, vcc, 0, v33, vcc
	global_load_dwordx4 v[24:27], v[24:25], off nt
	v_add_co_u32_e32 v28, vcc, s87, v32
	v_readlane_b32 s49, v253, 17
	s_nop 0
	v_addc_co_u32_e32 v29, vcc, 0, v33, vcc
	global_load_dwordx4 v[28:31], v[28:29], off nt
	v_add_co_u32_e32 v32, vcc, s89, v32
	v_readlane_b32 s50, v253, 18
	s_nop 0
	v_addc_co_u32_e32 v33, vcc, 0, v33, vcc
	global_load_dwordx4 v[32:35], v[32:33], off nt
	v_readlane_b32 s51, v253, 19
	v_readlane_b32 s52, v253, 20
	v_readlane_b32 s53, v253, 21
	v_readlane_b32 s54, v253, 22
	v_readlane_b32 s55, v253, 23
	v_readlane_b32 s56, v253, 24
	v_readlane_b32 s57, v253, 25
	v_readlane_b32 s58, v253, 26
	v_readlane_b32 s59, v253, 27
	v_readlane_b32 s62, v253, 30
	v_readlane_b32 s63, v253, 31
	s_waitcnt vmcnt(0)
	ds_write2_b32 v2, v4, v5 offset1:1
	ds_write2_b32 v2, v6, v7 offset0:2 offset1:3
	v_add_u32_e32 v4, 0x420, v2
	ds_write2_b32 v4, v8, v9 offset1:1
	v_add_u32_e32 v4, 0x428, v2
	ds_write2_b32 v4, v10, v11 offset1:1
	v_add_u32_e32 v4, 0x840, v2
	ds_write2_b32 v4, v12, v13 offset1:1
	v_add_u32_e32 v4, 0x848, v2
	ds_write2_b32 v4, v14, v15 offset1:1
	v_add_u32_e32 v4, 0xc60, v2
	ds_write2_b32 v4, v16, v17 offset1:1
	v_add_u32_e32 v4, 0xc68, v2
	ds_write2_b32 v4, v18, v19 offset1:1
	v_add_u32_e32 v4, 0x1080, v2
	ds_write2_b32 v4, v20, v21 offset1:1
	v_add_u32_e32 v4, 0x1088, v2
	ds_write2_b32 v4, v22, v23 offset1:1
	v_add_u32_e32 v4, 0x14a0, v2
	ds_write2_b32 v4, v24, v25 offset1:1
	v_add_u32_e32 v4, 0x14a8, v2
	ds_write2_b32 v4, v26, v27 offset1:1
	v_add_u32_e32 v4, 0x18c0, v2
	ds_write2_b32 v4, v28, v29 offset1:1
	v_add_u32_e32 v4, 0x18c8, v2
	ds_write2_b32 v4, v30, v31 offset1:1
	v_add_u32_e32 v4, 0x1ce0, v2
	v_add_u32_e32 v2, 0x1ce8, v2
	ds_write2_b32 v4, v32, v33 offset1:1
	ds_write2_b32 v2, v34, v35 offset1:1
	s_waitcnt lgkmcnt(0)
	ds_read2_b32 v[10:11], v49 offset0:33 offset1:41
	ds_read2_b32 v[12:13], v49 offset1:8
	v_lshlrev_b32_e32 v2, 1, v38
	ds_read2_b32 v[14:15], v49 offset0:66 offset1:74
	ds_read2_b32 v[16:17], v49 offset0:99 offset1:107
	ds_read2_b32 v[18:19], v49 offset0:132 offset1:140
	ds_read2_b32 v[20:21], v49 offset0:165 offset1:173
	ds_read2_b32 v[22:23], v49 offset0:198 offset1:206
	ds_read2_b32 v[24:25], v49 offset0:231 offset1:239
	v_lshl_add_u64 v[8:9], s[6:7], 0, v[2:3]
	v_or_b32_e32 v2, s2, v39
	v_lshlrev_b32_e32 v2, 11, v2
	v_lshl_add_u64 v[26:27], v[8:9], 0, v[2:3]
	v_or_b32_e32 v2, s2, v46
	s_waitcnt lgkmcnt(0)
	v_cvt_pk_bf16_f32 v4, v12, v10
	v_lshlrev_b32_e32 v2, 11, v2
	v_cvt_pk_bf16_f32 v5, v14, v16
	v_cvt_pk_bf16_f32 v6, v18, v20
	v_cvt_pk_bf16_f32 v7, v22, v24
	global_store_dwordx4 v[26:27], v[4:7], off sc1 nt
	s_nop 1
	v_cvt_pk_bf16_f32 v4, v13, v11
	v_lshl_add_u64 v[10:11], v[8:9], 0, v[2:3]
	v_cvt_pk_bf16_f32 v5, v15, v17
	v_cvt_pk_bf16_f32 v6, v19, v21
	v_cvt_pk_bf16_f32 v7, v23, v25
	global_store_dwordx4 v[10:11], v[4:7], off sc1 nt
	ds_read2_b32 v[10:11], v49 offset0:16 offset1:24
	ds_read2_b32 v[12:13], v49 offset0:49 offset1:57
	ds_read2_b32 v[14:15], v49 offset0:82 offset1:90
	ds_read2_b32 v[16:17], v49 offset0:115 offset1:123
	ds_read2_b32 v[18:19], v49 offset0:148 offset1:156
	ds_read2_b32 v[20:21], v49 offset0:181 offset1:189
	ds_read2_b32 v[22:23], v49 offset0:214 offset1:222
	ds_read2_b32 v[24:25], v49 offset0:247 offset1:255
	v_or_b32_e32 v2, s2, v47
	v_lshlrev_b32_e32 v2, 11, v2
	v_lshl_add_u64 v[26:27], v[8:9], 0, v[2:3]
	v_or_b32_e32 v2, s2, v48
	v_lshlrev_b32_e32 v2, 11, v2
	s_waitcnt lgkmcnt(6)
	v_cvt_pk_bf16_f32 v4, v10, v12
	s_waitcnt lgkmcnt(4)
	v_cvt_pk_bf16_f32 v5, v14, v16
	s_waitcnt lgkmcnt(2)
	v_cvt_pk_bf16_f32 v6, v18, v20
	s_waitcnt lgkmcnt(0)
	v_cvt_pk_bf16_f32 v7, v22, v24
	v_lshl_add_u64 v[8:9], v[8:9], 0, v[2:3]
	global_store_dwordx4 v[26:27], v[4:7], off sc1 nt
	s_nop 1
	v_cvt_pk_bf16_f32 v4, v11, v13
	v_cvt_pk_bf16_f32 v5, v15, v17
	v_cvt_pk_bf16_f32 v6, v19, v21
	v_cvt_pk_bf16_f32 v7, v23, v25
	global_store_dwordx4 v[8:9], v[4:7], off sc1 nt
	s_waitcnt lgkmcnt(0)

; #define LAS __attribute__((address_space(3)))
; __device__ __forceinline__ void transpose_item(const float* W, int K, int N, bf16* WT, int drow0, int kb, int n0, LAS float* scr, int lane) {
;     const int k0 = 64 * kb; const int c4 = 4 * (lane & 7); const bool ok = (n0 + c4) < N;
;     f32x4 v[8];
; #pragma unroll
;     for (int i = 0; i < 8; ++i) { const int kk = 8 * i + (lane >> 3); v[i] = ok ? *(const f32x4*)(W + (size_t)(k0 + kk) * N + n0 + c4) : (f32x4){0.f, 0.f, 0.f, 0.f}; }
; __device__ __forceinline__ void convert_item(const In& I, unsigned char* ws, int it, LAS float* scr, int lane) {
;     ...
;     if (r < 2 * I_FIN) { const int j = r / I_FIN; r -= j * I_FIN; const int kb = r / 104, nb = r % 104;
;         transpose_item(I.fox_w_in + (size_t)j * D * FOX_IN, D, FOX_IN, Wfin + (size_t)j * FOX_IN_PAD * D, 32 * nb, kb, 32 * nb, scr, lane); return; }
.LBB0_242:
	s_andn2_b64 vcc, exec, s[2:3]
	s_cbranch_vccnz .LBB0_260
	s_add_i32 s6, s40, 0x1500
	s_cmpk_gt_u32 s6, 0x67f
	s_cselect_b64 s[10:11], -1, 0
	s_and_b64 s[2:3], s[10:11], exec
	s_cselect_b32 s2, 0xf980, 0
	s_cselect_b32 s3, 0xc10000, 0
	s_add_i32 s6, s6, s2
	s_sext_i32_i16 s2, s6
	s_mulk_i32 s2, 0x4ec5
	s_lshr_b32 s7, s2, 31
	s_ashr_i32 s2, s2, 21
	s_add_i32 s2, s2, s7
	s_mul_i32 s7, s2, 0x68
	v_readlane_b32 s48, v253, 16
	s_sub_i32 s6, s6, s7
	v_readlane_b32 s56, v253, 24
	s_sext_i32_i16 s6, s6
	v_readlane_b32 s57, v253, 25
	s_add_u32 s9, s56, s3
	s_addc_u32 s45, s57, 0
	s_lshl_b32 s6, s6, 5
	s_ashr_i32 s7, s6, 31
	s_lshl_b32 s8, s2, 6
	s_lshl_b64 s[12:13], s[6:7], 2
	v_or_b32_e32 v2, s6, v36
	s_movk_i32 s2, 0xc10
	v_or_b32_e32 v5, s8, v39
	s_add_u32 s12, s9, s12
	v_cmp_gt_i32_e64 s[2:3], s2, v2
	s_addc_u32 s13, s45, s13
	v_lshlrev_b32_e32 v2, 2, v36
	v_mul_i32_i24_e32 v42, 0x3040, v5
	v_lshl_add_u64 v[40:41], s[12:13], 0, v[2:3]
	v_mov_b32_e32 v4, 0
	v_ashrrev_i32_e32 v43, 31, v42
	v_mov_b32_e32 v8, 0
	v_mov_b32_e32 v9, 0
	v_mov_b32_e32 v10, 0
	v_mov_b32_e32 v11, 0
	v_readlane_b32 s49, v253, 17
	v_readlane_b32 s50, v253, 18
	v_readlane_b32 s51, v253, 19
	v_readlane_b32 s52, v253, 20
	v_readlane_b32 s53, v253, 21
	v_readlane_b32 s54, v253, 22
	v_readlane_b32 s55, v253, 23
	v_readlane_b32 s58, v253, 26
	v_readlane_b32 s59, v253, 27
	v_readlane_b32 s60, v253, 28
	v_readlane_b32 s61, v253, 29
	v_readlane_b32 s62, v253, 30
	v_readlane_b32 s63, v253, 31
	s_and_saveexec_b64 s[12:13], s[2:3]
	s_cbranch_execz .LBB0_245
	v_lshl_add_u64 v[6:7], v[40:41], 0, v[42:43]
	global_load_dwordx4 v[8:11], v[6:7], off nt

; #define GAS __attribute__((address_space(1)))
; #define LAS __attribute__((address_space(3)))
; #define LDS_WAIT() asm volatile("s_waitcnt lgkmcnt(0)" ::: "memory")
; __device__ __forceinline__ unsigned pk2(float lo, float hi) { unsigned r; asm("v_cvt_pk_bf16_f32 %0, %1, %2" : "=v"(r) : "v"(lo), "v"(hi)); return r; }
; __device__ __forceinline__ void transpose_item(const float* W, int K, int N, bf16* WT, int drow0, int kb, int n0, LAS float* scr, int lane) {
;     const int k0 = 64 * kb; const int c4 = 4 * (lane & 7); const bool ok = (n0 + c4) < N;
;     f32x4 v[8];
; #pragma unroll
;     for (int i = 0; i < 8; ++i) { const int kk = 8 * i + (lane >> 3); v[i] = ok ? *(const f32x4*)(W + (size_t)(k0 + kk) * N + n0 + c4) : (f32x4){0.f, 0.f, 0.f, 0.f}; }
; #pragma unroll
;     for (int i = 0; i < 8; ++i) { const int kk = 8 * i + (lane >> 3); LAS float* d = scr + kk * 33 + c4; d[0] = v[i][0]; d[1] = v[i][1]; d[2] = v[i][2]; d[3] = v[i][3]; }
;     LDS_WAIT(); asm volatile("" ::: "memory");
;     const int c = lane & 7;
; #pragma unroll
;     for (int j = 0; j < 4; ++j) { const int n = (lane >> 3) + 8 * j; const LAS float* s = scr + (8 * c) * 33 + n;
;         v4u o; o.x = pk2(s[0 * 33], s[1 * 33]); o.y = pk2(s[2 * 33], s[3 * 33]); o.z = pk2(s[4 * 33], s[5 * 33]); o.w = pk2(s[6 * 33], s[7 * 33]);
;         *(GAS v4u*)(WT + (size_t)(drow0 + n) * K + k0 + 8 * c) = o; }
;     LDS_WAIT(); asm volatile("" ::: "memory");
; }
; __device__ __forceinline__ void convert_item(const In& I, unsigned char* ws, int it, LAS float* scr, int lane) {
;     ...
;     if (r < 2 * I_SQ) { const int j = r / I_SQ; r -= j * I_SQ; const int kb = r / 32, nb = r % 32;
;         transpose_item(I.nsa_w_out + (size_t)j * D * D, D, D, Wnout + (size_t)j * D * D, 32 * nb, kb, 32 * nb, scr, lane); return; }
.LBB0_261:
	s_andn2_b64 vcc, exec, s[2:3]
	s_cbranch_vccnz .LBB0_263
	s_add_i32 s2, s40, 0x1900
	s_lshr_b32 s68, s2, 9
	v_readlane_b32 s48, v253, 16
	s_lshl_b64 s[2:3], s[68:69], 22
	v_readlane_b32 s54, v253, 22
	v_readlane_b32 s55, v253, 23
	s_add_u32 s6, s54, s2
	s_addc_u32 s7, s55, s3
	s_lshl_b64 s[2:3], s[68:69], 21
	s_add_u32 s8, s23, s2
	s_addc_u32 s3, s24, s3
	s_and_b32 s2, s42, 0x3e0
	s_add_i32 s9, s43, 0x1a00
	s_and_b32 s9, s9, 0x3c0
	s_lshl_b32 s10, s2, 2
	s_add_u32 s6, s6, s10
	v_or_b32_e32 v6, s9, v39
	s_addc_u32 s7, s7, 0
	v_lshlrev_b32_e32 v2, 2, v36
	v_lshl_add_u64 v[4:5], s[6:7], 0, v[2:3]
	v_lshlrev_b32_e32 v2, 12, v6
	v_lshl_add_u64 v[32:33], v[4:5], 0, v[2:3]
	v_add_co_u32_e32 v8, vcc, s81, v32
	global_load_dwordx4 v[4:7], v[32:33], off nt
	s_nop 0
	v_addc_co_u32_e32 v9, vcc, 0, v33, vcc
	global_load_dwordx4 v[8:11], v[8:9], off nt
	v_add_co_u32_e32 v12, vcc, s79, v32
	v_add_u32_e32 v2, v44, v45
	s_nop 0
	v_addc_co_u32_e32 v13, vcc, 0, v33, vcc
	global_load_dwordx4 v[12:15], v[12:13], off nt
	v_add_co_u32_e32 v16, vcc, s80, v32
	s_lshl_b32 s6, s9, 1
	s_nop 0
	v_addc_co_u32_e32 v17, vcc, 0, v33, vcc
	global_load_dwordx4 v[16:19], v[16:17], off nt
	v_add_co_u32_e32 v20, vcc, s85, v32
	s_add_u32 s6, s8, s6
	s_nop 0
	v_addc_co_u32_e32 v21, vcc, 0, v33, vcc
	global_load_dwordx4 v[20:23], v[20:21], off nt
	v_add_co_u32_e32 v24, vcc, s86, v32
	s_addc_u32 s7, s3, 0
	s_nop 0
	v_addc_co_u32_e32 v25, vcc, 0, v33, vcc
	global_load_dwordx4 v[24:27], v[24:25], off nt
	v_add_co_u32_e32 v28, vcc, s87, v32
	v_readlane_b32 s49, v253, 17
	s_nop 0
	v_addc_co_u32_e32 v29, vcc, 0, v33, vcc
	global_load_dwordx4 v[28:31], v[28:29], off nt
	v_add_co_u32_e32 v32, vcc, s89, v32
	v_readlane_b32 s50, v253, 18
	s_nop 0
	v_addc_co_u32_e32 v33, vcc, 0, v33, vcc
	global_load_dwordx4 v[32:35], v[32:33], off nt
	v_readlane_b32 s51, v253, 19
	v_readlane_b32 s52, v253, 20
	v_readlane_b32 s53, v253, 21
	v_readlane_b32 s56, v253, 24
	v_readlane_b32 s57, v253, 25
	v_readlane_b32 s58, v253, 26
	v_readlane_b32 s59, v253, 27
	v_readlane_b32 s60, v253, 28
	v_readlane_b32 s61, v253, 29
	v_readlane_b32 s62, v253, 30
	v_readlane_b32 s63, v253, 31
	s_waitcnt vmcnt(0)
	ds_write2_b32 v2, v4, v5 offset1:1
	ds_write2_b32 v2, v6, v7 offset0:2 offset1:3
	v_add_u32_e32 v4, 0x420, v2
	ds_write2_b32 v4, v8, v9 offset1:1
	v_add_u32_e32 v4, 0x428, v2
	ds_write2_b32 v4, v10, v11 offset1:1
	v_add_u32_e32 v4, 0x840, v2
	ds_write2_b32 v4, v12, v13 offset1:1
	v_add_u32_e32 v4, 0x848, v2
	ds_write2_b32 v4, v14, v15 offset1:1
	v_add_u32_e32 v4, 0xc60, v2
	ds_write2_b32 v4, v16, v17 offset1:1
	v_add_u32_e32 v4, 0xc68, v2
	ds_write2_b32 v4, v18, v19 offset1:1
	v_add_u32_e32 v4, 0x1080, v2
	ds_write2_b32 v4, v20, v21 offset1:1
	v_add_u32_e32 v4, 0x1088, v2
	ds_write2_b32 v4, v22, v23 offset1:1
	v_add_u32_e32 v4, 0x14a0, v2
	ds_write2_b32 v4, v24, v25 offset1:1
	v_add_u32_e32 v4, 0x14a8, v2
	ds_write2_b32 v4, v26, v27 offset1:1
	v_add_u32_e32 v4, 0x18c0, v2
	ds_write2_b32 v4, v28, v29 offset1:1
	v_add_u32_e32 v4, 0x18c8, v2
	ds_write2_b32 v4, v30, v31 offset1:1
	v_add_u32_e32 v4, 0x1ce0, v2
	v_add_u32_e32 v2, 0x1ce8, v2
	ds_write2_b32 v4, v32, v33 offset1:1
	ds_write2_b32 v2, v34, v35 offset1:1
	s_waitcnt lgkmcnt(0)
	ds_read2_b32 v[10:11], v49 offset0:33 offset1:41
	ds_read2_b32 v[12:13], v49 offset1:8
	v_lshlrev_b32_e32 v2, 1, v38
	ds_read2_b32 v[14:15], v49 offset0:66 offset1:74
	ds_read2_b32 v[16:17], v49 offset0:99 offset1:107
	ds_read2_b32 v[18:19], v49 offset0:132 offset1:140
	ds_read2_b32 v[20:21], v49 offset0:165 offset1:173
	ds_read2_b32 v[22:23], v49 offset0:198 offset1:206
	ds_read2_b32 v[24:25], v49 offset0:231 offset1:239
	v_lshl_add_u64 v[8:9], s[6:7], 0, v[2:3]
	v_or_b32_e32 v2, s2, v39
	v_lshlrev_b32_e32 v2, 11, v2
	v_lshl_add_u64 v[26:27], v[8:9], 0, v[2:3]
	v_or_b32_e32 v2, s2, v46
	s_waitcnt lgkmcnt(0)
	v_cvt_pk_bf16_f32 v4, v12, v10
	v_lshlrev_b32_e32 v2, 11, v2
	v_cvt_pk_bf16_f32 v5, v14, v16
	v_cvt_pk_bf16_f32 v6, v18, v20
	v_cvt_pk_bf16_f32 v7, v22, v24
	global_store_dwordx4 v[26:27], v[4:7], off sc1 nt
	s_nop 1
	v_cvt_pk_bf16_f32 v4, v13, v11
	v_lshl_add_u64 v[10:11], v[8:9], 0, v[2:3]
	v_cvt_pk_bf16_f32 v5, v15, v17
	v_cvt_pk_bf16_f32 v6, v19, v21
	v_cvt_pk_bf16_f32 v7, v23, v25
	global_store_dwordx4 v[10:11], v[4:7], off sc1 nt
	ds_read2_b32 v[10:11], v49 offset0:16 offset1:24
	ds_read2_b32 v[12:13], v49 offset0:49 offset1:57
	ds_read2_b32 v[14:15], v49 offset0:82 offset1:90
	ds_read2_b32 v[16:17], v49 offset0:115 offset1:123
	ds_read2_b32 v[18:19], v49 offset0:148 offset1:156
	ds_read2_b32 v[20:21], v49 offset0:181 offset1:189
	ds_read2_b32 v[22:23], v49 offset0:214 offset1:222
	ds_read2_b32 v[24:25], v49 offset0:247 offset1:255
	v_or_b32_e32 v2, s2, v47
	v_lshlrev_b32_e32 v2, 11, v2
	v_lshl_add_u64 v[26:27], v[8:9], 0, v[2:3]
	v_or_b32_e32 v2, s2, v48
	v_lshlrev_b32_e32 v2, 11, v2
	s_waitcnt lgkmcnt(6)
	v_cvt_pk_bf16_f32 v4, v10, v12
	s_waitcnt lgkmcnt(4)
	v_cvt_pk_bf16_f32 v5, v14, v16
	s_waitcnt lgkmcnt(2)
	v_cvt_pk_bf16_f32 v6, v18, v20
	s_waitcnt lgkmcnt(0)
	v_cvt_pk_bf16_f32 v7, v22, v24
	v_lshl_add_u64 v[8:9], v[8:9], 0, v[2:3]
	global_store_dwordx4 v[26:27], v[4:7], off sc1 nt
	s_nop 1
	v_cvt_pk_bf16_f32 v4, v11, v13
	v_cvt_pk_bf16_f32 v5, v15, v17
	v_cvt_pk_bf16_f32 v6, v19, v21
	v_cvt_pk_bf16_f32 v7, v23, v25
	global_store_dwordx4 v[8:9], v[4:7], off sc1 nt
	s_waitcnt lgkmcnt(0)

; #define LAS __attribute__((address_space(3)))
; __device__ __forceinline__ void transpose_item(const float* W, int K, int N, bf16* WT, int drow0, int kb, int n0, LAS float* scr, int lane) {
;     const int k0 = 64 * kb; const int c4 = 4 * (lane & 7); const bool ok = (n0 + c4) < N;
;     f32x4 v[8];
; #pragma unroll
;     for (int i = 0; i < 8; ++i) { const int kk = 8 * i + (lane >> 3); v[i] = ok ? *(const f32x4*)(W + (size_t)(k0 + kk) * N + n0 + c4) : (f32x4){0.f, 0.f, 0.f, 0.f}; }
; __device__ __forceinline__ void convert_item(const In& I, unsigned char* ws, int it, LAS float* scr, int lane) {
;     ...
;     if (r < 2 * I_NIN) { const int j = r / I_NIN; r -= j * I_NIN; const int kb = r / 88, nb = r % 88;
;         transpose_item(I.nsa_w_in + (size_t)j * D * NSA_IN, D, NSA_IN, Wnin + (size_t)j * NSA_IN_PAD * D, 32 * nb, kb, 32 * nb, scr, lane); return; }
.LBB0_264:
	s_andn2_b64 vcc, exec, s[2:3]
	s_cbranch_vccnz .LBB0_282
	s_add_i32 s6, s40, 0x2400
	s_cmpk_gt_u32 s6, 0x57f
	s_cselect_b64 s[10:11], -1, 0
	s_and_b64 s[2:3], s[10:11], exec
	s_cselect_b32 s2, 0xfa80, 0
	s_cselect_b32 s3, 0xa30000, 0
	s_add_i32 s6, s6, s2
	s_sext_i32_i16 s2, s6
	s_mulk_i32 s2, 0xba3
	s_lshr_b32 s7, s2, 31
	s_ashr_i32 s2, s2, 18
	v_readlane_b32 s48, v253, 0
	s_add_i32 s2, s2, s7
	v_readlane_b32 s49, v253, 1
	v_readlane_b32 s50, v253, 2
	v_readlane_b32 s51, v253, 3
	v_readlane_b32 s52, v253, 4
	v_readlane_b32 s53, v253, 5
	s_mul_i32 s7, s2, 0x58
	v_readlane_b32 s54, v253, 6
	v_readlane_b32 s55, v253, 7
	v_readlane_b32 s56, v253, 8
	v_readlane_b32 s57, v253, 9
	v_readlane_b32 s60, v253, 12
	v_readlane_b32 s61, v253, 13
	s_mov_b64 s[48:49], s[52:53]
	s_sub_i32 s6, s6, s7
	s_mov_b64 s[50:51], s[54:55]
	s_mov_b64 s[52:53], s[56:57]
	s_mov_b64 s[56:57], s[60:61]
	s_sext_i32_i16 s6, s6
	s_add_u32 s9, s56, s3
	s_addc_u32 s45, s57, 0
	s_lshl_b32 s6, s6, 5
	s_ashr_i32 s7, s6, 31
	s_lshl_b32 s8, s2, 6
	s_lshl_b64 s[12:13], s[6:7], 2
	v_or_b32_e32 v2, s6, v36
	s_movk_i32 s2, 0xa30
	s_add_u32 s12, s9, s12
	v_cmp_gt_i32_e64 s[2:3], s2, v2
	s_addc_u32 s13, s45, s13
	v_lshlrev_b32_e32 v2, 2, v36
	v_or_b32_e32 v42, s8, v39
	v_lshl_add_u64 v[40:41], s[12:13], 0, v[2:3]
	v_mov_b32_e32 v8, 0
	v_mov_b32_e32 v4, 0
	v_mov_b32_e32 v5, 0
	v_mov_b32_e32 v6, 0
	v_mov_b32_e32 v7, 0
	v_readlane_b32 s58, v253, 10
	v_readlane_b32 s59, v253, 11
	v_readlane_b32 s62, v253, 14
	v_readlane_b32 s63, v253, 15
	s_and_saveexec_b64 s[12:13], s[2:3]
	s_cbranch_execz .LBB0_267
	v_mul_i32_i24_e32 v4, 0x28c0, v42
	v_ashrrev_i32_e32 v5, 31, v4
	v_lshl_add_u64 v[4:5], v[40:41], 0, v[4:5]
	global_load_dwordx4 v[4:7], v[4:5], off nt

; #define GAS __attribute__((address_space(1)))
; #define LAS __attribute__((address_space(3)))
; #define LDS_WAIT() asm volatile("s_waitcnt lgkmcnt(0)" ::: "memory")
; __device__ __forceinline__ unsigned pk2(float lo, float hi) { unsigned r; asm("v_cvt_pk_bf16_f32 %0, %1, %2" : "=v"(r) : "v"(lo), "v"(hi)); return r; }
; __device__ __forceinline__ void transpose_item(const float* W, int K, int N, bf16* WT, int drow0, int kb, int n0, LAS float* scr, int lane) {
;     const int k0 = 64 * kb; const int c4 = 4 * (lane & 7); const bool ok = (n0 + c4) < N;
;     f32x4 v[8];
; #pragma unroll
;     for (int i = 0; i < 8; ++i) { const int kk = 8 * i + (lane >> 3); v[i] = ok ? *(const f32x4*)(W + (size_t)(k0 + kk) * N + n0 + c4) : (f32x4){0.f, 0.f, 0.f, 0.f}; }
; #pragma unroll
;     for (int i = 0; i < 8; ++i) { const int kk = 8 * i + (lane >> 3); LAS float* d = scr + kk * 33 + c4; d[0] = v[i][0]; d[1] = v[i][1]; d[2] = v[i][2]; d[3] = v[i][3]; }
;     LDS_WAIT(); asm volatile("" ::: "memory");
;     const int c = lane & 7;
; #pragma unroll
;     for (int j = 0; j < 4; ++j) { const int n = (lane >> 3) + 8 * j; const LAS float* s = scr + (8 * c) * 33 + n;
;         v4u o; o.x = pk2(s[0 * 33], s[1 * 33]); o.y = pk2(s[2 * 33], s[3 * 33]); o.z = pk2(s[4 * 33], s[5 * 33]); o.w = pk2(s[6 * 33], s[7 * 33]);
;         *(GAS v4u*)(WT + (size_t)(drow0 + n) * K + k0 + 8 * c) = o; }
;     LDS_WAIT(); asm volatile("" ::: "memory");
; }
; __device__ __forceinline__ void convert_item(const In& I, unsigned char* ws, int it, LAS float* scr, int lane) {
;     ...
;     if (r < T0) { const int f = r / I_FFN; r -= f * I_FFN;
;     ...
;         else { r -= 2 * I_G; const int kb = r / 32, nb = r % 32; transpose_item(I.w_down + (size_t)f * FF * D, FF, D, Wd + (size_t)f * D * FF, 32 * nb, kb, 32 * nb, scr, lane); }
.LBB0_283:
	s_andn2_b64 vcc, exec, s[2:3]
	s_cbranch_vccnz .LBB0_228
	s_mul_hi_i32 s2, s44, 0x3e0f83e1
	s_lshr_b32 s3, s2, 31
	s_ashr_i32 s6, s2, 10
	s_add_i32 s6, s6, s3
	s_mul_i32 s2, s6, 0xffffef80
	s_add_i32 s7, s40, s2
	s_add_i32 s7, s7, 0xa800
	s_cmpk_gt_i32 s7, 0xaff
	s_mov_b64 s[2:3], -1
	s_cbranch_scc0 .LBB0_286
	v_readlane_b32 s48, v253, 0
	v_readlane_b32 s49, v253, 1
	v_readlane_b32 s50, v253, 2
	v_readlane_b32 s51, v253, 3
	v_readlane_b32 s52, v253, 4
	v_readlane_b32 s53, v253, 5
	v_readlane_b32 s54, v253, 6
	v_readlane_b32 s55, v253, 7
	v_readlane_b32 s56, v253, 8
	v_readlane_b32 s57, v253, 9
	s_mov_b64 s[48:49], s[52:53]
	s_mul_i32 s3, s6, 0xb00000
	s_mov_b64 s[50:51], s[54:55]
	s_mov_b64 s[52:53], s[56:57]
	s_mul_hi_i32 s2, s6, 0xb00000
	s_add_u32 s9, s52, s3
	s_addc_u32 s11, s53, s2
	s_mul_i32 s3, s6, 0x580000
	s_mul_hi_i32 s2, s6, 0x580000
	s_add_u32 s3, s19, s3
	s_mul_i32 s10, s6, 0xffffdf00
	s_addc_u32 s8, s20, s2
	s_add_i32 s10, s43, s10
	s_add_i32 s10, s10, 0x13800
	s_and_b32 s2, s42, 0x3e0
	s_andn2_b32 s10, s10, 63
	s_add_i32 s68, s10, 0xffffea00
	s_lshl_b32 s10, s2, 2
	v_or_b32_e32 v32, s68, v39
	s_add_u32 s10, s9, s10
	s_addc_u32 s11, s11, 0
	v_lshlrev_b32_e32 v2, 2, v36
	v_ashrrev_i32_e32 v33, 31, v32
	v_or_b32_e32 v8, 8, v32
	v_lshl_add_u64 v[34:35], s[10:11], 0, v[2:3]
	v_lshlrev_b64 v[4:5], 12, v[32:33]
	v_ashrrev_i32_e32 v9, 31, v8
	v_lshl_add_u64 v[4:5], v[34:35], 0, v[4:5]
	v_lshlrev_b64 v[8:9], 12, v[8:9]
	v_or_b32_e32 v12, 16, v32
	global_load_dwordx4 v[4:7], v[4:5], off nt
	v_lshl_add_u64 v[8:9], v[34:35], 0, v[8:9]
	v_ashrrev_i32_e32 v13, 31, v12
	global_load_dwordx4 v[8:11], v[8:9], off nt
	v_lshlrev_b64 v[12:13], 12, v[12:13]
	v_or_b32_e32 v16, 24, v32
	v_lshl_add_u64 v[12:13], v[34:35], 0, v[12:13]
	v_ashrrev_i32_e32 v17, 31, v16
	global_load_dwordx4 v[12:15], v[12:13], off nt
	v_lshlrev_b64 v[16:17], 12, v[16:17]
	v_or_b32_e32 v20, 32, v32
	v_lshl_add_u64 v[16:17], v[34:35], 0, v[16:17]
	v_ashrrev_i32_e32 v21, 31, v20
	global_load_dwordx4 v[16:19], v[16:17], off nt
	v_lshlrev_b64 v[20:21], 12, v[20:21]
	v_or_b32_e32 v24, 40, v32
	v_lshl_add_u64 v[20:21], v[34:35], 0, v[20:21]
	v_ashrrev_i32_e32 v25, 31, v24
	global_load_dwordx4 v[20:23], v[20:21], off nt
	v_lshlrev_b64 v[24:25], 12, v[24:25]
	v_or_b32_e32 v28, 48, v32
	v_lshl_add_u64 v[24:25], v[34:35], 0, v[24:25]
	v_ashrrev_i32_e32 v29, 31, v28
	global_load_dwordx4 v[24:27], v[24:25], off nt
	v_lshlrev_b64 v[28:29], 12, v[28:29]
	v_or_b32_e32 v32, 56, v32
	v_lshl_add_u64 v[28:29], v[34:35], 0, v[28:29]
	v_ashrrev_i32_e32 v33, 31, v32
	global_load_dwordx4 v[28:31], v[28:29], off nt
	v_lshlrev_b64 v[32:33], 12, v[32:33]
	v_lshl_add_u64 v[32:33], v[34:35], 0, v[32:33]
	global_load_dwordx4 v[32:35], v[32:33], off nt
	v_add_u32_e32 v2, v44, v45
	s_lshl_b64 s[10:11], s[68:69], 1
	s_add_u32 s10, s3, s10
	s_addc_u32 s11, s8, s11
	v_readlane_b32 s58, v253, 10
	v_readlane_b32 s59, v253, 11
	v_readlane_b32 s60, v253, 12
	v_readlane_b32 s61, v253, 13
	v_readlane_b32 s62, v253, 14
	v_readlane_b32 s63, v253, 15
	s_waitcnt vmcnt(0)
	ds_write2_b32 v2, v4, v5 offset1:1
	ds_write2_b32 v2, v6, v7 offset0:2 offset1:3
	v_add_u32_e32 v4, 0x420, v2
	ds_write2_b32 v4, v8, v9 offset1:1
	v_add_u32_e32 v4, 0x428, v2
	ds_write2_b32 v4, v10, v11 offset1:1
	v_add_u32_e32 v4, 0x840, v2
	ds_write2_b32 v4, v12, v13 offset1:1
	v_add_u32_e32 v4, 0x848, v2
	ds_write2_b32 v4, v14, v15 offset1:1
	v_add_u32_e32 v4, 0xc60, v2
	ds_write2_b32 v4, v16, v17 offset1:1
	v_add_u32_e32 v4, 0xc68, v2
	ds_write2_b32 v4, v18, v19 offset1:1
	v_add_u32_e32 v4, 0x1080, v2
	ds_write2_b32 v4, v20, v21 offset1:1
	v_add_u32_e32 v4, 0x1088, v2
	ds_write2_b32 v4, v22, v23 offset1:1
	v_add_u32_e32 v4, 0x14a0, v2
	ds_write2_b32 v4, v24, v25 offset1:1
	v_add_u32_e32 v4, 0x14a8, v2
	ds_write2_b32 v4, v26, v27 offset1:1
	v_add_u32_e32 v4, 0x18c0, v2
	ds_write2_b32 v4, v28, v29 offset1:1
	v_add_u32_e32 v4, 0x18c8, v2
	ds_write2_b32 v4, v30, v31 offset1:1
	v_add_u32_e32 v4, 0x1ce0, v2
	v_add_u32_e32 v2, 0x1ce8, v2
	ds_write2_b32 v4, v32, v33 offset1:1
	ds_write2_b32 v2, v34, v35 offset1:1
	s_waitcnt lgkmcnt(0)
	ds_read2_b32 v[10:11], v49 offset0:33 offset1:41
	ds_read2_b32 v[12:13], v49 offset1:8
	v_lshlrev_b32_e32 v2, 1, v38
	ds_read2_b32 v[14:15], v49 offset0:66 offset1:74
	ds_read2_b32 v[16:17], v49 offset0:99 offset1:107
	ds_read2_b32 v[18:19], v49 offset0:132 offset1:140
	ds_read2_b32 v[20:21], v49 offset0:165 offset1:173
	ds_read2_b32 v[22:23], v49 offset0:198 offset1:206
	ds_read2_b32 v[24:25], v49 offset0:231 offset1:239
	v_lshl_add_u64 v[8:9], s[10:11], 0, v[2:3]
	v_or_b32_e32 v2, s2, v39
	v_mul_u32_u24_e32 v2, 0x1600, v2
	v_lshl_add_u64 v[26:27], v[8:9], 0, v[2:3]
	v_or_b32_e32 v2, s2, v46
	s_waitcnt lgkmcnt(0)
	v_cvt_pk_bf16_f32 v4, v12, v10
	v_mul_u32_u24_e32 v2, 0x1600, v2
	v_cvt_pk_bf16_f32 v5, v14, v16
	v_cvt_pk_bf16_f32 v6, v18, v20
	v_cvt_pk_bf16_f32 v7, v22, v24
	global_store_dwordx4 v[26:27], v[4:7], off sc1 nt
	s_nop 1
	v_cvt_pk_bf16_f32 v4, v13, v11
	v_lshl_add_u64 v[10:11], v[8:9], 0, v[2:3]
	v_cvt_pk_bf16_f32 v5, v15, v17
	v_cvt_pk_bf16_f32 v6, v19, v21
	v_cvt_pk_bf16_f32 v7, v23, v25
	global_store_dwordx4 v[10:11], v[4:7], off sc1 nt
	ds_read2_b32 v[10:11], v49 offset0:16 offset1:24
	ds_read2_b32 v[12:13], v49 offset0:49 offset1:57
	ds_read2_b32 v[14:15], v49 offset0:82 offset1:90
	ds_read2_b32 v[16:17], v49 offset0:115 offset1:123
	ds_read2_b32 v[18:19], v49 offset0:148 offset1:156
	ds_read2_b32 v[20:21], v49 offset0:181 offset1:189
	ds_read2_b32 v[22:23], v49 offset0:214 offset1:222
	ds_read2_b32 v[24:25], v49 offset0:247 offset1:255
	v_or_b32_e32 v2, s2, v47
	v_mul_u32_u24_e32 v2, 0x1600, v2
	v_lshl_add_u64 v[26:27], v[8:9], 0, v[2:3]
	v_or_b32_e32 v2, s2, v48
	v_mul_u32_u24_e32 v2, 0x1600, v2
	s_waitcnt lgkmcnt(6)
	v_cvt_pk_bf16_f32 v4, v10, v12
	s_waitcnt lgkmcnt(4)
	v_cvt_pk_bf16_f32 v5, v14, v16
	s_waitcnt lgkmcnt(2)
	v_cvt_pk_bf16_f32 v6, v18, v20
	s_waitcnt lgkmcnt(0)
	v_cvt_pk_bf16_f32 v7, v22, v24
	v_lshl_add_u64 v[8:9], v[8:9], 0, v[2:3]
	global_store_dwordx4 v[26:27], v[4:7], off sc1 nt
	s_mov_b64 s[2:3], 0
	s_nop 0
	v_cvt_pk_bf16_f32 v4, v11, v13
	v_cvt_pk_bf16_f32 v5, v15, v17
	v_cvt_pk_bf16_f32 v6, v19, v21
	v_cvt_pk_bf16_f32 v7, v23, v25
	global_store_dwordx4 v[8:9], v[4:7], off sc1 nt
	s_waitcnt lgkmcnt(0)

; #define GAS __attribute__((address_space(1)))
; #define LAS __attribute__((address_space(3)))
; #define LDS_WAIT() asm volatile("s_waitcnt lgkmcnt(0)" ::: "memory")
; __device__ __forceinline__ unsigned pk2(float lo, float hi) { unsigned r; asm("v_cvt_pk_bf16_f32 %0, %1, %2" : "=v"(r) : "v"(lo), "v"(hi)); return r; }
; __device__ __forceinline__ void transpose_item(const float* W, int K, int N, bf16* WT, int drow0, int kb, int n0, LAS float* scr, int lane) {
;     const int k0 = 64 * kb; const int c4 = 4 * (lane & 7); const bool ok = (n0 + c4) < N;
;     f32x4 v[8];
; #pragma unroll
;     for (int i = 0; i < 8; ++i) { const int kk = 8 * i + (lane >> 3); v[i] = ok ? *(const f32x4*)(W + (size_t)(k0 + kk) * N + n0 + c4) : (f32x4){0.f, 0.f, 0.f, 0.f}; }
; #pragma unroll
;     for (int i = 0; i < 8; ++i) { const int kk = 8 * i + (lane >> 3); LAS float* d = scr + kk * 33 + c4; d[0] = v[i][0]; d[1] = v[i][1]; d[2] = v[i][2]; d[3] = v[i][3]; }
;     LDS_WAIT(); asm volatile("" ::: "memory");
;     const int c = lane & 7;
; #pragma unroll
;     for (int j = 0; j < 4; ++j) { const int n = (lane >> 3) + 8 * j; const LAS float* s = scr + (8 * c) * 33 + n;
;         v4u o; o.x = pk2(s[0 * 33], s[1 * 33]); o.y = pk2(s[2 * 33], s[3 * 33]); o.z = pk2(s[4 * 33], s[5 * 33]); o.w = pk2(s[6 * 33], s[7 * 33]);
;         *(GAS v4u*)(WT + (size_t)(drow0 + n) * K + k0 + 8 * c) = o; }
;     LDS_WAIT(); asm volatile("" ::: "memory");
; }
; __device__ __forceinline__ void convert_item(const In& I, unsigned char* ws, int it, LAS float* scr, int lane) {
;     ...
;     if (r < 2 * I_SQ) { const int j = r / I_SQ; r -= j * I_SQ; const int kb = r / 32, nb = r % 32;
;         transpose_item(I.fox_w_out + (size_t)j * D * D, D, D, Wfout + (size_t)j * D * D, 32 * nb, kb, 32 * nb, scr, lane); return; }
.LBB0_303:
	s_andn2_b64 vcc, exec, s[2:3]
	s_cbranch_vccnz .LBB0_305
	s_add_i32 s2, s40, 0x800
	s_lshr_b32 s68, s2, 9
	v_readlane_b32 s48, v253, 16
	s_lshl_b64 s[2:3], s[68:69], 22
	v_readlane_b32 s60, v253, 28
	v_readlane_b32 s61, v253, 29
	s_add_u32 s6, s60, s2
	s_addc_u32 s7, s61, s3
	s_lshl_b64 s[2:3], s[68:69], 21
	s_add_u32 s8, s27, s2
	s_addc_u32 s3, s31, s3
	s_and_b32 s2, s42, 0x3e0
	s_add_i32 s9, s43, 0x10000
	s_and_b32 s9, s9, 0x3c0
	s_lshl_b32 s10, s2, 2
	s_add_u32 s6, s6, s10
	v_or_b32_e32 v6, s9, v39
	s_addc_u32 s7, s7, 0
	v_lshlrev_b32_e32 v2, 2, v36
	v_lshl_add_u64 v[4:5], s[6:7], 0, v[2:3]
	v_lshlrev_b32_e32 v2, 12, v6
	v_lshl_add_u64 v[32:33], v[4:5], 0, v[2:3]
	v_add_co_u32_e32 v8, vcc, s81, v32
	global_load_dwordx4 v[4:7], v[32:33], off nt
	s_nop 0
	v_addc_co_u32_e32 v9, vcc, 0, v33, vcc
	global_load_dwordx4 v[8:11], v[8:9], off nt
	v_add_co_u32_e32 v12, vcc, s79, v32
	v_add_u32_e32 v2, v44, v45
	s_nop 0
	v_addc_co_u32_e32 v13, vcc, 0, v33, vcc
	global_load_dwordx4 v[12:15], v[12:13], off nt
	v_add_co_u32_e32 v16, vcc, s80, v32
	s_lshl_b32 s6, s9, 1
	s_nop 0
	v_addc_co_u32_e32 v17, vcc, 0, v33, vcc
	global_load_dwordx4 v[16:19], v[16:17], off nt
	v_add_co_u32_e32 v20, vcc, s85, v32
	s_add_u32 s6, s8, s6
	s_nop 0
	v_addc_co_u32_e32 v21, vcc, 0, v33, vcc
	global_load_dwordx4 v[20:23], v[20:21], off nt
	v_add_co_u32_e32 v24, vcc, s86, v32
	s_addc_u32 s7, s3, 0
	s_nop 0
	v_addc_co_u32_e32 v25, vcc, 0, v33, vcc
	global_load_dwordx4 v[24:27], v[24:25], off nt
	v_add_co_u32_e32 v28, vcc, s87, v32
	v_readlane_b32 s49, v253, 17
	s_nop 0
	v_addc_co_u32_e32 v29, vcc, 0, v33, vcc
	global_load_dwordx4 v[28:31], v[28:29], off nt
	v_add_co_u32_e32 v32, vcc, s89, v32
	v_readlane_b32 s50, v253, 18
	s_nop 0
	v_addc_co_u32_e32 v33, vcc, 0, v33, vcc
	global_load_dwordx4 v[32:35], v[32:33], off nt
	v_readlane_b32 s51, v253, 19
	v_readlane_b32 s52, v253, 20
	v_readlane_b32 s53, v253, 21
	v_readlane_b32 s54, v253, 22
	v_readlane_b32 s55, v253, 23
	v_readlane_b32 s56, v253, 24
	v_readlane_b32 s57, v253, 25
	v_readlane_b32 s58, v253, 26
	v_readlane_b32 s59, v253, 27
	v_readlane_b32 s62, v253, 30
	v_readlane_b32 s63, v253, 31
	s_waitcnt vmcnt(0)
	ds_write2_b32 v2, v4, v5 offset1:1
	ds_write2_b32 v2, v6, v7 offset0:2 offset1:3
	v_add_u32_e32 v4, 0x420, v2
	ds_write2_b32 v4, v8, v9 offset1:1
	v_add_u32_e32 v4, 0x428, v2
	ds_write2_b32 v4, v10, v11 offset1:1
	v_add_u32_e32 v4, 0x840, v2
	ds_write2_b32 v4, v12, v13 offset1:1
	v_add_u32_e32 v4, 0x848, v2
	ds_write2_b32 v4, v14, v15 offset1:1
	v_add_u32_e32 v4, 0xc60, v2
	ds_write2_b32 v4, v16, v17 offset1:1
	v_add_u32_e32 v4, 0xc68, v2
	ds_write2_b32 v4, v18, v19 offset1:1
	v_add_u32_e32 v4, 0x1080, v2
	ds_write2_b32 v4, v20, v21 offset1:1
	v_add_u32_e32 v4, 0x1088, v2
	ds_write2_b32 v4, v22, v23 offset1:1
	v_add_u32_e32 v4, 0x14a0, v2
	ds_write2_b32 v4, v24, v25 offset1:1
	v_add_u32_e32 v4, 0x14a8, v2
	ds_write2_b32 v4, v26, v27 offset1:1
	v_add_u32_e32 v4, 0x18c0, v2
	ds_write2_b32 v4, v28, v29 offset1:1
	v_add_u32_e32 v4, 0x18c8, v2
	ds_write2_b32 v4, v30, v31 offset1:1
	v_add_u32_e32 v4, 0x1ce0, v2
	v_add_u32_e32 v2, 0x1ce8, v2
	ds_write2_b32 v4, v32, v33 offset1:1
	ds_write2_b32 v2, v34, v35 offset1:1
	s_waitcnt lgkmcnt(0)
	ds_read2_b32 v[10:11], v49 offset0:33 offset1:41
	ds_read2_b32 v[12:13], v49 offset1:8
	v_lshlrev_b32_e32 v2, 1, v38
	ds_read2_b32 v[14:15], v49 offset0:66 offset1:74
	ds_read2_b32 v[16:17], v49 offset0:99 offset1:107
	ds_read2_b32 v[18:19], v49 offset0:132 offset1:140
	ds_read2_b32 v[20:21], v49 offset0:165 offset1:173
	ds_read2_b32 v[22:23], v49 offset0:198 offset1:206
	ds_read2_b32 v[24:25], v49 offset0:231 offset1:239
	v_lshl_add_u64 v[8:9], s[6:7], 0, v[2:3]
	v_or_b32_e32 v2, s2, v39
	v_lshlrev_b32_e32 v2, 11, v2
	v_lshl_add_u64 v[26:27], v[8:9], 0, v[2:3]
	v_or_b32_e32 v2, s2, v46
	s_waitcnt lgkmcnt(0)
	v_cvt_pk_bf16_f32 v4, v12, v10
	v_lshlrev_b32_e32 v2, 11, v2
	v_cvt_pk_bf16_f32 v5, v14, v16
	v_cvt_pk_bf16_f32 v6, v18, v20
	v_cvt_pk_bf16_f32 v7, v22, v24
	global_store_dwordx4 v[26:27], v[4:7], off sc1 nt
	s_nop 1
	v_cvt_pk_bf16_f32 v4, v13, v11
	v_lshl_add_u64 v[10:11], v[8:9], 0, v[2:3]
	v_cvt_pk_bf16_f32 v5, v15, v17
	v_cvt_pk_bf16_f32 v6, v19, v21
	v_cvt_pk_bf16_f32 v7, v23, v25
	global_store_dwordx4 v[10:11], v[4:7], off sc1 nt
	ds_read2_b32 v[10:11], v49 offset0:16 offset1:24
	ds_read2_b32 v[12:13], v49 offset0:49 offset1:57
	ds_read2_b32 v[14:15], v49 offset0:82 offset1:90
	ds_read2_b32 v[16:17], v49 offset0:115 offset1:123
	ds_read2_b32 v[18:19], v49 offset0:148 offset1:156
	ds_read2_b32 v[20:21], v49 offset0:181 offset1:189
	ds_read2_b32 v[22:23], v49 offset0:214 offset1:222
	ds_read2_b32 v[24:25], v49 offset0:247 offset1:255
	v_or_b32_e32 v2, s2, v47
	v_lshlrev_b32_e32 v2, 11, v2
	v_lshl_add_u64 v[26:27], v[8:9], 0, v[2:3]
	v_or_b32_e32 v2, s2, v48
	v_lshlrev_b32_e32 v2, 11, v2
	s_waitcnt lgkmcnt(6)
	v_cvt_pk_bf16_f32 v4, v10, v12
	s_waitcnt lgkmcnt(4)
	v_cvt_pk_bf16_f32 v5, v14, v16
	s_waitcnt lgkmcnt(2)
	v_cvt_pk_bf16_f32 v6, v18, v20
	s_waitcnt lgkmcnt(0)
	v_cvt_pk_bf16_f32 v7, v22, v24
	v_lshl_add_u64 v[8:9], v[8:9], 0, v[2:3]
	global_store_dwordx4 v[26:27], v[4:7], off sc1 nt
	s_nop 1
	v_cvt_pk_bf16_f32 v4, v11, v13
	v_cvt_pk_bf16_f32 v5, v15, v17
	v_cvt_pk_bf16_f32 v6, v19, v21
	v_cvt_pk_bf16_f32 v7, v23, v25
	global_store_dwordx4 v[8:9], v[4:7], off sc1 nt
	s_waitcnt lgkmcnt(0)

; #define GAS __attribute__((address_space(1)))
; #define LAS __attribute__((address_space(3)))
; #define LDS_WAIT() asm volatile("s_waitcnt lgkmcnt(0)" ::: "memory")
; __device__ __forceinline__ unsigned pk2(float lo, float hi) { unsigned r; asm("v_cvt_pk_bf16_f32 %0, %1, %2" : "=v"(r) : "v"(lo), "v"(hi)); return r; }
; __device__ __forceinline__ void transpose_item(const float* W, int K, int N, bf16* WT, int drow0, int kb, int n0, LAS float* scr, int lane) {
;     const int k0 = 64 * kb; const int c4 = 4 * (lane & 7); const bool ok = (n0 + c4) < N;
;     f32x4 v[8];
; #pragma unroll
;     for (int i = 0; i < 8; ++i) { const int kk = 8 * i + (lane >> 3); v[i] = ok ? *(const f32x4*)(W + (size_t)(k0 + kk) * N + n0 + c4) : (f32x4){0.f, 0.f, 0.f, 0.f}; }
; #pragma unroll
;     for (int i = 0; i < 8; ++i) { const int kk = 8 * i + (lane >> 3); LAS float* d = scr + kk * 33 + c4; d[0] = v[i][0]; d[1] = v[i][1]; d[2] = v[i][2]; d[3] = v[i][3]; }
;     LDS_WAIT(); asm volatile("" ::: "memory");
;     const int c = lane & 7;
; #pragma unroll
;     for (int j = 0; j < 4; ++j) { const int n = (lane >> 3) + 8 * j; const LAS float* s = scr + (8 * c) * 33 + n;
;         v4u o; o.x = pk2(s[0 * 33], s[1 * 33]); o.y = pk2(s[2 * 33], s[3 * 33]); o.z = pk2(s[4 * 33], s[5 * 33]); o.w = pk2(s[6 * 33], s[7 * 33]);
;         *(GAS v4u*)(WT + (size_t)(drow0 + n) * K + k0 + 8 * c) = o; }
;     LDS_WAIT(); asm volatile("" ::: "memory");
; }
; __device__ __forceinline__ void convert_item(const In& I, unsigned char* ws, int it, LAS float* scr, int lane) {
;     ...
;     if (r < 2 * I_SQ) { const int j = r / I_SQ; r -= j * I_SQ; const int kb = r / 32, nb = r % 32;
;         transpose_item(I.nsa_w_out + (size_t)j * D * D, D, D, Wnout + (size_t)j * D * D, 32 * nb, kb, 32 * nb, scr, lane); return; }
.LBB0_325:
	s_andn2_b64 vcc, exec, s[2:3]
	s_cbranch_vccnz .LBB0_327
	s_add_i32 s2, s40, 0x1900
	s_lshr_b32 s68, s2, 9
	v_readlane_b32 s48, v253, 16
	s_lshl_b64 s[2:3], s[68:69], 22
	v_readlane_b32 s54, v253, 22
	v_readlane_b32 s55, v253, 23
	s_add_u32 s6, s54, s2
	s_addc_u32 s7, s55, s3
	s_lshl_b64 s[2:3], s[68:69], 21
	s_add_u32 s8, s23, s2
	s_addc_u32 s3, s24, s3
	s_and_b32 s2, s42, 0x3e0
	s_add_i32 s9, s43, 0xffffe200
	s_and_b32 s9, s9, 0x3c0
	s_lshl_b32 s10, s2, 2
	s_add_u32 s6, s6, s10
	v_or_b32_e32 v6, s9, v39
	s_addc_u32 s7, s7, 0
	v_lshlrev_b32_e32 v2, 2, v36
	v_lshl_add_u64 v[4:5], s[6:7], 0, v[2:3]
	v_lshlrev_b32_e32 v2, 12, v6
	v_lshl_add_u64 v[32:33], v[4:5], 0, v[2:3]
	v_add_co_u32_e32 v8, vcc, s81, v32
	global_load_dwordx4 v[4:7], v[32:33], off nt
	s_nop 0
	v_addc_co_u32_e32 v9, vcc, 0, v33, vcc
	global_load_dwordx4 v[8:11], v[8:9], off nt
	v_add_co_u32_e32 v12, vcc, s79, v32
	v_add_u32_e32 v2, v44, v45
	s_nop 0
	v_addc_co_u32_e32 v13, vcc, 0, v33, vcc
	global_load_dwordx4 v[12:15], v[12:13], off nt
	v_add_co_u32_e32 v16, vcc, s80, v32
	s_lshl_b32 s6, s9, 1
	s_nop 0
	v_addc_co_u32_e32 v17, vcc, 0, v33, vcc
	global_load_dwordx4 v[16:19], v[16:17], off nt
	v_add_co_u32_e32 v20, vcc, s85, v32
	s_add_u32 s6, s8, s6
	s_nop 0
	v_addc_co_u32_e32 v21, vcc, 0, v33, vcc
	global_load_dwordx4 v[20:23], v[20:21], off nt
	v_add_co_u32_e32 v24, vcc, s86, v32
	s_addc_u32 s7, s3, 0
	s_nop 0
	v_addc_co_u32_e32 v25, vcc, 0, v33, vcc
	global_load_dwordx4 v[24:27], v[24:25], off nt
	v_add_co_u32_e32 v28, vcc, s87, v32
	v_readlane_b32 s49, v253, 17
	s_nop 0
	v_addc_co_u32_e32 v29, vcc, 0, v33, vcc
	global_load_dwordx4 v[28:31], v[28:29], off nt
	v_add_co_u32_e32 v32, vcc, s89, v32
	v_readlane_b32 s50, v253, 18
	s_nop 0
	v_addc_co_u32_e32 v33, vcc, 0, v33, vcc
	global_load_dwordx4 v[32:35], v[32:33], off nt
	v_readlane_b32 s51, v253, 19
	v_readlane_b32 s52, v253, 20
	v_readlane_b32 s53, v253, 21
	v_readlane_b32 s56, v253, 24
	v_readlane_b32 s57, v253, 25
	v_readlane_b32 s58, v253, 26
	v_readlane_b32 s59, v253, 27
	v_readlane_b32 s60, v253, 28
	v_readlane_b32 s61, v253, 29
	v_readlane_b32 s62, v253, 30
	v_readlane_b32 s63, v253, 31
	s_waitcnt vmcnt(0)
	ds_write2_b32 v2, v4, v5 offset1:1
	ds_write2_b32 v2, v6, v7 offset0:2 offset1:3
	v_add_u32_e32 v4, 0x420, v2
	ds_write2_b32 v4, v8, v9 offset1:1
	v_add_u32_e32 v4, 0x428, v2
	ds_write2_b32 v4, v10, v11 offset1:1
	v_add_u32_e32 v4, 0x840, v2
	ds_write2_b32 v4, v12, v13 offset1:1
	v_add_u32_e32 v4, 0x848, v2
	ds_write2_b32 v4, v14, v15 offset1:1
	v_add_u32_e32 v4, 0xc60, v2
	ds_write2_b32 v4, v16, v17 offset1:1
	v_add_u32_e32 v4, 0xc68, v2
	ds_write2_b32 v4, v18, v19 offset1:1
	v_add_u32_e32 v4, 0x1080, v2
	ds_write2_b32 v4, v20, v21 offset1:1
	v_add_u32_e32 v4, 0x1088, v2
	ds_write2_b32 v4, v22, v23 offset1:1
	v_add_u32_e32 v4, 0x14a0, v2
	ds_write2_b32 v4, v24, v25 offset1:1
	v_add_u32_e32 v4, 0x14a8, v2
	ds_write2_b32 v4, v26, v27 offset1:1
	v_add_u32_e32 v4, 0x18c0, v2
	ds_write2_b32 v4, v28, v29 offset1:1
	v_add_u32_e32 v4, 0x18c8, v2
	ds_write2_b32 v4, v30, v31 offset1:1
	v_add_u32_e32 v4, 0x1ce0, v2
	v_add_u32_e32 v2, 0x1ce8, v2
	ds_write2_b32 v4, v32, v33 offset1:1
	ds_write2_b32 v2, v34, v35 offset1:1
	s_waitcnt lgkmcnt(0)
	ds_read2_b32 v[10:11], v49 offset0:33 offset1:41
	ds_read2_b32 v[12:13], v49 offset1:8
	v_lshlrev_b32_e32 v2, 1, v38
	ds_read2_b32 v[14:15], v49 offset0:66 offset1:74
	ds_read2_b32 v[16:17], v49 offset0:99 offset1:107
	ds_read2_b32 v[18:19], v49 offset0:132 offset1:140
	ds_read2_b32 v[20:21], v49 offset0:165 offset1:173
	ds_read2_b32 v[22:23], v49 offset0:198 offset1:206
	ds_read2_b32 v[24:25], v49 offset0:231 offset1:239
	v_lshl_add_u64 v[8:9], s[6:7], 0, v[2:3]
	v_or_b32_e32 v2, s2, v39
	v_lshlrev_b32_e32 v2, 11, v2
	v_lshl_add_u64 v[26:27], v[8:9], 0, v[2:3]
	v_or_b32_e32 v2, s2, v46
	s_waitcnt lgkmcnt(0)
	v_cvt_pk_bf16_f32 v4, v12, v10
	v_lshlrev_b32_e32 v2, 11, v2
	v_cvt_pk_bf16_f32 v5, v14, v16
	v_cvt_pk_bf16_f32 v6, v18, v20
	v_cvt_pk_bf16_f32 v7, v22, v24
	global_store_dwordx4 v[26:27], v[4:7], off sc1 nt
	s_nop 1
	v_cvt_pk_bf16_f32 v4, v13, v11
	v_lshl_add_u64 v[10:11], v[8:9], 0, v[2:3]
	v_cvt_pk_bf16_f32 v5, v15, v17
	v_cvt_pk_bf16_f32 v6, v19, v21
	v_cvt_pk_bf16_f32 v7, v23, v25
	global_store_dwordx4 v[10:11], v[4:7], off sc1 nt
	ds_read2_b32 v[10:11], v49 offset0:16 offset1:24
	ds_read2_b32 v[12:13], v49 offset0:49 offset1:57
	ds_read2_b32 v[14:15], v49 offset0:82 offset1:90
	ds_read2_b32 v[16:17], v49 offset0:115 offset1:123
	ds_read2_b32 v[18:19], v49 offset0:148 offset1:156
	ds_read2_b32 v[20:21], v49 offset0:181 offset1:189
	ds_read2_b32 v[22:23], v49 offset0:214 offset1:222
	ds_read2_b32 v[24:25], v49 offset0:247 offset1:255
	v_or_b32_e32 v2, s2, v47
	v_lshlrev_b32_e32 v2, 11, v2
	v_lshl_add_u64 v[26:27], v[8:9], 0, v[2:3]
	v_or_b32_e32 v2, s2, v48
	v_lshlrev_b32_e32 v2, 11, v2
	s_waitcnt lgkmcnt(6)
	v_cvt_pk_bf16_f32 v4, v10, v12
	s_waitcnt lgkmcnt(4)
	v_cvt_pk_bf16_f32 v5, v14, v16
	s_waitcnt lgkmcnt(2)
	v_cvt_pk_bf16_f32 v6, v18, v20
	s_waitcnt lgkmcnt(0)
	v_cvt_pk_bf16_f32 v7, v22, v24
	v_lshl_add_u64 v[8:9], v[8:9], 0, v[2:3]
	global_store_dwordx4 v[26:27], v[4:7], off sc1 nt
	s_nop 1
	v_cvt_pk_bf16_f32 v4, v11, v13
	v_cvt_pk_bf16_f32 v5, v15, v17
	v_cvt_pk_bf16_f32 v6, v19, v21
	v_cvt_pk_bf16_f32 v7, v23, v25
	global_store_dwordx4 v[8:9], v[4:7], off sc1 nt
	s_waitcnt lgkmcnt(0)

; #define GAS __attribute__((address_space(1)))
; #define LAS __attribute__((address_space(3)))
; #define LDS_WAIT() asm volatile("s_waitcnt lgkmcnt(0)" ::: "memory")
; __device__ __forceinline__ unsigned pk2(float lo, float hi) { unsigned r; asm("v_cvt_pk_bf16_f32 %0, %1, %2" : "=v"(r) : "v"(lo), "v"(hi)); return r; }
; __device__ __forceinline__ void transpose_item(const float* W, int K, int N, bf16* WT, int drow0, int kb, int n0, LAS float* scr, int lane) {
;     const int k0 = 64 * kb; const int c4 = 4 * (lane & 7); const bool ok = (n0 + c4) < N;
;     f32x4 v[8];
; #pragma unroll
;     for (int i = 0; i < 8; ++i) { const int kk = 8 * i + (lane >> 3); v[i] = ok ? *(const f32x4*)(W + (size_t)(k0 + kk) * N + n0 + c4) : (f32x4){0.f, 0.f, 0.f, 0.f}; }
; #pragma unroll
;     for (int i = 0; i < 8; ++i) { const int kk = 8 * i + (lane >> 3); LAS float* d = scr + kk * 33 + c4; d[0] = v[i][0]; d[1] = v[i][1]; d[2] = v[i][2]; d[3] = v[i][3]; }
;     LDS_WAIT(); asm volatile("" ::: "memory");
;     const int c = lane & 7;
; #pragma unroll
;     for (int j = 0; j < 4; ++j) { const int n = (lane >> 3) + 8 * j; const LAS float* s = scr + (8 * c) * 33 + n;
;         v4u o; o.x = pk2(s[0 * 33], s[1 * 33]); o.y = pk2(s[2 * 33], s[3 * 33]); o.z = pk2(s[4 * 33], s[5 * 33]); o.w = pk2(s[6 * 33], s[7 * 33]);
;         *(GAS v4u*)(WT + (size_t)(drow0 + n) * K + k0 + 8 * c) = o; }
;     LDS_WAIT(); asm volatile("" ::: "memory");
; }
; __device__ __forceinline__ void convert_item(const In& I, unsigned char* ws, int it, LAS float* scr, int lane) {
;     ...
;     if (r < T0) { const int f = r / I_FFN; r -= f * I_FFN;
;     ...
;         else { r -= 2 * I_G; const int kb = r / 32, nb = r % 32; transpose_item(I.w_down + (size_t)f * FF * D, FF, D, Wd + (size_t)f * D * FF, 32 * nb, kb, 32 * nb, scr, lane); }
.LBB0_347:
	s_andn2_b64 vcc, exec, s[2:3]
	s_cbranch_vccnz .LBB0_292
	s_mul_hi_i32 s2, s44, 0x3e0f83e1
	s_lshr_b32 s3, s2, 31
	s_ashr_i32 s6, s2, 10
	s_add_i32 s6, s6, s3
	s_mul_i32 s2, s6, 0xffffef80
	s_add_i32 s7, s40, s2
	s_add_i32 s7, s7, 0xa800
	s_cmpk_gt_i32 s7, 0xaff
	s_mov_b64 s[2:3], -1
	s_cbranch_scc0 .LBB0_350
	v_readlane_b32 s48, v253, 0
	v_readlane_b32 s49, v253, 1
	v_readlane_b32 s50, v253, 2
	v_readlane_b32 s51, v253, 3
	v_readlane_b32 s52, v253, 4
	v_readlane_b32 s53, v253, 5
	v_readlane_b32 s54, v253, 6
	v_readlane_b32 s55, v253, 7
	v_readlane_b32 s56, v253, 8
	v_readlane_b32 s57, v253, 9
	s_mov_b64 s[48:49], s[52:53]
	s_mul_i32 s3, s6, 0xb00000
	s_mov_b64 s[50:51], s[54:55]
	s_mov_b64 s[52:53], s[56:57]
	s_mul_hi_i32 s2, s6, 0xb00000
	s_add_u32 s9, s52, s3
	s_addc_u32 s11, s53, s2
	s_mul_i32 s3, s6, 0x580000
	s_mul_hi_i32 s2, s6, 0x580000
	s_add_u32 s3, s19, s3
	s_mul_i32 s10, s6, 0xffffdf00
	s_addc_u32 s8, s20, s2
	s_add_i32 s10, s43, s10
	s_add_i32 s10, s10, 0x10000
	s_and_b32 s2, s42, 0x3e0
	s_andn2_b32 s10, s10, 63
	s_add_i32 s68, s10, 0xffffea00
	s_lshl_b32 s10, s2, 2
	v_or_b32_e32 v32, s68, v39
	s_add_u32 s10, s9, s10
	s_addc_u32 s11, s11, 0
	v_lshlrev_b32_e32 v2, 2, v36
	v_ashrrev_i32_e32 v33, 31, v32
	v_or_b32_e32 v8, 8, v32
	v_lshl_add_u64 v[34:35], s[10:11], 0, v[2:3]
	v_lshlrev_b64 v[4:5], 12, v[32:33]
	v_ashrrev_i32_e32 v9, 31, v8
	v_lshl_add_u64 v[4:5], v[34:35], 0, v[4:5]
	v_lshlrev_b64 v[8:9], 12, v[8:9]
	v_or_b32_e32 v12, 16, v32
	global_load_dwordx4 v[4:7], v[4:5], off nt
	v_lshl_add_u64 v[8:9], v[34:35], 0, v[8:9]
	v_ashrrev_i32_e32 v13, 31, v12
	global_load_dwordx4 v[8:11], v[8:9], off nt
	v_lshlrev_b64 v[12:13], 12, v[12:13]
	v_or_b32_e32 v16, 24, v32
	v_lshl_add_u64 v[12:13], v[34:35], 0, v[12:13]
	v_ashrrev_i32_e32 v17, 31, v16
	global_load_dwordx4 v[12:15], v[12:13], off nt
	v_lshlrev_b64 v[16:17], 12, v[16:17]
	v_or_b32_e32 v20, 32, v32
	v_lshl_add_u64 v[16:17], v[34:35], 0, v[16:17]
	v_ashrrev_i32_e32 v21, 31, v20
	global_load_dwordx4 v[16:19], v[16:17], off nt
	v_lshlrev_b64 v[20:21], 12, v[20:21]
	v_or_b32_e32 v24, 40, v32
	v_lshl_add_u64 v[20:21], v[34:35], 0, v[20:21]
	v_ashrrev_i32_e32 v25, 31, v24
	global_load_dwordx4 v[20:23], v[20:21], off nt
	v_lshlrev_b64 v[24:25], 12, v[24:25]
	v_or_b32_e32 v28, 48, v32
	v_lshl_add_u64 v[24:25], v[34:35], 0, v[24:25]
	v_ashrrev_i32_e32 v29, 31, v28
	global_load_dwordx4 v[24:27], v[24:25], off nt
	v_lshlrev_b64 v[28:29], 12, v[28:29]
	v_or_b32_e32 v32, 56, v32
	v_lshl_add_u64 v[28:29], v[34:35], 0, v[28:29]
	v_ashrrev_i32_e32 v33, 31, v32
	global_load_dwordx4 v[28:31], v[28:29], off nt
	v_lshlrev_b64 v[32:33], 12, v[32:33]
	v_lshl_add_u64 v[32:33], v[34:35], 0, v[32:33]
	global_load_dwordx4 v[32:35], v[32:33], off nt
	v_add_u32_e32 v2, v44, v45
	s_lshl_b64 s[10:11], s[68:69], 1
	s_add_u32 s10, s3, s10
	s_addc_u32 s11, s8, s11
	v_readlane_b32 s58, v253, 10
	v_readlane_b32 s59, v253, 11
	v_readlane_b32 s60, v253, 12
	v_readlane_b32 s61, v253, 13
	v_readlane_b32 s62, v253, 14
	v_readlane_b32 s63, v253, 15
	s_waitcnt vmcnt(0)
	ds_write2_b32 v2, v4, v5 offset1:1
	ds_write2_b32 v2, v6, v7 offset0:2 offset1:3
	v_add_u32_e32 v4, 0x420, v2
	ds_write2_b32 v4, v8, v9 offset1:1
	v_add_u32_e32 v4, 0x428, v2
	ds_write2_b32 v4, v10, v11 offset1:1
	v_add_u32_e32 v4, 0x840, v2
	ds_write2_b32 v4, v12, v13 offset1:1
	v_add_u32_e32 v4, 0x848, v2
	ds_write2_b32 v4, v14, v15 offset1:1
	v_add_u32_e32 v4, 0xc60, v2
	ds_write2_b32 v4, v16, v17 offset1:1
	v_add_u32_e32 v4, 0xc68, v2
	ds_write2_b32 v4, v18, v19 offset1:1
	v_add_u32_e32 v4, 0x1080, v2
	ds_write2_b32 v4, v20, v21 offset1:1
	v_add_u32_e32 v4, 0x1088, v2
	ds_write2_b32 v4, v22, v23 offset1:1
	v_add_u32_e32 v4, 0x14a0, v2
	ds_write2_b32 v4, v24, v25 offset1:1
	v_add_u32_e32 v4, 0x14a8, v2
	ds_write2_b32 v4, v26, v27 offset1:1
	v_add_u32_e32 v4, 0x18c0, v2
	ds_write2_b32 v4, v28, v29 offset1:1
	v_add_u32_e32 v4, 0x18c8, v2
	ds_write2_b32 v4, v30, v31 offset1:1
	v_add_u32_e32 v4, 0x1ce0, v2
	v_add_u32_e32 v2, 0x1ce8, v2
	ds_write2_b32 v4, v32, v33 offset1:1
	ds_write2_b32 v2, v34, v35 offset1:1
	s_waitcnt lgkmcnt(0)
	ds_read2_b32 v[10:11], v49 offset0:33 offset1:41
	ds_read2_b32 v[12:13], v49 offset1:8
	v_lshlrev_b32_e32 v2, 1, v38
	ds_read2_b32 v[14:15], v49 offset0:66 offset1:74
	ds_read2_b32 v[16:17], v49 offset0:99 offset1:107
	ds_read2_b32 v[18:19], v49 offset0:132 offset1:140
	ds_read2_b32 v[20:21], v49 offset0:165 offset1:173
	ds_read2_b32 v[22:23], v49 offset0:198 offset1:206
	ds_read2_b32 v[24:25], v49 offset0:231 offset1:239
	v_lshl_add_u64 v[8:9], s[10:11], 0, v[2:3]
	v_or_b32_e32 v2, s2, v39
	v_mul_u32_u24_e32 v2, 0x1600, v2
	v_lshl_add_u64 v[26:27], v[8:9], 0, v[2:3]
	v_or_b32_e32 v2, s2, v46
	s_waitcnt lgkmcnt(0)
	v_cvt_pk_bf16_f32 v4, v12, v10
	v_mul_u32_u24_e32 v2, 0x1600, v2
	v_cvt_pk_bf16_f32 v5, v14, v16
	v_cvt_pk_bf16_f32 v6, v18, v20
	v_cvt_pk_bf16_f32 v7, v22, v24
	global_store_dwordx4 v[26:27], v[4:7], off sc1 nt
	s_nop 1
	v_cvt_pk_bf16_f32 v4, v13, v11
	v_lshl_add_u64 v[10:11], v[8:9], 0, v[2:3]
	v_cvt_pk_bf16_f32 v5, v15, v17
	v_cvt_pk_bf16_f32 v6, v19, v21
	v_cvt_pk_bf16_f32 v7, v23, v25
	global_store_dwordx4 v[10:11], v[4:7], off sc1 nt
	ds_read2_b32 v[10:11], v49 offset0:16 offset1:24
	ds_read2_b32 v[12:13], v49 offset0:49 offset1:57
	ds_read2_b32 v[14:15], v49 offset0:82 offset1:90
	ds_read2_b32 v[16:17], v49 offset0:115 offset1:123
	ds_read2_b32 v[18:19], v49 offset0:148 offset1:156
	ds_read2_b32 v[20:21], v49 offset0:181 offset1:189
	ds_read2_b32 v[22:23], v49 offset0:214 offset1:222
	ds_read2_b32 v[24:25], v49 offset0:247 offset1:255
	v_or_b32_e32 v2, s2, v47
	v_mul_u32_u24_e32 v2, 0x1600, v2
	v_lshl_add_u64 v[26:27], v[8:9], 0, v[2:3]
	v_or_b32_e32 v2, s2, v48
	v_mul_u32_u24_e32 v2, 0x1600, v2
	s_waitcnt lgkmcnt(6)
	v_cvt_pk_bf16_f32 v4, v10, v12
	s_waitcnt lgkmcnt(4)
	v_cvt_pk_bf16_f32 v5, v14, v16
	s_waitcnt lgkmcnt(2)
	v_cvt_pk_bf16_f32 v6, v18, v20
	s_waitcnt lgkmcnt(0)
	v_cvt_pk_bf16_f32 v7, v22, v24
	v_lshl_add_u64 v[8:9], v[8:9], 0, v[2:3]
	global_store_dwordx4 v[26:27], v[4:7], off sc1 nt
	s_mov_b64 s[2:3], 0
	s_nop 0
	v_cvt_pk_bf16_f32 v4, v11, v13
	v_cvt_pk_bf16_f32 v5, v15, v17
	v_cvt_pk_bf16_f32 v6, v19, v21
	v_cvt_pk_bf16_f32 v7, v23, v25
	global_store_dwordx4 v[8:9], v[4:7], off sc1 nt
	s_waitcnt lgkmcnt(0)

; #define GAS __attribute__((address_space(1)))
; #define LAS __attribute__((address_space(3)))
; #define LDS_WAIT() asm volatile("s_waitcnt lgkmcnt(0)" ::: "memory")
; __device__ __forceinline__ unsigned pk2(float lo, float hi) { unsigned r; asm("v_cvt_pk_bf16_f32 %0, %1, %2" : "=v"(r) : "v"(lo), "v"(hi)); return r; }
; __device__ __forceinline__ void transpose_item(const float* W, int K, int N, bf16* WT, int drow0, int kb, int n0, LAS float* scr, int lane) {
;     const int k0 = 64 * kb; const int c4 = 4 * (lane & 7); const bool ok = (n0 + c4) < N;
;     f32x4 v[8];
; #pragma unroll
;     for (int i = 0; i < 8; ++i) { const int kk = 8 * i + (lane >> 3); v[i] = ok ? *(const f32x4*)(W + (size_t)(k0 + kk) * N + n0 + c4) : (f32x4){0.f, 0.f, 0.f, 0.f}; }
; #pragma unroll
;     for (int i = 0; i < 8; ++i) { const int kk = 8 * i + (lane >> 3); LAS float* d = scr + kk * 33 + c4; d[0] = v[i][0]; d[1] = v[i][1]; d[2] = v[i][2]; d[3] = v[i][3]; }
;     LDS_WAIT(); asm volatile("" ::: "memory");
;     const int c = lane & 7;
; #pragma unroll
;     for (int j = 0; j < 4; ++j) { const int n = (lane >> 3) + 8 * j; const LAS float* s = scr + (8 * c) * 33 + n;
;         v4u o; o.x = pk2(s[0 * 33], s[1 * 33]); o.y = pk2(s[2 * 33], s[3 * 33]); o.z = pk2(s[4 * 33], s[5 * 33]); o.w = pk2(s[6 * 33], s[7 * 33]);
;         *(GAS v4u*)(WT + (size_t)(drow0 + n) * K + k0 + 8 * c) = o; }
;     LDS_WAIT(); asm volatile("" ::: "memory");
; }
; __device__ __forceinline__ void convert_item(const In& I, unsigned char* ws, int it, LAS float* scr, int lane) {
;     ...
;     { const int jk = r >> 3; r &= 7; const int kb = r >> 1, nb = r & 1;
;         transpose_item(I.nsa_w2 + (size_t)jk * 256 * 64, 256, 64, W2t + (size_t)jk * 64 * 256, 32 * nb, kb, 32 * nb, scr, lane); }
.LBB0_355:
	s_add_i32 s45, s41, 0xa800
	s_cmp_gt_i32 s45, 0x83ff
	s_mov_b64 s[2:3], -1
	s_cbranch_scc0 .LBB0_409
	s_cmpk_gt_u32 s45, 0x8eff
	s_cbranch_scc0 .LBB0_390
	s_cmpk_gt_u32 s45, 0x92ff
	s_cbranch_scc0 .LBB0_387
	s_cmpk_gt_u32 s45, 0x9fff
	s_cbranch_scc0 .LBB0_368
	s_cmpk_gt_u32 s45, 0xa3ff
	s_cbranch_scc0 .LBB0_365
	s_cmpk_gt_u32 s45, 0xa7ff
	s_cbranch_scc0 .LBB0_362
	s_lshr_b32 s68, s41, 3
	v_readlane_b32 s48, v253, 16
	s_lshl_b64 s[2:3], s[68:69], 16
	v_readlane_b32 s52, v253, 20
	v_readlane_b32 s53, v253, 21
	s_add_u32 s6, s52, s2
	s_addc_u32 s7, s53, s3
	s_lshl_b64 s[2:3], s[68:69], 15
	s_add_u32 s8, s34, s2
	s_addc_u32 s3, s35, s3
	s_and_b32 s2, s43, 32
	s_and_b32 s9, s43, 0xc0
	s_lshl_b32 s10, s2, 2
	s_add_u32 s6, s6, s10
	v_or_b32_e32 v6, s9, v39
	s_addc_u32 s7, s7, 0
	v_lshlrev_b32_e32 v2, 2, v36
	v_lshl_add_u64 v[4:5], s[6:7], 0, v[2:3]
	v_lshlrev_b32_e32 v2, 8, v6
	v_lshl_add_u64 v[28:29], v[4:5], 0, v[2:3]
	v_add_co_u32_e32 v16, vcc, s84, v28
	global_load_dwordx4 v[4:7], v[28:29], off nt
	global_load_dwordx4 v[8:11], v[28:29], off offset:2048 nt
	v_addc_co_u32_e32 v17, vcc, 0, v29, vcc
	v_add_co_u32_e32 v24, vcc, s74, v28
	s_movk_i32 s6, 0x3000
	s_nop 0
	v_addc_co_u32_e32 v25, vcc, 0, v29, vcc
	global_load_dwordx4 v[12:15], v[24:25], off offset:-4096 nt
	s_nop 0
	global_load_dwordx4 v[16:19], v[16:17], off offset:2048 nt
	s_nop 0
	global_load_dwordx4 v[20:23], v[24:25], off nt
	s_nop 0
	global_load_dwordx4 v[24:27], v[24:25], off offset:2048 nt
	v_add_co_u32_e32 v32, vcc, s6, v28
	v_add_u32_e32 v2, v44, v47
	s_nop 0
	v_addc_co_u32_e32 v33, vcc, 0, v29, vcc
	global_load_dwordx4 v[28:31], v[32:33], off nt
	s_nop 0
	global_load_dwordx4 v[32:35], v[32:33], off offset:2048 nt
	s_lshl_b32 s6, s9, 1
	s_add_u32 s6, s8, s6
	s_addc_u32 s7, s3, 0
	v_readlane_b32 s49, v253, 17
	v_readlane_b32 s50, v253, 18
	v_readlane_b32 s51, v253, 19
	v_readlane_b32 s54, v253, 22
	v_readlane_b32 s55, v253, 23
	v_readlane_b32 s56, v253, 24
	v_readlane_b32 s57, v253, 25
	v_readlane_b32 s58, v253, 26
	v_readlane_b32 s59, v253, 27
	v_readlane_b32 s60, v253, 28
	v_readlane_b32 s61, v253, 29
	v_readlane_b32 s62, v253, 30
	v_readlane_b32 s63, v253, 31
	s_waitcnt vmcnt(0)
	ds_write2_b32 v45, v4, v5 offset1:1
	ds_write2_b32 v45, v6, v7 offset0:2 offset1:3
	v_add_u32_e32 v4, 0x420, v2
	ds_write2_b32 v2, v8, v9 offset1:1
	ds_write2_b32 v2, v10, v11 offset0:2 offset1:3
	ds_write2_b32 v4, v12, v13 offset1:1
	v_add_u32_e32 v4, 0x428, v2
	ds_write2_b32 v4, v14, v15 offset1:1
	v_add_u32_e32 v4, 0x840, v2
	v_add_u32_e32 v2, 0x848, v2
	ds_write2_b32 v2, v18, v19 offset1:1
	v_add_u32_e32 v2, 0x1080, v45
	ds_write2_b32 v2, v20, v21 offset1:1
	v_add_u32_e32 v2, 0x1088, v45
	ds_write2_b32 v2, v22, v23 offset1:1
	v_add_u32_e32 v2, 0x14a0, v45
	ds_write2_b32 v2, v24, v25 offset1:1
	v_add_u32_e32 v2, 0x14a8, v45
	ds_write2_b32 v2, v26, v27 offset1:1
	v_add_u32_e32 v2, 0x18c0, v45
	ds_write2_b32 v2, v28, v29 offset1:1
	v_add_u32_e32 v2, 0x18c8, v45
	ds_write2_b32 v2, v30, v31 offset1:1
	v_add_u32_e32 v2, 0x1ce0, v45
	ds_write2_b32 v2, v32, v33 offset1:1
	v_add_u32_e32 v2, 0x1ce8, v45
	ds_write2_b32 v4, v16, v17 offset1:1
	ds_write2_b32 v2, v34, v35 offset1:1
	s_waitcnt lgkmcnt(0)
	ds_read2_b32 v[10:11], v50 offset0:33 offset1:41
	ds_read2_b32 v[12:13], v50 offset1:8
	v_lshlrev_b32_e32 v2, 1, v38
	ds_read2_b32 v[14:15], v50 offset0:66 offset1:74
	ds_read2_b32 v[16:17], v50 offset0:99 offset1:107
	ds_read2_b32 v[18:19], v50 offset0:132 offset1:140
	ds_read2_b32 v[20:21], v50 offset0:165 offset1:173
	ds_read2_b32 v[22:23], v50 offset0:198 offset1:206
	ds_read2_b32 v[24:25], v50 offset0:231 offset1:239
	v_lshl_add_u64 v[4:5], s[6:7], 0, v[2:3]
	v_or_b32_e32 v2, s2, v39
	v_lshlrev_b32_e32 v2, 9, v2
	v_lshl_add_u64 v[26:27], v[4:5], 0, v[2:3]
	v_or_b32_e32 v2, s2, v46
	s_waitcnt lgkmcnt(0)
	v_cvt_pk_bf16_f32 v6, v12, v10
	v_lshlrev_b32_e32 v2, 9, v2
	v_cvt_pk_bf16_f32 v7, v14, v16
	v_cvt_pk_bf16_f32 v8, v18, v20
	v_cvt_pk_bf16_f32 v9, v22, v24
	global_store_dwordx4 v[26:27], v[6:9], off sc1 nt
	s_nop 1
	v_cvt_pk_bf16_f32 v6, v13, v11
	v_lshl_add_u64 v[10:11], v[4:5], 0, v[2:3]
	v_cvt_pk_bf16_f32 v7, v15, v17
	v_cvt_pk_bf16_f32 v8, v19, v21
	v_cvt_pk_bf16_f32 v9, v23, v25
	global_store_dwordx4 v[10:11], v[6:9], off sc1 nt
	ds_read2_b32 v[10:11], v50 offset0:16 offset1:24
	ds_read2_b32 v[12:13], v50 offset0:49 offset1:57
	ds_read2_b32 v[14:15], v50 offset0:82 offset1:90
	ds_read2_b32 v[16:17], v50 offset0:115 offset1:123
	ds_read2_b32 v[18:19], v50 offset0:148 offset1:156
	ds_read2_b32 v[20:21], v50 offset0:181 offset1:189
	ds_read2_b32 v[22:23], v50 offset0:214 offset1:222
	ds_read2_b32 v[24:25], v50 offset0:247 offset1:255
	v_or_b32_e32 v2, s2, v48
	v_lshlrev_b32_e32 v2, 9, v2
	v_lshl_add_u64 v[26:27], v[4:5], 0, v[2:3]
	v_or_b32_e32 v2, s2, v49
	v_lshlrev_b32_e32 v2, 9, v2
	s_waitcnt lgkmcnt(6)
	v_cvt_pk_bf16_f32 v6, v10, v12
	s_waitcnt lgkmcnt(4)
	v_cvt_pk_bf16_f32 v7, v14, v16
	s_waitcnt lgkmcnt(2)
	v_cvt_pk_bf16_f32 v8, v18, v20
	s_waitcnt lgkmcnt(0)
	v_cvt_pk_bf16_f32 v9, v22, v24
	v_lshl_add_u64 v[4:5], v[4:5], 0, v[2:3]
	global_store_dwordx4 v[26:27], v[6:9], off sc1 nt
	s_mov_b64 s[2:3], 0
	s_nop 0
	v_cvt_pk_bf16_f32 v6, v11, v13
	v_cvt_pk_bf16_f32 v7, v15, v17
	v_cvt_pk_bf16_f32 v8, v19, v21
	v_cvt_pk_bf16_f32 v9, v23, v25
	global_store_dwordx4 v[4:5], v[6:9], off sc1 nt
	s_waitcnt lgkmcnt(0)
; #define GAS __attribute__((address_space(1)))
; #define LAS __attribute__((address_space(3)))
; #define LDS_WAIT() asm volatile("s_waitcnt lgkmcnt(0)" ::: "memory")
; __device__ __forceinline__ unsigned pk2(float lo, float hi) { unsigned r; asm("v_cvt_pk_bf16_f32 %0, %1, %2" : "=v"(r) : "v"(lo), "v"(hi)); return r; }
; __device__ __forceinline__ void transpose_item(const float* W, int K, int N, bf16* WT, int drow0, int kb, int n0, LAS float* scr, int lane) {
;     const int k0 = 64 * kb; const int c4 = 4 * (lane & 7); const bool ok = (n0 + c4) < N;
;     f32x4 v[8];
; #pragma unroll
;     for (int i = 0; i < 8; ++i) { const int kk = 8 * i + (lane >> 3); v[i] = ok ? *(const f32x4*)(W + (size_t)(k0 + kk) * N + n0 + c4) : (f32x4){0.f, 0.f, 0.f, 0.f}; }
; #pragma unroll
;     for (int i = 0; i < 8; ++i) { const int kk = 8 * i + (lane >> 3); LAS float* d = scr + kk * 33 + c4; d[0] = v[i][0]; d[1] = v[i][1]; d[2] = v[i][2]; d[3] = v[i][3]; }
;     LDS_WAIT(); asm volatile("" ::: "memory");
;     const int c = lane & 7;
; #pragma unroll
;     for (int j = 0; j < 4; ++j) { const int n = (lane >> 3) + 8 * j; const LAS float* s = scr + (8 * c) * 33 + n;
;         v4u o; o.x = pk2(s[0 * 33], s[1 * 33]); o.y = pk2(s[2 * 33], s[3 * 33]); o.z = pk2(s[4 * 33], s[5 * 33]); o.w = pk2(s[6 * 33], s[7 * 33]);
;         *(GAS v4u*)(WT + (size_t)(drow0 + n) * K + k0 + 8 * c) = o; }
;     LDS_WAIT(); asm volatile("" ::: "memory");
; }
; __device__ __forceinline__ void convert_item(const In& I, unsigned char* ws, int it, LAS float* scr, int lane) {
;     ...
;     if (r < 4 * I_W1) { const int jk = r / I_W1; r -= jk * I_W1; const int kb = r / 8, nb = r % 8;
;         transpose_item(I.nsa_w1 + (size_t)jk * 2048 * 256, 2048, 256, W1t + (size_t)jk * 256 * 2048, 32 * nb, kb, 32 * nb, scr, lane); return; }
.LBB0_362:
	s_andn2_b64 vcc, exec, s[2:3]
	s_cbranch_vccnz .LBB0_364
	s_add_i32 s2, s41, 0x400
	s_lshr_b32 s68, s2, 8
	s_lshl_b64 s[2:3], s[68:69], 21
	v_readlane_b32 s48, v253, 16
	v_readlane_b32 s49, v253, 17
	s_add_u32 s6, s48, s2
	s_addc_u32 s7, s49, s3
	s_lshl_b64 s[2:3], s[68:69], 20
	s_add_u32 s8, s31, s2
	s_addc_u32 s3, s33, s3
	s_and_b32 s2, s43, 0xe0
	s_and_b32 s9, s42, 0x7c0
	s_lshl_b32 s10, s2, 2
	s_add_u32 s6, s6, s10
	v_or_b32_e32 v6, s9, v39
	s_addc_u32 s7, s7, 0
	v_lshlrev_b32_e32 v2, 2, v36
	v_lshl_add_u64 v[4:5], s[6:7], 0, v[2:3]
	v_lshlrev_b32_e32 v2, 10, v6
	v_lshl_add_u64 v[32:33], v[4:5], 0, v[2:3]
	v_add_co_u32_e32 v8, vcc, s74, v32
	s_movk_i32 s6, 0x4000
	s_nop 0
	v_addc_co_u32_e32 v9, vcc, 0, v33, vcc
	v_add_co_u32_e32 v12, vcc, s6, v32
	s_movk_i32 s6, 0x6000
	s_nop 0
	v_addc_co_u32_e32 v13, vcc, 0, v33, vcc
	global_load_dwordx4 v[4:7], v[32:33], off nt
	v_add_co_u32_e32 v16, vcc, s6, v32
	global_load_dwordx4 v[8:11], v[8:9], off nt
	s_nop 0
	v_addc_co_u32_e32 v17, vcc, 0, v33, vcc
	global_load_dwordx4 v[12:15], v[12:13], off nt
	v_add_co_u32_e32 v20, vcc, s81, v32
	global_load_dwordx4 v[16:19], v[16:17], off nt
	s_nop 0
	v_addc_co_u32_e32 v21, vcc, 0, v33, vcc
	s_mov_b32 s6, 0xa000
	global_load_dwordx4 v[20:23], v[20:21], off nt
	v_add_co_u32_e32 v24, vcc, s6, v32
	s_mov_b32 s6, 0xc000
	s_nop 0
	v_addc_co_u32_e32 v25, vcc, 0, v33, vcc
	global_load_dwordx4 v[24:27], v[24:25], off nt
	v_add_co_u32_e32 v28, vcc, s6, v32
	s_mov_b32 s6, 0xe000
	s_nop 0
	v_addc_co_u32_e32 v29, vcc, 0, v33, vcc
	global_load_dwordx4 v[28:31], v[28:29], off nt
	v_add_co_u32_e32 v32, vcc, s6, v32
	v_add_u32_e32 v2, v44, v47
	s_nop 0
	v_addc_co_u32_e32 v33, vcc, 0, v33, vcc
	global_load_dwordx4 v[32:35], v[32:33], off nt
	s_lshl_b32 s6, s9, 1
	s_add_u32 s6, s8, s6
	s_addc_u32 s7, s3, 0
	v_readlane_b32 s50, v253, 18
	v_readlane_b32 s51, v253, 19
	v_readlane_b32 s52, v253, 20
	v_readlane_b32 s53, v253, 21
	v_readlane_b32 s54, v253, 22
	v_readlane_b32 s55, v253, 23
	v_readlane_b32 s56, v253, 24
	v_readlane_b32 s57, v253, 25
	v_readlane_b32 s58, v253, 26
	v_readlane_b32 s59, v253, 27
	v_readlane_b32 s60, v253, 28
	v_readlane_b32 s61, v253, 29
	v_readlane_b32 s62, v253, 30
	v_readlane_b32 s63, v253, 31
	s_waitcnt vmcnt(0)
	ds_write2_b32 v45, v4, v5 offset1:1
	ds_write2_b32 v45, v6, v7 offset0:2 offset1:3
	v_add_u32_e32 v4, 0x420, v2
	ds_write2_b32 v2, v8, v9 offset1:1
	ds_write2_b32 v2, v10, v11 offset0:2 offset1:3
	ds_write2_b32 v4, v12, v13 offset1:1
	v_add_u32_e32 v4, 0x428, v2
	ds_write2_b32 v4, v14, v15 offset1:1
	v_add_u32_e32 v4, 0x840, v2
	v_add_u32_e32 v2, 0x848, v2
	ds_write2_b32 v2, v18, v19 offset1:1
	v_add_u32_e32 v2, 0x1080, v45
	ds_write2_b32 v2, v20, v21 offset1:1
	v_add_u32_e32 v2, 0x1088, v45
	ds_write2_b32 v2, v22, v23 offset1:1
	v_add_u32_e32 v2, 0x14a0, v45
	ds_write2_b32 v4, v16, v17 offset1:1
	ds_write2_b32 v2, v24, v25 offset1:1
	v_add_u32_e32 v2, 0x14a8, v45
	ds_write2_b32 v2, v26, v27 offset1:1
	v_add_u32_e32 v2, 0x18c0, v45
	ds_write2_b32 v2, v28, v29 offset1:1
	v_add_u32_e32 v2, 0x18c8, v45
	ds_write2_b32 v2, v30, v31 offset1:1
	v_add_u32_e32 v2, 0x1ce0, v45
	ds_write2_b32 v2, v32, v33 offset1:1
	v_add_u32_e32 v2, 0x1ce8, v45
	ds_write2_b32 v2, v34, v35 offset1:1
	s_waitcnt lgkmcnt(0)
	ds_read2_b32 v[10:11], v50 offset0:33 offset1:41
	ds_read2_b32 v[12:13], v50 offset1:8
	v_lshlrev_b32_e32 v2, 1, v38
	ds_read2_b32 v[14:15], v50 offset0:66 offset1:74
	ds_read2_b32 v[16:17], v50 offset0:99 offset1:107
	ds_read2_b32 v[18:19], v50 offset0:132 offset1:140
	ds_read2_b32 v[20:21], v50 offset0:165 offset1:173
	ds_read2_b32 v[22:23], v50 offset0:198 offset1:206
	ds_read2_b32 v[24:25], v50 offset0:231 offset1:239
	v_lshl_add_u64 v[4:5], s[6:7], 0, v[2:3]
	v_or_b32_e32 v2, s2, v39
	v_lshlrev_b32_e32 v2, 12, v2
	v_lshl_add_u64 v[26:27], v[4:5], 0, v[2:3]
	v_or_b32_e32 v2, s2, v46
	s_waitcnt lgkmcnt(0)
	v_cvt_pk_bf16_f32 v6, v12, v10
	v_lshlrev_b32_e32 v2, 12, v2
	v_cvt_pk_bf16_f32 v7, v14, v16
	v_cvt_pk_bf16_f32 v8, v18, v20
	v_cvt_pk_bf16_f32 v9, v22, v24
	global_store_dwordx4 v[26:27], v[6:9], off sc1 nt
	s_nop 1
	v_cvt_pk_bf16_f32 v6, v13, v11
	v_lshl_add_u64 v[10:11], v[4:5], 0, v[2:3]
	v_cvt_pk_bf16_f32 v7, v15, v17
	v_cvt_pk_bf16_f32 v8, v19, v21
	v_cvt_pk_bf16_f32 v9, v23, v25
	global_store_dwordx4 v[10:11], v[6:9], off sc1 nt
	ds_read2_b32 v[10:11], v50 offset0:16 offset1:24
	ds_read2_b32 v[12:13], v50 offset0:49 offset1:57
	ds_read2_b32 v[14:15], v50 offset0:82 offset1:90
	ds_read2_b32 v[16:17], v50 offset0:115 offset1:123
	ds_read2_b32 v[18:19], v50 offset0:148 offset1:156
	ds_read2_b32 v[20:21], v50 offset0:181 offset1:189
	ds_read2_b32 v[22:23], v50 offset0:214 offset1:222
	ds_read2_b32 v[24:25], v50 offset0:247 offset1:255
	v_or_b32_e32 v2, s2, v48
	v_lshlrev_b32_e32 v2, 12, v2
	v_lshl_add_u64 v[26:27], v[4:5], 0, v[2:3]
	v_or_b32_e32 v2, s2, v49
	v_lshlrev_b32_e32 v2, 12, v2
	s_waitcnt lgkmcnt(6)
	v_cvt_pk_bf16_f32 v6, v10, v12
	s_waitcnt lgkmcnt(4)
	v_cvt_pk_bf16_f32 v7, v14, v16
	s_waitcnt lgkmcnt(2)
	v_cvt_pk_bf16_f32 v8, v18, v20
	s_waitcnt lgkmcnt(0)
	v_cvt_pk_bf16_f32 v9, v22, v24
	v_lshl_add_u64 v[4:5], v[4:5], 0, v[2:3]
	global_store_dwordx4 v[26:27], v[6:9], off sc1 nt
	s_nop 1
	v_cvt_pk_bf16_f32 v6, v11, v13
	v_cvt_pk_bf16_f32 v7, v15, v17
	v_cvt_pk_bf16_f32 v8, v19, v21
	v_cvt_pk_bf16_f32 v9, v23, v25
	global_store_dwordx4 v[4:5], v[6:9], off sc1 nt
	s_waitcnt lgkmcnt(0)

; #define GAS __attribute__((address_space(1)))
; #define LAS __attribute__((address_space(3)))
; #define LDS_WAIT() asm volatile("s_waitcnt lgkmcnt(0)" ::: "memory")
; __device__ __forceinline__ unsigned pk2(float lo, float hi) { unsigned r; asm("v_cvt_pk_bf16_f32 %0, %1, %2" : "=v"(r) : "v"(lo), "v"(hi)); return r; }
; __device__ __forceinline__ void transpose_item(const float* W, int K, int N, bf16* WT, int drow0, int kb, int n0, LAS float* scr, int lane) {
;     const int k0 = 64 * kb; const int c4 = 4 * (lane & 7); const bool ok = (n0 + c4) < N;
;     f32x4 v[8];
; #pragma unroll
;     for (int i = 0; i < 8; ++i) { const int kk = 8 * i + (lane >> 3); v[i] = ok ? *(const f32x4*)(W + (size_t)(k0 + kk) * N + n0 + c4) : (f32x4){0.f, 0.f, 0.f, 0.f}; }
; #pragma unroll
;     for (int i = 0; i < 8; ++i) { const int kk = 8 * i + (lane >> 3); LAS float* d = scr + kk * 33 + c4; d[0] = v[i][0]; d[1] = v[i][1]; d[2] = v[i][2]; d[3] = v[i][3]; }
;     LDS_WAIT(); asm volatile("" ::: "memory");
;     const int c = lane & 7;
; #pragma unroll
;     for (int j = 0; j < 4; ++j) { const int n = (lane >> 3) + 8 * j; const LAS float* s = scr + (8 * c) * 33 + n;
;         v4u o; o.x = pk2(s[0 * 33], s[1 * 33]); o.y = pk2(s[2 * 33], s[3 * 33]); o.z = pk2(s[4 * 33], s[5 * 33]); o.w = pk2(s[6 * 33], s[7 * 33]);
;         *(GAS v4u*)(WT + (size_t)(drow0 + n) * K + k0 + 8 * c) = o; }
;     LDS_WAIT(); asm volatile("" ::: "memory");
; }
; __device__ __forceinline__ void convert_item(const In& I, unsigned char* ws, int it, LAS float* scr, int lane) {
;     ...
;     if (r < 2 * I_SQ) { const int j = r / I_SQ; r -= j * I_SQ; const int kb = r / 32, nb = r % 32;
;         transpose_item(I.fox_w_out + (size_t)j * D * D, D, D, Wfout + (size_t)j * D * D, 32 * nb, kb, 32 * nb, scr, lane); return; }
.LBB0_365:
	s_andn2_b64 vcc, exec, s[2:3]
	s_cbranch_vccnz .LBB0_367
	s_add_i32 s2, s41, 0x800
	s_lshr_b32 s68, s2, 9
	v_readlane_b32 s48, v253, 16
	s_lshl_b64 s[2:3], s[68:69], 22
	v_readlane_b32 s60, v253, 28
	v_readlane_b32 s61, v253, 29
	s_add_u32 s8, s60, s2
	s_addc_u32 s9, s61, s3
	s_lshl_b64 s[6:7], s[68:69], 21
	s_add_u32 s3, s26, s6
	s_addc_u32 s6, s27, s7
	s_and_b32 s2, s43, 0x3e0
	s_add_i32 s7, s44, 0x11600
	s_and_b32 s7, s7, 0x3c0
	s_lshl_b32 s10, s2, 2
	s_add_u32 s8, s8, s10
	v_or_b32_e32 v6, s7, v39
	s_addc_u32 s9, s9, 0
	v_lshlrev_b32_e32 v2, 2, v36
	v_lshl_add_u64 v[4:5], s[8:9], 0, v[2:3]
	v_lshlrev_b32_e32 v2, 12, v6
	v_lshl_add_u64 v[32:33], v[4:5], 0, v[2:3]
	v_add_co_u32_e32 v8, vcc, s81, v32
	global_load_dwordx4 v[4:7], v[32:33], off nt
	s_nop 0
	v_addc_co_u32_e32 v9, vcc, 0, v33, vcc
	v_add_co_u32_e32 v12, vcc, s79, v32
	global_load_dwordx4 v[8:11], v[8:9], off nt
	s_nop 0
	v_addc_co_u32_e32 v13, vcc, 0, v33, vcc
	v_add_co_u32_e32 v16, vcc, s80, v32
	global_load_dwordx4 v[12:15], v[12:13], off nt
	s_nop 0
	v_addc_co_u32_e32 v17, vcc, 0, v33, vcc
	v_add_co_u32_e32 v20, vcc, s85, v32
	global_load_dwordx4 v[16:19], v[16:17], off nt
	s_nop 0
	v_addc_co_u32_e32 v21, vcc, 0, v33, vcc
	global_load_dwordx4 v[20:23], v[20:21], off nt
	v_add_co_u32_e32 v24, vcc, s86, v32
	v_add_u32_e32 v2, v44, v47
	s_nop 0
	v_addc_co_u32_e32 v25, vcc, 0, v33, vcc
	global_load_dwordx4 v[24:27], v[24:25], off nt
	v_add_co_u32_e32 v28, vcc, s87, v32
	s_lshl_b32 s7, s7, 1
	s_nop 0
	v_addc_co_u32_e32 v29, vcc, 0, v33, vcc
	global_load_dwordx4 v[28:31], v[28:29], off nt
	v_add_co_u32_e32 v32, vcc, s89, v32
	s_add_u32 s8, s3, s7
	s_nop 0
	v_addc_co_u32_e32 v33, vcc, 0, v33, vcc
	global_load_dwordx4 v[32:35], v[32:33], off nt
	s_addc_u32 s9, s6, 0
	v_readlane_b32 s49, v253, 17
	v_readlane_b32 s50, v253, 18
	v_readlane_b32 s51, v253, 19
	v_readlane_b32 s52, v253, 20
	v_readlane_b32 s53, v253, 21
	v_readlane_b32 s54, v253, 22
	v_readlane_b32 s55, v253, 23
	v_readlane_b32 s56, v253, 24
	v_readlane_b32 s57, v253, 25
	v_readlane_b32 s58, v253, 26
	v_readlane_b32 s59, v253, 27
	v_readlane_b32 s62, v253, 30
	v_readlane_b32 s63, v253, 31
	s_waitcnt vmcnt(0)
	ds_write2_b32 v45, v4, v5 offset1:1
	ds_write2_b32 v45, v6, v7 offset0:2 offset1:3
	v_add_u32_e32 v4, 0x420, v2
	ds_write2_b32 v2, v8, v9 offset1:1
	ds_write2_b32 v2, v10, v11 offset0:2 offset1:3
	ds_write2_b32 v4, v12, v13 offset1:1
	v_add_u32_e32 v4, 0x428, v2
	ds_write2_b32 v4, v14, v15 offset1:1
	v_add_u32_e32 v4, 0x840, v2
	v_add_u32_e32 v2, 0x848, v2
	ds_write2_b32 v2, v18, v19 offset1:1
	v_add_u32_e32 v2, 0x1080, v45
	ds_write2_b32 v4, v16, v17 offset1:1
	ds_write2_b32 v2, v20, v21 offset1:1
	v_add_u32_e32 v2, 0x1088, v45
	ds_write2_b32 v2, v22, v23 offset1:1
	v_add_u32_e32 v2, 0x14a0, v45
	ds_write2_b32 v2, v24, v25 offset1:1
	v_add_u32_e32 v2, 0x14a8, v45
	ds_write2_b32 v2, v26, v27 offset1:1
	v_add_u32_e32 v2, 0x18c0, v45
	ds_write2_b32 v2, v28, v29 offset1:1
	v_add_u32_e32 v2, 0x18c8, v45
	ds_write2_b32 v2, v30, v31 offset1:1
	v_add_u32_e32 v2, 0x1ce0, v45
	ds_write2_b32 v2, v32, v33 offset1:1
	v_add_u32_e32 v2, 0x1ce8, v45
	ds_write2_b32 v2, v34, v35 offset1:1
	s_waitcnt lgkmcnt(0)
	ds_read2_b32 v[10:11], v50 offset0:33 offset1:41
	ds_read2_b32 v[12:13], v50 offset1:8
	v_lshlrev_b32_e32 v2, 1, v38
	ds_read2_b32 v[14:15], v50 offset0:66 offset1:74
	ds_read2_b32 v[16:17], v50 offset0:99 offset1:107
	ds_read2_b32 v[18:19], v50 offset0:132 offset1:140
	ds_read2_b32 v[20:21], v50 offset0:165 offset1:173
	ds_read2_b32 v[22:23], v50 offset0:198 offset1:206
	ds_read2_b32 v[24:25], v50 offset0:231 offset1:239
	v_lshl_add_u64 v[8:9], s[8:9], 0, v[2:3]
	v_or_b32_e32 v2, s2, v39
	v_lshlrev_b32_e32 v2, 11, v2
	v_lshl_add_u64 v[26:27], v[8:9], 0, v[2:3]
	v_or_b32_e32 v2, s2, v46
	s_waitcnt lgkmcnt(0)
	v_cvt_pk_bf16_f32 v4, v12, v10
	v_lshlrev_b32_e32 v2, 11, v2
	v_cvt_pk_bf16_f32 v5, v14, v16
	v_cvt_pk_bf16_f32 v6, v18, v20
	v_cvt_pk_bf16_f32 v7, v22, v24
	global_store_dwordx4 v[26:27], v[4:7], off sc1 nt
	s_nop 1
	v_cvt_pk_bf16_f32 v4, v13, v11
	v_lshl_add_u64 v[10:11], v[8:9], 0, v[2:3]
	v_cvt_pk_bf16_f32 v5, v15, v17
	v_cvt_pk_bf16_f32 v6, v19, v21
	v_cvt_pk_bf16_f32 v7, v23, v25
	global_store_dwordx4 v[10:11], v[4:7], off sc1 nt
	ds_read2_b32 v[10:11], v50 offset0:16 offset1:24
	ds_read2_b32 v[12:13], v50 offset0:49 offset1:57
	ds_read2_b32 v[14:15], v50 offset0:82 offset1:90
	ds_read2_b32 v[16:17], v50 offset0:115 offset1:123
	ds_read2_b32 v[18:19], v50 offset0:148 offset1:156
	ds_read2_b32 v[20:21], v50 offset0:181 offset1:189
	ds_read2_b32 v[22:23], v50 offset0:214 offset1:222
	ds_read2_b32 v[24:25], v50 offset0:247 offset1:255
	v_or_b32_e32 v2, s2, v48
	v_lshlrev_b32_e32 v2, 11, v2
	v_lshl_add_u64 v[26:27], v[8:9], 0, v[2:3]
	v_or_b32_e32 v2, s2, v49
	v_lshlrev_b32_e32 v2, 11, v2
	s_waitcnt lgkmcnt(6)
	v_cvt_pk_bf16_f32 v4, v10, v12
	s_waitcnt lgkmcnt(4)
	v_cvt_pk_bf16_f32 v5, v14, v16
	s_waitcnt lgkmcnt(2)
	v_cvt_pk_bf16_f32 v6, v18, v20
	s_waitcnt lgkmcnt(0)
	v_cvt_pk_bf16_f32 v7, v22, v24
	v_lshl_add_u64 v[8:9], v[8:9], 0, v[2:3]
	global_store_dwordx4 v[26:27], v[4:7], off sc1 nt
	s_nop 1
	v_cvt_pk_bf16_f32 v4, v11, v13
	v_cvt_pk_bf16_f32 v5, v15, v17
	v_cvt_pk_bf16_f32 v6, v19, v21
	v_cvt_pk_bf16_f32 v7, v23, v25
	global_store_dwordx4 v[8:9], v[4:7], off sc1 nt
	s_waitcnt lgkmcnt(0)

; #define LAS __attribute__((address_space(3)))
; __device__ __forceinline__ void transpose_item(const float* W, int K, int N, bf16* WT, int drow0, int kb, int n0, LAS float* scr, int lane) {
;     const int k0 = 64 * kb; const int c4 = 4 * (lane & 7); const bool ok = (n0 + c4) < N;
;     f32x4 v[8];
; #pragma unroll
;     for (int i = 0; i < 8; ++i) { const int kk = 8 * i + (lane >> 3); v[i] = ok ? *(const f32x4*)(W + (size_t)(k0 + kk) * N + n0 + c4) : (f32x4){0.f, 0.f, 0.f, 0.f}; }
; __device__ __forceinline__ void convert_item(const In& I, unsigned char* ws, int it, LAS float* scr, int lane) {
;     ...
;     if (r < 2 * I_FIN) { const int j = r / I_FIN; r -= j * I_FIN; const int kb = r / 104, nb = r % 104;
;         transpose_item(I.fox_w_in + (size_t)j * D * FOX_IN, D, FOX_IN, Wfin + (size_t)j * FOX_IN_PAD * D, 32 * nb, kb, 32 * nb, scr, lane); return; }
.LBB0_368:
	s_andn2_b64 vcc, exec, s[2:3]
	s_cbranch_vccnz .LBB0_386
	s_add_i32 s6, s41, 0x1500
	s_cmpk_gt_u32 s6, 0x67f
	s_cselect_b64 s[10:11], -1, 0
	s_and_b64 s[2:3], s[10:11], exec
	s_cselect_b32 s2, 0xf980, 0
	s_cselect_b32 s3, 0xc10000, 0
	s_add_i32 s6, s6, s2
	s_sext_i32_i16 s2, s6
	s_mulk_i32 s2, 0x4ec5
	s_lshr_b32 s7, s2, 31
	s_ashr_i32 s2, s2, 21
	s_add_i32 s2, s2, s7
	s_mul_i32 s7, s2, 0x68
	v_readlane_b32 s48, v253, 16
	s_sub_i32 s6, s6, s7
	v_readlane_b32 s56, v253, 24
	s_sext_i32_i16 s6, s6
	v_readlane_b32 s57, v253, 25
	s_add_u32 s9, s56, s3
	s_addc_u32 s46, s57, 0
	s_lshl_b32 s6, s6, 5
	s_ashr_i32 s7, s6, 31
	s_lshl_b32 s8, s2, 6
	s_lshl_b64 s[12:13], s[6:7], 2
	v_or_b32_e32 v2, s6, v36
	s_movk_i32 s2, 0xc10
	v_or_b32_e32 v4, s8, v39
	s_add_u32 s12, s9, s12
	v_cmp_gt_i32_e64 s[2:3], s2, v2
	s_addc_u32 s13, s46, s13
	v_lshlrev_b32_e32 v2, 2, v36
	v_mul_i32_i24_e32 v42, 0x3040, v4
	v_lshl_add_u64 v[40:41], s[12:13], 0, v[2:3]
	v_mov_b32_e32 v8, 0
	v_ashrrev_i32_e32 v43, 31, v42
	v_mov_b32_e32 v4, 0
	v_mov_b32_e32 v5, 0
	v_mov_b32_e32 v6, 0
	v_mov_b32_e32 v7, 0
	v_readlane_b32 s49, v253, 17
	v_readlane_b32 s50, v253, 18
	v_readlane_b32 s51, v253, 19
	v_readlane_b32 s52, v253, 20
	v_readlane_b32 s53, v253, 21
	v_readlane_b32 s54, v253, 22
	v_readlane_b32 s55, v253, 23
	v_readlane_b32 s58, v253, 26
	v_readlane_b32 s59, v253, 27
	v_readlane_b32 s60, v253, 28
	v_readlane_b32 s61, v253, 29
	v_readlane_b32 s62, v253, 30
	v_readlane_b32 s63, v253, 31
	s_and_saveexec_b64 s[12:13], s[2:3]
	s_cbranch_execz .LBB0_371
	v_lshl_add_u64 v[4:5], v[40:41], 0, v[42:43]
	global_load_dwordx4 v[4:7], v[4:5], off nt
.LBB0_371:
	s_or_b64 exec, exec, s[12:13]
	v_mov_b32_e32 v9, 0
	v_mov_b32_e32 v10, 0
	v_mov_b32_e32 v11, 0
	s_and_saveexec_b64 s[12:13], s[2:3]
	s_cbranch_execz .LBB0_373
	v_lshl_add_u64 v[8:9], v[40:41], 0, v[42:43]
	v_add_co_u32_e32 v8, vcc, 0x18000, v8
	s_nop 1
	v_addc_co_u32_e32 v9, vcc, 0, v9, vcc
	global_load_dwordx4 v[8:11], v[8:9], off offset:512 nt

; #define GAS __attribute__((address_space(1)))
; #define LAS __attribute__((address_space(3)))
; #define LDS_WAIT() asm volatile("s_waitcnt lgkmcnt(0)" ::: "memory")
; __device__ __forceinline__ unsigned pk2(float lo, float hi) { unsigned r; asm("v_cvt_pk_bf16_f32 %0, %1, %2" : "=v"(r) : "v"(lo), "v"(hi)); return r; }
; __device__ __forceinline__ void transpose_item(const float* W, int K, int N, bf16* WT, int drow0, int kb, int n0, LAS float* scr, int lane) {
;     ...
;     for (int i = 0; i < 8; ++i) { const int kk = 8 * i + (lane >> 3); v[i] = ok ? *(const f32x4*)(W + (size_t)(k0 + kk) * N + n0 + c4) : (f32x4){0.f, 0.f, 0.f, 0.f}; }
; #pragma unroll
;     for (int i = 0; i < 8; ++i) { const int kk = 8 * i + (lane >> 3); LAS float* d = scr + kk * 33 + c4; d[0] = v[i][0]; d[1] = v[i][1]; d[2] = v[i][2]; d[3] = v[i][3]; }
;     LDS_WAIT(); asm volatile("" ::: "memory");
;     const int c = lane & 7;
; #pragma unroll
;     for (int j = 0; j < 4; ++j) { const int n = (lane >> 3) + 8 * j; const LAS float* s = scr + (8 * c) * 33 + n;
;         v4u o; o.x = pk2(s[0 * 33], s[1 * 33]); o.y = pk2(s[2 * 33], s[3 * 33]); o.z = pk2(s[4 * 33], s[5 * 33]); o.w = pk2(s[6 * 33], s[7 * 33]);
;         *(GAS v4u*)(WT + (size_t)(drow0 + n) * K + k0 + 8 * c) = o; }
;     LDS_WAIT(); asm volatile("" ::: "memory");
; }
.LBB0_385:
	s_or_b64 exec, exec, s[12:13]
	v_add_u32_e32 v2, v44, v47
	s_waitcnt vmcnt(0)
	ds_write2_b32 v45, v4, v5 offset1:1
	ds_write2_b32 v45, v6, v7 offset0:2 offset1:3
	v_add_u32_e32 v4, 0x420, v2
	ds_write2_b32 v2, v8, v9 offset1:1
	ds_write2_b32 v2, v10, v11 offset0:2 offset1:3
	ds_write2_b32 v4, v16, v17 offset1:1
	v_add_u32_e32 v4, 0x428, v2
	ds_write2_b32 v4, v18, v19 offset1:1
	v_add_u32_e32 v4, 0x840, v2
	v_add_u32_e32 v2, 0x848, v2
	ds_write2_b32 v2, v14, v15 offset1:1
	v_add_u32_e32 v2, 0x1080, v45
	ds_write2_b32 v2, v24, v25 offset1:1
	v_add_u32_e32 v2, 0x1088, v45
	ds_write2_b32 v2, v26, v27 offset1:1
	v_add_u32_e32 v2, 0x14a0, v45
	ds_write2_b32 v2, v20, v21 offset1:1
	v_add_u32_e32 v2, 0x14a8, v45
	ds_write2_b32 v2, v22, v23 offset1:1
	v_add_u32_e32 v2, 0x18c0, v45
	ds_write2_b32 v2, v32, v33 offset1:1
	v_add_u32_e32 v2, 0x18c8, v45
	ds_write2_b32 v2, v34, v35 offset1:1
	v_add_u32_e32 v2, 0x1ce0, v45
	s_and_b64 s[2:3], s[10:11], exec
	ds_write2_b32 v2, v28, v29 offset1:1
	v_add_u32_e32 v2, 0x1ce8, v45
	s_cselect_b32 s2, 0x680000, 0
	ds_write2_b32 v4, v12, v13 offset1:1
	ds_write2_b32 v2, v30, v31 offset1:1
	s_add_u32 s7, s24, s2
	s_waitcnt lgkmcnt(0)
	s_addc_u32 s10, s25, 0
	s_ashr_i32 s9, s8, 31
	s_lshl_b64 s[2:3], s[8:9], 1
	ds_read2_b32 v[8:9], v50 offset0:33 offset1:41
	ds_read2_b32 v[10:11], v50 offset1:8
	ds_read2_b32 v[12:13], v50 offset0:66 offset1:74
	ds_read2_b32 v[14:15], v50 offset0:99 offset1:107
	ds_read2_b32 v[16:17], v50 offset0:132 offset1:140
	ds_read2_b32 v[18:19], v50 offset0:165 offset1:173
	ds_read2_b32 v[20:21], v50 offset0:198 offset1:206
	ds_read2_b32 v[22:23], v50 offset0:231 offset1:239
	s_add_u32 s2, s7, s2
	v_or_b32_e32 v26, s6, v39
	s_addc_u32 s3, s10, s3
	v_lshlrev_b32_e32 v2, 1, v38
	v_ashrrev_i32_e32 v27, 31, v26
	v_lshl_add_u64 v[24:25], s[2:3], 0, v[2:3]
	v_lshlrev_b64 v[26:27], 11, v[26:27]
	s_waitcnt lgkmcnt(0)
	v_cvt_pk_bf16_f32 v4, v10, v8
	v_lshl_add_u64 v[26:27], v[24:25], 0, v[26:27]
	v_or_b32_e32 v8, s6, v46
	v_cvt_pk_bf16_f32 v5, v12, v14
	v_cvt_pk_bf16_f32 v6, v16, v18
	v_cvt_pk_bf16_f32 v7, v20, v22
	global_store_dwordx4 v[26:27], v[4:7], off sc1 nt
	s_nop 1
	v_cvt_pk_bf16_f32 v4, v11, v9
	v_ashrrev_i32_e32 v9, 31, v8
	v_lshlrev_b64 v[8:9], 11, v[8:9]
	v_cvt_pk_bf16_f32 v5, v13, v15
	v_cvt_pk_bf16_f32 v6, v17, v19
	v_cvt_pk_bf16_f32 v7, v21, v23
	v_lshl_add_u64 v[8:9], v[24:25], 0, v[8:9]
	ds_read2_b32 v[10:11], v50 offset0:16 offset1:24
	ds_read2_b32 v[12:13], v50 offset0:49 offset1:57
	ds_read2_b32 v[14:15], v50 offset0:82 offset1:90
	ds_read2_b32 v[16:17], v50 offset0:115 offset1:123
	ds_read2_b32 v[18:19], v50 offset0:148 offset1:156
	ds_read2_b32 v[20:21], v50 offset0:181 offset1:189
	ds_read2_b32 v[22:23], v50 offset0:214 offset1:222
	ds_read2_b32 v[26:27], v50 offset0:247 offset1:255
	global_store_dwordx4 v[8:9], v[4:7], off sc1 nt
	v_or_b32_e32 v8, s6, v48
	v_ashrrev_i32_e32 v9, 31, v8
	v_lshlrev_b64 v[8:9], 11, v[8:9]
	v_lshl_add_u64 v[8:9], v[24:25], 0, v[8:9]
	s_waitcnt lgkmcnt(6)
	v_cvt_pk_bf16_f32 v4, v10, v12
	s_waitcnt lgkmcnt(4)
	v_cvt_pk_bf16_f32 v5, v14, v16
	s_waitcnt lgkmcnt(2)
	v_cvt_pk_bf16_f32 v6, v18, v20
	s_waitcnt lgkmcnt(0)
	v_cvt_pk_bf16_f32 v7, v22, v26
	global_store_dwordx4 v[8:9], v[4:7], off sc1 nt
	v_or_b32_e32 v8, s6, v49
	v_ashrrev_i32_e32 v9, 31, v8
	v_lshlrev_b64 v[8:9], 11, v[8:9]
	v_lshl_add_u64 v[8:9], v[24:25], 0, v[8:9]
	v_cvt_pk_bf16_f32 v4, v11, v13
	v_cvt_pk_bf16_f32 v5, v15, v17
	v_cvt_pk_bf16_f32 v6, v19, v21
	v_cvt_pk_bf16_f32 v7, v23, v27
	global_store_dwordx4 v[8:9], v[4:7], off sc1 nt
	s_waitcnt lgkmcnt(0)

; #define GAS __attribute__((address_space(1)))
; #define LAS __attribute__((address_space(3)))
; #define LDS_WAIT() asm volatile("s_waitcnt lgkmcnt(0)" ::: "memory")
; __device__ __forceinline__ unsigned pk2(float lo, float hi) { unsigned r; asm("v_cvt_pk_bf16_f32 %0, %1, %2" : "=v"(r) : "v"(lo), "v"(hi)); return r; }
; __device__ __forceinline__ void transpose_item(const float* W, int K, int N, bf16* WT, int drow0, int kb, int n0, LAS float* scr, int lane) {
;     const int k0 = 64 * kb; const int c4 = 4 * (lane & 7); const bool ok = (n0 + c4) < N;
;     f32x4 v[8];
; #pragma unroll
;     for (int i = 0; i < 8; ++i) { const int kk = 8 * i + (lane >> 3); v[i] = ok ? *(const f32x4*)(W + (size_t)(k0 + kk) * N + n0 + c4) : (f32x4){0.f, 0.f, 0.f, 0.f}; }
; #pragma unroll
;     for (int i = 0; i < 8; ++i) { const int kk = 8 * i + (lane >> 3); LAS float* d = scr + kk * 33 + c4; d[0] = v[i][0]; d[1] = v[i][1]; d[2] = v[i][2]; d[3] = v[i][3]; }
;     LDS_WAIT(); asm volatile("" ::: "memory");
;     const int c = lane & 7;
; #pragma unroll
;     for (int j = 0; j < 4; ++j) { const int n = (lane >> 3) + 8 * j; const LAS float* s = scr + (8 * c) * 33 + n;
;         v4u o; o.x = pk2(s[0 * 33], s[1 * 33]); o.y = pk2(s[2 * 33], s[3 * 33]); o.z = pk2(s[4 * 33], s[5 * 33]); o.w = pk2(s[6 * 33], s[7 * 33]);
;         *(GAS v4u*)(WT + (size_t)(drow0 + n) * K + k0 + 8 * c) = o; }
;     LDS_WAIT(); asm volatile("" ::: "memory");
; }
; __device__ __forceinline__ void convert_item(const In& I, unsigned char* ws, int it, LAS float* scr, int lane) {
;     ...
;     if (r < 2 * I_SQ) { const int j = r / I_SQ; r -= j * I_SQ; const int kb = r / 32, nb = r % 32;
;         transpose_item(I.nsa_w_out + (size_t)j * D * D, D, D, Wnout + (size_t)j * D * D, 32 * nb, kb, 32 * nb, scr, lane); return; }
.LBB0_387:
	s_andn2_b64 vcc, exec, s[2:3]
	s_cbranch_vccnz .LBB0_389
	s_add_i32 s2, s41, 0x1900
	s_lshr_b32 s68, s2, 9
	v_readlane_b32 s48, v253, 16
	s_lshl_b64 s[2:3], s[68:69], 22
	v_readlane_b32 s54, v253, 22
	v_readlane_b32 s55, v253, 23
	s_add_u32 s8, s54, s2
	s_addc_u32 s9, s55, s3
	s_lshl_b64 s[6:7], s[68:69], 21
	s_add_u32 s3, s22, s6
	s_addc_u32 s6, s23, s7
	s_and_b32 s2, s43, 0x3e0
	s_add_i32 s7, s44, 0xfffff800
	s_and_b32 s7, s7, 0x3c0
	s_lshl_b32 s10, s2, 2
	s_add_u32 s8, s8, s10
	v_or_b32_e32 v6, s7, v39
	s_addc_u32 s9, s9, 0
	v_lshlrev_b32_e32 v2, 2, v36
	v_lshl_add_u64 v[4:5], s[8:9], 0, v[2:3]
	v_lshlrev_b32_e32 v2, 12, v6
	v_lshl_add_u64 v[32:33], v[4:5], 0, v[2:3]
	v_add_co_u32_e32 v8, vcc, s81, v32
	global_load_dwordx4 v[4:7], v[32:33], off nt
	s_nop 0
	v_addc_co_u32_e32 v9, vcc, 0, v33, vcc
	v_add_co_u32_e32 v12, vcc, s79, v32
	global_load_dwordx4 v[8:11], v[8:9], off nt
	s_nop 0
	v_addc_co_u32_e32 v13, vcc, 0, v33, vcc
	v_add_co_u32_e32 v16, vcc, s80, v32
	global_load_dwordx4 v[12:15], v[12:13], off nt
	s_nop 0
	v_addc_co_u32_e32 v17, vcc, 0, v33, vcc
	v_add_co_u32_e32 v20, vcc, s85, v32
	global_load_dwordx4 v[16:19], v[16:17], off nt
	s_nop 0
	v_addc_co_u32_e32 v21, vcc, 0, v33, vcc
	global_load_dwordx4 v[20:23], v[20:21], off nt
	v_add_co_u32_e32 v24, vcc, s86, v32
	v_add_u32_e32 v2, v44, v47
	s_nop 0
	v_addc_co_u32_e32 v25, vcc, 0, v33, vcc
	global_load_dwordx4 v[24:27], v[24:25], off nt
	v_add_co_u32_e32 v28, vcc, s87, v32
	s_lshl_b32 s7, s7, 1
	s_nop 0
	v_addc_co_u32_e32 v29, vcc, 0, v33, vcc
	global_load_dwordx4 v[28:31], v[28:29], off nt
	v_add_co_u32_e32 v32, vcc, s89, v32
	s_add_u32 s8, s3, s7
	s_nop 0
	v_addc_co_u32_e32 v33, vcc, 0, v33, vcc
	global_load_dwordx4 v[32:35], v[32:33], off nt
	s_addc_u32 s9, s6, 0
	v_readlane_b32 s49, v253, 17
	v_readlane_b32 s50, v253, 18
	v_readlane_b32 s51, v253, 19
	v_readlane_b32 s52, v253, 20
	v_readlane_b32 s53, v253, 21
	v_readlane_b32 s56, v253, 24
	v_readlane_b32 s57, v253, 25
	v_readlane_b32 s58, v253, 26
	v_readlane_b32 s59, v253, 27
	v_readlane_b32 s60, v253, 28
	v_readlane_b32 s61, v253, 29
	v_readlane_b32 s62, v253, 30
	v_readlane_b32 s63, v253, 31
	s_waitcnt vmcnt(0)
	ds_write2_b32 v45, v4, v5 offset1:1
	ds_write2_b32 v45, v6, v7 offset0:2 offset1:3
	v_add_u32_e32 v4, 0x420, v2
	ds_write2_b32 v2, v8, v9 offset1:1
	ds_write2_b32 v2, v10, v11 offset0:2 offset1:3
	ds_write2_b32 v4, v12, v13 offset1:1
	v_add_u32_e32 v4, 0x428, v2
	ds_write2_b32 v4, v14, v15 offset1:1
	v_add_u32_e32 v4, 0x840, v2
	v_add_u32_e32 v2, 0x848, v2
	ds_write2_b32 v2, v18, v19 offset1:1
	v_add_u32_e32 v2, 0x1080, v45
	ds_write2_b32 v4, v16, v17 offset1:1
	ds_write2_b32 v2, v20, v21 offset1:1
	v_add_u32_e32 v2, 0x1088, v45
	ds_write2_b32 v2, v22, v23 offset1:1
	v_add_u32_e32 v2, 0x14a0, v45
	ds_write2_b32 v2, v24, v25 offset1:1
	v_add_u32_e32 v2, 0x14a8, v45
	ds_write2_b32 v2, v26, v27 offset1:1
	v_add_u32_e32 v2, 0x18c0, v45
	ds_write2_b32 v2, v28, v29 offset1:1
	v_add_u32_e32 v2, 0x18c8, v45
	ds_write2_b32 v2, v30, v31 offset1:1
	v_add_u32_e32 v2, 0x1ce0, v45
	ds_write2_b32 v2, v32, v33 offset1:1
	v_add_u32_e32 v2, 0x1ce8, v45
	ds_write2_b32 v2, v34, v35 offset1:1
	s_waitcnt lgkmcnt(0)
	ds_read2_b32 v[10:11], v50 offset0:33 offset1:41
	ds_read2_b32 v[12:13], v50 offset1:8
	v_lshlrev_b32_e32 v2, 1, v38
	ds_read2_b32 v[14:15], v50 offset0:66 offset1:74
	ds_read2_b32 v[16:17], v50 offset0:99 offset1:107
	ds_read2_b32 v[18:19], v50 offset0:132 offset1:140
	ds_read2_b32 v[20:21], v50 offset0:165 offset1:173
	ds_read2_b32 v[22:23], v50 offset0:198 offset1:206
	ds_read2_b32 v[24:25], v50 offset0:231 offset1:239
	v_lshl_add_u64 v[8:9], s[8:9], 0, v[2:3]
	v_or_b32_e32 v2, s2, v39
	v_lshlrev_b32_e32 v2, 11, v2
	v_lshl_add_u64 v[26:27], v[8:9], 0, v[2:3]
	v_or_b32_e32 v2, s2, v46
	s_waitcnt lgkmcnt(0)
	v_cvt_pk_bf16_f32 v4, v12, v10
	v_lshlrev_b32_e32 v2, 11, v2
	v_cvt_pk_bf16_f32 v5, v14, v16
	v_cvt_pk_bf16_f32 v6, v18, v20
	v_cvt_pk_bf16_f32 v7, v22, v24
	global_store_dwordx4 v[26:27], v[4:7], off sc1 nt
	s_nop 1
	v_cvt_pk_bf16_f32 v4, v13, v11
	v_lshl_add_u64 v[10:11], v[8:9], 0, v[2:3]
	v_cvt_pk_bf16_f32 v5, v15, v17
	v_cvt_pk_bf16_f32 v6, v19, v21
	v_cvt_pk_bf16_f32 v7, v23, v25
	global_store_dwordx4 v[10:11], v[4:7], off sc1 nt
	ds_read2_b32 v[10:11], v50 offset0:16 offset1:24
	ds_read2_b32 v[12:13], v50 offset0:49 offset1:57
	ds_read2_b32 v[14:15], v50 offset0:82 offset1:90
	ds_read2_b32 v[16:17], v50 offset0:115 offset1:123
	ds_read2_b32 v[18:19], v50 offset0:148 offset1:156
	ds_read2_b32 v[20:21], v50 offset0:181 offset1:189
	ds_read2_b32 v[22:23], v50 offset0:214 offset1:222
	ds_read2_b32 v[24:25], v50 offset0:247 offset1:255
	v_or_b32_e32 v2, s2, v48
	v_lshlrev_b32_e32 v2, 11, v2
	v_lshl_add_u64 v[26:27], v[8:9], 0, v[2:3]
	v_or_b32_e32 v2, s2, v49
	v_lshlrev_b32_e32 v2, 11, v2
	s_waitcnt lgkmcnt(6)
	v_cvt_pk_bf16_f32 v4, v10, v12
	s_waitcnt lgkmcnt(4)
	v_cvt_pk_bf16_f32 v5, v14, v16
	s_waitcnt lgkmcnt(2)
	v_cvt_pk_bf16_f32 v6, v18, v20
	s_waitcnt lgkmcnt(0)
	v_cvt_pk_bf16_f32 v7, v22, v24
	v_lshl_add_u64 v[8:9], v[8:9], 0, v[2:3]
	global_store_dwordx4 v[26:27], v[4:7], off sc1 nt
	s_nop 1
	v_cvt_pk_bf16_f32 v4, v11, v13
	v_cvt_pk_bf16_f32 v5, v15, v17
	v_cvt_pk_bf16_f32 v6, v19, v21
	v_cvt_pk_bf16_f32 v7, v23, v25
	global_store_dwordx4 v[8:9], v[4:7], off sc1 nt
	s_waitcnt lgkmcnt(0)

; #define LAS __attribute__((address_space(3)))
; __device__ __forceinline__ void transpose_item(const float* W, int K, int N, bf16* WT, int drow0, int kb, int n0, LAS float* scr, int lane) {
;     const int k0 = 64 * kb; const int c4 = 4 * (lane & 7); const bool ok = (n0 + c4) < N;
;     f32x4 v[8];
; #pragma unroll
;     for (int i = 0; i < 8; ++i) { const int kk = 8 * i + (lane >> 3); v[i] = ok ? *(const f32x4*)(W + (size_t)(k0 + kk) * N + n0 + c4) : (f32x4){0.f, 0.f, 0.f, 0.f}; }
; __device__ __forceinline__ void convert_item(const In& I, unsigned char* ws, int it, LAS float* scr, int lane) {
;     ...
;     if (r < 2 * I_NIN) { const int j = r / I_NIN; r -= j * I_NIN; const int kb = r / 88, nb = r % 88;
;         transpose_item(I.nsa_w_in + (size_t)j * D * NSA_IN, D, NSA_IN, Wnin + (size_t)j * NSA_IN_PAD * D, 32 * nb, kb, 32 * nb, scr, lane); return; }
.LBB0_390:
	s_andn2_b64 vcc, exec, s[2:3]
	s_cbranch_vccnz .LBB0_408
	s_add_i32 s6, s41, 0x2400
	s_cmpk_gt_u32 s6, 0x57f
	s_cselect_b64 s[10:11], -1, 0
	s_and_b64 s[2:3], s[10:11], exec
	s_cselect_b32 s2, 0xfa80, 0
	s_cselect_b32 s3, 0xa30000, 0
	s_add_i32 s6, s6, s2
	s_sext_i32_i16 s2, s6
	s_mulk_i32 s2, 0xba3
	s_lshr_b32 s7, s2, 31
	s_ashr_i32 s2, s2, 18
	v_readlane_b32 s48, v253, 0
	s_add_i32 s2, s2, s7
	v_readlane_b32 s49, v253, 1
	v_readlane_b32 s50, v253, 2
	v_readlane_b32 s51, v253, 3
	v_readlane_b32 s52, v253, 4
	v_readlane_b32 s53, v253, 5
	s_mul_i32 s7, s2, 0x58
	v_readlane_b32 s54, v253, 6
	v_readlane_b32 s55, v253, 7
	v_readlane_b32 s56, v253, 8
	v_readlane_b32 s57, v253, 9
	v_readlane_b32 s60, v253, 12
	v_readlane_b32 s61, v253, 13
	s_mov_b64 s[48:49], s[52:53]
	s_sub_i32 s6, s6, s7
	s_mov_b64 s[50:51], s[54:55]
	s_mov_b64 s[52:53], s[56:57]
	s_mov_b64 s[56:57], s[60:61]
	s_sext_i32_i16 s6, s6
	s_add_u32 s9, s56, s3
	s_addc_u32 s46, s57, 0
	s_lshl_b32 s6, s6, 5
	s_ashr_i32 s7, s6, 31
	s_lshl_b32 s8, s2, 6
	s_lshl_b64 s[12:13], s[6:7], 2
	v_or_b32_e32 v2, s6, v36
	s_movk_i32 s2, 0xa30
	s_add_u32 s12, s9, s12
	v_cmp_gt_i32_e64 s[2:3], s2, v2
	s_addc_u32 s13, s46, s13
	v_lshlrev_b32_e32 v2, 2, v36
	v_or_b32_e32 v42, s8, v39
	v_lshl_add_u64 v[40:41], s[12:13], 0, v[2:3]
	v_mov_b32_e32 v8, 0
	v_mov_b32_e32 v4, 0
	v_mov_b32_e32 v5, 0
	v_mov_b32_e32 v6, 0
	v_mov_b32_e32 v7, 0
	v_readlane_b32 s58, v253, 10
	v_readlane_b32 s59, v253, 11
	v_readlane_b32 s62, v253, 14
	v_readlane_b32 s63, v253, 15
	s_and_saveexec_b64 s[12:13], s[2:3]
	s_cbranch_execz .LBB0_393
	v_mul_i32_i24_e32 v4, 0x28c0, v42
	v_ashrrev_i32_e32 v5, 31, v4
	v_lshl_add_u64 v[4:5], v[40:41], 0, v[4:5]
	global_load_dwordx4 v[4:7], v[4:5], off nt

; #define GAS __attribute__((address_space(1)))
; #define LAS __attribute__((address_space(3)))
; #define LDS_WAIT() asm volatile("s_waitcnt lgkmcnt(0)" ::: "memory")
; __device__ __forceinline__ unsigned pk2(float lo, float hi) { unsigned r; asm("v_cvt_pk_bf16_f32 %0, %1, %2" : "=v"(r) : "v"(lo), "v"(hi)); return r; }
; __device__ __forceinline__ void transpose_item(const float* W, int K, int N, bf16* WT, int drow0, int kb, int n0, LAS float* scr, int lane) {
;     ...
;     for (int i = 0; i < 8; ++i) { const int kk = 8 * i + (lane >> 3); v[i] = ok ? *(const f32x4*)(W + (size_t)(k0 + kk) * N + n0 + c4) : (f32x4){0.f, 0.f, 0.f, 0.f}; }
; #pragma unroll
;     for (int i = 0; i < 8; ++i) { const int kk = 8 * i + (lane >> 3); LAS float* d = scr + kk * 33 + c4; d[0] = v[i][0]; d[1] = v[i][1]; d[2] = v[i][2]; d[3] = v[i][3]; }
;     LDS_WAIT(); asm volatile("" ::: "memory");
;     const int c = lane & 7;
; #pragma unroll
;     for (int j = 0; j < 4; ++j) { const int n = (lane >> 3) + 8 * j; const LAS float* s = scr + (8 * c) * 33 + n;
;         v4u o; o.x = pk2(s[0 * 33], s[1 * 33]); o.y = pk2(s[2 * 33], s[3 * 33]); o.z = pk2(s[4 * 33], s[5 * 33]); o.w = pk2(s[6 * 33], s[7 * 33]);
;         *(GAS v4u*)(WT + (size_t)(drow0 + n) * K + k0 + 8 * c) = o; }
;     LDS_WAIT(); asm volatile("" ::: "memory");
; }
.LBB0_407:
	s_or_b64 exec, exec, s[12:13]
	v_add_u32_e32 v2, v44, v47
	s_waitcnt vmcnt(0)
	ds_write2_b32 v45, v4, v5 offset1:1
	ds_write2_b32 v45, v6, v7 offset0:2 offset1:3
	v_add_u32_e32 v4, 0x420, v2
	ds_write2_b32 v2, v8, v9 offset1:1
	ds_write2_b32 v2, v10, v11 offset0:2 offset1:3
	ds_write2_b32 v4, v16, v17 offset1:1
	v_add_u32_e32 v4, 0x428, v2
	ds_write2_b32 v4, v18, v19 offset1:1
	v_add_u32_e32 v4, 0x840, v2
	v_add_u32_e32 v2, 0x848, v2
	ds_write2_b32 v2, v14, v15 offset1:1
	v_add_u32_e32 v2, 0x1080, v45
	ds_write2_b32 v2, v24, v25 offset1:1
	v_add_u32_e32 v2, 0x1088, v45
	ds_write2_b32 v2, v26, v27 offset1:1
	v_add_u32_e32 v2, 0x14a0, v45
	ds_write2_b32 v2, v20, v21 offset1:1
	v_add_u32_e32 v2, 0x14a8, v45
	ds_write2_b32 v2, v22, v23 offset1:1
	v_add_u32_e32 v2, 0x18c0, v45
	ds_write2_b32 v2, v32, v33 offset1:1
	v_add_u32_e32 v2, 0x18c8, v45
	ds_write2_b32 v2, v34, v35 offset1:1
	v_add_u32_e32 v2, 0x1ce0, v45
	s_and_b64 s[2:3], s[10:11], exec
	ds_write2_b32 v2, v28, v29 offset1:1
	v_add_u32_e32 v2, 0x1ce8, v45
	s_cselect_b32 s2, 0x580000, 0
	ds_write2_b32 v4, v12, v13 offset1:1
	ds_write2_b32 v2, v30, v31 offset1:1
	s_add_u32 s7, s20, s2
	s_waitcnt lgkmcnt(0)
	s_addc_u32 s10, s21, 0
	s_ashr_i32 s9, s8, 31
	s_lshl_b64 s[2:3], s[8:9], 1
	ds_read2_b32 v[8:9], v50 offset0:33 offset1:41
	ds_read2_b32 v[10:11], v50 offset1:8
	ds_read2_b32 v[12:13], v50 offset0:66 offset1:74
	ds_read2_b32 v[14:15], v50 offset0:99 offset1:107
	ds_read2_b32 v[16:17], v50 offset0:132 offset1:140
	ds_read2_b32 v[18:19], v50 offset0:165 offset1:173
	ds_read2_b32 v[20:21], v50 offset0:198 offset1:206
	ds_read2_b32 v[22:23], v50 offset0:231 offset1:239
	s_add_u32 s2, s7, s2
	v_or_b32_e32 v26, s6, v39
	s_addc_u32 s3, s10, s3
	v_lshlrev_b32_e32 v2, 1, v38
	v_ashrrev_i32_e32 v27, 31, v26
	v_lshl_add_u64 v[24:25], s[2:3], 0, v[2:3]
	v_lshlrev_b64 v[26:27], 11, v[26:27]
	s_waitcnt lgkmcnt(0)
	v_cvt_pk_bf16_f32 v4, v10, v8
	v_lshl_add_u64 v[26:27], v[24:25], 0, v[26:27]
	v_or_b32_e32 v8, s6, v46
	v_cvt_pk_bf16_f32 v5, v12, v14
	v_cvt_pk_bf16_f32 v6, v16, v18
	v_cvt_pk_bf16_f32 v7, v20, v22
	global_store_dwordx4 v[26:27], v[4:7], off sc1 nt
	s_nop 1
	v_cvt_pk_bf16_f32 v4, v11, v9
	v_ashrrev_i32_e32 v9, 31, v8
	v_lshlrev_b64 v[8:9], 11, v[8:9]
	v_cvt_pk_bf16_f32 v5, v13, v15
	v_cvt_pk_bf16_f32 v6, v17, v19
	v_cvt_pk_bf16_f32 v7, v21, v23
	v_lshl_add_u64 v[8:9], v[24:25], 0, v[8:9]
	ds_read2_b32 v[10:11], v50 offset0:16 offset1:24
	ds_read2_b32 v[12:13], v50 offset0:49 offset1:57
	ds_read2_b32 v[14:15], v50 offset0:82 offset1:90
	ds_read2_b32 v[16:17], v50 offset0:115 offset1:123
	ds_read2_b32 v[18:19], v50 offset0:148 offset1:156
	ds_read2_b32 v[20:21], v50 offset0:181 offset1:189
	ds_read2_b32 v[22:23], v50 offset0:214 offset1:222
	ds_read2_b32 v[26:27], v50 offset0:247 offset1:255
	global_store_dwordx4 v[8:9], v[4:7], off sc1 nt
	v_or_b32_e32 v8, s6, v48
	v_ashrrev_i32_e32 v9, 31, v8
	v_lshlrev_b64 v[8:9], 11, v[8:9]
	v_lshl_add_u64 v[8:9], v[24:25], 0, v[8:9]
	s_waitcnt lgkmcnt(6)
	v_cvt_pk_bf16_f32 v4, v10, v12
	s_waitcnt lgkmcnt(4)
	v_cvt_pk_bf16_f32 v5, v14, v16
	s_waitcnt lgkmcnt(2)
	v_cvt_pk_bf16_f32 v6, v18, v20
	s_waitcnt lgkmcnt(0)
	v_cvt_pk_bf16_f32 v7, v22, v26
	global_store_dwordx4 v[8:9], v[4:7], off sc1 nt
	v_or_b32_e32 v8, s6, v49
	v_ashrrev_i32_e32 v9, 31, v8
	v_lshlrev_b64 v[8:9], 11, v[8:9]
	v_lshl_add_u64 v[8:9], v[24:25], 0, v[8:9]
	v_cvt_pk_bf16_f32 v4, v11, v13
	v_cvt_pk_bf16_f32 v5, v15, v17
	v_cvt_pk_bf16_f32 v6, v19, v21
	v_cvt_pk_bf16_f32 v7, v23, v27
	global_store_dwordx4 v[8:9], v[4:7], off sc1 nt
	s_waitcnt lgkmcnt(0)

; #define GAS __attribute__((address_space(1)))
; #define LAS __attribute__((address_space(3)))
; #define LDS_WAIT() asm volatile("s_waitcnt lgkmcnt(0)" ::: "memory")
; __device__ __forceinline__ unsigned pk2(float lo, float hi) { unsigned r; asm("v_cvt_pk_bf16_f32 %0, %1, %2" : "=v"(r) : "v"(lo), "v"(hi)); return r; }
; __device__ __forceinline__ void transpose_item(const float* W, int K, int N, bf16* WT, int drow0, int kb, int n0, LAS float* scr, int lane) {
;     const int k0 = 64 * kb; const int c4 = 4 * (lane & 7); const bool ok = (n0 + c4) < N;
;     f32x4 v[8];
; #pragma unroll
;     for (int i = 0; i < 8; ++i) { const int kk = 8 * i + (lane >> 3); v[i] = ok ? *(const f32x4*)(W + (size_t)(k0 + kk) * N + n0 + c4) : (f32x4){0.f, 0.f, 0.f, 0.f}; }
; #pragma unroll
;     for (int i = 0; i < 8; ++i) { const int kk = 8 * i + (lane >> 3); LAS float* d = scr + kk * 33 + c4; d[0] = v[i][0]; d[1] = v[i][1]; d[2] = v[i][2]; d[3] = v[i][3]; }
;     LDS_WAIT(); asm volatile("" ::: "memory");
;     const int c = lane & 7;
; #pragma unroll
;     for (int j = 0; j < 4; ++j) { const int n = (lane >> 3) + 8 * j; const LAS float* s = scr + (8 * c) * 33 + n;
;         v4u o; o.x = pk2(s[0 * 33], s[1 * 33]); o.y = pk2(s[2 * 33], s[3 * 33]); o.z = pk2(s[4 * 33], s[5 * 33]); o.w = pk2(s[6 * 33], s[7 * 33]);
;         *(GAS v4u*)(WT + (size_t)(drow0 + n) * K + k0 + 8 * c) = o; }
;     LDS_WAIT(); asm volatile("" ::: "memory");
; }
; __device__ __forceinline__ void convert_item(const In& I, unsigned char* ws, int it, LAS float* scr, int lane) {
;     ...
;     if (r < T0) { const int f = r / I_FFN; r -= f * I_FFN;
;     ...
;         else { r -= 2 * I_G; const int kb = r / 32, nb = r % 32; transpose_item(I.w_down + (size_t)f * FF * D, FF, D, Wd + (size_t)f * D * FF, 32 * nb, kb, 32 * nb, scr, lane); }
.LBB0_409:
	s_andn2_b64 vcc, exec, s[2:3]
	s_cbranch_vccnz .LBB0_354
	s_mul_hi_i32 s2, s45, 0x3e0f83e1
	s_lshr_b32 s3, s2, 31
	s_ashr_i32 s6, s2, 10
	s_add_i32 s6, s6, s3
	s_mul_i32 s2, s6, 0xffffef80
	s_add_i32 s7, s41, s2
	s_add_i32 s7, s7, 0xa800
	s_cmpk_gt_i32 s7, 0xaff
	s_mov_b64 s[2:3], -1
	s_cbranch_scc0 .LBB0_412
	v_readlane_b32 s48, v253, 0
	v_readlane_b32 s49, v253, 1
	v_readlane_b32 s50, v253, 2
	v_readlane_b32 s51, v253, 3
	v_readlane_b32 s52, v253, 4
	v_readlane_b32 s53, v253, 5
	v_readlane_b32 s54, v253, 6
	v_readlane_b32 s55, v253, 7
	v_readlane_b32 s56, v253, 8
	v_readlane_b32 s57, v253, 9
	s_mov_b64 s[48:49], s[52:53]
	s_mul_i32 s3, s6, 0xb00000
	s_mov_b64 s[50:51], s[54:55]
	s_mov_b64 s[52:53], s[56:57]
	s_mul_hi_i32 s2, s6, 0xb00000
	s_add_u32 s9, s52, s3
	s_addc_u32 s11, s53, s2
	s_mul_i32 s3, s6, 0x580000
	s_mul_hi_i32 s2, s6, 0x580000
	s_add_u32 s3, s1, s3
	s_mul_i32 s10, s6, 0xffffdf00
	s_addc_u32 s8, s19, s2
	s_add_i32 s10, s44, s10
	s_add_i32 s10, s10, 0x11600
	s_and_b32 s2, s43, 0x3e0
	s_andn2_b32 s10, s10, 63
	s_add_i32 s68, s10, 0xffffea00
	s_lshl_b32 s10, s2, 2
	v_or_b32_e32 v32, s68, v39
	s_add_u32 s10, s9, s10
	s_addc_u32 s11, s11, 0
	v_lshlrev_b32_e32 v2, 2, v36
	v_ashrrev_i32_e32 v33, 31, v32
	v_or_b32_e32 v8, 8, v32
	v_or_b32_e32 v12, 16, v32
	v_lshl_add_u64 v[34:35], s[10:11], 0, v[2:3]
	v_lshlrev_b64 v[4:5], 12, v[32:33]
	v_ashrrev_i32_e32 v9, 31, v8
	v_ashrrev_i32_e32 v13, 31, v12
	v_lshl_add_u64 v[4:5], v[34:35], 0, v[4:5]
	v_lshlrev_b64 v[8:9], 12, v[8:9]
	v_lshlrev_b64 v[12:13], 12, v[12:13]
	v_or_b32_e32 v16, 24, v32
	global_load_dwordx4 v[4:7], v[4:5], off nt
	v_lshl_add_u64 v[8:9], v[34:35], 0, v[8:9]
	v_lshl_add_u64 v[12:13], v[34:35], 0, v[12:13]
	v_ashrrev_i32_e32 v17, 31, v16
	v_or_b32_e32 v20, 32, v32
	global_load_dwordx4 v[8:11], v[8:9], off nt
	v_lshlrev_b64 v[16:17], 12, v[16:17]
	global_load_dwordx4 v[12:15], v[12:13], off nt
	v_ashrrev_i32_e32 v21, 31, v20
	v_lshl_add_u64 v[16:17], v[34:35], 0, v[16:17]
	v_lshlrev_b64 v[20:21], 12, v[20:21]
	v_or_b32_e32 v24, 40, v32
	global_load_dwordx4 v[16:19], v[16:17], off nt
	v_lshl_add_u64 v[20:21], v[34:35], 0, v[20:21]
	v_ashrrev_i32_e32 v25, 31, v24
	global_load_dwordx4 v[20:23], v[20:21], off nt
	v_lshlrev_b64 v[24:25], 12, v[24:25]
	v_or_b32_e32 v28, 48, v32
	v_lshl_add_u64 v[24:25], v[34:35], 0, v[24:25]
	v_ashrrev_i32_e32 v29, 31, v28
	global_load_dwordx4 v[24:27], v[24:25], off nt
	v_lshlrev_b64 v[28:29], 12, v[28:29]
	v_or_b32_e32 v32, 56, v32
	v_lshl_add_u64 v[28:29], v[34:35], 0, v[28:29]
	v_ashrrev_i32_e32 v33, 31, v32
	global_load_dwordx4 v[28:31], v[28:29], off nt
	v_lshlrev_b64 v[32:33], 12, v[32:33]
	v_lshl_add_u64 v[32:33], v[34:35], 0, v[32:33]
	global_load_dwordx4 v[32:35], v[32:33], off nt
	v_add_u32_e32 v2, v44, v47
	s_lshl_b64 s[10:11], s[68:69], 1
	s_add_u32 s10, s3, s10
	s_addc_u32 s11, s8, s11
	v_readlane_b32 s58, v253, 10
	v_readlane_b32 s59, v253, 11
	v_readlane_b32 s60, v253, 12
	v_readlane_b32 s61, v253, 13
	v_readlane_b32 s62, v253, 14
	v_readlane_b32 s63, v253, 15
	s_waitcnt vmcnt(0)
	ds_write2_b32 v45, v4, v5 offset1:1
	ds_write2_b32 v45, v6, v7 offset0:2 offset1:3
	v_add_u32_e32 v4, 0x420, v2
	ds_write2_b32 v2, v8, v9 offset1:1
	ds_write2_b32 v2, v10, v11 offset0:2 offset1:3
	ds_write2_b32 v4, v12, v13 offset1:1
	v_add_u32_e32 v4, 0x428, v2
	ds_write2_b32 v4, v14, v15 offset1:1
	v_add_u32_e32 v4, 0x840, v2
	v_add_u32_e32 v2, 0x848, v2
	ds_write2_b32 v2, v18, v19 offset1:1
	v_add_u32_e32 v2, 0x1080, v45
	ds_write2_b32 v4, v16, v17 offset1:1
	ds_write2_b32 v2, v20, v21 offset1:1
	v_add_u32_e32 v2, 0x1088, v45
	ds_write2_b32 v2, v22, v23 offset1:1
	v_add_u32_e32 v2, 0x14a0, v45
	ds_write2_b32 v2, v24, v25 offset1:1
	v_add_u32_e32 v2, 0x14a8, v45
	ds_write2_b32 v2, v26, v27 offset1:1
	v_add_u32_e32 v2, 0x18c0, v45
	ds_write2_b32 v2, v28, v29 offset1:1
	v_add_u32_e32 v2, 0x18c8, v45
	ds_write2_b32 v2, v30, v31 offset1:1
	v_add_u32_e32 v2, 0x1ce0, v45
	ds_write2_b32 v2, v32, v33 offset1:1
	v_add_u32_e32 v2, 0x1ce8, v45
	ds_write2_b32 v2, v34, v35 offset1:1
	s_waitcnt lgkmcnt(0)
	ds_read2_b32 v[10:11], v50 offset0:33 offset1:41
	ds_read2_b32 v[12:13], v50 offset1:8
	v_lshlrev_b32_e32 v2, 1, v38
	ds_read2_b32 v[14:15], v50 offset0:66 offset1:74
	ds_read2_b32 v[16:17], v50 offset0:99 offset1:107
	ds_read2_b32 v[18:19], v50 offset0:132 offset1:140
	ds_read2_b32 v[20:21], v50 offset0:165 offset1:173
	ds_read2_b32 v[22:23], v50 offset0:198 offset1:206
	ds_read2_b32 v[24:25], v50 offset0:231 offset1:239
	v_lshl_add_u64 v[8:9], s[10:11], 0, v[2:3]
	v_or_b32_e32 v2, s2, v39
	v_mul_u32_u24_e32 v2, 0x1600, v2
	v_lshl_add_u64 v[26:27], v[8:9], 0, v[2:3]
	v_or_b32_e32 v2, s2, v46
	s_waitcnt lgkmcnt(0)
	v_cvt_pk_bf16_f32 v4, v12, v10
	v_mul_u32_u24_e32 v2, 0x1600, v2
	v_cvt_pk_bf16_f32 v5, v14, v16
	v_cvt_pk_bf16_f32 v6, v18, v20
	v_cvt_pk_bf16_f32 v7, v22, v24
	global_store_dwordx4 v[26:27], v[4:7], off sc1 nt
	s_nop 1
	v_cvt_pk_bf16_f32 v4, v13, v11
	v_lshl_add_u64 v[10:11], v[8:9], 0, v[2:3]
	v_cvt_pk_bf16_f32 v5, v15, v17
	v_cvt_pk_bf16_f32 v6, v19, v21
	v_cvt_pk_bf16_f32 v7, v23, v25
	global_store_dwordx4 v[10:11], v[4:7], off sc1 nt
	ds_read2_b32 v[10:11], v50 offset0:16 offset1:24
	ds_read2_b32 v[12:13], v50 offset0:49 offset1:57
	ds_read2_b32 v[14:15], v50 offset0:82 offset1:90
	ds_read2_b32 v[16:17], v50 offset0:115 offset1:123
	ds_read2_b32 v[18:19], v50 offset0:148 offset1:156
	ds_read2_b32 v[20:21], v50 offset0:181 offset1:189
	ds_read2_b32 v[22:23], v50 offset0:214 offset1:222
	ds_read2_b32 v[24:25], v50 offset0:247 offset1:255
	v_or_b32_e32 v2, s2, v48
	v_mul_u32_u24_e32 v2, 0x1600, v2
	v_lshl_add_u64 v[26:27], v[8:9], 0, v[2:3]
	v_or_b32_e32 v2, s2, v49
	v_mul_u32_u24_e32 v2, 0x1600, v2
	s_waitcnt lgkmcnt(6)
	v_cvt_pk_bf16_f32 v4, v10, v12
	s_waitcnt lgkmcnt(4)
	v_cvt_pk_bf16_f32 v5, v14, v16
	s_waitcnt lgkmcnt(2)
	v_cvt_pk_bf16_f32 v6, v18, v20
	s_waitcnt lgkmcnt(0)
	v_cvt_pk_bf16_f32 v7, v22, v24
	v_lshl_add_u64 v[8:9], v[8:9], 0, v[2:3]
	global_store_dwordx4 v[26:27], v[4:7], off sc1 nt
	s_mov_b64 s[2:3], 0
	s_nop 0
	v_cvt_pk_bf16_f32 v4, v11, v13
	v_cvt_pk_bf16_f32 v5, v15, v17
	v_cvt_pk_bf16_f32 v6, v19, v21
	v_cvt_pk_bf16_f32 v7, v23, v25
	global_store_dwordx4 v[8:9], v[4:7], off sc1 nt
	s_waitcnt lgkmcnt(0)
; #define GAS __attribute__((address_space(1)))
; #define LAS __attribute__((address_space(3)))
; #define LDS_WAIT() asm volatile("s_waitcnt lgkmcnt(0)" ::: "memory")
; __device__ __forceinline__ unsigned pk2(float lo, float hi) { unsigned r; asm("v_cvt_pk_bf16_f32 %0, %1, %2" : "=v"(r) : "v"(lo), "v"(hi)); return r; }
; __device__ __forceinline__ void transpose_item(const float* W, int K, int N, bf16* WT, int drow0, int kb, int n0, LAS float* scr, int lane) {
;     const int k0 = 64 * kb; const int c4 = 4 * (lane & 7); const bool ok = (n0 + c4) < N;
;     f32x4 v[8];
; #pragma unroll
;     for (int i = 0; i < 8; ++i) { const int kk = 8 * i + (lane >> 3); v[i] = ok ? *(const f32x4*)(W + (size_t)(k0 + kk) * N + n0 + c4) : (f32x4){0.f, 0.f, 0.f, 0.f}; }
; #pragma unroll
;     for (int i = 0; i < 8; ++i) { const int kk = 8 * i + (lane >> 3); LAS float* d = scr + kk * 33 + c4; d[0] = v[i][0]; d[1] = v[i][1]; d[2] = v[i][2]; d[3] = v[i][3]; }
;     LDS_WAIT(); asm volatile("" ::: "memory");
;     const int c = lane & 7;
; #pragma unroll
;     for (int j = 0; j < 4; ++j) { const int n = (lane >> 3) + 8 * j; const LAS float* s = scr + (8 * c) * 33 + n;
;         v4u o; o.x = pk2(s[0 * 33], s[1 * 33]); o.y = pk2(s[2 * 33], s[3 * 33]); o.z = pk2(s[4 * 33], s[5 * 33]); o.w = pk2(s[6 * 33], s[7 * 33]);
;         *(GAS v4u*)(WT + (size_t)(drow0 + n) * K + k0 + 8 * c) = o; }
;     LDS_WAIT(); asm volatile("" ::: "memory");
; }
; __device__ __forceinline__ void convert_item(const In& I, unsigned char* ws, int it, LAS float* scr, int lane) {
;     ...
;     if (r < T0) { const int f = r / I_FFN; r -= f * I_FFN;
;         if (r < 2 * I_G) { const int up = r >= I_G; r -= up * I_G; const int kb = r / 88, nb = r % 88;
;             transpose_item((up ? I.w_up : I.w_gate) + (size_t)f * D * FF, D, FF, Wgu + (size_t)f * NGU * D, 256 * (nb >> 2) + 32 * (nb & 3) + 128 * up, kb, 32 * nb, scr, lane); }
.LBB0_412:
	s_andn2_b64 vcc, exec, s[2:3]
	s_cbranch_vccnz .LBB0_354
	v_readlane_b32 s48, v253, 0
	v_readlane_b32 s49, v253, 1
	v_readlane_b32 s50, v253, 2
	v_readlane_b32 s51, v253, 3
	v_readlane_b32 s52, v253, 4
	v_readlane_b32 s53, v253, 5
	s_cmpk_gt_i32 s7, 0x57f
	v_readlane_b32 s54, v253, 6
	v_readlane_b32 s55, v253, 7
	v_readlane_b32 s56, v253, 8
	v_readlane_b32 s57, v253, 9
	s_mov_b64 s[48:49], s[52:53]
	s_cselect_b32 s2, 0xfffffa80, 0
	s_mul_i32 s3, s6, 0x1080
	s_mov_b64 s[50:51], s[54:55]
	s_cselect_b32 s9, 0x80, 0
	s_cselect_b32 s7, s50, s48
	s_cselect_b32 s8, s51, s49
	s_sub_i32 s2, s2, s3
	s_add_i32 s2, s41, s2
	s_add_i32 s2, s2, 0xa800
	s_mul_hi_i32 s3, s2, 0x2e8ba2e9
	s_lshr_b32 s10, s3, 31
	s_ashr_i32 s3, s3, 4
	s_add_i32 s3, s3, s10
	s_mul_i32 s10, s3, 0x58
	s_sub_i32 s2, s2, s10
	s_mul_hi_i32 s10, s6, 0xb00000
	s_mul_i32 s6, s6, 0xb00000
	s_add_u32 s12, s7, s6
	s_addc_u32 s13, s8, s10
	s_add_u32 s7, s28, s6
	s_addc_u32 s8, s29, s10
	s_lshl_b32 s10, s2, 5
	s_lshl_b32 s6, s2, 6
	s_and_b32 s2, s10, 0x60
	s_and_b32 s6, s6, 0xffffff00
	s_or_b32 s2, s2, s9
	s_ashr_i32 s11, s10, 31
	s_or_b32 s6, s2, s6
	s_lshl_b32 s2, s3, 6
	s_lshl_b64 s[10:11], s[10:11], 2
	s_add_u32 s10, s12, s10
	v_or_b32_e32 v34, s2, v39
	s_addc_u32 s11, s13, s11
	v_lshlrev_b32_e32 v2, 2, v36
	v_lshl_add_u64 v[32:33], s[10:11], 0, v[2:3]
	s_movk_i32 s3, 0x2c00
	v_or_b32_e32 v2, 8, v34
	v_mad_i64_i32 v[4:5], s[10:11], v34, s3, v[32:33]
	v_mad_i64_i32 v[8:9], s[10:11], v2, s3, v[32:33]
	v_or_b32_e32 v2, 16, v34
	global_load_dwordx4 v[4:7], v[4:5], off nt
	v_mad_i64_i32 v[12:13], s[10:11], v2, s3, v[32:33]
	global_load_dwordx4 v[8:11], v[8:9], off nt
	v_or_b32_e32 v2, 24, v34
	global_load_dwordx4 v[12:15], v[12:13], off nt
	v_mad_i64_i32 v[16:17], s[10:11], v2, s3, v[32:33]
	v_or_b32_e32 v2, 32, v34
	global_load_dwordx4 v[16:19], v[16:17], off nt
	v_mad_i64_i32 v[20:21], s[10:11], v2, s3, v[32:33]
	global_load_dwordx4 v[20:23], v[20:21], off nt
	v_or_b32_e32 v2, 40, v34
	v_mad_i64_i32 v[24:25], s[10:11], v2, s3, v[32:33]
	global_load_dwordx4 v[24:27], v[24:25], off nt
	v_or_b32_e32 v2, 48, v34
	v_mad_i64_i32 v[28:29], s[10:11], v2, s3, v[32:33]
	global_load_dwordx4 v[28:31], v[28:29], off nt
	v_or_b32_e32 v2, 56, v34
	v_mad_i64_i32 v[32:33], s[10:11], v2, s3, v[32:33]
	global_load_dwordx4 v[32:35], v[32:33], off nt
	v_add_u32_e32 v2, v44, v47
	s_ashr_i32 s3, s2, 31
	s_lshl_b64 s[2:3], s[2:3], 1
	s_add_u32 s2, s7, s2
	s_addc_u32 s3, s8, s3
	v_readlane_b32 s58, v253, 10
	v_readlane_b32 s59, v253, 11
	v_readlane_b32 s60, v253, 12
	v_readlane_b32 s61, v253, 13
	v_readlane_b32 s62, v253, 14
	v_readlane_b32 s63, v253, 15
	s_mov_b64 s[52:53], s[56:57]
	s_waitcnt vmcnt(0)
	ds_write2_b32 v45, v4, v5 offset1:1
	ds_write2_b32 v45, v6, v7 offset0:2 offset1:3
	v_add_u32_e32 v4, 0x420, v2
	ds_write2_b32 v2, v8, v9 offset1:1
	ds_write2_b32 v2, v10, v11 offset0:2 offset1:3
	ds_write2_b32 v4, v12, v13 offset1:1
	v_add_u32_e32 v4, 0x428, v2
	ds_write2_b32 v4, v14, v15 offset1:1
	v_add_u32_e32 v4, 0x840, v2
	v_add_u32_e32 v2, 0x848, v2
	ds_write2_b32 v2, v18, v19 offset1:1
	v_add_u32_e32 v2, 0x1080, v45
	ds_write2_b32 v2, v20, v21 offset1:1
	v_add_u32_e32 v2, 0x1088, v45
	ds_write2_b32 v2, v22, v23 offset1:1
	v_add_u32_e32 v2, 0x14a0, v45
	ds_write2_b32 v2, v24, v25 offset1:1
	v_add_u32_e32 v2, 0x14a8, v45
	ds_write2_b32 v2, v26, v27 offset1:1
	v_add_u32_e32 v2, 0x18c0, v45
	ds_write2_b32 v2, v28, v29 offset1:1
	v_add_u32_e32 v2, 0x18c8, v45
	ds_write2_b32 v2, v30, v31 offset1:1
	v_add_u32_e32 v2, 0x1ce0, v45
	ds_write2_b32 v2, v32, v33 offset1:1
	v_add_u32_e32 v2, 0x1ce8, v45
	ds_write2_b32 v4, v16, v17 offset1:1
	ds_write2_b32 v2, v34, v35 offset1:1
	s_waitcnt lgkmcnt(0)
	ds_read2_b32 v[10:11], v50 offset0:33 offset1:41
	ds_read2_b32 v[12:13], v50 offset1:8
	ds_read2_b32 v[14:15], v50 offset0:66 offset1:74
	ds_read2_b32 v[16:17], v50 offset0:99 offset1:107
	ds_read2_b32 v[18:19], v50 offset0:132 offset1:140
	ds_read2_b32 v[20:21], v50 offset0:165 offset1:173
	ds_read2_b32 v[22:23], v50 offset0:198 offset1:206
	ds_read2_b32 v[24:25], v50 offset0:231 offset1:239
	v_or_b32_e32 v26, s6, v39
	v_lshlrev_b32_e32 v2, 1, v38
	v_ashrrev_i32_e32 v27, 31, v26
	v_lshl_add_u64 v[8:9], s[2:3], 0, v[2:3]
	v_lshlrev_b64 v[26:27], 11, v[26:27]
	s_waitcnt lgkmcnt(0)
	v_cvt_pk_bf16_f32 v4, v12, v10
	v_lshl_add_u64 v[26:27], v[8:9], 0, v[26:27]
	v_or_b32_e32 v10, s6, v46
	v_cvt_pk_bf16_f32 v5, v14, v16
	v_cvt_pk_bf16_f32 v6, v18, v20
	v_cvt_pk_bf16_f32 v7, v22, v24
	global_store_dwordx4 v[26:27], v[4:7], off sc1 nt
	v_or_b32_e32 v26, s6, v48
	v_ashrrev_i32_e32 v27, 31, v26
	v_cvt_pk_bf16_f32 v4, v13, v11
	v_ashrrev_i32_e32 v11, 31, v10
	v_lshlrev_b64 v[10:11], 11, v[10:11]
	v_lshl_add_u64 v[10:11], v[8:9], 0, v[10:11]
	v_cvt_pk_bf16_f32 v5, v15, v17
	v_cvt_pk_bf16_f32 v6, v19, v21
	v_cvt_pk_bf16_f32 v7, v23, v25
	global_store_dwordx4 v[10:11], v[4:7], off sc1 nt
	ds_read2_b32 v[10:11], v50 offset0:16 offset1:24
	ds_read2_b32 v[12:13], v50 offset0:49 offset1:57
	ds_read2_b32 v[14:15], v50 offset0:82 offset1:90
	ds_read2_b32 v[16:17], v50 offset0:115 offset1:123
	ds_read2_b32 v[18:19], v50 offset0:148 offset1:156
	ds_read2_b32 v[20:21], v50 offset0:181 offset1:189
	ds_read2_b32 v[22:23], v50 offset0:214 offset1:222
	ds_read2_b32 v[24:25], v50 offset0:247 offset1:255
	v_lshlrev_b64 v[26:27], 11, v[26:27]
	s_waitcnt lgkmcnt(6)
	v_cvt_pk_bf16_f32 v4, v10, v12
	v_lshl_add_u64 v[26:27], v[8:9], 0, v[26:27]
	v_or_b32_e32 v10, s6, v49
	s_waitcnt lgkmcnt(4)
	v_cvt_pk_bf16_f32 v5, v14, v16
	s_waitcnt lgkmcnt(2)
	v_cvt_pk_bf16_f32 v6, v18, v20
	s_waitcnt lgkmcnt(0)
	v_cvt_pk_bf16_f32 v7, v22, v24
	global_store_dwordx4 v[26:27], v[4:7], off sc1 nt
	s_nop 1
	v_cvt_pk_bf16_f32 v4, v11, v13
	v_ashrrev_i32_e32 v11, 31, v10
	v_lshlrev_b64 v[10:11], 11, v[10:11]
	v_lshl_add_u64 v[8:9], v[8:9], 0, v[10:11]
	v_cvt_pk_bf16_f32 v5, v15, v17
	v_cvt_pk_bf16_f32 v6, v19, v21
	v_cvt_pk_bf16_f32 v7, v23, v25
	global_store_dwordx4 v[8:9], v[4:7], off sc1 nt
	s_waitcnt lgkmcnt(0)
	s_branch .LBB0_354

; #define GAS __attribute__((address_space(1)))
; __device__ __forceinline__ void transpose_item(const float* W, int K, int N, bf16* WT, int drow0, int kb, int n0, LAS float* scr, int lane) {
;     const int k0 = 64 * kb; const int c4 = 4 * (lane & 7); const bool ok = (n0 + c4) < N;
;     f32x4 v[8];
; #pragma unroll
;     for (int i = 0; i < 8; ++i) { const int kk = 8 * i + (lane >> 3); v[i] = ok ? *(const f32x4*)(W + (size_t)(k0 + kk) * N + n0 + c4) : (f32x4){0.f, 0.f, 0.f, 0.f}; }
; #pragma unroll
;     for (int i = 0; i < 8; ++i) { const int kk = 8 * i + (lane >> 3); LAS float* d = scr + kk * 33 + c4; d[0] = v[i][0]; d[1] = v[i][1]; d[2] = v[i][2]; d[3] = v[i][3]; }
;     LDS_WAIT(); asm volatile("" ::: "memory");
;     const int c = lane & 7;
; #pragma unroll
;     for (int j = 0; j < 4; ++j) { const int n = (lane >> 3) + 8 * j; const LAS float* s = scr + (8 * c) * 33 + n;
;         v4u o; o.x = pk2(s[0 * 33], s[1 * 33]); o.y = pk2(s[2 * 33], s[3 * 33]); o.z = pk2(s[4 * 33], s[5 * 33]); o.w = pk2(s[6 * 33], s[7 * 33]);
;         *(GAS v4u*)(WT + (size_t)(drow0 + n) * K + k0 + 8 * c) = o; }
;     LDS_WAIT(); asm volatile("" ::: "memory");
; }
; __device__ __forceinline__ void convert_item(const In& I, unsigned char* ws, int it, LAS float* scr, int lane) {
;     ...
;     int r = it;
;     if (r < T0) { const int f = r / I_FFN; r -= f * I_FFN;
;         if (r < 2 * I_G) { const int up = r >= I_G; r -= up * I_G; const int kb = r / 88, nb = r % 88;
;             transpose_item((up ? I.w_up : I.w_gate) + (size_t)f * D * FF, D, FF, Wgu + (size_t)f * NGU * D, 256 * (nb >> 2) + 32 * (nb & 3) + 128 * up, kb, 32 * nb, scr, lane); }
;         else { r -= 2 * I_G; const int kb = r / 32, nb = r % 32; transpose_item(I.w_down + (size_t)f * FF * D, FF, D, Wd + (size_t)f * D * FF, 32 * nb, kb, 32 * nb, scr, lane); }
;         return; }
;     r -= T0;
;     if (r < 2 * I_NIN) { const int j = r / I_NIN; r -= j * I_NIN; const int kb = r / 88, nb = r % 88;
;         transpose_item(I.nsa_w_in + (size_t)j * D * NSA_IN, D, NSA_IN, Wnin + (size_t)j * NSA_IN_PAD * D, 32 * nb, kb, 32 * nb, scr, lane); return; }
;     r -= 2 * I_NIN;
;     if (r < 2 * I_SQ) { const int j = r / I_SQ; r -= j * I_SQ; const int kb = r / 32, nb = r % 32;
;         transpose_item(I.nsa_w_out + (size_t)j * D * D, D, D, Wnout + (size_t)j * D * D, 32 * nb, kb, 32 * nb, scr, lane); return; }
;     r -= 2 * I_SQ;
.LBB0_416:
	s_add_i32 s43, s41, 0xa800
	s_cmp_gt_i32 s43, 0x83ff
	s_mov_b64 s[2:3], -1
	s_cbranch_scc0 .LBB0_470
	s_cmpk_gt_u32 s43, 0x8eff
	s_cbranch_scc0 .LBB0_451
	s_cmpk_gt_u32 s43, 0x92ff
	s_cbranch_scc0 .LBB0_448
	s_cmpk_gt_u32 s43, 0x9fff
	s_cbranch_scc0 .LBB0_429
	s_cmpk_gt_u32 s43, 0xa3ff
	s_cbranch_scc0 .LBB0_426
	s_cmpk_gt_u32 s43, 0xa7ff
	s_cbranch_scc0 .LBB0_423
	s_lshr_b32 s68, s41, 3
	v_readlane_b32 s44, v253, 16
	s_lshl_b64 s[2:3], s[68:69], 16
	v_readlane_b32 s48, v253, 20
	v_readlane_b32 s49, v253, 21
	s_add_u32 s6, s48, s2
	s_addc_u32 s7, s49, s3
	s_lshl_b64 s[2:3], s[68:69], 15
	s_add_u32 s8, s34, s2
	s_addc_u32 s3, s35, s3
	s_and_b32 s2, s42, 32
	s_and_b32 s9, s42, 0xc0
	s_lshl_b32 s10, s2, 2
	s_add_u32 s6, s6, s10
	v_or_b32_e32 v6, s9, v39
	s_addc_u32 s7, s7, 0
	v_lshlrev_b32_e32 v2, 2, v36
	v_lshl_add_u64 v[4:5], s[6:7], 0, v[2:3]
	v_lshlrev_b32_e32 v2, 8, v6
	v_lshl_add_u64 v[28:29], v[4:5], 0, v[2:3]
	v_add_co_u32_e32 v16, vcc, s84, v28
	global_load_dwordx4 v[4:7], v[28:29], off nt
	global_load_dwordx4 v[8:11], v[28:29], off offset:2048 nt
	v_addc_co_u32_e32 v17, vcc, 0, v29, vcc
	v_add_co_u32_e32 v24, vcc, s74, v28
	s_movk_i32 s6, 0x3000
	s_nop 0
	v_addc_co_u32_e32 v25, vcc, 0, v29, vcc
	global_load_dwordx4 v[12:15], v[24:25], off offset:-4096 nt
	s_nop 0
	global_load_dwordx4 v[16:19], v[16:17], off offset:2048 nt
	s_nop 0
	global_load_dwordx4 v[20:23], v[24:25], off nt
	s_nop 0
	global_load_dwordx4 v[24:27], v[24:25], off offset:2048 nt
	v_add_co_u32_e32 v32, vcc, s6, v28
	v_add_u32_e32 v2, v44, v47
	s_nop 0
	v_addc_co_u32_e32 v33, vcc, 0, v29, vcc
	global_load_dwordx4 v[28:31], v[32:33], off nt
	s_nop 0
	global_load_dwordx4 v[32:35], v[32:33], off offset:2048 nt
	s_lshl_b32 s6, s9, 1
	s_add_u32 s6, s8, s6
	s_addc_u32 s7, s3, 0
	v_readlane_b32 s45, v253, 17
	v_readlane_b32 s46, v253, 18
	v_readlane_b32 s47, v253, 19
	v_readlane_b32 s50, v253, 22
	v_readlane_b32 s51, v253, 23
	v_readlane_b32 s52, v253, 24
	v_readlane_b32 s53, v253, 25
	v_readlane_b32 s54, v253, 26
	v_readlane_b32 s55, v253, 27
	v_readlane_b32 s56, v253, 28
	v_readlane_b32 s57, v253, 29
	v_readlane_b32 s58, v253, 30
	v_readlane_b32 s59, v253, 31
	s_waitcnt vmcnt(0)
	ds_write2_b32 v45, v4, v5 offset1:1
	ds_write2_b32 v45, v6, v7 offset0:2 offset1:3
	v_add_u32_e32 v4, 0x420, v2
	ds_write2_b32 v2, v8, v9 offset1:1
	ds_write2_b32 v2, v10, v11 offset0:2 offset1:3
	ds_write2_b32 v4, v12, v13 offset1:1
	v_add_u32_e32 v4, 0x428, v2
	ds_write2_b32 v4, v14, v15 offset1:1
	v_add_u32_e32 v4, 0x840, v2
	v_add_u32_e32 v2, 0x848, v2
	ds_write2_b32 v2, v18, v19 offset1:1
	v_add_u32_e32 v2, 0x1080, v45
	ds_write2_b32 v2, v20, v21 offset1:1
	v_add_u32_e32 v2, 0x1088, v45
	ds_write2_b32 v2, v22, v23 offset1:1
	v_add_u32_e32 v2, 0x14a0, v45
	ds_write2_b32 v2, v24, v25 offset1:1
	v_add_u32_e32 v2, 0x14a8, v45
	ds_write2_b32 v2, v26, v27 offset1:1
	v_add_u32_e32 v2, 0x18c0, v45
	ds_write2_b32 v2, v28, v29 offset1:1
	v_add_u32_e32 v2, 0x18c8, v45
	ds_write2_b32 v2, v30, v31 offset1:1
	v_add_u32_e32 v2, 0x1ce0, v45
	ds_write2_b32 v2, v32, v33 offset1:1
	v_add_u32_e32 v2, 0x1ce8, v45
	ds_write2_b32 v4, v16, v17 offset1:1
	ds_write2_b32 v2, v34, v35 offset1:1
	s_waitcnt lgkmcnt(0)
	ds_read2_b32 v[10:11], v50 offset0:33 offset1:41
	ds_read2_b32 v[12:13], v50 offset1:8
	v_lshlrev_b32_e32 v2, 1, v38
	ds_read2_b32 v[14:15], v50 offset0:66 offset1:74
	ds_read2_b32 v[16:17], v50 offset0:99 offset1:107
	ds_read2_b32 v[18:19], v50 offset0:132 offset1:140
	ds_read2_b32 v[20:21], v50 offset0:165 offset1:173
	ds_read2_b32 v[22:23], v50 offset0:198 offset1:206
	ds_read2_b32 v[24:25], v50 offset0:231 offset1:239
	v_lshl_add_u64 v[4:5], s[6:7], 0, v[2:3]
	v_or_b32_e32 v2, s2, v39
	v_lshlrev_b32_e32 v2, 9, v2
	v_lshl_add_u64 v[26:27], v[4:5], 0, v[2:3]
	v_or_b32_e32 v2, s2, v46
	s_waitcnt lgkmcnt(0)
	v_cvt_pk_bf16_f32 v6, v12, v10
	v_lshlrev_b32_e32 v2, 9, v2
	v_cvt_pk_bf16_f32 v7, v14, v16
	v_cvt_pk_bf16_f32 v8, v18, v20
	v_cvt_pk_bf16_f32 v9, v22, v24
	global_store_dwordx4 v[26:27], v[6:9], off sc1 nt
	s_nop 1
	v_cvt_pk_bf16_f32 v6, v13, v11
	v_lshl_add_u64 v[10:11], v[4:5], 0, v[2:3]
	v_cvt_pk_bf16_f32 v7, v15, v17
	v_cvt_pk_bf16_f32 v8, v19, v21
	v_cvt_pk_bf16_f32 v9, v23, v25
	global_store_dwordx4 v[10:11], v[6:9], off sc1 nt
	ds_read2_b32 v[10:11], v50 offset0:16 offset1:24
	ds_read2_b32 v[12:13], v50 offset0:49 offset1:57
	ds_read2_b32 v[14:15], v50 offset0:82 offset1:90
	ds_read2_b32 v[16:17], v50 offset0:115 offset1:123
	ds_read2_b32 v[18:19], v50 offset0:148 offset1:156
	ds_read2_b32 v[20:21], v50 offset0:181 offset1:189
	ds_read2_b32 v[22:23], v50 offset0:214 offset1:222
	ds_read2_b32 v[24:25], v50 offset0:247 offset1:255
	v_or_b32_e32 v2, s2, v48
	v_lshlrev_b32_e32 v2, 9, v2
	v_lshl_add_u64 v[26:27], v[4:5], 0, v[2:3]
	v_or_b32_e32 v2, s2, v49
	v_lshlrev_b32_e32 v2, 9, v2
	s_waitcnt lgkmcnt(6)
	v_cvt_pk_bf16_f32 v6, v10, v12
	s_waitcnt lgkmcnt(4)
	v_cvt_pk_bf16_f32 v7, v14, v16
	s_waitcnt lgkmcnt(2)
	v_cvt_pk_bf16_f32 v8, v18, v20
	s_waitcnt lgkmcnt(0)
	v_cvt_pk_bf16_f32 v9, v22, v24
	v_lshl_add_u64 v[4:5], v[4:5], 0, v[2:3]
	global_store_dwordx4 v[26:27], v[6:9], off sc1 nt
	s_mov_b64 s[2:3], 0
	s_nop 0
	v_cvt_pk_bf16_f32 v6, v11, v13
	v_cvt_pk_bf16_f32 v7, v15, v17
	v_cvt_pk_bf16_f32 v8, v19, v21
	v_cvt_pk_bf16_f32 v9, v23, v25
	global_store_dwordx4 v[4:5], v[6:9], off sc1 nt
	s_waitcnt lgkmcnt(0)
; #define GAS __attribute__((address_space(1)))
; #define LAS __attribute__((address_space(3)))
; #define LDS_WAIT() asm volatile("s_waitcnt lgkmcnt(0)" ::: "memory")
; __device__ __forceinline__ unsigned pk2(float lo, float hi) { unsigned r; asm("v_cvt_pk_bf16_f32 %0, %1, %2" : "=v"(r) : "v"(lo), "v"(hi)); return r; }
; __device__ __forceinline__ void transpose_item(const float* W, int K, int N, bf16* WT, int drow0, int kb, int n0, LAS float* scr, int lane) {
;     const int k0 = 64 * kb; const int c4 = 4 * (lane & 7); const bool ok = (n0 + c4) < N;
;     f32x4 v[8];
; #pragma unroll
;     for (int i = 0; i < 8; ++i) { const int kk = 8 * i + (lane >> 3); v[i] = ok ? *(const f32x4*)(W + (size_t)(k0 + kk) * N + n0 + c4) : (f32x4){0.f, 0.f, 0.f, 0.f}; }
; #pragma unroll
;     for (int i = 0; i < 8; ++i) { const int kk = 8 * i + (lane >> 3); LAS float* d = scr + kk * 33 + c4; d[0] = v[i][0]; d[1] = v[i][1]; d[2] = v[i][2]; d[3] = v[i][3]; }
;     LDS_WAIT(); asm volatile("" ::: "memory");
;     const int c = lane & 7;
; #pragma unroll
;     for (int j = 0; j < 4; ++j) { const int n = (lane >> 3) + 8 * j; const LAS float* s = scr + (8 * c) * 33 + n;
;         v4u o; o.x = pk2(s[0 * 33], s[1 * 33]); o.y = pk2(s[2 * 33], s[3 * 33]); o.z = pk2(s[4 * 33], s[5 * 33]); o.w = pk2(s[6 * 33], s[7 * 33]);
;         *(GAS v4u*)(WT + (size_t)(drow0 + n) * K + k0 + 8 * c) = o; }
;     LDS_WAIT(); asm volatile("" ::: "memory");
; }
; __device__ __forceinline__ void convert_item(const In& I, unsigned char* ws, int it, LAS float* scr, int lane) {
;     ...
;     if (r < 4 * I_W1) { const int jk = r / I_W1; r -= jk * I_W1; const int kb = r / 8, nb = r % 8;
;         transpose_item(I.nsa_w1 + (size_t)jk * 2048 * 256, 2048, 256, W1t + (size_t)jk * 256 * 2048, 32 * nb, kb, 32 * nb, scr, lane); return; }
.LBB0_423:
	s_andn2_b64 vcc, exec, s[2:3]
	s_cbranch_vccnz .LBB0_425
	s_add_i32 s2, s41, 0x400
	s_lshr_b32 s68, s2, 8
	s_lshl_b64 s[2:3], s[68:69], 21
	v_readlane_b32 s44, v253, 16
	v_readlane_b32 s45, v253, 17
	s_add_u32 s6, s44, s2
	s_addc_u32 s7, s45, s3
	s_lshl_b64 s[2:3], s[68:69], 20
	s_add_u32 s8, s31, s2
	s_addc_u32 s3, s33, s3
	s_and_b32 s2, s42, 0xe0
	s_and_b32 s9, s40, 0x7c0
	s_lshl_b32 s10, s2, 2
	s_add_u32 s6, s6, s10
	v_or_b32_e32 v6, s9, v39
	s_addc_u32 s7, s7, 0
	v_lshlrev_b32_e32 v2, 2, v36
	v_lshl_add_u64 v[4:5], s[6:7], 0, v[2:3]
	v_lshlrev_b32_e32 v2, 10, v6
	v_lshl_add_u64 v[32:33], v[4:5], 0, v[2:3]
	v_add_co_u32_e32 v8, vcc, s74, v32
	s_movk_i32 s6, 0x4000
	s_nop 0
	v_addc_co_u32_e32 v9, vcc, 0, v33, vcc
	v_add_co_u32_e32 v12, vcc, s6, v32
	s_movk_i32 s6, 0x6000
	s_nop 0
	v_addc_co_u32_e32 v13, vcc, 0, v33, vcc
	global_load_dwordx4 v[4:7], v[32:33], off nt
	v_add_co_u32_e32 v16, vcc, s6, v32
	global_load_dwordx4 v[8:11], v[8:9], off nt
	s_nop 0
	v_addc_co_u32_e32 v17, vcc, 0, v33, vcc
	global_load_dwordx4 v[12:15], v[12:13], off nt
	v_add_co_u32_e32 v20, vcc, s81, v32
	global_load_dwordx4 v[16:19], v[16:17], off nt
	s_nop 0
	v_addc_co_u32_e32 v21, vcc, 0, v33, vcc
	s_mov_b32 s6, 0xa000
	global_load_dwordx4 v[20:23], v[20:21], off nt
	v_add_co_u32_e32 v24, vcc, s6, v32
	s_mov_b32 s6, 0xc000
	s_nop 0
	v_addc_co_u32_e32 v25, vcc, 0, v33, vcc
	global_load_dwordx4 v[24:27], v[24:25], off nt
	v_add_co_u32_e32 v28, vcc, s6, v32
	s_mov_b32 s6, 0xe000
	s_nop 0
	v_addc_co_u32_e32 v29, vcc, 0, v33, vcc
	global_load_dwordx4 v[28:31], v[28:29], off nt
	v_add_co_u32_e32 v32, vcc, s6, v32
	v_add_u32_e32 v2, v44, v47
	s_nop 0
	v_addc_co_u32_e32 v33, vcc, 0, v33, vcc
	global_load_dwordx4 v[32:35], v[32:33], off nt
	s_lshl_b32 s6, s9, 1
	s_add_u32 s6, s8, s6
	s_addc_u32 s7, s3, 0
	v_readlane_b32 s46, v253, 18
	v_readlane_b32 s47, v253, 19
	v_readlane_b32 s48, v253, 20
	v_readlane_b32 s49, v253, 21
	v_readlane_b32 s50, v253, 22
	v_readlane_b32 s51, v253, 23
	v_readlane_b32 s52, v253, 24
	v_readlane_b32 s53, v253, 25
	v_readlane_b32 s54, v253, 26
	v_readlane_b32 s55, v253, 27
	v_readlane_b32 s56, v253, 28
	v_readlane_b32 s57, v253, 29
	v_readlane_b32 s58, v253, 30
	v_readlane_b32 s59, v253, 31
	s_waitcnt vmcnt(0)
	ds_write2_b32 v45, v4, v5 offset1:1
	ds_write2_b32 v45, v6, v7 offset0:2 offset1:3
	v_add_u32_e32 v4, 0x420, v2
	ds_write2_b32 v2, v8, v9 offset1:1
	ds_write2_b32 v2, v10, v11 offset0:2 offset1:3
	ds_write2_b32 v4, v12, v13 offset1:1
	v_add_u32_e32 v4, 0x428, v2
	ds_write2_b32 v4, v14, v15 offset1:1
	v_add_u32_e32 v4, 0x840, v2
	v_add_u32_e32 v2, 0x848, v2
	ds_write2_b32 v2, v18, v19 offset1:1
	v_add_u32_e32 v2, 0x1080, v45
	ds_write2_b32 v2, v20, v21 offset1:1
	v_add_u32_e32 v2, 0x1088, v45
	ds_write2_b32 v2, v22, v23 offset1:1
	v_add_u32_e32 v2, 0x14a0, v45
	ds_write2_b32 v4, v16, v17 offset1:1
	ds_write2_b32 v2, v24, v25 offset1:1
	v_add_u32_e32 v2, 0x14a8, v45
	ds_write2_b32 v2, v26, v27 offset1:1
	v_add_u32_e32 v2, 0x18c0, v45
	ds_write2_b32 v2, v28, v29 offset1:1
	v_add_u32_e32 v2, 0x18c8, v45
	ds_write2_b32 v2, v30, v31 offset1:1
	v_add_u32_e32 v2, 0x1ce0, v45
	ds_write2_b32 v2, v32, v33 offset1:1
	v_add_u32_e32 v2, 0x1ce8, v45
	ds_write2_b32 v2, v34, v35 offset1:1
	s_waitcnt lgkmcnt(0)
	ds_read2_b32 v[10:11], v50 offset0:33 offset1:41
	ds_read2_b32 v[12:13], v50 offset1:8
	v_lshlrev_b32_e32 v2, 1, v38
	ds_read2_b32 v[14:15], v50 offset0:66 offset1:74
	ds_read2_b32 v[16:17], v50 offset0:99 offset1:107
	ds_read2_b32 v[18:19], v50 offset0:132 offset1:140
	ds_read2_b32 v[20:21], v50 offset0:165 offset1:173
	ds_read2_b32 v[22:23], v50 offset0:198 offset1:206
	ds_read2_b32 v[24:25], v50 offset0:231 offset1:239
	v_lshl_add_u64 v[4:5], s[6:7], 0, v[2:3]
	v_or_b32_e32 v2, s2, v39
	v_lshlrev_b32_e32 v2, 12, v2
	v_lshl_add_u64 v[26:27], v[4:5], 0, v[2:3]
	v_or_b32_e32 v2, s2, v46
	s_waitcnt lgkmcnt(0)
	v_cvt_pk_bf16_f32 v6, v12, v10
	v_lshlrev_b32_e32 v2, 12, v2
	v_cvt_pk_bf16_f32 v7, v14, v16
	v_cvt_pk_bf16_f32 v8, v18, v20
	v_cvt_pk_bf16_f32 v9, v22, v24
	global_store_dwordx4 v[26:27], v[6:9], off sc1 nt
	s_nop 1
	v_cvt_pk_bf16_f32 v6, v13, v11
	v_lshl_add_u64 v[10:11], v[4:5], 0, v[2:3]
	v_cvt_pk_bf16_f32 v7, v15, v17
	v_cvt_pk_bf16_f32 v8, v19, v21
	v_cvt_pk_bf16_f32 v9, v23, v25
	global_store_dwordx4 v[10:11], v[6:9], off sc1 nt
	ds_read2_b32 v[10:11], v50 offset0:16 offset1:24
	ds_read2_b32 v[12:13], v50 offset0:49 offset1:57
	ds_read2_b32 v[14:15], v50 offset0:82 offset1:90
	ds_read2_b32 v[16:17], v50 offset0:115 offset1:123
	ds_read2_b32 v[18:19], v50 offset0:148 offset1:156
	ds_read2_b32 v[20:21], v50 offset0:181 offset1:189
	ds_read2_b32 v[22:23], v50 offset0:214 offset1:222
	ds_read2_b32 v[24:25], v50 offset0:247 offset1:255
	v_or_b32_e32 v2, s2, v48
	v_lshlrev_b32_e32 v2, 12, v2
	v_lshl_add_u64 v[26:27], v[4:5], 0, v[2:3]
	v_or_b32_e32 v2, s2, v49
	v_lshlrev_b32_e32 v2, 12, v2
	s_waitcnt lgkmcnt(6)
	v_cvt_pk_bf16_f32 v6, v10, v12
	s_waitcnt lgkmcnt(4)
	v_cvt_pk_bf16_f32 v7, v14, v16
	s_waitcnt lgkmcnt(2)
	v_cvt_pk_bf16_f32 v8, v18, v20
	s_waitcnt lgkmcnt(0)
	v_cvt_pk_bf16_f32 v9, v22, v24
	v_lshl_add_u64 v[4:5], v[4:5], 0, v[2:3]
	global_store_dwordx4 v[26:27], v[6:9], off sc1 nt
	s_nop 1
	v_cvt_pk_bf16_f32 v6, v11, v13
	v_cvt_pk_bf16_f32 v7, v15, v17
	v_cvt_pk_bf16_f32 v8, v19, v21
	v_cvt_pk_bf16_f32 v9, v23, v25
	global_store_dwordx4 v[4:5], v[6:9], off sc1 nt
	s_waitcnt lgkmcnt(0)

; #define GAS __attribute__((address_space(1)))
; #define LAS __attribute__((address_space(3)))
; #define LDS_WAIT() asm volatile("s_waitcnt lgkmcnt(0)" ::: "memory")
; __device__ __forceinline__ unsigned pk2(float lo, float hi) { unsigned r; asm("v_cvt_pk_bf16_f32 %0, %1, %2" : "=v"(r) : "v"(lo), "v"(hi)); return r; }
; __device__ __forceinline__ void transpose_item(const float* W, int K, int N, bf16* WT, int drow0, int kb, int n0, LAS float* scr, int lane) {
;     const int k0 = 64 * kb; const int c4 = 4 * (lane & 7); const bool ok = (n0 + c4) < N;
;     f32x4 v[8];
; #pragma unroll
;     for (int i = 0; i < 8; ++i) { const int kk = 8 * i + (lane >> 3); v[i] = ok ? *(const f32x4*)(W + (size_t)(k0 + kk) * N + n0 + c4) : (f32x4){0.f, 0.f, 0.f, 0.f}; }
; #pragma unroll
;     for (int i = 0; i < 8; ++i) { const int kk = 8 * i + (lane >> 3); LAS float* d = scr + kk * 33 + c4; d[0] = v[i][0]; d[1] = v[i][1]; d[2] = v[i][2]; d[3] = v[i][3]; }
;     LDS_WAIT(); asm volatile("" ::: "memory");
;     const int c = lane & 7;
; #pragma unroll
;     for (int j = 0; j < 4; ++j) { const int n = (lane >> 3) + 8 * j; const LAS float* s = scr + (8 * c) * 33 + n;
;         v4u o; o.x = pk2(s[0 * 33], s[1 * 33]); o.y = pk2(s[2 * 33], s[3 * 33]); o.z = pk2(s[4 * 33], s[5 * 33]); o.w = pk2(s[6 * 33], s[7 * 33]);
;         *(GAS v4u*)(WT + (size_t)(drow0 + n) * K + k0 + 8 * c) = o; }
;     LDS_WAIT(); asm volatile("" ::: "memory");
; }
; __device__ __forceinline__ void convert_item(const In& I, unsigned char* ws, int it, LAS float* scr, int lane) {
;     ...
;     if (r < 2 * I_SQ) { const int j = r / I_SQ; r -= j * I_SQ; const int kb = r / 32, nb = r % 32;
;         transpose_item(I.fox_w_out + (size_t)j * D * D, D, D, Wfout + (size_t)j * D * D, 32 * nb, kb, 32 * nb, scr, lane); return; }
.LBB0_426:
	s_andn2_b64 vcc, exec, s[2:3]
	s_cbranch_vccnz .LBB0_428
	s_add_i32 s2, s41, 0x800
	s_lshr_b32 s68, s2, 9
	v_readlane_b32 s44, v253, 16
	s_lshl_b64 s[2:3], s[68:69], 22
	v_readlane_b32 s56, v253, 28
	v_readlane_b32 s57, v253, 29
	s_add_u32 s8, s56, s2
	s_addc_u32 s9, s57, s3
	s_lshl_b64 s[6:7], s[68:69], 21
	s_add_u32 s3, s26, s6
	s_addc_u32 s6, s27, s7
	s_and_b32 s2, s42, 0x3e0
	s_add_i32 s7, s0, 0x14000
	s_and_b32 s7, s7, 0x3c0
	s_lshl_b32 s10, s2, 2
	s_add_u32 s8, s8, s10
	v_or_b32_e32 v6, s7, v39
	s_addc_u32 s9, s9, 0
	v_lshlrev_b32_e32 v2, 2, v36
	v_lshl_add_u64 v[4:5], s[8:9], 0, v[2:3]
	v_lshlrev_b32_e32 v2, 12, v6
	v_lshl_add_u64 v[32:33], v[4:5], 0, v[2:3]
	v_add_co_u32_e32 v8, vcc, s81, v32
	global_load_dwordx4 v[4:7], v[32:33], off nt
	s_nop 0
	v_addc_co_u32_e32 v9, vcc, 0, v33, vcc
	v_add_co_u32_e32 v12, vcc, s79, v32
	global_load_dwordx4 v[8:11], v[8:9], off nt
	s_nop 0
	v_addc_co_u32_e32 v13, vcc, 0, v33, vcc
	v_add_co_u32_e32 v16, vcc, s80, v32
	global_load_dwordx4 v[12:15], v[12:13], off nt
	s_nop 0
	v_addc_co_u32_e32 v17, vcc, 0, v33, vcc
	v_add_co_u32_e32 v20, vcc, s85, v32
	global_load_dwordx4 v[16:19], v[16:17], off nt
	s_nop 0
	v_addc_co_u32_e32 v21, vcc, 0, v33, vcc
	global_load_dwordx4 v[20:23], v[20:21], off nt
	v_add_co_u32_e32 v24, vcc, s86, v32
	v_add_u32_e32 v2, v44, v47
	s_nop 0
	v_addc_co_u32_e32 v25, vcc, 0, v33, vcc
	global_load_dwordx4 v[24:27], v[24:25], off nt
	v_add_co_u32_e32 v28, vcc, s87, v32
	s_lshl_b32 s7, s7, 1
	s_nop 0
	v_addc_co_u32_e32 v29, vcc, 0, v33, vcc
	global_load_dwordx4 v[28:31], v[28:29], off nt
	v_add_co_u32_e32 v32, vcc, s89, v32
	s_add_u32 s8, s3, s7
	s_nop 0
	v_addc_co_u32_e32 v33, vcc, 0, v33, vcc
	global_load_dwordx4 v[32:35], v[32:33], off nt
	s_addc_u32 s9, s6, 0
	v_readlane_b32 s45, v253, 17
	v_readlane_b32 s46, v253, 18
	v_readlane_b32 s47, v253, 19
	v_readlane_b32 s48, v253, 20
	v_readlane_b32 s49, v253, 21
	v_readlane_b32 s50, v253, 22
	v_readlane_b32 s51, v253, 23
	v_readlane_b32 s52, v253, 24
	v_readlane_b32 s53, v253, 25
	v_readlane_b32 s54, v253, 26
	v_readlane_b32 s55, v253, 27
	v_readlane_b32 s58, v253, 30
	v_readlane_b32 s59, v253, 31
	s_waitcnt vmcnt(0)
	ds_write2_b32 v45, v4, v5 offset1:1
	ds_write2_b32 v45, v6, v7 offset0:2 offset1:3
	v_add_u32_e32 v4, 0x420, v2
	ds_write2_b32 v2, v8, v9 offset1:1
	ds_write2_b32 v2, v10, v11 offset0:2 offset1:3
	ds_write2_b32 v4, v12, v13 offset1:1
	v_add_u32_e32 v4, 0x428, v2
	ds_write2_b32 v4, v14, v15 offset1:1
	v_add_u32_e32 v4, 0x840, v2
	v_add_u32_e32 v2, 0x848, v2
	ds_write2_b32 v2, v18, v19 offset1:1
	v_add_u32_e32 v2, 0x1080, v45
	ds_write2_b32 v4, v16, v17 offset1:1
	ds_write2_b32 v2, v20, v21 offset1:1
	v_add_u32_e32 v2, 0x1088, v45
	ds_write2_b32 v2, v22, v23 offset1:1
	v_add_u32_e32 v2, 0x14a0, v45
	ds_write2_b32 v2, v24, v25 offset1:1
	v_add_u32_e32 v2, 0x14a8, v45
	ds_write2_b32 v2, v26, v27 offset1:1
	v_add_u32_e32 v2, 0x18c0, v45
	ds_write2_b32 v2, v28, v29 offset1:1
	v_add_u32_e32 v2, 0x18c8, v45
	ds_write2_b32 v2, v30, v31 offset1:1
	v_add_u32_e32 v2, 0x1ce0, v45
	ds_write2_b32 v2, v32, v33 offset1:1
	v_add_u32_e32 v2, 0x1ce8, v45
	ds_write2_b32 v2, v34, v35 offset1:1
	s_waitcnt lgkmcnt(0)
	ds_read2_b32 v[10:11], v50 offset0:33 offset1:41
	ds_read2_b32 v[12:13], v50 offset1:8
	v_lshlrev_b32_e32 v2, 1, v38
	ds_read2_b32 v[14:15], v50 offset0:66 offset1:74
	ds_read2_b32 v[16:17], v50 offset0:99 offset1:107
	ds_read2_b32 v[18:19], v50 offset0:132 offset1:140
	ds_read2_b32 v[20:21], v50 offset0:165 offset1:173
	ds_read2_b32 v[22:23], v50 offset0:198 offset1:206
	ds_read2_b32 v[24:25], v50 offset0:231 offset1:239
	v_lshl_add_u64 v[8:9], s[8:9], 0, v[2:3]
	v_or_b32_e32 v2, s2, v39
	v_lshlrev_b32_e32 v2, 11, v2
	v_lshl_add_u64 v[26:27], v[8:9], 0, v[2:3]
	v_or_b32_e32 v2, s2, v46
	s_waitcnt lgkmcnt(0)
	v_cvt_pk_bf16_f32 v4, v12, v10
	v_lshlrev_b32_e32 v2, 11, v2
	v_cvt_pk_bf16_f32 v5, v14, v16
	v_cvt_pk_bf16_f32 v6, v18, v20
	v_cvt_pk_bf16_f32 v7, v22, v24
	global_store_dwordx4 v[26:27], v[4:7], off sc1 nt
	s_nop 1
	v_cvt_pk_bf16_f32 v4, v13, v11
	v_lshl_add_u64 v[10:11], v[8:9], 0, v[2:3]
	v_cvt_pk_bf16_f32 v5, v15, v17
	v_cvt_pk_bf16_f32 v6, v19, v21
	v_cvt_pk_bf16_f32 v7, v23, v25
	global_store_dwordx4 v[10:11], v[4:7], off sc1 nt
	ds_read2_b32 v[10:11], v50 offset0:16 offset1:24
	ds_read2_b32 v[12:13], v50 offset0:49 offset1:57
	ds_read2_b32 v[14:15], v50 offset0:82 offset1:90
	ds_read2_b32 v[16:17], v50 offset0:115 offset1:123
	ds_read2_b32 v[18:19], v50 offset0:148 offset1:156
	ds_read2_b32 v[20:21], v50 offset0:181 offset1:189
	ds_read2_b32 v[22:23], v50 offset0:214 offset1:222
	ds_read2_b32 v[24:25], v50 offset0:247 offset1:255
	v_or_b32_e32 v2, s2, v48
	v_lshlrev_b32_e32 v2, 11, v2
	v_lshl_add_u64 v[26:27], v[8:9], 0, v[2:3]
	v_or_b32_e32 v2, s2, v49
	v_lshlrev_b32_e32 v2, 11, v2
	s_waitcnt lgkmcnt(6)
	v_cvt_pk_bf16_f32 v4, v10, v12
	s_waitcnt lgkmcnt(4)
	v_cvt_pk_bf16_f32 v5, v14, v16
	s_waitcnt lgkmcnt(2)
	v_cvt_pk_bf16_f32 v6, v18, v20
	s_waitcnt lgkmcnt(0)
	v_cvt_pk_bf16_f32 v7, v22, v24
	v_lshl_add_u64 v[8:9], v[8:9], 0, v[2:3]
	global_store_dwordx4 v[26:27], v[4:7], off sc1 nt
	s_nop 1
	v_cvt_pk_bf16_f32 v4, v11, v13
	v_cvt_pk_bf16_f32 v5, v15, v17
	v_cvt_pk_bf16_f32 v6, v19, v21
	v_cvt_pk_bf16_f32 v7, v23, v25
	global_store_dwordx4 v[8:9], v[4:7], off sc1 nt
	s_waitcnt lgkmcnt(0)

; #define LAS __attribute__((address_space(3)))
; __device__ __forceinline__ void transpose_item(const float* W, int K, int N, bf16* WT, int drow0, int kb, int n0, LAS float* scr, int lane) {
;     const int k0 = 64 * kb; const int c4 = 4 * (lane & 7); const bool ok = (n0 + c4) < N;
;     f32x4 v[8];
; #pragma unroll
;     for (int i = 0; i < 8; ++i) { const int kk = 8 * i + (lane >> 3); v[i] = ok ? *(const f32x4*)(W + (size_t)(k0 + kk) * N + n0 + c4) : (f32x4){0.f, 0.f, 0.f, 0.f}; }
; __device__ __forceinline__ void convert_item(const In& I, unsigned char* ws, int it, LAS float* scr, int lane) {
;     ...
;     if (r < 2 * I_FIN) { const int j = r / I_FIN; r -= j * I_FIN; const int kb = r / 104, nb = r % 104;
;         transpose_item(I.fox_w_in + (size_t)j * D * FOX_IN, D, FOX_IN, Wfin + (size_t)j * FOX_IN_PAD * D, 32 * nb, kb, 32 * nb, scr, lane); return; }
.LBB0_429:
	s_andn2_b64 vcc, exec, s[2:3]
	s_cbranch_vccnz .LBB0_447
	s_add_i32 s6, s41, 0x1500
	s_cmpk_gt_u32 s6, 0x67f
	s_cselect_b64 s[10:11], -1, 0
	s_and_b64 s[2:3], s[10:11], exec
	s_cselect_b32 s2, 0xf980, 0
	s_cselect_b32 s3, 0xc10000, 0
	s_add_i32 s6, s6, s2
	s_sext_i32_i16 s2, s6
	s_mulk_i32 s2, 0x4ec5
	s_lshr_b32 s7, s2, 31
	s_ashr_i32 s2, s2, 21
	s_add_i32 s2, s2, s7
	s_mul_i32 s7, s2, 0x68
	v_readlane_b32 s44, v253, 16
	s_sub_i32 s6, s6, s7
	v_readlane_b32 s52, v253, 24
	s_sext_i32_i16 s6, s6
	v_readlane_b32 s53, v253, 25
	s_add_u32 s9, s52, s3
	s_addc_u32 s44, s53, 0
	s_lshl_b32 s6, s6, 5
	s_ashr_i32 s7, s6, 31
	s_lshl_b32 s8, s2, 6
	s_lshl_b64 s[12:13], s[6:7], 2
	v_or_b32_e32 v2, s6, v36
	s_movk_i32 s2, 0xc10
	v_or_b32_e32 v4, s8, v39
	s_add_u32 s12, s9, s12
	v_cmp_gt_i32_e64 s[2:3], s2, v2
	s_addc_u32 s13, s44, s13
	v_lshlrev_b32_e32 v2, 2, v36
	v_mul_i32_i24_e32 v42, 0x3040, v4
	v_lshl_add_u64 v[40:41], s[12:13], 0, v[2:3]
	v_mov_b32_e32 v8, 0
	v_ashrrev_i32_e32 v43, 31, v42
	v_mov_b32_e32 v4, 0
	v_mov_b32_e32 v5, 0
	v_mov_b32_e32 v6, 0
	v_mov_b32_e32 v7, 0
	v_readlane_b32 s45, v253, 17
	v_readlane_b32 s46, v253, 18
	v_readlane_b32 s47, v253, 19
	v_readlane_b32 s48, v253, 20
	v_readlane_b32 s49, v253, 21
	v_readlane_b32 s50, v253, 22
	v_readlane_b32 s51, v253, 23
	v_readlane_b32 s54, v253, 26
	v_readlane_b32 s55, v253, 27
	v_readlane_b32 s56, v253, 28
	v_readlane_b32 s57, v253, 29
	v_readlane_b32 s58, v253, 30
	v_readlane_b32 s59, v253, 31
	s_and_saveexec_b64 s[12:13], s[2:3]
	s_cbranch_execz .LBB0_432
	v_lshl_add_u64 v[4:5], v[40:41], 0, v[42:43]
	global_load_dwordx4 v[4:7], v[4:5], off nt

; #define GAS __attribute__((address_space(1)))
; #define LAS __attribute__((address_space(3)))
; #define LDS_WAIT() asm volatile("s_waitcnt lgkmcnt(0)" ::: "memory")
; __device__ __forceinline__ unsigned pk2(float lo, float hi) { unsigned r; asm("v_cvt_pk_bf16_f32 %0, %1, %2" : "=v"(r) : "v"(lo), "v"(hi)); return r; }
; __device__ __forceinline__ void transpose_item(const float* W, int K, int N, bf16* WT, int drow0, int kb, int n0, LAS float* scr, int lane) {
;     const int k0 = 64 * kb; const int c4 = 4 * (lane & 7); const bool ok = (n0 + c4) < N;
;     f32x4 v[8];
; #pragma unroll
;     for (int i = 0; i < 8; ++i) { const int kk = 8 * i + (lane >> 3); v[i] = ok ? *(const f32x4*)(W + (size_t)(k0 + kk) * N + n0 + c4) : (f32x4){0.f, 0.f, 0.f, 0.f}; }
; #pragma unroll
;     for (int i = 0; i < 8; ++i) { const int kk = 8 * i + (lane >> 3); LAS float* d = scr + kk * 33 + c4; d[0] = v[i][0]; d[1] = v[i][1]; d[2] = v[i][2]; d[3] = v[i][3]; }
;     LDS_WAIT(); asm volatile("" ::: "memory");
;     const int c = lane & 7;
; #pragma unroll
;     for (int j = 0; j < 4; ++j) { const int n = (lane >> 3) + 8 * j; const LAS float* s = scr + (8 * c) * 33 + n;
;         v4u o; o.x = pk2(s[0 * 33], s[1 * 33]); o.y = pk2(s[2 * 33], s[3 * 33]); o.z = pk2(s[4 * 33], s[5 * 33]); o.w = pk2(s[6 * 33], s[7 * 33]);
;         *(GAS v4u*)(WT + (size_t)(drow0 + n) * K + k0 + 8 * c) = o; }
;     LDS_WAIT(); asm volatile("" ::: "memory");
; }
; __device__ __forceinline__ void convert_item(const In& I, unsigned char* ws, int it, LAS float* scr, int lane) {
;     ...
;     if (r < 2 * I_SQ) { const int j = r / I_SQ; r -= j * I_SQ; const int kb = r / 32, nb = r % 32;
;         transpose_item(I.nsa_w_out + (size_t)j * D * D, D, D, Wnout + (size_t)j * D * D, 32 * nb, kb, 32 * nb, scr, lane); return; }
.LBB0_448:
	s_andn2_b64 vcc, exec, s[2:3]
	s_cbranch_vccnz .LBB0_450
	s_add_i32 s2, s41, 0x1900
	s_lshr_b32 s68, s2, 9
	v_readlane_b32 s44, v253, 16
	s_lshl_b64 s[2:3], s[68:69], 22
	v_readlane_b32 s50, v253, 22
	v_readlane_b32 s51, v253, 23
	s_add_u32 s8, s50, s2
	s_addc_u32 s9, s51, s3
	s_lshl_b64 s[6:7], s[68:69], 21
	s_add_u32 s3, s22, s6
	s_addc_u32 s6, s23, s7
	s_and_b32 s2, s42, 0x3e0
	s_add_i32 s7, s0, 0x2200
	s_and_b32 s7, s7, 0x3c0
	s_lshl_b32 s10, s2, 2
	s_add_u32 s8, s8, s10
	v_or_b32_e32 v6, s7, v39
	s_addc_u32 s9, s9, 0
	v_lshlrev_b32_e32 v2, 2, v36
	v_lshl_add_u64 v[4:5], s[8:9], 0, v[2:3]
	v_lshlrev_b32_e32 v2, 12, v6
	v_lshl_add_u64 v[32:33], v[4:5], 0, v[2:3]
	v_add_co_u32_e32 v8, vcc, s81, v32
	global_load_dwordx4 v[4:7], v[32:33], off nt
	s_nop 0
	v_addc_co_u32_e32 v9, vcc, 0, v33, vcc
	v_add_co_u32_e32 v12, vcc, s79, v32
	global_load_dwordx4 v[8:11], v[8:9], off nt
	s_nop 0
	v_addc_co_u32_e32 v13, vcc, 0, v33, vcc
	v_add_co_u32_e32 v16, vcc, s80, v32
	global_load_dwordx4 v[12:15], v[12:13], off nt
	s_nop 0
	v_addc_co_u32_e32 v17, vcc, 0, v33, vcc
	v_add_co_u32_e32 v20, vcc, s85, v32
	global_load_dwordx4 v[16:19], v[16:17], off nt
	s_nop 0
	v_addc_co_u32_e32 v21, vcc, 0, v33, vcc
	global_load_dwordx4 v[20:23], v[20:21], off nt
	v_add_co_u32_e32 v24, vcc, s86, v32
	v_add_u32_e32 v2, v44, v47
	s_nop 0
	v_addc_co_u32_e32 v25, vcc, 0, v33, vcc
	global_load_dwordx4 v[24:27], v[24:25], off nt
	v_add_co_u32_e32 v28, vcc, s87, v32
	s_lshl_b32 s7, s7, 1
	s_nop 0
	v_addc_co_u32_e32 v29, vcc, 0, v33, vcc
	global_load_dwordx4 v[28:31], v[28:29], off nt
	v_add_co_u32_e32 v32, vcc, s89, v32
	s_add_u32 s8, s3, s7
	s_nop 0
	v_addc_co_u32_e32 v33, vcc, 0, v33, vcc
	global_load_dwordx4 v[32:35], v[32:33], off nt
	s_addc_u32 s9, s6, 0
	v_readlane_b32 s45, v253, 17
	v_readlane_b32 s46, v253, 18
	v_readlane_b32 s47, v253, 19
	v_readlane_b32 s48, v253, 20
	v_readlane_b32 s49, v253, 21
	v_readlane_b32 s52, v253, 24
	v_readlane_b32 s53, v253, 25
	v_readlane_b32 s54, v253, 26
	v_readlane_b32 s55, v253, 27
	v_readlane_b32 s56, v253, 28
	v_readlane_b32 s57, v253, 29
	v_readlane_b32 s58, v253, 30
	v_readlane_b32 s59, v253, 31
	s_waitcnt vmcnt(0)
	ds_write2_b32 v45, v4, v5 offset1:1
	ds_write2_b32 v45, v6, v7 offset0:2 offset1:3
	v_add_u32_e32 v4, 0x420, v2
	ds_write2_b32 v2, v8, v9 offset1:1
	ds_write2_b32 v2, v10, v11 offset0:2 offset1:3
	ds_write2_b32 v4, v12, v13 offset1:1
	v_add_u32_e32 v4, 0x428, v2
	ds_write2_b32 v4, v14, v15 offset1:1
	v_add_u32_e32 v4, 0x840, v2
	v_add_u32_e32 v2, 0x848, v2
	ds_write2_b32 v2, v18, v19 offset1:1
	v_add_u32_e32 v2, 0x1080, v45
	ds_write2_b32 v4, v16, v17 offset1:1
	ds_write2_b32 v2, v20, v21 offset1:1
	v_add_u32_e32 v2, 0x1088, v45
	ds_write2_b32 v2, v22, v23 offset1:1
	v_add_u32_e32 v2, 0x14a0, v45
	ds_write2_b32 v2, v24, v25 offset1:1
	v_add_u32_e32 v2, 0x14a8, v45
	ds_write2_b32 v2, v26, v27 offset1:1
	v_add_u32_e32 v2, 0x18c0, v45
	ds_write2_b32 v2, v28, v29 offset1:1
	v_add_u32_e32 v2, 0x18c8, v45
	ds_write2_b32 v2, v30, v31 offset1:1
	v_add_u32_e32 v2, 0x1ce0, v45
	ds_write2_b32 v2, v32, v33 offset1:1
	v_add_u32_e32 v2, 0x1ce8, v45
	ds_write2_b32 v2, v34, v35 offset1:1
	s_waitcnt lgkmcnt(0)
	ds_read2_b32 v[10:11], v50 offset0:33 offset1:41
	ds_read2_b32 v[12:13], v50 offset1:8
	v_lshlrev_b32_e32 v2, 1, v38
	ds_read2_b32 v[14:15], v50 offset0:66 offset1:74
	ds_read2_b32 v[16:17], v50 offset0:99 offset1:107
	ds_read2_b32 v[18:19], v50 offset0:132 offset1:140
	ds_read2_b32 v[20:21], v50 offset0:165 offset1:173
	ds_read2_b32 v[22:23], v50 offset0:198 offset1:206
	ds_read2_b32 v[24:25], v50 offset0:231 offset1:239
	v_lshl_add_u64 v[8:9], s[8:9], 0, v[2:3]
	v_or_b32_e32 v2, s2, v39
	v_lshlrev_b32_e32 v2, 11, v2
	v_lshl_add_u64 v[26:27], v[8:9], 0, v[2:3]
	v_or_b32_e32 v2, s2, v46
	s_waitcnt lgkmcnt(0)
	v_cvt_pk_bf16_f32 v4, v12, v10
	v_lshlrev_b32_e32 v2, 11, v2
	v_cvt_pk_bf16_f32 v5, v14, v16
	v_cvt_pk_bf16_f32 v6, v18, v20
	v_cvt_pk_bf16_f32 v7, v22, v24
	global_store_dwordx4 v[26:27], v[4:7], off sc1 nt
	s_nop 1
	v_cvt_pk_bf16_f32 v4, v13, v11
	v_lshl_add_u64 v[10:11], v[8:9], 0, v[2:3]
	v_cvt_pk_bf16_f32 v5, v15, v17
	v_cvt_pk_bf16_f32 v6, v19, v21
	v_cvt_pk_bf16_f32 v7, v23, v25
	global_store_dwordx4 v[10:11], v[4:7], off sc1 nt
	ds_read2_b32 v[10:11], v50 offset0:16 offset1:24
	ds_read2_b32 v[12:13], v50 offset0:49 offset1:57
	ds_read2_b32 v[14:15], v50 offset0:82 offset1:90
	ds_read2_b32 v[16:17], v50 offset0:115 offset1:123
	ds_read2_b32 v[18:19], v50 offset0:148 offset1:156
	ds_read2_b32 v[20:21], v50 offset0:181 offset1:189
	ds_read2_b32 v[22:23], v50 offset0:214 offset1:222
	ds_read2_b32 v[24:25], v50 offset0:247 offset1:255
	v_or_b32_e32 v2, s2, v48
	v_lshlrev_b32_e32 v2, 11, v2
	v_lshl_add_u64 v[26:27], v[8:9], 0, v[2:3]
	v_or_b32_e32 v2, s2, v49
	v_lshlrev_b32_e32 v2, 11, v2
	s_waitcnt lgkmcnt(6)
	v_cvt_pk_bf16_f32 v4, v10, v12
	s_waitcnt lgkmcnt(4)
	v_cvt_pk_bf16_f32 v5, v14, v16
	s_waitcnt lgkmcnt(2)
	v_cvt_pk_bf16_f32 v6, v18, v20
	s_waitcnt lgkmcnt(0)
	v_cvt_pk_bf16_f32 v7, v22, v24
	v_lshl_add_u64 v[8:9], v[8:9], 0, v[2:3]
	global_store_dwordx4 v[26:27], v[4:7], off sc1 nt
	s_nop 1
	v_cvt_pk_bf16_f32 v4, v11, v13
	v_cvt_pk_bf16_f32 v5, v15, v17
	v_cvt_pk_bf16_f32 v6, v19, v21
	v_cvt_pk_bf16_f32 v7, v23, v25
	global_store_dwordx4 v[8:9], v[4:7], off sc1 nt
	s_waitcnt lgkmcnt(0)

; #define LAS __attribute__((address_space(3)))
; __device__ __forceinline__ void transpose_item(const float* W, int K, int N, bf16* WT, int drow0, int kb, int n0, LAS float* scr, int lane) {
;     const int k0 = 64 * kb; const int c4 = 4 * (lane & 7); const bool ok = (n0 + c4) < N;
;     f32x4 v[8];
; #pragma unroll
;     for (int i = 0; i < 8; ++i) { const int kk = 8 * i + (lane >> 3); v[i] = ok ? *(const f32x4*)(W + (size_t)(k0 + kk) * N + n0 + c4) : (f32x4){0.f, 0.f, 0.f, 0.f}; }
; __device__ __forceinline__ void convert_item(const In& I, unsigned char* ws, int it, LAS float* scr, int lane) {
;     ...
;     if (r < 2 * I_NIN) { const int j = r / I_NIN; r -= j * I_NIN; const int kb = r / 88, nb = r % 88;
;         transpose_item(I.nsa_w_in + (size_t)j * D * NSA_IN, D, NSA_IN, Wnin + (size_t)j * NSA_IN_PAD * D, 32 * nb, kb, 32 * nb, scr, lane); return; }
.LBB0_451:
	s_andn2_b64 vcc, exec, s[2:3]
	s_cbranch_vccnz .LBB0_469
	s_add_i32 s6, s41, 0x2400
	s_cmpk_gt_u32 s6, 0x57f
	s_cselect_b64 s[10:11], -1, 0
	s_and_b64 s[2:3], s[10:11], exec
	s_cselect_b32 s2, 0xfa80, 0
	s_cselect_b32 s3, 0xa30000, 0
	s_add_i32 s6, s6, s2
	s_sext_i32_i16 s2, s6
	s_mulk_i32 s2, 0xba3
	s_lshr_b32 s7, s2, 31
	s_ashr_i32 s2, s2, 18
	s_add_i32 s2, s2, s7
	s_mul_i32 s7, s2, 0x58
	v_readlane_b32 s44, v253, 0
	s_sub_i32 s6, s6, s7
	v_readlane_b32 s56, v253, 12
	s_sext_i32_i16 s6, s6
	v_readlane_b32 s57, v253, 13
	s_add_u32 s9, s56, s3
	s_addc_u32 s44, s57, 0
	s_lshl_b32 s6, s6, 5
	s_ashr_i32 s7, s6, 31
	s_lshl_b32 s8, s2, 6
	s_lshl_b64 s[12:13], s[6:7], 2
	v_or_b32_e32 v2, s6, v36
	s_movk_i32 s2, 0xa30
	s_add_u32 s12, s9, s12
	v_cmp_gt_i32_e64 s[2:3], s2, v2
	s_addc_u32 s13, s44, s13
	v_lshlrev_b32_e32 v2, 2, v36
	v_or_b32_e32 v42, s8, v39
	v_lshl_add_u64 v[40:41], s[12:13], 0, v[2:3]
	v_mov_b32_e32 v8, 0
	v_mov_b32_e32 v4, 0
	v_mov_b32_e32 v5, 0
	v_mov_b32_e32 v6, 0
	v_mov_b32_e32 v7, 0
	v_readlane_b32 s45, v253, 1
	v_readlane_b32 s46, v253, 2
	v_readlane_b32 s47, v253, 3
	v_readlane_b32 s48, v253, 4
	v_readlane_b32 s49, v253, 5
	v_readlane_b32 s50, v253, 6
	v_readlane_b32 s51, v253, 7
	v_readlane_b32 s52, v253, 8
	v_readlane_b32 s53, v253, 9
	v_readlane_b32 s54, v253, 10
	v_readlane_b32 s55, v253, 11
	v_readlane_b32 s58, v253, 14
	v_readlane_b32 s59, v253, 15
	s_and_saveexec_b64 s[12:13], s[2:3]
	s_cbranch_execz .LBB0_454
	v_mul_i32_i24_e32 v4, 0x28c0, v42
	v_ashrrev_i32_e32 v5, 31, v4
	v_lshl_add_u64 v[4:5], v[40:41], 0, v[4:5]
	global_load_dwordx4 v[4:7], v[4:5], off nt

; #define GAS __attribute__((address_space(1)))
; #define LAS __attribute__((address_space(3)))
; #define LDS_WAIT() asm volatile("s_waitcnt lgkmcnt(0)" ::: "memory")
; __device__ __forceinline__ unsigned pk2(float lo, float hi) { unsigned r; asm("v_cvt_pk_bf16_f32 %0, %1, %2" : "=v"(r) : "v"(lo), "v"(hi)); return r; }
; __device__ __forceinline__ void transpose_item(const float* W, int K, int N, bf16* WT, int drow0, int kb, int n0, LAS float* scr, int lane) {
;     const int k0 = 64 * kb; const int c4 = 4 * (lane & 7); const bool ok = (n0 + c4) < N;
;     f32x4 v[8];
; #pragma unroll
;     for (int i = 0; i < 8; ++i) { const int kk = 8 * i + (lane >> 3); v[i] = ok ? *(const f32x4*)(W + (size_t)(k0 + kk) * N + n0 + c4) : (f32x4){0.f, 0.f, 0.f, 0.f}; }
; #pragma unroll
;     for (int i = 0; i < 8; ++i) { const int kk = 8 * i + (lane >> 3); LAS float* d = scr + kk * 33 + c4; d[0] = v[i][0]; d[1] = v[i][1]; d[2] = v[i][2]; d[3] = v[i][3]; }
;     LDS_WAIT(); asm volatile("" ::: "memory");
;     const int c = lane & 7;
; #pragma unroll
;     for (int j = 0; j < 4; ++j) { const int n = (lane >> 3) + 8 * j; const LAS float* s = scr + (8 * c) * 33 + n;
;         v4u o; o.x = pk2(s[0 * 33], s[1 * 33]); o.y = pk2(s[2 * 33], s[3 * 33]); o.z = pk2(s[4 * 33], s[5 * 33]); o.w = pk2(s[6 * 33], s[7 * 33]);
;         *(GAS v4u*)(WT + (size_t)(drow0 + n) * K + k0 + 8 * c) = o; }
;     LDS_WAIT(); asm volatile("" ::: "memory");
; }
; __device__ __forceinline__ void convert_item(const In& I, unsigned char* ws, int it, LAS float* scr, int lane) {
;     ...
;     if (r < T0) { const int f = r / I_FFN; r -= f * I_FFN;
;         if (r < 2 * I_G) { const int up = r >= I_G; r -= up * I_G; const int kb = r / 88, nb = r % 88;
;             transpose_item((up ? I.w_up : I.w_gate) + (size_t)f * D * FF, D, FF, Wgu + (size_t)f * NGU * D, 256 * (nb >> 2) + 32 * (nb & 3) + 128 * up, kb, 32 * nb, scr, lane); }
;         else { r -= 2 * I_G; const int kb = r / 32, nb = r % 32; transpose_item(I.w_down + (size_t)f * FF * D, FF, D, Wd + (size_t)f * D * FF, 32 * nb, kb, 32 * nb, scr, lane); }
.LBB0_470:
	s_andn2_b64 vcc, exec, s[2:3]
	s_cbranch_vccnz .LBB0_415
	s_mul_hi_i32 s2, s43, 0x3e0f83e1
	s_lshr_b32 s3, s2, 31
	s_ashr_i32 s6, s2, 10
	s_add_i32 s6, s6, s3
	s_mul_i32 s2, s6, 0xffffef80
	s_add_i32 s7, s41, s2
	s_add_i32 s7, s7, 0xa800
	s_cmpk_gt_i32 s7, 0xaff
	s_mov_b64 s[2:3], -1
	s_cbranch_scc0 .LBB0_473
	v_readlane_b32 s44, v253, 0
	s_mul_i32 s3, s6, 0xb00000
	v_readlane_b32 s52, v253, 8
	s_mul_hi_i32 s2, s6, 0xb00000
	v_readlane_b32 s53, v253, 9
	s_add_u32 s9, s52, s3
	s_addc_u32 s11, s53, s2
	s_mul_i32 s3, s6, 0x580000
	s_mul_hi_i32 s2, s6, 0x580000
	s_add_u32 s3, s1, s3
	s_mul_i32 s10, s6, 0xffffdf00
	s_addc_u32 s8, s19, s2
	s_add_i32 s10, s0, s10
	s_add_i32 s10, s10, 0x14000
	s_and_b32 s2, s42, 0x3e0
	s_andn2_b32 s10, s10, 63
	s_add_i32 s68, s10, 0xffffea00
	s_lshl_b32 s10, s2, 2
	v_or_b32_e32 v32, s68, v39
	s_add_u32 s10, s9, s10
	s_addc_u32 s11, s11, 0
	v_lshlrev_b32_e32 v2, 2, v36
	v_ashrrev_i32_e32 v33, 31, v32
	v_or_b32_e32 v8, 8, v32
	v_or_b32_e32 v12, 16, v32
	v_lshl_add_u64 v[34:35], s[10:11], 0, v[2:3]
	v_lshlrev_b64 v[4:5], 12, v[32:33]
	v_ashrrev_i32_e32 v9, 31, v8
	v_ashrrev_i32_e32 v13, 31, v12
	v_lshl_add_u64 v[4:5], v[34:35], 0, v[4:5]
	v_lshlrev_b64 v[8:9], 12, v[8:9]
	v_lshlrev_b64 v[12:13], 12, v[12:13]
	v_or_b32_e32 v16, 24, v32
	global_load_dwordx4 v[4:7], v[4:5], off nt
	v_lshl_add_u64 v[8:9], v[34:35], 0, v[8:9]
	v_lshl_add_u64 v[12:13], v[34:35], 0, v[12:13]
	v_ashrrev_i32_e32 v17, 31, v16
	v_or_b32_e32 v20, 32, v32
	global_load_dwordx4 v[8:11], v[8:9], off nt
	v_lshlrev_b64 v[16:17], 12, v[16:17]
	global_load_dwordx4 v[12:15], v[12:13], off nt
	v_ashrrev_i32_e32 v21, 31, v20
	v_lshl_add_u64 v[16:17], v[34:35], 0, v[16:17]
	v_lshlrev_b64 v[20:21], 12, v[20:21]
	v_or_b32_e32 v24, 40, v32
	global_load_dwordx4 v[16:19], v[16:17], off nt
	v_lshl_add_u64 v[20:21], v[34:35], 0, v[20:21]
	v_ashrrev_i32_e32 v25, 31, v24
	global_load_dwordx4 v[20:23], v[20:21], off nt
	v_lshlrev_b64 v[24:25], 12, v[24:25]
	v_or_b32_e32 v28, 48, v32
	v_lshl_add_u64 v[24:25], v[34:35], 0, v[24:25]
	v_ashrrev_i32_e32 v29, 31, v28
	global_load_dwordx4 v[24:27], v[24:25], off nt
	v_lshlrev_b64 v[28:29], 12, v[28:29]
	v_or_b32_e32 v32, 56, v32
	v_lshl_add_u64 v[28:29], v[34:35], 0, v[28:29]
	v_ashrrev_i32_e32 v33, 31, v32
	global_load_dwordx4 v[28:31], v[28:29], off nt
	v_lshlrev_b64 v[32:33], 12, v[32:33]
	v_lshl_add_u64 v[32:33], v[34:35], 0, v[32:33]
	global_load_dwordx4 v[32:35], v[32:33], off nt
	v_add_u32_e32 v2, v44, v47
	s_lshl_b64 s[10:11], s[68:69], 1
	s_add_u32 s10, s3, s10
	s_addc_u32 s11, s8, s11
	v_readlane_b32 s45, v253, 1
	v_readlane_b32 s46, v253, 2
	v_readlane_b32 s47, v253, 3
	v_readlane_b32 s48, v253, 4
	v_readlane_b32 s49, v253, 5
	v_readlane_b32 s50, v253, 6
	v_readlane_b32 s51, v253, 7
	v_readlane_b32 s54, v253, 10
	v_readlane_b32 s55, v253, 11
	v_readlane_b32 s56, v253, 12
	v_readlane_b32 s57, v253, 13
	v_readlane_b32 s58, v253, 14
	v_readlane_b32 s59, v253, 15
	s_waitcnt vmcnt(0)
	ds_write2_b32 v45, v4, v5 offset1:1
	ds_write2_b32 v45, v6, v7 offset0:2 offset1:3
	v_add_u32_e32 v4, 0x420, v2
	ds_write2_b32 v2, v8, v9 offset1:1
	ds_write2_b32 v2, v10, v11 offset0:2 offset1:3
	ds_write2_b32 v4, v12, v13 offset1:1
	v_add_u32_e32 v4, 0x428, v2
	ds_write2_b32 v4, v14, v15 offset1:1
	v_add_u32_e32 v4, 0x840, v2
	v_add_u32_e32 v2, 0x848, v2
	ds_write2_b32 v2, v18, v19 offset1:1
	v_add_u32_e32 v2, 0x1080, v45
	ds_write2_b32 v4, v16, v17 offset1:1
	ds_write2_b32 v2, v20, v21 offset1:1
	v_add_u32_e32 v2, 0x1088, v45
	ds_write2_b32 v2, v22, v23 offset1:1
	v_add_u32_e32 v2, 0x14a0, v45
	ds_write2_b32 v2, v24, v25 offset1:1
	v_add_u32_e32 v2, 0x14a8, v45
	ds_write2_b32 v2, v26, v27 offset1:1
	v_add_u32_e32 v2, 0x18c0, v45
	ds_write2_b32 v2, v28, v29 offset1:1
	v_add_u32_e32 v2, 0x18c8, v45
	ds_write2_b32 v2, v30, v31 offset1:1
	v_add_u32_e32 v2, 0x1ce0, v45
	ds_write2_b32 v2, v32, v33 offset1:1
	v_add_u32_e32 v2, 0x1ce8, v45
	ds_write2_b32 v2, v34, v35 offset1:1
	s_waitcnt lgkmcnt(0)
	ds_read2_b32 v[10:11], v50 offset0:33 offset1:41
	ds_read2_b32 v[12:13], v50 offset1:8
	v_lshlrev_b32_e32 v2, 1, v38
	ds_read2_b32 v[14:15], v50 offset0:66 offset1:74
	ds_read2_b32 v[16:17], v50 offset0:99 offset1:107
	ds_read2_b32 v[18:19], v50 offset0:132 offset1:140
	ds_read2_b32 v[20:21], v50 offset0:165 offset1:173
	ds_read2_b32 v[22:23], v50 offset0:198 offset1:206
	ds_read2_b32 v[24:25], v50 offset0:231 offset1:239
	v_lshl_add_u64 v[8:9], s[10:11], 0, v[2:3]
	v_or_b32_e32 v2, s2, v39
	v_mul_u32_u24_e32 v2, 0x1600, v2
	v_lshl_add_u64 v[26:27], v[8:9], 0, v[2:3]
	v_or_b32_e32 v2, s2, v46
	s_waitcnt lgkmcnt(0)
	v_cvt_pk_bf16_f32 v4, v12, v10
	v_mul_u32_u24_e32 v2, 0x1600, v2
	v_cvt_pk_bf16_f32 v5, v14, v16
	v_cvt_pk_bf16_f32 v6, v18, v20
	v_cvt_pk_bf16_f32 v7, v22, v24
	global_store_dwordx4 v[26:27], v[4:7], off sc1 nt
	s_nop 1
	v_cvt_pk_bf16_f32 v4, v13, v11
	v_lshl_add_u64 v[10:11], v[8:9], 0, v[2:3]
	v_cvt_pk_bf16_f32 v5, v15, v17
	v_cvt_pk_bf16_f32 v6, v19, v21
	v_cvt_pk_bf16_f32 v7, v23, v25
	global_store_dwordx4 v[10:11], v[4:7], off sc1 nt
	ds_read2_b32 v[10:11], v50 offset0:16 offset1:24
	ds_read2_b32 v[12:13], v50 offset0:49 offset1:57
	ds_read2_b32 v[14:15], v50 offset0:82 offset1:90
	ds_read2_b32 v[16:17], v50 offset0:115 offset1:123
	ds_read2_b32 v[18:19], v50 offset0:148 offset1:156
	ds_read2_b32 v[20:21], v50 offset0:181 offset1:189
	ds_read2_b32 v[22:23], v50 offset0:214 offset1:222
	ds_read2_b32 v[24:25], v50 offset0:247 offset1:255
	v_or_b32_e32 v2, s2, v48
	v_mul_u32_u24_e32 v2, 0x1600, v2
	v_lshl_add_u64 v[26:27], v[8:9], 0, v[2:3]
	v_or_b32_e32 v2, s2, v49
	v_mul_u32_u24_e32 v2, 0x1600, v2
	s_waitcnt lgkmcnt(6)
	v_cvt_pk_bf16_f32 v4, v10, v12
	s_waitcnt lgkmcnt(4)
	v_cvt_pk_bf16_f32 v5, v14, v16
	s_waitcnt lgkmcnt(2)
	v_cvt_pk_bf16_f32 v6, v18, v20
	s_waitcnt lgkmcnt(0)
	v_cvt_pk_bf16_f32 v7, v22, v24
	v_lshl_add_u64 v[8:9], v[8:9], 0, v[2:3]
	global_store_dwordx4 v[26:27], v[4:7], off sc1 nt
	s_mov_b64 s[2:3], 0
	s_nop 0
	v_cvt_pk_bf16_f32 v4, v11, v13
	v_cvt_pk_bf16_f32 v5, v15, v17
	v_cvt_pk_bf16_f32 v6, v19, v21
	v_cvt_pk_bf16_f32 v7, v23, v25
	global_store_dwordx4 v[8:9], v[4:7], off sc1 nt
	s_waitcnt lgkmcnt(0)
; #define GAS __attribute__((address_space(1)))
; #define LAS __attribute__((address_space(3)))
; #define LDS_WAIT() asm volatile("s_waitcnt lgkmcnt(0)" ::: "memory")
; __device__ __forceinline__ unsigned pk2(float lo, float hi) { unsigned r; asm("v_cvt_pk_bf16_f32 %0, %1, %2" : "=v"(r) : "v"(lo), "v"(hi)); return r; }
; __device__ __forceinline__ void transpose_item(const float* W, int K, int N, bf16* WT, int drow0, int kb, int n0, LAS float* scr, int lane) {
;     const int k0 = 64 * kb; const int c4 = 4 * (lane & 7); const bool ok = (n0 + c4) < N;
;     f32x4 v[8];
; #pragma unroll
;     for (int i = 0; i < 8; ++i) { const int kk = 8 * i + (lane >> 3); v[i] = ok ? *(const f32x4*)(W + (size_t)(k0 + kk) * N + n0 + c4) : (f32x4){0.f, 0.f, 0.f, 0.f}; }
; #pragma unroll
;     for (int i = 0; i < 8; ++i) { const int kk = 8 * i + (lane >> 3); LAS float* d = scr + kk * 33 + c4; d[0] = v[i][0]; d[1] = v[i][1]; d[2] = v[i][2]; d[3] = v[i][3]; }
;     LDS_WAIT(); asm volatile("" ::: "memory");
;     const int c = lane & 7;
; #pragma unroll
;     for (int j = 0; j < 4; ++j) { const int n = (lane >> 3) + 8 * j; const LAS float* s = scr + (8 * c) * 33 + n;
;         v4u o; o.x = pk2(s[0 * 33], s[1 * 33]); o.y = pk2(s[2 * 33], s[3 * 33]); o.z = pk2(s[4 * 33], s[5 * 33]); o.w = pk2(s[6 * 33], s[7 * 33]);
;         *(GAS v4u*)(WT + (size_t)(drow0 + n) * K + k0 + 8 * c) = o; }
;     LDS_WAIT(); asm volatile("" ::: "memory");
; }
; __device__ __forceinline__ void convert_item(const In& I, unsigned char* ws, int it, LAS float* scr, int lane) {
;     ...
;     if (r < T0) { const int f = r / I_FFN; r -= f * I_FFN;
;         if (r < 2 * I_G) { const int up = r >= I_G; r -= up * I_G; const int kb = r / 88, nb = r % 88;
;             transpose_item((up ? I.w_up : I.w_gate) + (size_t)f * D * FF, D, FF, Wgu + (size_t)f * NGU * D, 256 * (nb >> 2) + 32 * (nb & 3) + 128 * up, kb, 32 * nb, scr, lane); }
.LBB0_473:
	s_andn2_b64 vcc, exec, s[2:3]
	s_cbranch_vccnz .LBB0_415
	s_cmpk_gt_i32 s7, 0x57f
	v_readlane_b32 s44, v253, 0
	s_cselect_b32 s2, 0xfffffa80, 0
	s_mul_i32 s3, s6, 0x1080
	v_readlane_b32 s48, v253, 4
	v_readlane_b32 s49, v253, 5
	v_readlane_b32 s50, v253, 6
	v_readlane_b32 s51, v253, 7
	s_cselect_b32 s9, 0x80, 0
	s_cselect_b32 s7, s50, s48
	s_cselect_b32 s8, s51, s49
	s_sub_i32 s2, s2, s3
	s_add_i32 s2, s41, s2
	s_add_i32 s2, s2, 0xa800
	s_mul_hi_i32 s3, s2, 0x2e8ba2e9
	s_lshr_b32 s10, s3, 31
	s_ashr_i32 s3, s3, 4
	s_add_i32 s3, s3, s10
	s_mul_i32 s10, s3, 0x58
	s_sub_i32 s2, s2, s10
	s_mul_hi_i32 s10, s6, 0xb00000
	s_mul_i32 s6, s6, 0xb00000
	s_add_u32 s12, s7, s6
	s_addc_u32 s13, s8, s10
	s_add_u32 s7, s28, s6
	s_addc_u32 s8, s29, s10
	s_lshl_b32 s10, s2, 5
	s_lshl_b32 s6, s2, 6
	s_and_b32 s2, s10, 0x60
	s_and_b32 s6, s6, 0xffffff00
	s_or_b32 s2, s2, s9
	s_ashr_i32 s11, s10, 31
	s_or_b32 s6, s2, s6
	s_lshl_b32 s2, s3, 6
	s_lshl_b64 s[10:11], s[10:11], 2
	s_add_u32 s10, s12, s10
	v_or_b32_e32 v34, s2, v39
	s_addc_u32 s11, s13, s11
	v_lshlrev_b32_e32 v2, 2, v36
	v_lshl_add_u64 v[32:33], s[10:11], 0, v[2:3]
	s_movk_i32 s3, 0x2c00
	v_or_b32_e32 v2, 8, v34
	v_mad_i64_i32 v[4:5], s[10:11], v34, s3, v[32:33]
	v_mad_i64_i32 v[8:9], s[10:11], v2, s3, v[32:33]
	v_or_b32_e32 v2, 16, v34
	global_load_dwordx4 v[4:7], v[4:5], off nt
	v_mad_i64_i32 v[12:13], s[10:11], v2, s3, v[32:33]
	global_load_dwordx4 v[8:11], v[8:9], off nt
	v_or_b32_e32 v2, 24, v34
	global_load_dwordx4 v[12:15], v[12:13], off nt
	v_mad_i64_i32 v[16:17], s[10:11], v2, s3, v[32:33]
	v_or_b32_e32 v2, 32, v34
	global_load_dwordx4 v[16:19], v[16:17], off nt
	v_mad_i64_i32 v[20:21], s[10:11], v2, s3, v[32:33]
	global_load_dwordx4 v[20:23], v[20:21], off nt
	v_or_b32_e32 v2, 40, v34
	v_mad_i64_i32 v[24:25], s[10:11], v2, s3, v[32:33]
	global_load_dwordx4 v[24:27], v[24:25], off nt
	v_or_b32_e32 v2, 48, v34
	v_mad_i64_i32 v[28:29], s[10:11], v2, s3, v[32:33]
	global_load_dwordx4 v[28:31], v[28:29], off nt
	v_or_b32_e32 v2, 56, v34
	v_mad_i64_i32 v[32:33], s[10:11], v2, s3, v[32:33]
	global_load_dwordx4 v[32:35], v[32:33], off nt
	v_add_u32_e32 v2, v44, v47
	s_ashr_i32 s3, s2, 31
	s_lshl_b64 s[2:3], s[2:3], 1
	s_add_u32 s2, s7, s2
	s_addc_u32 s3, s8, s3
	v_readlane_b32 s45, v253, 1
	v_readlane_b32 s46, v253, 2
	v_readlane_b32 s47, v253, 3
	v_readlane_b32 s52, v253, 8
	v_readlane_b32 s53, v253, 9
	v_readlane_b32 s54, v253, 10
	v_readlane_b32 s55, v253, 11
	v_readlane_b32 s56, v253, 12
	v_readlane_b32 s57, v253, 13
	v_readlane_b32 s58, v253, 14
	v_readlane_b32 s59, v253, 15
	s_waitcnt vmcnt(0)
	ds_write2_b32 v45, v4, v5 offset1:1
	ds_write2_b32 v45, v6, v7 offset0:2 offset1:3
	v_add_u32_e32 v4, 0x420, v2
	ds_write2_b32 v2, v8, v9 offset1:1
	ds_write2_b32 v2, v10, v11 offset0:2 offset1:3
	ds_write2_b32 v4, v12, v13 offset1:1
	v_add_u32_e32 v4, 0x428, v2
	ds_write2_b32 v4, v14, v15 offset1:1
	v_add_u32_e32 v4, 0x840, v2
	v_add_u32_e32 v2, 0x848, v2
	ds_write2_b32 v2, v18, v19 offset1:1
	v_add_u32_e32 v2, 0x1080, v45
	ds_write2_b32 v2, v20, v21 offset1:1
	v_add_u32_e32 v2, 0x1088, v45
	ds_write2_b32 v2, v22, v23 offset1:1
	v_add_u32_e32 v2, 0x14a0, v45
	ds_write2_b32 v2, v24, v25 offset1:1
	v_add_u32_e32 v2, 0x14a8, v45
	ds_write2_b32 v2, v26, v27 offset1:1
	v_add_u32_e32 v2, 0x18c0, v45
	ds_write2_b32 v2, v28, v29 offset1:1
	v_add_u32_e32 v2, 0x18c8, v45
	ds_write2_b32 v2, v30, v31 offset1:1
	v_add_u32_e32 v2, 0x1ce0, v45
	ds_write2_b32 v2, v32, v33 offset1:1
	v_add_u32_e32 v2, 0x1ce8, v45
	ds_write2_b32 v4, v16, v17 offset1:1
	ds_write2_b32 v2, v34, v35 offset1:1
	s_waitcnt lgkmcnt(0)
	ds_read2_b32 v[10:11], v50 offset0:33 offset1:41
	ds_read2_b32 v[12:13], v50 offset1:8
	ds_read2_b32 v[14:15], v50 offset0:66 offset1:74
	ds_read2_b32 v[16:17], v50 offset0:99 offset1:107
	ds_read2_b32 v[18:19], v50 offset0:132 offset1:140
	ds_read2_b32 v[20:21], v50 offset0:165 offset1:173
	ds_read2_b32 v[22:23], v50 offset0:198 offset1:206
	ds_read2_b32 v[24:25], v50 offset0:231 offset1:239
	v_or_b32_e32 v26, s6, v39
	v_lshlrev_b32_e32 v2, 1, v38
	v_ashrrev_i32_e32 v27, 31, v26
	v_lshl_add_u64 v[8:9], s[2:3], 0, v[2:3]
	v_lshlrev_b64 v[26:27], 11, v[26:27]
	s_waitcnt lgkmcnt(0)
	v_cvt_pk_bf16_f32 v4, v12, v10
	v_lshl_add_u64 v[26:27], v[8:9], 0, v[26:27]
	v_or_b32_e32 v10, s6, v46
	v_cvt_pk_bf16_f32 v5, v14, v16
	v_cvt_pk_bf16_f32 v6, v18, v20
	v_cvt_pk_bf16_f32 v7, v22, v24
	global_store_dwordx4 v[26:27], v[4:7], off sc1 nt
	v_or_b32_e32 v26, s6, v48
	v_ashrrev_i32_e32 v27, 31, v26
	v_cvt_pk_bf16_f32 v4, v13, v11
	v_ashrrev_i32_e32 v11, 31, v10
	v_lshlrev_b64 v[10:11], 11, v[10:11]
	v_lshl_add_u64 v[10:11], v[8:9], 0, v[10:11]
	v_cvt_pk_bf16_f32 v5, v15, v17
	v_cvt_pk_bf16_f32 v6, v19, v21
	v_cvt_pk_bf16_f32 v7, v23, v25
	global_store_dwordx4 v[10:11], v[4:7], off sc1 nt
	ds_read2_b32 v[10:11], v50 offset0:16 offset1:24
	ds_read2_b32 v[12:13], v50 offset0:49 offset1:57
	ds_read2_b32 v[14:15], v50 offset0:82 offset1:90
	ds_read2_b32 v[16:17], v50 offset0:115 offset1:123
	ds_read2_b32 v[18:19], v50 offset0:148 offset1:156
	ds_read2_b32 v[20:21], v50 offset0:181 offset1:189
	ds_read2_b32 v[22:23], v50 offset0:214 offset1:222
	ds_read2_b32 v[24:25], v50 offset0:247 offset1:255
	v_lshlrev_b64 v[26:27], 11, v[26:27]
	s_waitcnt lgkmcnt(6)
	v_cvt_pk_bf16_f32 v4, v10, v12
	v_lshl_add_u64 v[26:27], v[8:9], 0, v[26:27]
	v_or_b32_e32 v10, s6, v49
	s_waitcnt lgkmcnt(4)
	v_cvt_pk_bf16_f32 v5, v14, v16
	s_waitcnt lgkmcnt(2)
	v_cvt_pk_bf16_f32 v6, v18, v20
	s_waitcnt lgkmcnt(0)
	v_cvt_pk_bf16_f32 v7, v22, v24
	global_store_dwordx4 v[26:27], v[4:7], off sc1 nt
	s_nop 1
	v_cvt_pk_bf16_f32 v4, v11, v13
	v_ashrrev_i32_e32 v11, 31, v10
	v_lshlrev_b64 v[10:11], 11, v[10:11]
	v_lshl_add_u64 v[8:9], v[8:9], 0, v[10:11]
	v_cvt_pk_bf16_f32 v5, v15, v17
	v_cvt_pk_bf16_f32 v6, v19, v21
	v_cvt_pk_bf16_f32 v7, v23, v25
	global_store_dwordx4 v[8:9], v[4:7], off sc1 nt
	s_waitcnt lgkmcnt(0)
	s_branch .LBB0_415

; #define GAS __attribute__((address_space(1)))
; __device__ __forceinline__ void transpose_item(const float* W, int K, int N, bf16* WT, int drow0, int kb, int n0, LAS float* scr, int lane) {
;     const int k0 = 64 * kb; const int c4 = 4 * (lane & 7); const bool ok = (n0 + c4) < N;
;     f32x4 v[8];
; #pragma unroll
;     for (int i = 0; i < 8; ++i) { const int kk = 8 * i + (lane >> 3); v[i] = ok ? *(const f32x4*)(W + (size_t)(k0 + kk) * N + n0 + c4) : (f32x4){0.f, 0.f, 0.f, 0.f}; }
; #pragma unroll
;     for (int i = 0; i < 8; ++i) { const int kk = 8 * i + (lane >> 3); LAS float* d = scr + kk * 33 + c4; d[0] = v[i][0]; d[1] = v[i][1]; d[2] = v[i][2]; d[3] = v[i][3]; }
;     LDS_WAIT(); asm volatile("" ::: "memory");
;     const int c = lane & 7;
; #pragma unroll
;     for (int j = 0; j < 4; ++j) { const int n = (lane >> 3) + 8 * j; const LAS float* s = scr + (8 * c) * 33 + n;
;         v4u o; o.x = pk2(s[0 * 33], s[1 * 33]); o.y = pk2(s[2 * 33], s[3 * 33]); o.z = pk2(s[4 * 33], s[5 * 33]); o.w = pk2(s[6 * 33], s[7 * 33]);
;         *(GAS v4u*)(WT + (size_t)(drow0 + n) * K + k0 + 8 * c) = o; }
;     LDS_WAIT(); asm volatile("" ::: "memory");
; }
; __device__ __forceinline__ void convert_item(const In& I, unsigned char* ws, int it, LAS float* scr, int lane) {
;     ...
;     int r = it;
;     if (r < T0) { const int f = r / I_FFN; r -= f * I_FFN;
;         if (r < 2 * I_G) { const int up = r >= I_G; r -= up * I_G; const int kb = r / 88, nb = r % 88;
;             transpose_item((up ? I.w_up : I.w_gate) + (size_t)f * D * FF, D, FF, Wgu + (size_t)f * NGU * D, 256 * (nb >> 2) + 32 * (nb & 3) + 128 * up, kb, 32 * nb, scr, lane); }
;         else { r -= 2 * I_G; const int kb = r / 32, nb = r % 32; transpose_item(I.w_down + (size_t)f * FF * D, FF, D, Wd + (size_t)f * D * FF, 32 * nb, kb, 32 * nb, scr, lane); }
;         return; }
;     r -= T0;
;     if (r < 2 * I_NIN) { const int j = r / I_NIN; r -= j * I_NIN; const int kb = r / 88, nb = r % 88;
;         transpose_item(I.nsa_w_in + (size_t)j * D * NSA_IN, D, NSA_IN, Wnin + (size_t)j * NSA_IN_PAD * D, 32 * nb, kb, 32 * nb, scr, lane); return; }
;     r -= 2 * I_NIN;
;     if (r < 2 * I_SQ) { const int j = r / I_SQ; r -= j * I_SQ; const int kb = r / 32, nb = r % 32;
;         transpose_item(I.nsa_w_out + (size_t)j * D * D, D, D, Wnout + (size_t)j * D * D, 32 * nb, kb, 32 * nb, scr, lane); return; }
;     r -= 2 * I_SQ;
.LBB0_478:
	s_add_i32 s42, s18, 0xa800
	s_cmp_gt_i32 s42, 0x83ff
	s_mov_b64 s[2:3], -1
	s_cbranch_scc0 .LBB0_532
	s_cmpk_gt_u32 s42, 0x8eff
	s_cbranch_scc0 .LBB0_513
	s_cmpk_gt_u32 s42, 0x92ff
	s_cbranch_scc0 .LBB0_510
	s_cmpk_gt_u32 s42, 0x9fff
	s_cbranch_scc0 .LBB0_491
	s_cmpk_gt_u32 s42, 0xa3ff
	s_cbranch_scc0 .LBB0_488
	s_cmpk_gt_u32 s42, 0xa7ff
	s_cbranch_scc0 .LBB0_485
	s_lshr_b32 s68, s18, 3
	v_readlane_b32 s44, v253, 16
	s_lshl_b64 s[2:3], s[68:69], 16
	v_readlane_b32 s48, v253, 20
	v_readlane_b32 s49, v253, 21
	s_add_u32 s6, s48, s2
	s_addc_u32 s7, s49, s3
	s_lshl_b64 s[2:3], s[68:69], 15
	s_add_u32 s8, s34, s2
	s_addc_u32 s3, s35, s3
	s_and_b32 s2, s40, 32
	s_and_b32 s9, s40, 0xc0
	s_lshl_b32 s10, s2, 2
	s_add_u32 s6, s6, s10
	v_or_b32_e32 v6, s9, v39
	s_addc_u32 s7, s7, 0
	v_lshlrev_b32_e32 v2, 2, v36
	v_lshl_add_u64 v[4:5], s[6:7], 0, v[2:3]
	v_lshlrev_b32_e32 v2, 8, v6
	v_lshl_add_u64 v[28:29], v[4:5], 0, v[2:3]
	global_load_dwordx4 v[4:7], v[28:29], off nt
	global_load_dwordx4 v[8:11], v[28:29], off offset:2048 nt
	v_add_co_u32_e32 v16, vcc, s84, v28
	s_movk_i32 s6, 0x3000
	s_nop 0
	v_addc_co_u32_e32 v17, vcc, 0, v29, vcc
	v_add_co_u32_e32 v24, vcc, s74, v28
	v_add_u32_e32 v2, v44, v45
	s_nop 0
	v_addc_co_u32_e32 v25, vcc, 0, v29, vcc
	global_load_dwordx4 v[12:15], v[24:25], off offset:-4096 nt
	s_nop 0
	global_load_dwordx4 v[16:19], v[16:17], off offset:2048 nt
	s_nop 0
	global_load_dwordx4 v[20:23], v[24:25], off nt
	s_nop 0
	global_load_dwordx4 v[24:27], v[24:25], off offset:2048 nt
	v_add_co_u32_e32 v32, vcc, s6, v28
	s_lshl_b32 s6, s9, 1
	s_nop 0
	v_addc_co_u32_e32 v33, vcc, 0, v29, vcc
	global_load_dwordx4 v[28:31], v[32:33], off nt
	s_nop 0
	global_load_dwordx4 v[32:35], v[32:33], off offset:2048 nt
	s_add_u32 s6, s8, s6
	s_addc_u32 s7, s3, 0
	v_readlane_b32 s45, v253, 17
	v_readlane_b32 s46, v253, 18
	v_readlane_b32 s47, v253, 19
	v_readlane_b32 s50, v253, 22
	v_readlane_b32 s51, v253, 23
	v_readlane_b32 s52, v253, 24
	v_readlane_b32 s53, v253, 25
	v_readlane_b32 s54, v253, 26
	v_readlane_b32 s55, v253, 27
	v_readlane_b32 s56, v253, 28
	v_readlane_b32 s57, v253, 29
	v_readlane_b32 s58, v253, 30
	v_readlane_b32 s59, v253, 31
	s_waitcnt vmcnt(0)
	ds_write2_b32 v2, v4, v5 offset1:1
	ds_write2_b32 v2, v6, v7 offset0:2 offset1:3
	v_add_u32_e32 v4, 0x420, v2
	ds_write2_b32 v4, v8, v9 offset1:1
	v_add_u32_e32 v4, 0x428, v2
	ds_write2_b32 v4, v10, v11 offset1:1
	v_add_u32_e32 v4, 0x840, v2
	ds_write2_b32 v4, v12, v13 offset1:1
	v_add_u32_e32 v4, 0x848, v2
	ds_write2_b32 v4, v14, v15 offset1:1
	v_add_u32_e32 v4, 0xc60, v2
	ds_write2_b32 v4, v16, v17 offset1:1
	v_add_u32_e32 v4, 0xc68, v2
	ds_write2_b32 v4, v18, v19 offset1:1
	v_add_u32_e32 v4, 0x1080, v2
	ds_write2_b32 v4, v20, v21 offset1:1
	v_add_u32_e32 v4, 0x1088, v2
	ds_write2_b32 v4, v22, v23 offset1:1
	v_add_u32_e32 v4, 0x14a0, v2
	ds_write2_b32 v4, v24, v25 offset1:1
	v_add_u32_e32 v4, 0x14a8, v2
	ds_write2_b32 v4, v26, v27 offset1:1
	v_add_u32_e32 v4, 0x18c0, v2
	ds_write2_b32 v4, v28, v29 offset1:1
	v_add_u32_e32 v4, 0x18c8, v2
	ds_write2_b32 v4, v30, v31 offset1:1
	v_add_u32_e32 v4, 0x1ce0, v2
	v_add_u32_e32 v2, 0x1ce8, v2
	ds_write2_b32 v4, v32, v33 offset1:1
	ds_write2_b32 v2, v34, v35 offset1:1
	s_waitcnt lgkmcnt(0)
	ds_read2_b32 v[10:11], v49 offset0:33 offset1:41
	ds_read2_b32 v[12:13], v49 offset1:8
	v_lshlrev_b32_e32 v2, 1, v38
	ds_read2_b32 v[14:15], v49 offset0:66 offset1:74
	ds_read2_b32 v[16:17], v49 offset0:99 offset1:107
	ds_read2_b32 v[18:19], v49 offset0:132 offset1:140
	ds_read2_b32 v[20:21], v49 offset0:165 offset1:173
	ds_read2_b32 v[22:23], v49 offset0:198 offset1:206
	ds_read2_b32 v[24:25], v49 offset0:231 offset1:239
	v_lshl_add_u64 v[4:5], s[6:7], 0, v[2:3]
	v_or_b32_e32 v2, s2, v39
	v_lshlrev_b32_e32 v2, 9, v2
	v_lshl_add_u64 v[26:27], v[4:5], 0, v[2:3]
	v_or_b32_e32 v2, s2, v46
	s_waitcnt lgkmcnt(0)
	v_cvt_pk_bf16_f32 v6, v12, v10
	v_lshlrev_b32_e32 v2, 9, v2
	v_cvt_pk_bf16_f32 v7, v14, v16
	v_cvt_pk_bf16_f32 v8, v18, v20
	v_cvt_pk_bf16_f32 v9, v22, v24
	global_store_dwordx4 v[26:27], v[6:9], off sc1 nt
	s_nop 1
	v_cvt_pk_bf16_f32 v6, v13, v11
	v_lshl_add_u64 v[10:11], v[4:5], 0, v[2:3]
	v_cvt_pk_bf16_f32 v7, v15, v17
	v_cvt_pk_bf16_f32 v8, v19, v21
	v_cvt_pk_bf16_f32 v9, v23, v25
	global_store_dwordx4 v[10:11], v[6:9], off sc1 nt
	ds_read2_b32 v[10:11], v49 offset0:16 offset1:24
	ds_read2_b32 v[12:13], v49 offset0:49 offset1:57
	ds_read2_b32 v[14:15], v49 offset0:82 offset1:90
	ds_read2_b32 v[16:17], v49 offset0:115 offset1:123
	ds_read2_b32 v[18:19], v49 offset0:148 offset1:156
	ds_read2_b32 v[20:21], v49 offset0:181 offset1:189
	ds_read2_b32 v[22:23], v49 offset0:214 offset1:222
	ds_read2_b32 v[24:25], v49 offset0:247 offset1:255
	v_or_b32_e32 v2, s2, v47
	v_lshlrev_b32_e32 v2, 9, v2
	v_lshl_add_u64 v[26:27], v[4:5], 0, v[2:3]
	v_or_b32_e32 v2, s2, v48
	v_lshlrev_b32_e32 v2, 9, v2
	s_waitcnt lgkmcnt(6)
	v_cvt_pk_bf16_f32 v6, v10, v12
	s_waitcnt lgkmcnt(4)
	v_cvt_pk_bf16_f32 v7, v14, v16
	s_waitcnt lgkmcnt(2)
	v_cvt_pk_bf16_f32 v8, v18, v20
	s_waitcnt lgkmcnt(0)
	v_cvt_pk_bf16_f32 v9, v22, v24
	v_lshl_add_u64 v[4:5], v[4:5], 0, v[2:3]
	global_store_dwordx4 v[26:27], v[6:9], off sc1 nt
	s_mov_b64 s[2:3], 0
	s_nop 0
	v_cvt_pk_bf16_f32 v6, v11, v13
	v_cvt_pk_bf16_f32 v7, v15, v17
	v_cvt_pk_bf16_f32 v8, v19, v21
	v_cvt_pk_bf16_f32 v9, v23, v25
	global_store_dwordx4 v[4:5], v[6:9], off sc1 nt
	s_waitcnt lgkmcnt(0)
; #define GAS __attribute__((address_space(1)))
; #define LAS __attribute__((address_space(3)))
; #define LDS_WAIT() asm volatile("s_waitcnt lgkmcnt(0)" ::: "memory")
; __device__ __forceinline__ unsigned pk2(float lo, float hi) { unsigned r; asm("v_cvt_pk_bf16_f32 %0, %1, %2" : "=v"(r) : "v"(lo), "v"(hi)); return r; }
; __device__ __forceinline__ void transpose_item(const float* W, int K, int N, bf16* WT, int drow0, int kb, int n0, LAS float* scr, int lane) {
;     const int k0 = 64 * kb; const int c4 = 4 * (lane & 7); const bool ok = (n0 + c4) < N;
;     f32x4 v[8];
; #pragma unroll
;     for (int i = 0; i < 8; ++i) { const int kk = 8 * i + (lane >> 3); v[i] = ok ? *(const f32x4*)(W + (size_t)(k0 + kk) * N + n0 + c4) : (f32x4){0.f, 0.f, 0.f, 0.f}; }
; #pragma unroll
;     for (int i = 0; i < 8; ++i) { const int kk = 8 * i + (lane >> 3); LAS float* d = scr + kk * 33 + c4; d[0] = v[i][0]; d[1] = v[i][1]; d[2] = v[i][2]; d[3] = v[i][3]; }
;     LDS_WAIT(); asm volatile("" ::: "memory");
;     const int c = lane & 7;
; #pragma unroll
;     for (int j = 0; j < 4; ++j) { const int n = (lane >> 3) + 8 * j; const LAS float* s = scr + (8 * c) * 33 + n;
;         v4u o; o.x = pk2(s[0 * 33], s[1 * 33]); o.y = pk2(s[2 * 33], s[3 * 33]); o.z = pk2(s[4 * 33], s[5 * 33]); o.w = pk2(s[6 * 33], s[7 * 33]);
;         *(GAS v4u*)(WT + (size_t)(drow0 + n) * K + k0 + 8 * c) = o; }
;     LDS_WAIT(); asm volatile("" ::: "memory");
; }
; __device__ __forceinline__ void convert_item(const In& I, unsigned char* ws, int it, LAS float* scr, int lane) {
;     ...
;     if (r < 4 * I_W1) { const int jk = r / I_W1; r -= jk * I_W1; const int kb = r / 8, nb = r % 8;
;         transpose_item(I.nsa_w1 + (size_t)jk * 2048 * 256, 2048, 256, W1t + (size_t)jk * 256 * 2048, 32 * nb, kb, 32 * nb, scr, lane); return; }
.LBB0_485:
	s_andn2_b64 vcc, exec, s[2:3]
	s_cbranch_vccnz .LBB0_487
	s_add_i32 s2, s18, 0x400
	s_lshr_b32 s68, s2, 8
	s_lshl_b64 s[2:3], s[68:69], 21
	v_readlane_b32 s44, v253, 16
	v_readlane_b32 s45, v253, 17
	s_add_u32 s6, s44, s2
	s_addc_u32 s7, s45, s3
	s_lshl_b64 s[2:3], s[68:69], 20
	s_add_u32 s8, s31, s2
	s_addc_u32 s3, s33, s3
	s_and_b32 s2, s40, 0xe0
	s_and_b32 s9, s39, 0x7c0
	s_lshl_b32 s10, s2, 2
	s_add_u32 s6, s6, s10
	v_or_b32_e32 v6, s9, v39
	s_addc_u32 s7, s7, 0
	v_lshlrev_b32_e32 v2, 2, v36
	v_lshl_add_u64 v[4:5], s[6:7], 0, v[2:3]
	v_lshlrev_b32_e32 v2, 10, v6
	v_lshl_add_u64 v[32:33], v[4:5], 0, v[2:3]
	v_add_co_u32_e32 v8, vcc, s74, v32
	global_load_dwordx4 v[4:7], v[32:33], off nt
	s_nop 0
	v_addc_co_u32_e32 v9, vcc, 0, v33, vcc
	s_movk_i32 s6, 0x4000
	global_load_dwordx4 v[8:11], v[8:9], off nt
	v_add_co_u32_e32 v12, vcc, s6, v32
	s_movk_i32 s6, 0x6000
	s_nop 0
	v_addc_co_u32_e32 v13, vcc, 0, v33, vcc
	global_load_dwordx4 v[12:15], v[12:13], off nt
	v_add_co_u32_e32 v16, vcc, s6, v32
	s_mov_b32 s6, 0xa000
	s_nop 0
	v_addc_co_u32_e32 v17, vcc, 0, v33, vcc
	global_load_dwordx4 v[16:19], v[16:17], off nt
	v_add_co_u32_e32 v20, vcc, s81, v32
	v_add_u32_e32 v2, v44, v45
	s_nop 0
	v_addc_co_u32_e32 v21, vcc, 0, v33, vcc
	global_load_dwordx4 v[20:23], v[20:21], off nt
	v_add_co_u32_e32 v24, vcc, s6, v32
	s_mov_b32 s6, 0xc000
	s_nop 0
	v_addc_co_u32_e32 v25, vcc, 0, v33, vcc
	global_load_dwordx4 v[24:27], v[24:25], off nt
	v_add_co_u32_e32 v28, vcc, s6, v32
	s_mov_b32 s6, 0xe000
	s_nop 0
	v_addc_co_u32_e32 v29, vcc, 0, v33, vcc
	global_load_dwordx4 v[28:31], v[28:29], off nt
	v_add_co_u32_e32 v32, vcc, s6, v32
	s_lshl_b32 s6, s9, 1
	s_nop 0
	v_addc_co_u32_e32 v33, vcc, 0, v33, vcc
	global_load_dwordx4 v[32:35], v[32:33], off nt
	s_add_u32 s6, s8, s6
	s_addc_u32 s7, s3, 0
	v_readlane_b32 s46, v253, 18
	v_readlane_b32 s47, v253, 19
	v_readlane_b32 s48, v253, 20
	v_readlane_b32 s49, v253, 21
	v_readlane_b32 s50, v253, 22
	v_readlane_b32 s51, v253, 23
	v_readlane_b32 s52, v253, 24
	v_readlane_b32 s53, v253, 25
	v_readlane_b32 s54, v253, 26
	v_readlane_b32 s55, v253, 27
	v_readlane_b32 s56, v253, 28
	v_readlane_b32 s57, v253, 29
	v_readlane_b32 s58, v253, 30
	v_readlane_b32 s59, v253, 31
	s_waitcnt vmcnt(0)
	ds_write2_b32 v2, v4, v5 offset1:1
	ds_write2_b32 v2, v6, v7 offset0:2 offset1:3
	v_add_u32_e32 v4, 0x420, v2
	ds_write2_b32 v4, v8, v9 offset1:1
	v_add_u32_e32 v4, 0x428, v2
	ds_write2_b32 v4, v10, v11 offset1:1
	v_add_u32_e32 v4, 0x840, v2
	ds_write2_b32 v4, v12, v13 offset1:1
	v_add_u32_e32 v4, 0x848, v2
	ds_write2_b32 v4, v14, v15 offset1:1
	v_add_u32_e32 v4, 0xc60, v2
	ds_write2_b32 v4, v16, v17 offset1:1
	v_add_u32_e32 v4, 0xc68, v2
	ds_write2_b32 v4, v18, v19 offset1:1
	v_add_u32_e32 v4, 0x1080, v2
	ds_write2_b32 v4, v20, v21 offset1:1
	v_add_u32_e32 v4, 0x1088, v2
	ds_write2_b32 v4, v22, v23 offset1:1
	v_add_u32_e32 v4, 0x14a0, v2
	ds_write2_b32 v4, v24, v25 offset1:1
	v_add_u32_e32 v4, 0x14a8, v2
	ds_write2_b32 v4, v26, v27 offset1:1
	v_add_u32_e32 v4, 0x18c0, v2
	ds_write2_b32 v4, v28, v29 offset1:1
	v_add_u32_e32 v4, 0x18c8, v2
	ds_write2_b32 v4, v30, v31 offset1:1
	v_add_u32_e32 v4, 0x1ce0, v2
	v_add_u32_e32 v2, 0x1ce8, v2
	ds_write2_b32 v4, v32, v33 offset1:1
	ds_write2_b32 v2, v34, v35 offset1:1
	s_waitcnt lgkmcnt(0)
	ds_read2_b32 v[10:11], v49 offset0:33 offset1:41
	ds_read2_b32 v[12:13], v49 offset1:8
	v_lshlrev_b32_e32 v2, 1, v38
	ds_read2_b32 v[14:15], v49 offset0:66 offset1:74
	ds_read2_b32 v[16:17], v49 offset0:99 offset1:107
	ds_read2_b32 v[18:19], v49 offset0:132 offset1:140
	ds_read2_b32 v[20:21], v49 offset0:165 offset1:173
	ds_read2_b32 v[22:23], v49 offset0:198 offset1:206
	ds_read2_b32 v[24:25], v49 offset0:231 offset1:239
	v_lshl_add_u64 v[8:9], s[6:7], 0, v[2:3]
	v_or_b32_e32 v2, s2, v39
	v_lshlrev_b32_e32 v2, 12, v2
	v_lshl_add_u64 v[26:27], v[8:9], 0, v[2:3]
	v_or_b32_e32 v2, s2, v46
	s_waitcnt lgkmcnt(0)
	v_cvt_pk_bf16_f32 v4, v12, v10
	v_lshlrev_b32_e32 v2, 12, v2
	v_cvt_pk_bf16_f32 v5, v14, v16
	v_cvt_pk_bf16_f32 v6, v18, v20
	v_cvt_pk_bf16_f32 v7, v22, v24
	global_store_dwordx4 v[26:27], v[4:7], off sc1 nt
	s_nop 1
	v_cvt_pk_bf16_f32 v4, v13, v11
	v_lshl_add_u64 v[10:11], v[8:9], 0, v[2:3]
	v_cvt_pk_bf16_f32 v5, v15, v17
	v_cvt_pk_bf16_f32 v6, v19, v21
	v_cvt_pk_bf16_f32 v7, v23, v25
	global_store_dwordx4 v[10:11], v[4:7], off sc1 nt
	ds_read2_b32 v[10:11], v49 offset0:16 offset1:24
	ds_read2_b32 v[12:13], v49 offset0:49 offset1:57
	ds_read2_b32 v[14:15], v49 offset0:82 offset1:90
	ds_read2_b32 v[16:17], v49 offset0:115 offset1:123
	ds_read2_b32 v[18:19], v49 offset0:148 offset1:156
	ds_read2_b32 v[20:21], v49 offset0:181 offset1:189
	ds_read2_b32 v[22:23], v49 offset0:214 offset1:222
	ds_read2_b32 v[24:25], v49 offset0:247 offset1:255
	v_or_b32_e32 v2, s2, v47
	v_lshlrev_b32_e32 v2, 12, v2
	v_lshl_add_u64 v[26:27], v[8:9], 0, v[2:3]
	v_or_b32_e32 v2, s2, v48
	v_lshlrev_b32_e32 v2, 12, v2
	s_waitcnt lgkmcnt(6)
	v_cvt_pk_bf16_f32 v4, v10, v12
	s_waitcnt lgkmcnt(4)
	v_cvt_pk_bf16_f32 v5, v14, v16
	s_waitcnt lgkmcnt(2)
	v_cvt_pk_bf16_f32 v6, v18, v20
	s_waitcnt lgkmcnt(0)
	v_cvt_pk_bf16_f32 v7, v22, v24
	v_lshl_add_u64 v[8:9], v[8:9], 0, v[2:3]
	global_store_dwordx4 v[26:27], v[4:7], off sc1 nt
	s_nop 1
	v_cvt_pk_bf16_f32 v4, v11, v13
	v_cvt_pk_bf16_f32 v5, v15, v17
	v_cvt_pk_bf16_f32 v6, v19, v21
	v_cvt_pk_bf16_f32 v7, v23, v25
	global_store_dwordx4 v[8:9], v[4:7], off sc1 nt
	s_waitcnt lgkmcnt(0)

; #define GAS __attribute__((address_space(1)))
; #define LAS __attribute__((address_space(3)))
; #define LDS_WAIT() asm volatile("s_waitcnt lgkmcnt(0)" ::: "memory")
; __device__ __forceinline__ unsigned pk2(float lo, float hi) { unsigned r; asm("v_cvt_pk_bf16_f32 %0, %1, %2" : "=v"(r) : "v"(lo), "v"(hi)); return r; }
; __device__ __forceinline__ void transpose_item(const float* W, int K, int N, bf16* WT, int drow0, int kb, int n0, LAS float* scr, int lane) {
;     const int k0 = 64 * kb; const int c4 = 4 * (lane & 7); const bool ok = (n0 + c4) < N;
;     f32x4 v[8];
; #pragma unroll
;     for (int i = 0; i < 8; ++i) { const int kk = 8 * i + (lane >> 3); v[i] = ok ? *(const f32x4*)(W + (size_t)(k0 + kk) * N + n0 + c4) : (f32x4){0.f, 0.f, 0.f, 0.f}; }
; #pragma unroll
;     for (int i = 0; i < 8; ++i) { const int kk = 8 * i + (lane >> 3); LAS float* d = scr + kk * 33 + c4; d[0] = v[i][0]; d[1] = v[i][1]; d[2] = v[i][2]; d[3] = v[i][3]; }
;     LDS_WAIT(); asm volatile("" ::: "memory");
;     const int c = lane & 7;
; #pragma unroll
;     for (int j = 0; j < 4; ++j) { const int n = (lane >> 3) + 8 * j; const LAS float* s = scr + (8 * c) * 33 + n;
;         v4u o; o.x = pk2(s[0 * 33], s[1 * 33]); o.y = pk2(s[2 * 33], s[3 * 33]); o.z = pk2(s[4 * 33], s[5 * 33]); o.w = pk2(s[6 * 33], s[7 * 33]);
;         *(GAS v4u*)(WT + (size_t)(drow0 + n) * K + k0 + 8 * c) = o; }
;     LDS_WAIT(); asm volatile("" ::: "memory");
; }
; __device__ __forceinline__ void convert_item(const In& I, unsigned char* ws, int it, LAS float* scr, int lane) {
;     ...
;     if (r < 2 * I_SQ) { const int j = r / I_SQ; r -= j * I_SQ; const int kb = r / 32, nb = r % 32;
;         transpose_item(I.fox_w_out + (size_t)j * D * D, D, D, Wfout + (size_t)j * D * D, 32 * nb, kb, 32 * nb, scr, lane); return; }
.LBB0_488:
	s_andn2_b64 vcc, exec, s[2:3]
	s_cbranch_vccnz .LBB0_490
	s_add_i32 s2, s18, 0x800
	s_lshr_b32 s68, s2, 9
	v_readlane_b32 s44, v253, 16
	s_lshl_b64 s[2:3], s[68:69], 22
	v_readlane_b32 s56, v253, 28
	v_readlane_b32 s57, v253, 29
	s_add_u32 s6, s56, s2
	s_addc_u32 s7, s57, s3
	s_lshl_b64 s[2:3], s[68:69], 21
	s_add_u32 s8, s26, s2
	s_addc_u32 s3, s27, s3
	s_and_b32 s2, s40, 0x3e0
	s_add_i32 s9, s41, 0x14800
	s_and_b32 s9, s9, 0x3c0
	s_lshl_b32 s10, s2, 2
	s_add_u32 s6, s6, s10
	v_or_b32_e32 v6, s9, v39
	s_addc_u32 s7, s7, 0
	v_lshlrev_b32_e32 v2, 2, v36
	v_lshl_add_u64 v[4:5], s[6:7], 0, v[2:3]
	v_lshlrev_b32_e32 v2, 12, v6
	v_lshl_add_u64 v[32:33], v[4:5], 0, v[2:3]
	v_add_co_u32_e32 v8, vcc, s81, v32
	global_load_dwordx4 v[4:7], v[32:33], off nt
	s_nop 0
	v_addc_co_u32_e32 v9, vcc, 0, v33, vcc
	global_load_dwordx4 v[8:11], v[8:9], off nt
	v_add_co_u32_e32 v12, vcc, s79, v32
	v_add_u32_e32 v2, v44, v45
	s_nop 0
	v_addc_co_u32_e32 v13, vcc, 0, v33, vcc
	global_load_dwordx4 v[12:15], v[12:13], off nt
	v_add_co_u32_e32 v16, vcc, s80, v32
	s_lshl_b32 s6, s9, 1
	s_nop 0
	v_addc_co_u32_e32 v17, vcc, 0, v33, vcc
	global_load_dwordx4 v[16:19], v[16:17], off nt
	v_add_co_u32_e32 v20, vcc, s85, v32
	s_add_u32 s6, s8, s6
	s_nop 0
	v_addc_co_u32_e32 v21, vcc, 0, v33, vcc
	global_load_dwordx4 v[20:23], v[20:21], off nt
	v_add_co_u32_e32 v24, vcc, s86, v32
	s_addc_u32 s7, s3, 0
	s_nop 0
	v_addc_co_u32_e32 v25, vcc, 0, v33, vcc
	global_load_dwordx4 v[24:27], v[24:25], off nt
	v_add_co_u32_e32 v28, vcc, s87, v32
	v_readlane_b32 s45, v253, 17
	s_nop 0
	v_addc_co_u32_e32 v29, vcc, 0, v33, vcc
	global_load_dwordx4 v[28:31], v[28:29], off nt
	v_add_co_u32_e32 v32, vcc, s89, v32
	v_readlane_b32 s46, v253, 18
	s_nop 0
	v_addc_co_u32_e32 v33, vcc, 0, v33, vcc
	global_load_dwordx4 v[32:35], v[32:33], off nt
	v_readlane_b32 s47, v253, 19
	v_readlane_b32 s48, v253, 20
	v_readlane_b32 s49, v253, 21
	v_readlane_b32 s50, v253, 22
	v_readlane_b32 s51, v253, 23
	v_readlane_b32 s52, v253, 24
	v_readlane_b32 s53, v253, 25
	v_readlane_b32 s54, v253, 26
	v_readlane_b32 s55, v253, 27
	v_readlane_b32 s58, v253, 30
	v_readlane_b32 s59, v253, 31
	s_waitcnt vmcnt(0)
	ds_write2_b32 v2, v4, v5 offset1:1
	ds_write2_b32 v2, v6, v7 offset0:2 offset1:3
	v_add_u32_e32 v4, 0x420, v2
	ds_write2_b32 v4, v8, v9 offset1:1
	v_add_u32_e32 v4, 0x428, v2
	ds_write2_b32 v4, v10, v11 offset1:1
	v_add_u32_e32 v4, 0x840, v2
	ds_write2_b32 v4, v12, v13 offset1:1
	v_add_u32_e32 v4, 0x848, v2
	ds_write2_b32 v4, v14, v15 offset1:1
	v_add_u32_e32 v4, 0xc60, v2
	ds_write2_b32 v4, v16, v17 offset1:1
	v_add_u32_e32 v4, 0xc68, v2
	ds_write2_b32 v4, v18, v19 offset1:1
	v_add_u32_e32 v4, 0x1080, v2
	ds_write2_b32 v4, v20, v21 offset1:1
	v_add_u32_e32 v4, 0x1088, v2
	ds_write2_b32 v4, v22, v23 offset1:1
	v_add_u32_e32 v4, 0x14a0, v2
	ds_write2_b32 v4, v24, v25 offset1:1
	v_add_u32_e32 v4, 0x14a8, v2
	ds_write2_b32 v4, v26, v27 offset1:1
	v_add_u32_e32 v4, 0x18c0, v2
	ds_write2_b32 v4, v28, v29 offset1:1
	v_add_u32_e32 v4, 0x18c8, v2
	ds_write2_b32 v4, v30, v31 offset1:1
	v_add_u32_e32 v4, 0x1ce0, v2
	v_add_u32_e32 v2, 0x1ce8, v2
	ds_write2_b32 v4, v32, v33 offset1:1
	ds_write2_b32 v2, v34, v35 offset1:1
	s_waitcnt lgkmcnt(0)
	ds_read2_b32 v[10:11], v49 offset0:33 offset1:41
	ds_read2_b32 v[12:13], v49 offset1:8
	v_lshlrev_b32_e32 v2, 1, v38
	ds_read2_b32 v[14:15], v49 offset0:66 offset1:74
	ds_read2_b32 v[16:17], v49 offset0:99 offset1:107
	ds_read2_b32 v[18:19], v49 offset0:132 offset1:140
	ds_read2_b32 v[20:21], v49 offset0:165 offset1:173
	ds_read2_b32 v[22:23], v49 offset0:198 offset1:206
	ds_read2_b32 v[24:25], v49 offset0:231 offset1:239
	v_lshl_add_u64 v[8:9], s[6:7], 0, v[2:3]
	v_or_b32_e32 v2, s2, v39
	v_lshlrev_b32_e32 v2, 11, v2
	v_lshl_add_u64 v[26:27], v[8:9], 0, v[2:3]
	v_or_b32_e32 v2, s2, v46
	s_waitcnt lgkmcnt(0)
	v_cvt_pk_bf16_f32 v4, v12, v10
	v_lshlrev_b32_e32 v2, 11, v2
	v_cvt_pk_bf16_f32 v5, v14, v16
	v_cvt_pk_bf16_f32 v6, v18, v20
	v_cvt_pk_bf16_f32 v7, v22, v24
	global_store_dwordx4 v[26:27], v[4:7], off sc1 nt
	s_nop 1
	v_cvt_pk_bf16_f32 v4, v13, v11
	v_lshl_add_u64 v[10:11], v[8:9], 0, v[2:3]
	v_cvt_pk_bf16_f32 v5, v15, v17
	v_cvt_pk_bf16_f32 v6, v19, v21
	v_cvt_pk_bf16_f32 v7, v23, v25
	global_store_dwordx4 v[10:11], v[4:7], off sc1 nt
	ds_read2_b32 v[10:11], v49 offset0:16 offset1:24
	ds_read2_b32 v[12:13], v49 offset0:49 offset1:57
	ds_read2_b32 v[14:15], v49 offset0:82 offset1:90
	ds_read2_b32 v[16:17], v49 offset0:115 offset1:123
	ds_read2_b32 v[18:19], v49 offset0:148 offset1:156
	ds_read2_b32 v[20:21], v49 offset0:181 offset1:189
	ds_read2_b32 v[22:23], v49 offset0:214 offset1:222
	ds_read2_b32 v[24:25], v49 offset0:247 offset1:255
	v_or_b32_e32 v2, s2, v47
	v_lshlrev_b32_e32 v2, 11, v2
	v_lshl_add_u64 v[26:27], v[8:9], 0, v[2:3]
	v_or_b32_e32 v2, s2, v48
	v_lshlrev_b32_e32 v2, 11, v2
	s_waitcnt lgkmcnt(6)
	v_cvt_pk_bf16_f32 v4, v10, v12
	s_waitcnt lgkmcnt(4)
	v_cvt_pk_bf16_f32 v5, v14, v16
	s_waitcnt lgkmcnt(2)
	v_cvt_pk_bf16_f32 v6, v18, v20
	s_waitcnt lgkmcnt(0)
	v_cvt_pk_bf16_f32 v7, v22, v24
	v_lshl_add_u64 v[8:9], v[8:9], 0, v[2:3]
	global_store_dwordx4 v[26:27], v[4:7], off sc1 nt
	s_nop 1
	v_cvt_pk_bf16_f32 v4, v11, v13
	v_cvt_pk_bf16_f32 v5, v15, v17
	v_cvt_pk_bf16_f32 v6, v19, v21
	v_cvt_pk_bf16_f32 v7, v23, v25
	global_store_dwordx4 v[8:9], v[4:7], off sc1 nt
	s_waitcnt lgkmcnt(0)

; #define LAS __attribute__((address_space(3)))
; __device__ __forceinline__ void transpose_item(const float* W, int K, int N, bf16* WT, int drow0, int kb, int n0, LAS float* scr, int lane) {
;     const int k0 = 64 * kb; const int c4 = 4 * (lane & 7); const bool ok = (n0 + c4) < N;
;     f32x4 v[8];
; #pragma unroll
;     for (int i = 0; i < 8; ++i) { const int kk = 8 * i + (lane >> 3); v[i] = ok ? *(const f32x4*)(W + (size_t)(k0 + kk) * N + n0 + c4) : (f32x4){0.f, 0.f, 0.f, 0.f}; }
; __device__ __forceinline__ void convert_item(const In& I, unsigned char* ws, int it, LAS float* scr, int lane) {
;     ...
;     if (r < 2 * I_FIN) { const int j = r / I_FIN; r -= j * I_FIN; const int kb = r / 104, nb = r % 104;
;         transpose_item(I.fox_w_in + (size_t)j * D * FOX_IN, D, FOX_IN, Wfin + (size_t)j * FOX_IN_PAD * D, 32 * nb, kb, 32 * nb, scr, lane); return; }
.LBB0_491:
	s_andn2_b64 vcc, exec, s[2:3]
	s_cbranch_vccnz .LBB0_509
	s_add_i32 s6, s18, 0x1500
	s_cmpk_gt_u32 s6, 0x67f
	s_cselect_b64 s[10:11], -1, 0
	s_and_b64 s[2:3], s[10:11], exec
	s_cselect_b32 s2, 0xf980, 0
	s_cselect_b32 s3, 0xc10000, 0
	s_add_i32 s6, s6, s2
	s_sext_i32_i16 s2, s6
	s_mulk_i32 s2, 0x4ec5
	s_lshr_b32 s7, s2, 31
	s_ashr_i32 s2, s2, 21
	s_add_i32 s2, s2, s7
	s_mul_i32 s7, s2, 0x68
	v_readlane_b32 s44, v253, 16
	s_sub_i32 s6, s6, s7
	v_readlane_b32 s52, v253, 24
	s_sext_i32_i16 s6, s6
	v_readlane_b32 s53, v253, 25
	s_add_u32 s9, s52, s3
	s_addc_u32 s43, s53, 0
	s_lshl_b32 s6, s6, 5
	s_ashr_i32 s7, s6, 31
	s_lshl_b32 s8, s2, 6
	s_lshl_b64 s[12:13], s[6:7], 2
	v_or_b32_e32 v2, s6, v36
	s_movk_i32 s2, 0xc10
	v_or_b32_e32 v5, s8, v39
	s_add_u32 s12, s9, s12
	v_cmp_gt_i32_e64 s[2:3], s2, v2
	s_addc_u32 s13, s43, s13
	v_lshlrev_b32_e32 v2, 2, v36
	v_mul_i32_i24_e32 v42, 0x3040, v5
	v_lshl_add_u64 v[40:41], s[12:13], 0, v[2:3]
	v_mov_b32_e32 v4, 0
	v_ashrrev_i32_e32 v43, 31, v42
	v_mov_b32_e32 v8, 0
	v_mov_b32_e32 v9, 0
	v_mov_b32_e32 v10, 0
	v_mov_b32_e32 v11, 0
	v_readlane_b32 s45, v253, 17
	v_readlane_b32 s46, v253, 18
	v_readlane_b32 s47, v253, 19
	v_readlane_b32 s48, v253, 20
	v_readlane_b32 s49, v253, 21
	v_readlane_b32 s50, v253, 22
	v_readlane_b32 s51, v253, 23
	v_readlane_b32 s54, v253, 26
	v_readlane_b32 s55, v253, 27
	v_readlane_b32 s56, v253, 28
	v_readlane_b32 s57, v253, 29
	v_readlane_b32 s58, v253, 30
	v_readlane_b32 s59, v253, 31
	s_and_saveexec_b64 s[12:13], s[2:3]
	s_cbranch_execz .LBB0_494
	v_lshl_add_u64 v[6:7], v[40:41], 0, v[42:43]
	global_load_dwordx4 v[8:11], v[6:7], off nt

; #define GAS __attribute__((address_space(1)))
; #define LAS __attribute__((address_space(3)))
; #define LDS_WAIT() asm volatile("s_waitcnt lgkmcnt(0)" ::: "memory")
; __device__ __forceinline__ unsigned pk2(float lo, float hi) { unsigned r; asm("v_cvt_pk_bf16_f32 %0, %1, %2" : "=v"(r) : "v"(lo), "v"(hi)); return r; }
; __device__ __forceinline__ void transpose_item(const float* W, int K, int N, bf16* WT, int drow0, int kb, int n0, LAS float* scr, int lane) {
;     ...
;     for (int i = 0; i < 8; ++i) { const int kk = 8 * i + (lane >> 3); v[i] = ok ? *(const f32x4*)(W + (size_t)(k0 + kk) * N + n0 + c4) : (f32x4){0.f, 0.f, 0.f, 0.f}; }
; #pragma unroll
;     for (int i = 0; i < 8; ++i) { const int kk = 8 * i + (lane >> 3); LAS float* d = scr + kk * 33 + c4; d[0] = v[i][0]; d[1] = v[i][1]; d[2] = v[i][2]; d[3] = v[i][3]; }
;     LDS_WAIT(); asm volatile("" ::: "memory");
;     const int c = lane & 7;
; #pragma unroll
;     for (int j = 0; j < 4; ++j) { const int n = (lane >> 3) + 8 * j; const LAS float* s = scr + (8 * c) * 33 + n;
;         v4u o; o.x = pk2(s[0 * 33], s[1 * 33]); o.y = pk2(s[2 * 33], s[3 * 33]); o.z = pk2(s[4 * 33], s[5 * 33]); o.w = pk2(s[6 * 33], s[7 * 33]);
;         *(GAS v4u*)(WT + (size_t)(drow0 + n) * K + k0 + 8 * c) = o; }
; __device__ __forceinline__ void convert_item(const In& I, unsigned char* ws, int it, LAS float* scr, int lane) {
;     ...
;     if (r < 2 * I_FIN) { const int j = r / I_FIN; r -= j * I_FIN; const int kb = r / 104, nb = r % 104;
;         transpose_item(I.fox_w_in + (size_t)j * D * FOX_IN, D, FOX_IN, Wfin + (size_t)j * FOX_IN_PAD * D, 32 * nb, kb, 32 * nb, scr, lane); return; }
.LBB0_508:
	s_or_b64 exec, exec, s[12:13]
	v_add_u32_e32 v2, v44, v45
	s_waitcnt vmcnt(0)
	ds_write2_b32 v2, v8, v9 offset1:1
	ds_write2_b32 v2, v10, v11 offset0:2 offset1:3
	v_add_u32_e32 v8, 0x420, v2
	ds_write2_b32 v8, v4, v5 offset1:1
	v_add_u32_e32 v4, 0x428, v2
	ds_write2_b32 v4, v6, v7 offset1:1
	v_add_u32_e32 v4, 0x840, v2
	ds_write2_b32 v4, v16, v17 offset1:1
	v_add_u32_e32 v4, 0x848, v2
	ds_write2_b32 v4, v18, v19 offset1:1
	v_add_u32_e32 v4, 0xc60, v2
	ds_write2_b32 v4, v12, v13 offset1:1
	v_add_u32_e32 v4, 0xc68, v2
	ds_write2_b32 v4, v14, v15 offset1:1
	v_add_u32_e32 v4, 0x1080, v2
	ds_write2_b32 v4, v24, v25 offset1:1
	v_add_u32_e32 v4, 0x1088, v2
	ds_write2_b32 v4, v26, v27 offset1:1
	v_add_u32_e32 v4, 0x14a0, v2
	ds_write2_b32 v4, v20, v21 offset1:1
	v_add_u32_e32 v4, 0x14a8, v2
	ds_write2_b32 v4, v22, v23 offset1:1
	v_add_u32_e32 v4, 0x18c0, v2
	ds_write2_b32 v4, v32, v33 offset1:1
	v_add_u32_e32 v4, 0x18c8, v2
	s_and_b64 s[2:3], s[10:11], exec
	ds_write2_b32 v4, v34, v35 offset1:1
	v_add_u32_e32 v4, 0x1ce0, v2
	v_add_u32_e32 v2, 0x1ce8, v2
	s_cselect_b32 s2, 0x680000, 0
	ds_write2_b32 v4, v28, v29 offset1:1
	ds_write2_b32 v2, v30, v31 offset1:1
	s_add_u32 s7, s24, s2
	s_waitcnt lgkmcnt(0)
	s_addc_u32 s10, s25, 0
	s_ashr_i32 s9, s8, 31
	s_lshl_b64 s[2:3], s[8:9], 1
	ds_read2_b32 v[8:9], v49 offset0:33 offset1:41
	ds_read2_b32 v[10:11], v49 offset1:8
	ds_read2_b32 v[12:13], v49 offset0:66 offset1:74
	ds_read2_b32 v[14:15], v49 offset0:99 offset1:107
	ds_read2_b32 v[16:17], v49 offset0:132 offset1:140
	ds_read2_b32 v[18:19], v49 offset0:165 offset1:173
	ds_read2_b32 v[20:21], v49 offset0:198 offset1:206
	ds_read2_b32 v[22:23], v49 offset0:231 offset1:239
	s_add_u32 s2, s7, s2
	v_or_b32_e32 v26, s6, v39
	s_addc_u32 s3, s10, s3
	v_lshlrev_b32_e32 v2, 1, v38
	v_ashrrev_i32_e32 v27, 31, v26
	v_lshl_add_u64 v[24:25], s[2:3], 0, v[2:3]
	v_lshlrev_b64 v[26:27], 11, v[26:27]
	s_waitcnt lgkmcnt(0)
	v_cvt_pk_bf16_f32 v4, v10, v8
	v_lshl_add_u64 v[26:27], v[24:25], 0, v[26:27]
	v_or_b32_e32 v8, s6, v46
	v_cvt_pk_bf16_f32 v5, v12, v14
	v_cvt_pk_bf16_f32 v6, v16, v18
	v_cvt_pk_bf16_f32 v7, v20, v22
	global_store_dwordx4 v[26:27], v[4:7], off sc1 nt
	s_nop 1
	v_cvt_pk_bf16_f32 v4, v11, v9
	v_ashrrev_i32_e32 v9, 31, v8
	v_lshlrev_b64 v[8:9], 11, v[8:9]
	v_cvt_pk_bf16_f32 v5, v13, v15
	v_cvt_pk_bf16_f32 v6, v17, v19
	v_cvt_pk_bf16_f32 v7, v21, v23
	v_lshl_add_u64 v[8:9], v[24:25], 0, v[8:9]
	ds_read2_b32 v[10:11], v49 offset0:16 offset1:24
	ds_read2_b32 v[12:13], v49 offset0:49 offset1:57
	ds_read2_b32 v[14:15], v49 offset0:82 offset1:90
	ds_read2_b32 v[16:17], v49 offset0:115 offset1:123
	ds_read2_b32 v[18:19], v49 offset0:148 offset1:156
	ds_read2_b32 v[20:21], v49 offset0:181 offset1:189
	ds_read2_b32 v[22:23], v49 offset0:214 offset1:222
	ds_read2_b32 v[26:27], v49 offset0:247 offset1:255
	global_store_dwordx4 v[8:9], v[4:7], off sc1 nt
	v_or_b32_e32 v8, s6, v47
	v_ashrrev_i32_e32 v9, 31, v8
	v_lshlrev_b64 v[8:9], 11, v[8:9]
	v_lshl_add_u64 v[8:9], v[24:25], 0, v[8:9]
	s_waitcnt lgkmcnt(6)
	v_cvt_pk_bf16_f32 v4, v10, v12
	s_waitcnt lgkmcnt(4)
	v_cvt_pk_bf16_f32 v5, v14, v16
	s_waitcnt lgkmcnt(2)
	v_cvt_pk_bf16_f32 v6, v18, v20
	s_waitcnt lgkmcnt(0)
	v_cvt_pk_bf16_f32 v7, v22, v26
	global_store_dwordx4 v[8:9], v[4:7], off sc1 nt
	v_or_b32_e32 v8, s6, v48
	v_ashrrev_i32_e32 v9, 31, v8
	v_lshlrev_b64 v[8:9], 11, v[8:9]
	v_lshl_add_u64 v[8:9], v[24:25], 0, v[8:9]
	v_cvt_pk_bf16_f32 v4, v11, v13
	v_cvt_pk_bf16_f32 v5, v15, v17
	v_cvt_pk_bf16_f32 v6, v19, v21
	v_cvt_pk_bf16_f32 v7, v23, v27
	global_store_dwordx4 v[8:9], v[4:7], off sc1 nt
	s_waitcnt lgkmcnt(0)

; #define GAS __attribute__((address_space(1)))
; #define LAS __attribute__((address_space(3)))
; #define LDS_WAIT() asm volatile("s_waitcnt lgkmcnt(0)" ::: "memory")
; __device__ __forceinline__ unsigned pk2(float lo, float hi) { unsigned r; asm("v_cvt_pk_bf16_f32 %0, %1, %2" : "=v"(r) : "v"(lo), "v"(hi)); return r; }
; __device__ __forceinline__ void transpose_item(const float* W, int K, int N, bf16* WT, int drow0, int kb, int n0, LAS float* scr, int lane) {
;     const int k0 = 64 * kb; const int c4 = 4 * (lane & 7); const bool ok = (n0 + c4) < N;
;     f32x4 v[8];
; #pragma unroll
;     for (int i = 0; i < 8; ++i) { const int kk = 8 * i + (lane >> 3); v[i] = ok ? *(const f32x4*)(W + (size_t)(k0 + kk) * N + n0 + c4) : (f32x4){0.f, 0.f, 0.f, 0.f}; }
; #pragma unroll
;     for (int i = 0; i < 8; ++i) { const int kk = 8 * i + (lane >> 3); LAS float* d = scr + kk * 33 + c4; d[0] = v[i][0]; d[1] = v[i][1]; d[2] = v[i][2]; d[3] = v[i][3]; }
;     LDS_WAIT(); asm volatile("" ::: "memory");
;     const int c = lane & 7;
; #pragma unroll
;     for (int j = 0; j < 4; ++j) { const int n = (lane >> 3) + 8 * j; const LAS float* s = scr + (8 * c) * 33 + n;
;         v4u o; o.x = pk2(s[0 * 33], s[1 * 33]); o.y = pk2(s[2 * 33], s[3 * 33]); o.z = pk2(s[4 * 33], s[5 * 33]); o.w = pk2(s[6 * 33], s[7 * 33]);
;         *(GAS v4u*)(WT + (size_t)(drow0 + n) * K + k0 + 8 * c) = o; }
;     LDS_WAIT(); asm volatile("" ::: "memory");
; }
; __device__ __forceinline__ void convert_item(const In& I, unsigned char* ws, int it, LAS float* scr, int lane) {
;     ...
;     if (r < 2 * I_SQ) { const int j = r / I_SQ; r -= j * I_SQ; const int kb = r / 32, nb = r % 32;
;         transpose_item(I.nsa_w_out + (size_t)j * D * D, D, D, Wnout + (size_t)j * D * D, 32 * nb, kb, 32 * nb, scr, lane); return; }
.LBB0_510:
	s_andn2_b64 vcc, exec, s[2:3]
	s_cbranch_vccnz .LBB0_512
	s_add_i32 s2, s18, 0x1900
	s_lshr_b32 s68, s2, 9
	v_readlane_b32 s44, v253, 16
	s_lshl_b64 s[2:3], s[68:69], 22
	v_readlane_b32 s50, v253, 22
	v_readlane_b32 s51, v253, 23
	s_add_u32 s6, s50, s2
	s_addc_u32 s7, s51, s3
	s_lshl_b64 s[2:3], s[68:69], 21
	s_add_u32 s8, s22, s2
	s_addc_u32 s3, s23, s3
	s_and_b32 s2, s40, 0x3e0
	s_add_i32 s9, s41, 0x2a00
	s_and_b32 s9, s9, 0x3c0
	s_lshl_b32 s10, s2, 2
	s_add_u32 s6, s6, s10
	v_or_b32_e32 v6, s9, v39
	s_addc_u32 s7, s7, 0
	v_lshlrev_b32_e32 v2, 2, v36
	v_lshl_add_u64 v[4:5], s[6:7], 0, v[2:3]
	v_lshlrev_b32_e32 v2, 12, v6
	v_lshl_add_u64 v[32:33], v[4:5], 0, v[2:3]
	v_add_co_u32_e32 v8, vcc, s81, v32
	global_load_dwordx4 v[4:7], v[32:33], off nt
	s_nop 0
	v_addc_co_u32_e32 v9, vcc, 0, v33, vcc
	global_load_dwordx4 v[8:11], v[8:9], off nt
	v_add_co_u32_e32 v12, vcc, s79, v32
	v_add_u32_e32 v2, v44, v45
	s_nop 0
	v_addc_co_u32_e32 v13, vcc, 0, v33, vcc
	global_load_dwordx4 v[12:15], v[12:13], off nt
	v_add_co_u32_e32 v16, vcc, s80, v32
	s_lshl_b32 s6, s9, 1
	s_nop 0
	v_addc_co_u32_e32 v17, vcc, 0, v33, vcc
	global_load_dwordx4 v[16:19], v[16:17], off nt
	v_add_co_u32_e32 v20, vcc, s85, v32
	s_add_u32 s6, s8, s6
	s_nop 0
	v_addc_co_u32_e32 v21, vcc, 0, v33, vcc
	global_load_dwordx4 v[20:23], v[20:21], off nt
	v_add_co_u32_e32 v24, vcc, s86, v32
	s_addc_u32 s7, s3, 0
	s_nop 0
	v_addc_co_u32_e32 v25, vcc, 0, v33, vcc
	global_load_dwordx4 v[24:27], v[24:25], off nt
	v_add_co_u32_e32 v28, vcc, s87, v32
	v_readlane_b32 s45, v253, 17
	s_nop 0
	v_addc_co_u32_e32 v29, vcc, 0, v33, vcc
	global_load_dwordx4 v[28:31], v[28:29], off nt
	v_add_co_u32_e32 v32, vcc, s89, v32
	v_readlane_b32 s46, v253, 18
	s_nop 0
	v_addc_co_u32_e32 v33, vcc, 0, v33, vcc
	global_load_dwordx4 v[32:35], v[32:33], off nt
	v_readlane_b32 s47, v253, 19
	v_readlane_b32 s48, v253, 20
	v_readlane_b32 s49, v253, 21
	v_readlane_b32 s52, v253, 24
	v_readlane_b32 s53, v253, 25
	v_readlane_b32 s54, v253, 26
	v_readlane_b32 s55, v253, 27
	v_readlane_b32 s56, v253, 28
	v_readlane_b32 s57, v253, 29
	v_readlane_b32 s58, v253, 30
	v_readlane_b32 s59, v253, 31
	s_waitcnt vmcnt(0)
	ds_write2_b32 v2, v4, v5 offset1:1
	ds_write2_b32 v2, v6, v7 offset0:2 offset1:3
	v_add_u32_e32 v4, 0x420, v2
	ds_write2_b32 v4, v8, v9 offset1:1
	v_add_u32_e32 v4, 0x428, v2
	ds_write2_b32 v4, v10, v11 offset1:1
	v_add_u32_e32 v4, 0x840, v2
	ds_write2_b32 v4, v12, v13 offset1:1
	v_add_u32_e32 v4, 0x848, v2
	ds_write2_b32 v4, v14, v15 offset1:1
	v_add_u32_e32 v4, 0xc60, v2
	ds_write2_b32 v4, v16, v17 offset1:1
	v_add_u32_e32 v4, 0xc68, v2
	ds_write2_b32 v4, v18, v19 offset1:1
	v_add_u32_e32 v4, 0x1080, v2
	ds_write2_b32 v4, v20, v21 offset1:1
	v_add_u32_e32 v4, 0x1088, v2
	ds_write2_b32 v4, v22, v23 offset1:1
	v_add_u32_e32 v4, 0x14a0, v2
	ds_write2_b32 v4, v24, v25 offset1:1
	v_add_u32_e32 v4, 0x14a8, v2
	ds_write2_b32 v4, v26, v27 offset1:1
	v_add_u32_e32 v4, 0x18c0, v2
	ds_write2_b32 v4, v28, v29 offset1:1
	v_add_u32_e32 v4, 0x18c8, v2
	ds_write2_b32 v4, v30, v31 offset1:1
	v_add_u32_e32 v4, 0x1ce0, v2
	v_add_u32_e32 v2, 0x1ce8, v2
	ds_write2_b32 v4, v32, v33 offset1:1
	ds_write2_b32 v2, v34, v35 offset1:1
	s_waitcnt lgkmcnt(0)
	ds_read2_b32 v[10:11], v49 offset0:33 offset1:41
	ds_read2_b32 v[12:13], v49 offset1:8
	v_lshlrev_b32_e32 v2, 1, v38
	ds_read2_b32 v[14:15], v49 offset0:66 offset1:74
	ds_read2_b32 v[16:17], v49 offset0:99 offset1:107
	ds_read2_b32 v[18:19], v49 offset0:132 offset1:140
	ds_read2_b32 v[20:21], v49 offset0:165 offset1:173
	ds_read2_b32 v[22:23], v49 offset0:198 offset1:206
	ds_read2_b32 v[24:25], v49 offset0:231 offset1:239
	v_lshl_add_u64 v[8:9], s[6:7], 0, v[2:3]
	v_or_b32_e32 v2, s2, v39
	v_lshlrev_b32_e32 v2, 11, v2
	v_lshl_add_u64 v[26:27], v[8:9], 0, v[2:3]
	v_or_b32_e32 v2, s2, v46
	s_waitcnt lgkmcnt(0)
	v_cvt_pk_bf16_f32 v4, v12, v10
	v_lshlrev_b32_e32 v2, 11, v2
	v_cvt_pk_bf16_f32 v5, v14, v16
	v_cvt_pk_bf16_f32 v6, v18, v20
	v_cvt_pk_bf16_f32 v7, v22, v24
	global_store_dwordx4 v[26:27], v[4:7], off sc1 nt
	s_nop 1
	v_cvt_pk_bf16_f32 v4, v13, v11
	v_lshl_add_u64 v[10:11], v[8:9], 0, v[2:3]
	v_cvt_pk_bf16_f32 v5, v15, v17
	v_cvt_pk_bf16_f32 v6, v19, v21
	v_cvt_pk_bf16_f32 v7, v23, v25
	global_store_dwordx4 v[10:11], v[4:7], off sc1 nt
	ds_read2_b32 v[10:11], v49 offset0:16 offset1:24
	ds_read2_b32 v[12:13], v49 offset0:49 offset1:57
	ds_read2_b32 v[14:15], v49 offset0:82 offset1:90
	ds_read2_b32 v[16:17], v49 offset0:115 offset1:123
	ds_read2_b32 v[18:19], v49 offset0:148 offset1:156
	ds_read2_b32 v[20:21], v49 offset0:181 offset1:189
	ds_read2_b32 v[22:23], v49 offset0:214 offset1:222
	ds_read2_b32 v[24:25], v49 offset0:247 offset1:255
	v_or_b32_e32 v2, s2, v47
	v_lshlrev_b32_e32 v2, 11, v2
	v_lshl_add_u64 v[26:27], v[8:9], 0, v[2:3]
	v_or_b32_e32 v2, s2, v48
	v_lshlrev_b32_e32 v2, 11, v2
	s_waitcnt lgkmcnt(6)
	v_cvt_pk_bf16_f32 v4, v10, v12
	s_waitcnt lgkmcnt(4)
	v_cvt_pk_bf16_f32 v5, v14, v16
	s_waitcnt lgkmcnt(2)
	v_cvt_pk_bf16_f32 v6, v18, v20
	s_waitcnt lgkmcnt(0)
	v_cvt_pk_bf16_f32 v7, v22, v24
	v_lshl_add_u64 v[8:9], v[8:9], 0, v[2:3]
	global_store_dwordx4 v[26:27], v[4:7], off sc1 nt
	s_nop 1
	v_cvt_pk_bf16_f32 v4, v11, v13
	v_cvt_pk_bf16_f32 v5, v15, v17
	v_cvt_pk_bf16_f32 v6, v19, v21
	v_cvt_pk_bf16_f32 v7, v23, v25
	global_store_dwordx4 v[8:9], v[4:7], off sc1 nt
	s_waitcnt lgkmcnt(0)

; #define LAS __attribute__((address_space(3)))
; __device__ __forceinline__ void transpose_item(const float* W, int K, int N, bf16* WT, int drow0, int kb, int n0, LAS float* scr, int lane) {
;     const int k0 = 64 * kb; const int c4 = 4 * (lane & 7); const bool ok = (n0 + c4) < N;
;     f32x4 v[8];
; #pragma unroll
;     for (int i = 0; i < 8; ++i) { const int kk = 8 * i + (lane >> 3); v[i] = ok ? *(const f32x4*)(W + (size_t)(k0 + kk) * N + n0 + c4) : (f32x4){0.f, 0.f, 0.f, 0.f}; }
; __device__ __forceinline__ void convert_item(const In& I, unsigned char* ws, int it, LAS float* scr, int lane) {
;     ...
;     if (r < 2 * I_NIN) { const int j = r / I_NIN; r -= j * I_NIN; const int kb = r / 88, nb = r % 88;
;         transpose_item(I.nsa_w_in + (size_t)j * D * NSA_IN, D, NSA_IN, Wnin + (size_t)j * NSA_IN_PAD * D, 32 * nb, kb, 32 * nb, scr, lane); return; }
.LBB0_513:
	s_andn2_b64 vcc, exec, s[2:3]
	s_cbranch_vccnz .LBB0_531
	s_add_i32 s6, s18, 0x2400
	s_cmpk_gt_u32 s6, 0x57f
	s_cselect_b64 s[10:11], -1, 0
	s_and_b64 s[2:3], s[10:11], exec
	s_cselect_b32 s2, 0xfa80, 0
	s_cselect_b32 s3, 0xa30000, 0
	s_add_i32 s6, s6, s2
	s_sext_i32_i16 s2, s6
	s_mulk_i32 s2, 0xba3
	s_lshr_b32 s7, s2, 31
	s_ashr_i32 s2, s2, 18
	s_add_i32 s2, s2, s7
	s_mul_i32 s7, s2, 0x58
	v_readlane_b32 s44, v253, 0
	s_sub_i32 s6, s6, s7
	v_readlane_b32 s56, v253, 12
	s_sext_i32_i16 s6, s6
	v_readlane_b32 s57, v253, 13
	s_add_u32 s9, s56, s3
	s_addc_u32 s43, s57, 0
	s_lshl_b32 s6, s6, 5
	s_ashr_i32 s7, s6, 31
	s_lshl_b32 s8, s2, 6
	s_lshl_b64 s[12:13], s[6:7], 2
	v_or_b32_e32 v2, s6, v36
	s_movk_i32 s2, 0xa30
	s_add_u32 s12, s9, s12
	v_cmp_gt_i32_e64 s[2:3], s2, v2
	s_addc_u32 s13, s43, s13
	v_lshlrev_b32_e32 v2, 2, v36
	v_or_b32_e32 v42, s8, v39
	v_lshl_add_u64 v[40:41], s[12:13], 0, v[2:3]
	v_mov_b32_e32 v8, 0
	v_mov_b32_e32 v4, 0
	v_mov_b32_e32 v5, 0
	v_mov_b32_e32 v6, 0
	v_mov_b32_e32 v7, 0
	v_readlane_b32 s45, v253, 1
	v_readlane_b32 s46, v253, 2
	v_readlane_b32 s47, v253, 3
	v_readlane_b32 s48, v253, 4
	v_readlane_b32 s49, v253, 5
	v_readlane_b32 s50, v253, 6
	v_readlane_b32 s51, v253, 7
	v_readlane_b32 s52, v253, 8
	v_readlane_b32 s53, v253, 9
	v_readlane_b32 s54, v253, 10
	v_readlane_b32 s55, v253, 11
	v_readlane_b32 s58, v253, 14
	v_readlane_b32 s59, v253, 15
	s_and_saveexec_b64 s[12:13], s[2:3]
	s_cbranch_execz .LBB0_516
	v_mul_i32_i24_e32 v4, 0x28c0, v42
	v_ashrrev_i32_e32 v5, 31, v4
	v_lshl_add_u64 v[4:5], v[40:41], 0, v[4:5]
	global_load_dwordx4 v[4:7], v[4:5], off nt

; #define GAS __attribute__((address_space(1)))
; #define LAS __attribute__((address_space(3)))
; #define LDS_WAIT() asm volatile("s_waitcnt lgkmcnt(0)" ::: "memory")
; __device__ __forceinline__ unsigned pk2(float lo, float hi) { unsigned r; asm("v_cvt_pk_bf16_f32 %0, %1, %2" : "=v"(r) : "v"(lo), "v"(hi)); return r; }
; __device__ __forceinline__ void transpose_item(const float* W, int K, int N, bf16* WT, int drow0, int kb, int n0, LAS float* scr, int lane) {
;     ...
;     for (int i = 0; i < 8; ++i) { const int kk = 8 * i + (lane >> 3); v[i] = ok ? *(const f32x4*)(W + (size_t)(k0 + kk) * N + n0 + c4) : (f32x4){0.f, 0.f, 0.f, 0.f}; }
; #pragma unroll
;     for (int i = 0; i < 8; ++i) { const int kk = 8 * i + (lane >> 3); LAS float* d = scr + kk * 33 + c4; d[0] = v[i][0]; d[1] = v[i][1]; d[2] = v[i][2]; d[3] = v[i][3]; }
;     LDS_WAIT(); asm volatile("" ::: "memory");
;     const int c = lane & 7;
; #pragma unroll
;     for (int j = 0; j < 4; ++j) { const int n = (lane >> 3) + 8 * j; const LAS float* s = scr + (8 * c) * 33 + n;
;         v4u o; o.x = pk2(s[0 * 33], s[1 * 33]); o.y = pk2(s[2 * 33], s[3 * 33]); o.z = pk2(s[4 * 33], s[5 * 33]); o.w = pk2(s[6 * 33], s[7 * 33]);
;         *(GAS v4u*)(WT + (size_t)(drow0 + n) * K + k0 + 8 * c) = o; }
; __device__ __forceinline__ void convert_item(const In& I, unsigned char* ws, int it, LAS float* scr, int lane) {
;     ...
;     if (r < 2 * I_NIN) { const int j = r / I_NIN; r -= j * I_NIN; const int kb = r / 88, nb = r % 88;
;         transpose_item(I.nsa_w_in + (size_t)j * D * NSA_IN, D, NSA_IN, Wnin + (size_t)j * NSA_IN_PAD * D, 32 * nb, kb, 32 * nb, scr, lane); return; }
.LBB0_530:
	s_or_b64 exec, exec, s[12:13]
	v_add_u32_e32 v2, v44, v45
	s_waitcnt vmcnt(0)
	ds_write2_b32 v2, v4, v5 offset1:1
	ds_write2_b32 v2, v6, v7 offset0:2 offset1:3
	v_add_u32_e32 v4, 0x420, v2
	ds_write2_b32 v4, v8, v9 offset1:1
	v_add_u32_e32 v4, 0x428, v2
	ds_write2_b32 v4, v10, v11 offset1:1
	v_add_u32_e32 v4, 0x840, v2
	ds_write2_b32 v4, v16, v17 offset1:1
	v_add_u32_e32 v4, 0x848, v2
	ds_write2_b32 v4, v18, v19 offset1:1
	v_add_u32_e32 v4, 0xc60, v2
	ds_write2_b32 v4, v12, v13 offset1:1
	v_add_u32_e32 v4, 0xc68, v2
	ds_write2_b32 v4, v14, v15 offset1:1
	v_add_u32_e32 v4, 0x1080, v2
	ds_write2_b32 v4, v24, v25 offset1:1
	v_add_u32_e32 v4, 0x1088, v2
	ds_write2_b32 v4, v26, v27 offset1:1
	v_add_u32_e32 v4, 0x14a0, v2
	ds_write2_b32 v4, v20, v21 offset1:1
	v_add_u32_e32 v4, 0x14a8, v2
	ds_write2_b32 v4, v22, v23 offset1:1
	v_add_u32_e32 v4, 0x18c0, v2
	ds_write2_b32 v4, v32, v33 offset1:1
	v_add_u32_e32 v4, 0x18c8, v2
	s_and_b64 s[2:3], s[10:11], exec
	ds_write2_b32 v4, v34, v35 offset1:1
	v_add_u32_e32 v4, 0x1ce0, v2
	v_add_u32_e32 v2, 0x1ce8, v2
	s_cselect_b32 s2, 0x580000, 0
	ds_write2_b32 v4, v28, v29 offset1:1
	ds_write2_b32 v2, v30, v31 offset1:1
	s_add_u32 s7, s20, s2
	s_waitcnt lgkmcnt(0)
	s_addc_u32 s10, s21, 0
	s_ashr_i32 s9, s8, 31
	s_lshl_b64 s[2:3], s[8:9], 1
	ds_read2_b32 v[8:9], v49 offset0:33 offset1:41
	ds_read2_b32 v[10:11], v49 offset1:8
	ds_read2_b32 v[12:13], v49 offset0:66 offset1:74
	ds_read2_b32 v[14:15], v49 offset0:99 offset1:107
	ds_read2_b32 v[16:17], v49 offset0:132 offset1:140
	ds_read2_b32 v[18:19], v49 offset0:165 offset1:173
	ds_read2_b32 v[20:21], v49 offset0:198 offset1:206
	ds_read2_b32 v[22:23], v49 offset0:231 offset1:239
	s_add_u32 s2, s7, s2
	v_or_b32_e32 v26, s6, v39
	s_addc_u32 s3, s10, s3
	v_lshlrev_b32_e32 v2, 1, v38
	v_ashrrev_i32_e32 v27, 31, v26
	v_lshl_add_u64 v[24:25], s[2:3], 0, v[2:3]
	v_lshlrev_b64 v[26:27], 11, v[26:27]
	s_waitcnt lgkmcnt(0)
	v_cvt_pk_bf16_f32 v4, v10, v8
	v_lshl_add_u64 v[26:27], v[24:25], 0, v[26:27]
	v_or_b32_e32 v8, s6, v46
	v_cvt_pk_bf16_f32 v5, v12, v14
	v_cvt_pk_bf16_f32 v6, v16, v18
	v_cvt_pk_bf16_f32 v7, v20, v22
	global_store_dwordx4 v[26:27], v[4:7], off sc1 nt
	s_nop 1
	v_cvt_pk_bf16_f32 v4, v11, v9
	v_ashrrev_i32_e32 v9, 31, v8
	v_lshlrev_b64 v[8:9], 11, v[8:9]
	v_cvt_pk_bf16_f32 v5, v13, v15
	v_cvt_pk_bf16_f32 v6, v17, v19
	v_cvt_pk_bf16_f32 v7, v21, v23
	v_lshl_add_u64 v[8:9], v[24:25], 0, v[8:9]
	ds_read2_b32 v[10:11], v49 offset0:16 offset1:24
	ds_read2_b32 v[12:13], v49 offset0:49 offset1:57
	ds_read2_b32 v[14:15], v49 offset0:82 offset1:90
	ds_read2_b32 v[16:17], v49 offset0:115 offset1:123
	ds_read2_b32 v[18:19], v49 offset0:148 offset1:156
	ds_read2_b32 v[20:21], v49 offset0:181 offset1:189
	ds_read2_b32 v[22:23], v49 offset0:214 offset1:222
	ds_read2_b32 v[26:27], v49 offset0:247 offset1:255
	global_store_dwordx4 v[8:9], v[4:7], off sc1 nt
	v_or_b32_e32 v8, s6, v47
	v_ashrrev_i32_e32 v9, 31, v8
	v_lshlrev_b64 v[8:9], 11, v[8:9]
	v_lshl_add_u64 v[8:9], v[24:25], 0, v[8:9]
	s_waitcnt lgkmcnt(6)
	v_cvt_pk_bf16_f32 v4, v10, v12
	s_waitcnt lgkmcnt(4)
	v_cvt_pk_bf16_f32 v5, v14, v16
	s_waitcnt lgkmcnt(2)
	v_cvt_pk_bf16_f32 v6, v18, v20
	s_waitcnt lgkmcnt(0)
	v_cvt_pk_bf16_f32 v7, v22, v26
	global_store_dwordx4 v[8:9], v[4:7], off sc1 nt
	v_or_b32_e32 v8, s6, v48
	v_ashrrev_i32_e32 v9, 31, v8
	v_lshlrev_b64 v[8:9], 11, v[8:9]
	v_lshl_add_u64 v[8:9], v[24:25], 0, v[8:9]
	v_cvt_pk_bf16_f32 v4, v11, v13
	v_cvt_pk_bf16_f32 v5, v15, v17
	v_cvt_pk_bf16_f32 v6, v19, v21
	v_cvt_pk_bf16_f32 v7, v23, v27
	global_store_dwordx4 v[8:9], v[4:7], off sc1 nt
	s_waitcnt lgkmcnt(0)

; #define GAS __attribute__((address_space(1)))
; #define LAS __attribute__((address_space(3)))
; #define LDS_WAIT() asm volatile("s_waitcnt lgkmcnt(0)" ::: "memory")
; __device__ __forceinline__ unsigned pk2(float lo, float hi) { unsigned r; asm("v_cvt_pk_bf16_f32 %0, %1, %2" : "=v"(r) : "v"(lo), "v"(hi)); return r; }
; __device__ __forceinline__ void transpose_item(const float* W, int K, int N, bf16* WT, int drow0, int kb, int n0, LAS float* scr, int lane) {
;     const int k0 = 64 * kb; const int c4 = 4 * (lane & 7); const bool ok = (n0 + c4) < N;
;     f32x4 v[8];
; #pragma unroll
;     for (int i = 0; i < 8; ++i) { const int kk = 8 * i + (lane >> 3); v[i] = ok ? *(const f32x4*)(W + (size_t)(k0 + kk) * N + n0 + c4) : (f32x4){0.f, 0.f, 0.f, 0.f}; }
; #pragma unroll
;     for (int i = 0; i < 8; ++i) { const int kk = 8 * i + (lane >> 3); LAS float* d = scr + kk * 33 + c4; d[0] = v[i][0]; d[1] = v[i][1]; d[2] = v[i][2]; d[3] = v[i][3]; }
;     LDS_WAIT(); asm volatile("" ::: "memory");
;     const int c = lane & 7;
; #pragma unroll
;     for (int j = 0; j < 4; ++j) { const int n = (lane >> 3) + 8 * j; const LAS float* s = scr + (8 * c) * 33 + n;
;         v4u o; o.x = pk2(s[0 * 33], s[1 * 33]); o.y = pk2(s[2 * 33], s[3 * 33]); o.z = pk2(s[4 * 33], s[5 * 33]); o.w = pk2(s[6 * 33], s[7 * 33]);
;         *(GAS v4u*)(WT + (size_t)(drow0 + n) * K + k0 + 8 * c) = o; }
;     LDS_WAIT(); asm volatile("" ::: "memory");
; }
; __device__ __forceinline__ void convert_item(const In& I, unsigned char* ws, int it, LAS float* scr, int lane) {
;     ...
;     if (r < T0) { const int f = r / I_FFN; r -= f * I_FFN;
;         if (r < 2 * I_G) { const int up = r >= I_G; r -= up * I_G; const int kb = r / 88, nb = r % 88;
;             transpose_item((up ? I.w_up : I.w_gate) + (size_t)f * D * FF, D, FF, Wgu + (size_t)f * NGU * D, 256 * (nb >> 2) + 32 * (nb & 3) + 128 * up, kb, 32 * nb, scr, lane); }
;         else { r -= 2 * I_G; const int kb = r / 32, nb = r % 32; transpose_item(I.w_down + (size_t)f * FF * D, FF, D, Wd + (size_t)f * D * FF, 32 * nb, kb, 32 * nb, scr, lane); }
.LBB0_532:
	s_andn2_b64 vcc, exec, s[2:3]
	s_cbranch_vccnz .LBB0_477
	s_mul_hi_i32 s2, s42, 0x3e0f83e1
	s_lshr_b32 s3, s2, 31
	s_ashr_i32 s6, s2, 10
	s_add_i32 s6, s6, s3
	s_mul_i32 s2, s6, 0xffffef80
	s_add_i32 s7, s18, s2
	s_add_i32 s7, s7, 0xa800
	s_cmpk_gt_i32 s7, 0xaff
	s_mov_b64 s[2:3], -1
	s_cbranch_scc0 .LBB0_535
	v_readlane_b32 s44, v253, 0
	s_mul_i32 s3, s6, 0xb00000
	v_readlane_b32 s52, v253, 8
	s_mul_hi_i32 s2, s6, 0xb00000
	v_readlane_b32 s53, v253, 9
	s_add_u32 s9, s52, s3
	s_addc_u32 s11, s53, s2
	s_mul_i32 s3, s6, 0x580000
	s_mul_hi_i32 s2, s6, 0x580000
	s_add_u32 s3, s1, s3
	s_mul_i32 s10, s6, 0xffffdf00
	s_addc_u32 s8, s19, s2
	s_add_i32 s10, s41, s10
	s_add_i32 s10, s10, 0x14800
	s_and_b32 s2, s40, 0x3e0
	s_andn2_b32 s10, s10, 63
	s_add_i32 s68, s10, 0xffffea00
	s_lshl_b32 s10, s2, 2
	v_or_b32_e32 v32, s68, v39
	s_add_u32 s10, s9, s10
	s_addc_u32 s11, s11, 0
	v_lshlrev_b32_e32 v2, 2, v36
	v_ashrrev_i32_e32 v33, 31, v32
	v_or_b32_e32 v8, 8, v32
	v_lshl_add_u64 v[34:35], s[10:11], 0, v[2:3]
	v_lshlrev_b64 v[4:5], 12, v[32:33]
	v_ashrrev_i32_e32 v9, 31, v8
	v_lshl_add_u64 v[4:5], v[34:35], 0, v[4:5]
	v_lshlrev_b64 v[8:9], 12, v[8:9]
	v_or_b32_e32 v12, 16, v32
	global_load_dwordx4 v[4:7], v[4:5], off nt
	v_lshl_add_u64 v[8:9], v[34:35], 0, v[8:9]
	v_ashrrev_i32_e32 v13, 31, v12
	global_load_dwordx4 v[8:11], v[8:9], off nt
	v_lshlrev_b64 v[12:13], 12, v[12:13]
	v_or_b32_e32 v16, 24, v32
	v_lshl_add_u64 v[12:13], v[34:35], 0, v[12:13]
	v_ashrrev_i32_e32 v17, 31, v16
	global_load_dwordx4 v[12:15], v[12:13], off nt
	v_lshlrev_b64 v[16:17], 12, v[16:17]
	v_or_b32_e32 v20, 32, v32
	v_lshl_add_u64 v[16:17], v[34:35], 0, v[16:17]
	v_ashrrev_i32_e32 v21, 31, v20
	global_load_dwordx4 v[16:19], v[16:17], off nt
	v_lshlrev_b64 v[20:21], 12, v[20:21]
	v_or_b32_e32 v24, 40, v32
	v_lshl_add_u64 v[20:21], v[34:35], 0, v[20:21]
	v_ashrrev_i32_e32 v25, 31, v24
	global_load_dwordx4 v[20:23], v[20:21], off nt
	v_lshlrev_b64 v[24:25], 12, v[24:25]
	v_or_b32_e32 v28, 48, v32
	v_lshl_add_u64 v[24:25], v[34:35], 0, v[24:25]
	v_ashrrev_i32_e32 v29, 31, v28
	global_load_dwordx4 v[24:27], v[24:25], off nt
	v_lshlrev_b64 v[28:29], 12, v[28:29]
	v_or_b32_e32 v32, 56, v32
	v_lshl_add_u64 v[28:29], v[34:35], 0, v[28:29]
	v_ashrrev_i32_e32 v33, 31, v32
	global_load_dwordx4 v[28:31], v[28:29], off nt
	v_lshlrev_b64 v[32:33], 12, v[32:33]
	v_lshl_add_u64 v[32:33], v[34:35], 0, v[32:33]
	global_load_dwordx4 v[32:35], v[32:33], off nt
	v_add_u32_e32 v2, v44, v45
	s_lshl_b64 s[10:11], s[68:69], 1
	s_add_u32 s10, s3, s10
	s_addc_u32 s11, s8, s11
	v_readlane_b32 s45, v253, 1
	v_readlane_b32 s46, v253, 2
	v_readlane_b32 s47, v253, 3
	v_readlane_b32 s48, v253, 4
	v_readlane_b32 s49, v253, 5
	v_readlane_b32 s50, v253, 6
	v_readlane_b32 s51, v253, 7
	v_readlane_b32 s54, v253, 10
	v_readlane_b32 s55, v253, 11
	v_readlane_b32 s56, v253, 12
	v_readlane_b32 s57, v253, 13
	v_readlane_b32 s58, v253, 14
	v_readlane_b32 s59, v253, 15
	s_waitcnt vmcnt(0)
	ds_write2_b32 v2, v4, v5 offset1:1
	ds_write2_b32 v2, v6, v7 offset0:2 offset1:3
	v_add_u32_e32 v4, 0x420, v2
	ds_write2_b32 v4, v8, v9 offset1:1
	v_add_u32_e32 v4, 0x428, v2
	ds_write2_b32 v4, v10, v11 offset1:1
	v_add_u32_e32 v4, 0x840, v2
	ds_write2_b32 v4, v12, v13 offset1:1
	v_add_u32_e32 v4, 0x848, v2
	ds_write2_b32 v4, v14, v15 offset1:1
	v_add_u32_e32 v4, 0xc60, v2
	ds_write2_b32 v4, v16, v17 offset1:1
	v_add_u32_e32 v4, 0xc68, v2
	ds_write2_b32 v4, v18, v19 offset1:1
	v_add_u32_e32 v4, 0x1080, v2
	ds_write2_b32 v4, v20, v21 offset1:1
	v_add_u32_e32 v4, 0x1088, v2
	ds_write2_b32 v4, v22, v23 offset1:1
	v_add_u32_e32 v4, 0x14a0, v2
	ds_write2_b32 v4, v24, v25 offset1:1
	v_add_u32_e32 v4, 0x14a8, v2
	ds_write2_b32 v4, v26, v27 offset1:1
	v_add_u32_e32 v4, 0x18c0, v2
	ds_write2_b32 v4, v28, v29 offset1:1
	v_add_u32_e32 v4, 0x18c8, v2
	ds_write2_b32 v4, v30, v31 offset1:1
	v_add_u32_e32 v4, 0x1ce0, v2
	v_add_u32_e32 v2, 0x1ce8, v2
	ds_write2_b32 v4, v32, v33 offset1:1
	ds_write2_b32 v2, v34, v35 offset1:1
	s_waitcnt lgkmcnt(0)
	ds_read2_b32 v[10:11], v49 offset0:33 offset1:41
	ds_read2_b32 v[12:13], v49 offset1:8
	v_lshlrev_b32_e32 v2, 1, v38
	ds_read2_b32 v[14:15], v49 offset0:66 offset1:74
	ds_read2_b32 v[16:17], v49 offset0:99 offset1:107
	ds_read2_b32 v[18:19], v49 offset0:132 offset1:140
	ds_read2_b32 v[20:21], v49 offset0:165 offset1:173
	ds_read2_b32 v[22:23], v49 offset0:198 offset1:206
	ds_read2_b32 v[24:25], v49 offset0:231 offset1:239
	v_lshl_add_u64 v[8:9], s[10:11], 0, v[2:3]
	v_or_b32_e32 v2, s2, v39
	v_mul_u32_u24_e32 v2, 0x1600, v2
	v_lshl_add_u64 v[26:27], v[8:9], 0, v[2:3]
	v_or_b32_e32 v2, s2, v46
	s_waitcnt lgkmcnt(0)
	v_cvt_pk_bf16_f32 v4, v12, v10
	v_mul_u32_u24_e32 v2, 0x1600, v2
	v_cvt_pk_bf16_f32 v5, v14, v16
	v_cvt_pk_bf16_f32 v6, v18, v20
	v_cvt_pk_bf16_f32 v7, v22, v24
	global_store_dwordx4 v[26:27], v[4:7], off sc1 nt
	s_nop 1
	v_cvt_pk_bf16_f32 v4, v13, v11
	v_lshl_add_u64 v[10:11], v[8:9], 0, v[2:3]
	v_cvt_pk_bf16_f32 v5, v15, v17
	v_cvt_pk_bf16_f32 v6, v19, v21
	v_cvt_pk_bf16_f32 v7, v23, v25
	global_store_dwordx4 v[10:11], v[4:7], off sc1 nt
	ds_read2_b32 v[10:11], v49 offset0:16 offset1:24
	ds_read2_b32 v[12:13], v49 offset0:49 offset1:57
	ds_read2_b32 v[14:15], v49 offset0:82 offset1:90
	ds_read2_b32 v[16:17], v49 offset0:115 offset1:123
	ds_read2_b32 v[18:19], v49 offset0:148 offset1:156
	ds_read2_b32 v[20:21], v49 offset0:181 offset1:189
	ds_read2_b32 v[22:23], v49 offset0:214 offset1:222
	ds_read2_b32 v[24:25], v49 offset0:247 offset1:255
	v_or_b32_e32 v2, s2, v47
	v_mul_u32_u24_e32 v2, 0x1600, v2
	v_lshl_add_u64 v[26:27], v[8:9], 0, v[2:3]
	v_or_b32_e32 v2, s2, v48
	v_mul_u32_u24_e32 v2, 0x1600, v2
	s_waitcnt lgkmcnt(6)
	v_cvt_pk_bf16_f32 v4, v10, v12
	s_waitcnt lgkmcnt(4)
	v_cvt_pk_bf16_f32 v5, v14, v16
	s_waitcnt lgkmcnt(2)
	v_cvt_pk_bf16_f32 v6, v18, v20
	s_waitcnt lgkmcnt(0)
	v_cvt_pk_bf16_f32 v7, v22, v24
	v_lshl_add_u64 v[8:9], v[8:9], 0, v[2:3]
	global_store_dwordx4 v[26:27], v[4:7], off sc1 nt
	s_mov_b64 s[2:3], 0
	s_nop 0
	v_cvt_pk_bf16_f32 v4, v11, v13
	v_cvt_pk_bf16_f32 v5, v15, v17
	v_cvt_pk_bf16_f32 v6, v19, v21
	v_cvt_pk_bf16_f32 v7, v23, v25
	global_store_dwordx4 v[8:9], v[4:7], off sc1 nt
	s_waitcnt lgkmcnt(0)
; #define GAS __attribute__((address_space(1)))
; #define LAS __attribute__((address_space(3)))
; #define LDS_WAIT() asm volatile("s_waitcnt lgkmcnt(0)" ::: "memory")
; __device__ __forceinline__ unsigned pk2(float lo, float hi) { unsigned r; asm("v_cvt_pk_bf16_f32 %0, %1, %2" : "=v"(r) : "v"(lo), "v"(hi)); return r; }
; __device__ __forceinline__ void transpose_item(const float* W, int K, int N, bf16* WT, int drow0, int kb, int n0, LAS float* scr, int lane) {
;     const int k0 = 64 * kb; const int c4 = 4 * (lane & 7); const bool ok = (n0 + c4) < N;
;     f32x4 v[8];
; #pragma unroll
;     for (int i = 0; i < 8; ++i) { const int kk = 8 * i + (lane >> 3); v[i] = ok ? *(const f32x4*)(W + (size_t)(k0 + kk) * N + n0 + c4) : (f32x4){0.f, 0.f, 0.f, 0.f}; }
; #pragma unroll
;     for (int i = 0; i < 8; ++i) { const int kk = 8 * i + (lane >> 3); LAS float* d = scr + kk * 33 + c4; d[0] = v[i][0]; d[1] = v[i][1]; d[2] = v[i][2]; d[3] = v[i][3]; }
;     LDS_WAIT(); asm volatile("" ::: "memory");
;     const int c = lane & 7;
; #pragma unroll
;     for (int j = 0; j < 4; ++j) { const int n = (lane >> 3) + 8 * j; const LAS float* s = scr + (8 * c) * 33 + n;
;         v4u o; o.x = pk2(s[0 * 33], s[1 * 33]); o.y = pk2(s[2 * 33], s[3 * 33]); o.z = pk2(s[4 * 33], s[5 * 33]); o.w = pk2(s[6 * 33], s[7 * 33]);
;         *(GAS v4u*)(WT + (size_t)(drow0 + n) * K + k0 + 8 * c) = o; }
;     LDS_WAIT(); asm volatile("" ::: "memory");
; }
; __device__ __forceinline__ void convert_item(const In& I, unsigned char* ws, int it, LAS float* scr, int lane) {
;     ...
;     if (r < T0) { const int f = r / I_FFN; r -= f * I_FFN;
;         if (r < 2 * I_G) { const int up = r >= I_G; r -= up * I_G; const int kb = r / 88, nb = r % 88;
;             transpose_item((up ? I.w_up : I.w_gate) + (size_t)f * D * FF, D, FF, Wgu + (size_t)f * NGU * D, 256 * (nb >> 2) + 32 * (nb & 3) + 128 * up, kb, 32 * nb, scr, lane); }
.LBB0_535:
	s_andn2_b64 vcc, exec, s[2:3]
	s_cbranch_vccnz .LBB0_477
	s_cmpk_gt_i32 s7, 0x57f
	v_readlane_b32 s44, v253, 0
	s_cselect_b32 s2, 0xfffffa80, 0
	s_mul_i32 s3, s6, 0x1080
	v_readlane_b32 s48, v253, 4
	v_readlane_b32 s49, v253, 5
	v_readlane_b32 s50, v253, 6
	v_readlane_b32 s51, v253, 7
	s_cselect_b32 s7, 0x80, 0
	s_cselect_b32 s8, s50, s48
	s_cselect_b32 s9, s51, s49
	s_sub_i32 s2, s2, s3
	s_add_i32 s2, s18, s2
	s_add_i32 s2, s2, 0xa800
	s_mul_hi_i32 s3, s2, 0x2e8ba2e9
	s_lshr_b32 s10, s3, 31
	s_ashr_i32 s3, s3, 4
	s_add_i32 s3, s3, s10
	s_mul_i32 s10, s3, 0x58
	s_sub_i32 s2, s2, s10
	s_mul_hi_i32 s10, s6, 0xb00000
	s_mul_i32 s6, s6, 0xb00000
	s_add_u32 s11, s8, s6
	s_addc_u32 s12, s9, s10
	s_add_u32 s13, s28, s6
	s_addc_u32 s10, s29, s10
	s_lshl_b32 s8, s2, 5
	s_lshl_b32 s6, s2, 6
	s_and_b32 s2, s8, 0x60
	s_and_b32 s6, s6, 0xffffff00
	s_or_b32 s2, s2, s7
	s_ashr_i32 s9, s8, 31
	s_or_b32 s6, s2, s6
	s_lshl_b32 s2, s3, 6
	s_lshl_b64 s[8:9], s[8:9], 2
	s_add_u32 s8, s11, s8
	s_addc_u32 s9, s12, s9
	v_lshlrev_b32_e32 v2, 2, v36
	v_or_b32_e32 v34, s2, v39
	v_lshl_add_u64 v[32:33], s[8:9], 0, v[2:3]
	s_movk_i32 s3, 0x2c00
	v_mad_i64_i32 v[4:5], s[8:9], v34, s3, v[32:33]
	v_or_b32_e32 v2, 8, v34
	global_load_dwordx4 v[4:7], v[4:5], off nt
	v_mad_i64_i32 v[8:9], s[8:9], v2, s3, v[32:33]
	global_load_dwordx4 v[8:11], v[8:9], off nt
	v_or_b32_e32 v2, 16, v34
	v_mad_i64_i32 v[12:13], s[8:9], v2, s3, v[32:33]
	global_load_dwordx4 v[12:15], v[12:13], off nt
	v_or_b32_e32 v2, 24, v34
	v_mad_i64_i32 v[16:17], s[8:9], v2, s3, v[32:33]
	global_load_dwordx4 v[16:19], v[16:17], off nt
	v_or_b32_e32 v2, 32, v34
	v_mad_i64_i32 v[20:21], s[8:9], v2, s3, v[32:33]
	global_load_dwordx4 v[20:23], v[20:21], off nt
	v_or_b32_e32 v2, 40, v34
	v_mad_i64_i32 v[24:25], s[8:9], v2, s3, v[32:33]
	global_load_dwordx4 v[24:27], v[24:25], off nt
	v_or_b32_e32 v2, 48, v34
	v_mad_i64_i32 v[28:29], s[8:9], v2, s3, v[32:33]
	global_load_dwordx4 v[28:31], v[28:29], off nt
	v_or_b32_e32 v2, 56, v34
	v_mad_i64_i32 v[32:33], s[8:9], v2, s3, v[32:33]
	global_load_dwordx4 v[32:35], v[32:33], off nt
	v_add_u32_e32 v2, v44, v45
	s_ashr_i32 s3, s2, 31
	s_lshl_b64 s[2:3], s[2:3], 1
	s_add_u32 s2, s13, s2
	s_addc_u32 s3, s10, s3
	v_readlane_b32 s45, v253, 1
	v_readlane_b32 s46, v253, 2
	v_readlane_b32 s47, v253, 3
	v_readlane_b32 s52, v253, 8
	v_readlane_b32 s53, v253, 9
	v_readlane_b32 s54, v253, 10
	v_readlane_b32 s55, v253, 11
	v_readlane_b32 s56, v253, 12
	v_readlane_b32 s57, v253, 13
	v_readlane_b32 s58, v253, 14
	v_readlane_b32 s59, v253, 15
	s_waitcnt vmcnt(0)
	ds_write2_b32 v2, v4, v5 offset1:1
	ds_write2_b32 v2, v6, v7 offset0:2 offset1:3
	v_add_u32_e32 v4, 0x420, v2
	ds_write2_b32 v4, v8, v9 offset1:1
	v_add_u32_e32 v4, 0x428, v2
	ds_write2_b32 v4, v10, v11 offset1:1
	v_add_u32_e32 v4, 0x840, v2
	ds_write2_b32 v4, v12, v13 offset1:1
	v_add_u32_e32 v4, 0x848, v2
	ds_write2_b32 v4, v14, v15 offset1:1
	v_add_u32_e32 v4, 0xc60, v2
	ds_write2_b32 v4, v16, v17 offset1:1
	v_add_u32_e32 v4, 0xc68, v2
	ds_write2_b32 v4, v18, v19 offset1:1
	v_add_u32_e32 v4, 0x1080, v2
	ds_write2_b32 v4, v20, v21 offset1:1
	v_add_u32_e32 v4, 0x1088, v2
	ds_write2_b32 v4, v22, v23 offset1:1
	v_add_u32_e32 v4, 0x14a0, v2
	ds_write2_b32 v4, v24, v25 offset1:1
	v_add_u32_e32 v4, 0x14a8, v2
	ds_write2_b32 v4, v26, v27 offset1:1
	v_add_u32_e32 v4, 0x18c0, v2
	ds_write2_b32 v4, v28, v29 offset1:1
	v_add_u32_e32 v4, 0x18c8, v2
	ds_write2_b32 v4, v30, v31 offset1:1
	v_add_u32_e32 v4, 0x1ce0, v2
	v_add_u32_e32 v2, 0x1ce8, v2
	ds_write2_b32 v4, v32, v33 offset1:1
	ds_write2_b32 v2, v34, v35 offset1:1
	s_waitcnt lgkmcnt(0)
	ds_read2_b32 v[10:11], v49 offset0:33 offset1:41
	ds_read2_b32 v[12:13], v49 offset1:8
	ds_read2_b32 v[14:15], v49 offset0:66 offset1:74
	ds_read2_b32 v[16:17], v49 offset0:99 offset1:107
	ds_read2_b32 v[18:19], v49 offset0:132 offset1:140
	ds_read2_b32 v[20:21], v49 offset0:165 offset1:173
	ds_read2_b32 v[22:23], v49 offset0:198 offset1:206
	ds_read2_b32 v[24:25], v49 offset0:231 offset1:239
	v_or_b32_e32 v26, s6, v39
	v_lshlrev_b32_e32 v2, 1, v38
	v_ashrrev_i32_e32 v27, 31, v26
	v_lshl_add_u64 v[8:9], s[2:3], 0, v[2:3]
	v_lshlrev_b64 v[26:27], 11, v[26:27]
	s_waitcnt lgkmcnt(0)
	v_cvt_pk_bf16_f32 v4, v12, v10
	v_lshl_add_u64 v[26:27], v[8:9], 0, v[26:27]
	v_or_b32_e32 v10, s6, v46
	v_cvt_pk_bf16_f32 v5, v14, v16
	v_cvt_pk_bf16_f32 v6, v18, v20
	v_cvt_pk_bf16_f32 v7, v22, v24
	global_store_dwordx4 v[26:27], v[4:7], off sc1 nt
	v_or_b32_e32 v26, s6, v47
	v_ashrrev_i32_e32 v27, 31, v26
	v_cvt_pk_bf16_f32 v4, v13, v11
	v_ashrrev_i32_e32 v11, 31, v10
	v_lshlrev_b64 v[10:11], 11, v[10:11]
	v_lshl_add_u64 v[10:11], v[8:9], 0, v[10:11]
	v_cvt_pk_bf16_f32 v5, v15, v17
	v_cvt_pk_bf16_f32 v6, v19, v21
	v_cvt_pk_bf16_f32 v7, v23, v25
	global_store_dwordx4 v[10:11], v[4:7], off sc1 nt
	ds_read2_b32 v[10:11], v49 offset0:16 offset1:24
	ds_read2_b32 v[12:13], v49 offset0:49 offset1:57
	ds_read2_b32 v[14:15], v49 offset0:82 offset1:90
	ds_read2_b32 v[16:17], v49 offset0:115 offset1:123
	ds_read2_b32 v[18:19], v49 offset0:148 offset1:156
	ds_read2_b32 v[20:21], v49 offset0:181 offset1:189
	ds_read2_b32 v[22:23], v49 offset0:214 offset1:222
	ds_read2_b32 v[24:25], v49 offset0:247 offset1:255
	v_lshlrev_b64 v[26:27], 11, v[26:27]
	s_waitcnt lgkmcnt(6)
	v_cvt_pk_bf16_f32 v4, v10, v12
	v_lshl_add_u64 v[26:27], v[8:9], 0, v[26:27]
	v_or_b32_e32 v10, s6, v48
	s_waitcnt lgkmcnt(4)
	v_cvt_pk_bf16_f32 v5, v14, v16
	s_waitcnt lgkmcnt(2)
	v_cvt_pk_bf16_f32 v6, v18, v20
	s_waitcnt lgkmcnt(0)
	v_cvt_pk_bf16_f32 v7, v22, v24
	global_store_dwordx4 v[26:27], v[4:7], off sc1 nt
	s_nop 1
	v_cvt_pk_bf16_f32 v4, v11, v13
	v_ashrrev_i32_e32 v11, 31, v10
	v_lshlrev_b64 v[10:11], 11, v[10:11]
	v_lshl_add_u64 v[8:9], v[8:9], 0, v[10:11]
	v_cvt_pk_bf16_f32 v5, v15, v17
	v_cvt_pk_bf16_f32 v6, v19, v21
	v_cvt_pk_bf16_f32 v7, v23, v25
	global_store_dwordx4 v[8:9], v[4:7], off sc1 nt
	s_waitcnt lgkmcnt(0)
	s_branch .LBB0_477

; #define GAS __attribute__((address_space(1)))
; __device__ __forceinline__ void transpose_item(const float* W, int K, int N, bf16* WT, int drow0, int kb, int n0, LAS float* scr, int lane) {
;     const int k0 = 64 * kb; const int c4 = 4 * (lane & 7); const bool ok = (n0 + c4) < N;
;     f32x4 v[8];
; #pragma unroll
;     for (int i = 0; i < 8; ++i) { const int kk = 8 * i + (lane >> 3); v[i] = ok ? *(const f32x4*)(W + (size_t)(k0 + kk) * N + n0 + c4) : (f32x4){0.f, 0.f, 0.f, 0.f}; }
; #pragma unroll
;     for (int i = 0; i < 8; ++i) { const int kk = 8 * i + (lane >> 3); LAS float* d = scr + kk * 33 + c4; d[0] = v[i][0]; d[1] = v[i][1]; d[2] = v[i][2]; d[3] = v[i][3]; }
;     LDS_WAIT(); asm volatile("" ::: "memory");
;     const int c = lane & 7;
; #pragma unroll
;     for (int j = 0; j < 4; ++j) { const int n = (lane >> 3) + 8 * j; const LAS float* s = scr + (8 * c) * 33 + n;
;         v4u o; o.x = pk2(s[0 * 33], s[1 * 33]); o.y = pk2(s[2 * 33], s[3 * 33]); o.z = pk2(s[4 * 33], s[5 * 33]); o.w = pk2(s[6 * 33], s[7 * 33]);
;         *(GAS v4u*)(WT + (size_t)(drow0 + n) * K + k0 + 8 * c) = o; }
;     LDS_WAIT(); asm volatile("" ::: "memory");
; }
; __device__ __forceinline__ void convert_item(const In& I, unsigned char* ws, int it, LAS float* scr, int lane) {
;     ...
;     int r = it;
;     if (r < T0) { const int f = r / I_FFN; r -= f * I_FFN;
;         if (r < 2 * I_G) { const int up = r >= I_G; r -= up * I_G; const int kb = r / 88, nb = r % 88;
;             transpose_item((up ? I.w_up : I.w_gate) + (size_t)f * D * FF, D, FF, Wgu + (size_t)f * NGU * D, 256 * (nb >> 2) + 32 * (nb & 3) + 128 * up, kb, 32 * nb, scr, lane); }
;         else { r -= 2 * I_G; const int kb = r / 32, nb = r % 32; transpose_item(I.w_down + (size_t)f * FF * D, FF, D, Wd + (size_t)f * D * FF, 32 * nb, kb, 32 * nb, scr, lane); }
;         return; }
;     r -= T0;
;     if (r < 2 * I_NIN) { const int j = r / I_NIN; r -= j * I_NIN; const int kb = r / 88, nb = r % 88;
;         transpose_item(I.nsa_w_in + (size_t)j * D * NSA_IN, D, NSA_IN, Wnin + (size_t)j * NSA_IN_PAD * D, 32 * nb, kb, 32 * nb, scr, lane); return; }
;     r -= 2 * I_NIN;
;     if (r < 2 * I_SQ) { const int j = r / I_SQ; r -= j * I_SQ; const int kb = r / 32, nb = r % 32;
;         transpose_item(I.nsa_w_out + (size_t)j * D * D, D, D, Wnout + (size_t)j * D * D, 32 * nb, kb, 32 * nb, scr, lane); return; }
;     r -= 2 * I_SQ;
.LBB0_540:
	s_add_i32 s30, s14, s16
	s_add_i32 s34, s30, 0xa800
	s_cmp_gt_i32 s34, 0x83ff
	s_mov_b64 s[2:3], -1
	s_cbranch_scc0 .LBB0_594
	s_cmpk_gt_u32 s34, 0x8eff
	s_cbranch_scc0 .LBB0_575
	s_cmpk_gt_u32 s34, 0x92ff
	s_cbranch_scc0 .LBB0_572
	s_cmpk_gt_u32 s34, 0x9fff
	s_cbranch_scc0 .LBB0_553
	s_cmpk_gt_u32 s34, 0xa3ff
	s_cbranch_scc0 .LBB0_550
	s_cmpk_gt_u32 s34, 0xa7ff
	s_cbranch_scc0 .LBB0_547
	s_lshr_b32 s68, s30, 3
	v_readlane_b32 s40, v253, 16
	s_lshl_b64 s[2:3], s[68:69], 16
	v_readlane_b32 s44, v253, 20
	v_readlane_b32 s45, v253, 21
	s_add_u32 s5, s44, s2
	s_addc_u32 s6, s45, s3
	s_lshl_b64 s[2:3], s[68:69], 15
	s_add_u32 s7, s26, s2
	s_addc_u32 s8, s27, s3
	s_and_b32 s4, s33, 32
	s_and_b32 s9, s33, 0xc0
	s_lshl_b32 s2, s4, 2
	s_add_u32 s2, s5, s2
	v_or_b32_e32 v2, s9, v37
	s_addc_u32 s3, s6, 0
	v_lshlrev_b32_e32 v4, 2, v36
	v_mov_b32_e32 v5, v3
	v_lshl_add_u64 v[4:5], s[2:3], 0, v[4:5]
	v_lshlrev_b32_e32 v6, 8, v2
	v_mov_b32_e32 v7, v3
	v_lshl_add_u64 v[28:29], v[4:5], 0, v[6:7]
	global_load_dwordx4 v[4:7], v[28:29], off nt
	global_load_dwordx4 v[8:11], v[28:29], off offset:2048 nt
	v_add_co_u32_e32 v16, vcc, s84, v28
	s_movk_i32 s2, 0x3000
	s_nop 0
	v_addc_co_u32_e32 v17, vcc, 0, v29, vcc
	v_add_co_u32_e32 v24, vcc, s74, v28
	v_add_u32_e32 v2, v39, v44
	s_nop 0
	v_addc_co_u32_e32 v25, vcc, 0, v29, vcc
	global_load_dwordx4 v[12:15], v[24:25], off offset:-4096 nt
	s_nop 0
	global_load_dwordx4 v[16:19], v[16:17], off offset:2048 nt
	s_nop 0
	global_load_dwordx4 v[20:23], v[24:25], off nt
	s_nop 0
	global_load_dwordx4 v[24:27], v[24:25], off offset:2048 nt
	v_add_co_u32_e32 v32, vcc, s2, v28
	s_lshl_b32 s2, s9, 1
	s_nop 0
	v_addc_co_u32_e32 v33, vcc, 0, v29, vcc
	global_load_dwordx4 v[28:31], v[32:33], off nt
	s_nop 0
	global_load_dwordx4 v[32:35], v[32:33], off offset:2048 nt
	s_add_u32 s2, s7, s2
	s_addc_u32 s3, s8, 0
	v_readlane_b32 s41, v253, 17
	v_readlane_b32 s42, v253, 18
	v_readlane_b32 s43, v253, 19
	v_readlane_b32 s46, v253, 22
	v_readlane_b32 s47, v253, 23
	v_readlane_b32 s48, v253, 24
	v_readlane_b32 s49, v253, 25
	v_readlane_b32 s50, v253, 26
	v_readlane_b32 s51, v253, 27
	v_readlane_b32 s52, v253, 28
	v_readlane_b32 s53, v253, 29
	v_readlane_b32 s54, v253, 30
	v_readlane_b32 s55, v253, 31
	s_waitcnt vmcnt(0)
	ds_write2_b32 v2, v4, v5 offset1:1
	ds_write2_b32 v2, v6, v7 offset0:2 offset1:3
	v_add_u32_e32 v4, 0x420, v2
	ds_write2_b32 v4, v8, v9 offset1:1
	v_add_u32_e32 v4, 0x428, v2
	ds_write2_b32 v4, v10, v11 offset1:1
	v_add_u32_e32 v4, 0x840, v2
	v_mov_b32_e32 v5, v3
	ds_write2_b32 v4, v12, v13 offset1:1
	v_add_u32_e32 v4, 0x848, v2
	ds_write2_b32 v4, v14, v15 offset1:1
	v_add_u32_e32 v4, 0xc60, v2
	ds_write2_b32 v4, v16, v17 offset1:1
	v_add_u32_e32 v4, 0xc68, v2
	ds_write2_b32 v4, v18, v19 offset1:1
	v_add_u32_e32 v4, 0x1080, v2
	ds_write2_b32 v4, v20, v21 offset1:1
	v_add_u32_e32 v4, 0x1088, v2
	ds_write2_b32 v4, v22, v23 offset1:1
	v_add_u32_e32 v4, 0x14a0, v2
	ds_write2_b32 v4, v24, v25 offset1:1
	v_add_u32_e32 v4, 0x14a8, v2
	ds_write2_b32 v4, v26, v27 offset1:1
	v_add_u32_e32 v4, 0x18c0, v2
	ds_write2_b32 v4, v28, v29 offset1:1
	v_add_u32_e32 v4, 0x18c8, v2
	ds_write2_b32 v4, v30, v31 offset1:1
	v_add_u32_e32 v4, 0x1ce0, v2
	v_add_u32_e32 v2, 0x1ce8, v2
	ds_write2_b32 v4, v32, v33 offset1:1
	ds_write2_b32 v2, v34, v35 offset1:1
	s_waitcnt lgkmcnt(0)
	ds_read2_b32 v[10:11], v48 offset0:33 offset1:41
	ds_read2_b32 v[12:13], v48 offset1:8
	ds_read2_b32 v[14:15], v48 offset0:66 offset1:74
	ds_read2_b32 v[16:17], v48 offset0:99 offset1:107
	ds_read2_b32 v[18:19], v48 offset0:132 offset1:140
	ds_read2_b32 v[20:21], v48 offset0:165 offset1:173
	ds_read2_b32 v[22:23], v48 offset0:198 offset1:206
	ds_read2_b32 v[24:25], v48 offset0:231 offset1:239
	v_lshlrev_b32_e32 v4, 1, v38
	v_or_b32_e32 v2, s4, v37
	v_lshl_add_u64 v[8:9], s[2:3], 0, v[4:5]
	v_lshlrev_b32_e32 v26, 9, v2
	v_mov_b32_e32 v27, v3
	s_waitcnt lgkmcnt(0)
	v_cvt_pk_bf16_f32 v4, v12, v10
	v_lshl_add_u64 v[26:27], v[8:9], 0, v[26:27]
	v_or_b32_e32 v2, s4, v45
	v_cvt_pk_bf16_f32 v5, v14, v16
	v_cvt_pk_bf16_f32 v6, v18, v20
	v_cvt_pk_bf16_f32 v7, v22, v24
	global_store_dwordx4 v[26:27], v[4:7], off sc1 nt
	v_lshlrev_b32_e32 v10, 9, v2
	v_or_b32_e32 v2, s4, v46
	v_cvt_pk_bf16_f32 v4, v13, v11
	v_mov_b32_e32 v11, v3
	v_lshl_add_u64 v[10:11], v[8:9], 0, v[10:11]
	v_cvt_pk_bf16_f32 v5, v15, v17
	v_cvt_pk_bf16_f32 v6, v19, v21
	v_cvt_pk_bf16_f32 v7, v23, v25
	global_store_dwordx4 v[10:11], v[4:7], off sc1 nt
	ds_read2_b32 v[10:11], v48 offset0:16 offset1:24
	ds_read2_b32 v[12:13], v48 offset0:49 offset1:57
	ds_read2_b32 v[14:15], v48 offset0:82 offset1:90
	ds_read2_b32 v[16:17], v48 offset0:115 offset1:123
	ds_read2_b32 v[18:19], v48 offset0:148 offset1:156
	ds_read2_b32 v[20:21], v48 offset0:181 offset1:189
	ds_read2_b32 v[22:23], v48 offset0:214 offset1:222
	ds_read2_b32 v[24:25], v48 offset0:247 offset1:255
	v_lshlrev_b32_e32 v26, 9, v2
	v_mov_b32_e32 v27, v3
	s_waitcnt lgkmcnt(6)
	v_cvt_pk_bf16_f32 v4, v10, v12
	v_lshl_add_u64 v[26:27], v[8:9], 0, v[26:27]
	v_or_b32_e32 v2, s4, v47
	s_waitcnt lgkmcnt(4)
	v_cvt_pk_bf16_f32 v5, v14, v16
	s_waitcnt lgkmcnt(2)
	v_cvt_pk_bf16_f32 v6, v18, v20
	s_waitcnt lgkmcnt(0)
	v_cvt_pk_bf16_f32 v7, v22, v24
	global_store_dwordx4 v[26:27], v[4:7], off sc1 nt
	v_lshlrev_b32_e32 v10, 9, v2
	s_mov_b64 s[2:3], 0
	v_cvt_pk_bf16_f32 v4, v11, v13
	v_mov_b32_e32 v11, v3
	v_lshl_add_u64 v[8:9], v[8:9], 0, v[10:11]
	v_cvt_pk_bf16_f32 v5, v15, v17
	v_cvt_pk_bf16_f32 v6, v19, v21
	v_cvt_pk_bf16_f32 v7, v23, v25
	global_store_dwordx4 v[8:9], v[4:7], off sc1 nt
	s_waitcnt lgkmcnt(0)
; #define GAS __attribute__((address_space(1)))
; #define LAS __attribute__((address_space(3)))
; #define LDS_WAIT() asm volatile("s_waitcnt lgkmcnt(0)" ::: "memory")
; __device__ __forceinline__ unsigned pk2(float lo, float hi) { unsigned r; asm("v_cvt_pk_bf16_f32 %0, %1, %2" : "=v"(r) : "v"(lo), "v"(hi)); return r; }
; __device__ __forceinline__ void transpose_item(const float* W, int K, int N, bf16* WT, int drow0, int kb, int n0, LAS float* scr, int lane) {
;     const int k0 = 64 * kb; const int c4 = 4 * (lane & 7); const bool ok = (n0 + c4) < N;
;     f32x4 v[8];
; #pragma unroll
;     for (int i = 0; i < 8; ++i) { const int kk = 8 * i + (lane >> 3); v[i] = ok ? *(const f32x4*)(W + (size_t)(k0 + kk) * N + n0 + c4) : (f32x4){0.f, 0.f, 0.f, 0.f}; }
; #pragma unroll
;     for (int i = 0; i < 8; ++i) { const int kk = 8 * i + (lane >> 3); LAS float* d = scr + kk * 33 + c4; d[0] = v[i][0]; d[1] = v[i][1]; d[2] = v[i][2]; d[3] = v[i][3]; }
;     LDS_WAIT(); asm volatile("" ::: "memory");
;     const int c = lane & 7;
; #pragma unroll
;     for (int j = 0; j < 4; ++j) { const int n = (lane >> 3) + 8 * j; const LAS float* s = scr + (8 * c) * 33 + n;
;         v4u o; o.x = pk2(s[0 * 33], s[1 * 33]); o.y = pk2(s[2 * 33], s[3 * 33]); o.z = pk2(s[4 * 33], s[5 * 33]); o.w = pk2(s[6 * 33], s[7 * 33]);
;         *(GAS v4u*)(WT + (size_t)(drow0 + n) * K + k0 + 8 * c) = o; }
;     LDS_WAIT(); asm volatile("" ::: "memory");
; }
; __device__ __forceinline__ void convert_item(const In& I, unsigned char* ws, int it, LAS float* scr, int lane) {
;     ...
;     if (r < 4 * I_W1) { const int jk = r / I_W1; r -= jk * I_W1; const int kb = r / 8, nb = r % 8;
;         transpose_item(I.nsa_w1 + (size_t)jk * 2048 * 256, 2048, 256, W1t + (size_t)jk * 256 * 2048, 32 * nb, kb, 32 * nb, scr, lane); return; }
.LBB0_547:
	s_andn2_b64 vcc, exec, s[2:3]
	s_cbranch_vccnz .LBB0_549
	s_add_i32 s2, s30, 0x400
	s_lshr_b32 s68, s2, 8
	s_lshl_b64 s[2:3], s[68:69], 21
	v_readlane_b32 s40, v253, 16
	v_readlane_b32 s41, v253, 17
	s_add_u32 s4, s40, s2
	s_addc_u32 s5, s41, s3
	s_lshl_b64 s[2:3], s[68:69], 20
	s_add_u32 s6, s24, s2
	s_addc_u32 s3, s25, s3
	s_and_b32 s2, s33, 0xe0
	s_and_b32 s7, s31, 0x7c0
	s_lshl_b32 s8, s2, 2
	s_add_u32 s4, s4, s8
	v_or_b32_e32 v6, s7, v37
	s_addc_u32 s5, s5, 0
	v_lshlrev_b32_e32 v2, 2, v36
	v_lshl_add_u64 v[4:5], s[4:5], 0, v[2:3]
	v_lshlrev_b32_e32 v2, 10, v6
	v_lshl_add_u64 v[32:33], v[4:5], 0, v[2:3]
	v_add_co_u32_e32 v8, vcc, s74, v32
	global_load_dwordx4 v[4:7], v[32:33], off nt
	s_nop 0
	v_addc_co_u32_e32 v9, vcc, 0, v33, vcc
	s_movk_i32 s4, 0x4000
	global_load_dwordx4 v[8:11], v[8:9], off nt
	v_add_co_u32_e32 v12, vcc, s4, v32
	s_movk_i32 s4, 0x6000
	s_nop 0
	v_addc_co_u32_e32 v13, vcc, 0, v33, vcc
	global_load_dwordx4 v[12:15], v[12:13], off nt
	v_add_co_u32_e32 v16, vcc, s4, v32
	s_mov_b32 s4, 0xa000
	s_nop 0
	v_addc_co_u32_e32 v17, vcc, 0, v33, vcc
	global_load_dwordx4 v[16:19], v[16:17], off nt
	v_add_co_u32_e32 v20, vcc, s81, v32
	v_add_u32_e32 v2, v39, v44
	s_nop 0
	v_addc_co_u32_e32 v21, vcc, 0, v33, vcc
	global_load_dwordx4 v[20:23], v[20:21], off nt
	v_add_co_u32_e32 v24, vcc, s4, v32
	s_mov_b32 s4, 0xc000
	s_nop 0
	v_addc_co_u32_e32 v25, vcc, 0, v33, vcc
	global_load_dwordx4 v[24:27], v[24:25], off nt
	v_add_co_u32_e32 v28, vcc, s4, v32
	s_mov_b32 s4, 0xe000
	s_nop 0
	v_addc_co_u32_e32 v29, vcc, 0, v33, vcc
	global_load_dwordx4 v[28:31], v[28:29], off nt
	v_add_co_u32_e32 v32, vcc, s4, v32
	s_lshl_b32 s4, s7, 1
	s_nop 0
	v_addc_co_u32_e32 v33, vcc, 0, v33, vcc
	global_load_dwordx4 v[32:35], v[32:33], off nt
	s_add_u32 s4, s6, s4
	s_addc_u32 s5, s3, 0
	v_readlane_b32 s42, v253, 18
	v_readlane_b32 s43, v253, 19
	v_readlane_b32 s44, v253, 20
	v_readlane_b32 s45, v253, 21
	v_readlane_b32 s46, v253, 22
	v_readlane_b32 s47, v253, 23
	v_readlane_b32 s48, v253, 24
	v_readlane_b32 s49, v253, 25
	v_readlane_b32 s50, v253, 26
	v_readlane_b32 s51, v253, 27
	v_readlane_b32 s52, v253, 28
	v_readlane_b32 s53, v253, 29
	v_readlane_b32 s54, v253, 30
	v_readlane_b32 s55, v253, 31
	s_waitcnt vmcnt(0)
	ds_write2_b32 v2, v4, v5 offset1:1
	ds_write2_b32 v2, v6, v7 offset0:2 offset1:3
	v_add_u32_e32 v4, 0x420, v2
	ds_write2_b32 v4, v8, v9 offset1:1
	v_add_u32_e32 v4, 0x428, v2
	ds_write2_b32 v4, v10, v11 offset1:1
	v_add_u32_e32 v4, 0x840, v2
	ds_write2_b32 v4, v12, v13 offset1:1
	v_add_u32_e32 v4, 0x848, v2
	ds_write2_b32 v4, v14, v15 offset1:1
	v_add_u32_e32 v4, 0xc60, v2
	ds_write2_b32 v4, v16, v17 offset1:1
	v_add_u32_e32 v4, 0xc68, v2
	ds_write2_b32 v4, v18, v19 offset1:1
	v_add_u32_e32 v4, 0x1080, v2
	ds_write2_b32 v4, v20, v21 offset1:1
	v_add_u32_e32 v4, 0x1088, v2
	ds_write2_b32 v4, v22, v23 offset1:1
	v_add_u32_e32 v4, 0x14a0, v2
	ds_write2_b32 v4, v24, v25 offset1:1
	v_add_u32_e32 v4, 0x14a8, v2
	ds_write2_b32 v4, v26, v27 offset1:1
	v_add_u32_e32 v4, 0x18c0, v2
	ds_write2_b32 v4, v28, v29 offset1:1
	v_add_u32_e32 v4, 0x18c8, v2
	ds_write2_b32 v4, v30, v31 offset1:1
	v_add_u32_e32 v4, 0x1ce0, v2
	v_add_u32_e32 v2, 0x1ce8, v2
	ds_write2_b32 v4, v32, v33 offset1:1
	ds_write2_b32 v2, v34, v35 offset1:1
	s_waitcnt lgkmcnt(0)
	ds_read2_b32 v[10:11], v48 offset0:33 offset1:41
	ds_read2_b32 v[12:13], v48 offset1:8
	ds_read2_b32 v[14:15], v48 offset0:66 offset1:74
	ds_read2_b32 v[16:17], v48 offset0:99 offset1:107
	ds_read2_b32 v[18:19], v48 offset0:132 offset1:140
	ds_read2_b32 v[20:21], v48 offset0:165 offset1:173
	ds_read2_b32 v[22:23], v48 offset0:198 offset1:206
	ds_read2_b32 v[24:25], v48 offset0:231 offset1:239
	v_lshlrev_b32_e32 v2, 1, v38
	v_lshl_add_u64 v[8:9], s[4:5], 0, v[2:3]
	v_or_b32_e32 v2, s2, v37
	v_lshlrev_b32_e32 v2, 12, v2
	s_waitcnt lgkmcnt(0)
	v_cvt_pk_bf16_f32 v4, v12, v10
	v_lshl_add_u64 v[26:27], v[8:9], 0, v[2:3]
	v_or_b32_e32 v2, s2, v45
	v_cvt_pk_bf16_f32 v5, v14, v16
	v_cvt_pk_bf16_f32 v6, v18, v20
	v_cvt_pk_bf16_f32 v7, v22, v24
	global_store_dwordx4 v[26:27], v[4:7], off sc1 nt
	v_lshlrev_b32_e32 v10, 12, v2
	v_or_b32_e32 v2, s2, v46
	v_cvt_pk_bf16_f32 v4, v13, v11
	v_mov_b32_e32 v11, v3
	v_lshl_add_u64 v[10:11], v[8:9], 0, v[10:11]
	v_cvt_pk_bf16_f32 v5, v15, v17
	v_cvt_pk_bf16_f32 v6, v19, v21
	v_cvt_pk_bf16_f32 v7, v23, v25
	global_store_dwordx4 v[10:11], v[4:7], off sc1 nt
	ds_read2_b32 v[10:11], v48 offset0:16 offset1:24
	ds_read2_b32 v[12:13], v48 offset0:49 offset1:57
	ds_read2_b32 v[14:15], v48 offset0:82 offset1:90
	ds_read2_b32 v[16:17], v48 offset0:115 offset1:123
	ds_read2_b32 v[18:19], v48 offset0:148 offset1:156
	ds_read2_b32 v[20:21], v48 offset0:181 offset1:189
	ds_read2_b32 v[22:23], v48 offset0:214 offset1:222
	ds_read2_b32 v[24:25], v48 offset0:247 offset1:255
	v_lshlrev_b32_e32 v26, 12, v2
	v_mov_b32_e32 v27, v3
	s_waitcnt lgkmcnt(6)
	v_cvt_pk_bf16_f32 v4, v10, v12
	v_lshl_add_u64 v[26:27], v[8:9], 0, v[26:27]
	v_or_b32_e32 v2, s2, v47
	s_waitcnt lgkmcnt(4)
	v_cvt_pk_bf16_f32 v5, v14, v16
	s_waitcnt lgkmcnt(2)
	v_cvt_pk_bf16_f32 v6, v18, v20
	s_waitcnt lgkmcnt(0)
	v_cvt_pk_bf16_f32 v7, v22, v24
	global_store_dwordx4 v[26:27], v[4:7], off sc1 nt
	v_lshlrev_b32_e32 v10, 12, v2
	s_nop 0
	v_cvt_pk_bf16_f32 v4, v11, v13
	v_mov_b32_e32 v11, v3
	v_lshl_add_u64 v[8:9], v[8:9], 0, v[10:11]
	v_cvt_pk_bf16_f32 v5, v15, v17
	v_cvt_pk_bf16_f32 v6, v19, v21
	v_cvt_pk_bf16_f32 v7, v23, v25
	global_store_dwordx4 v[8:9], v[4:7], off sc1 nt
	s_waitcnt lgkmcnt(0)

; #define GAS __attribute__((address_space(1)))
; #define LAS __attribute__((address_space(3)))
; #define LDS_WAIT() asm volatile("s_waitcnt lgkmcnt(0)" ::: "memory")
; __device__ __forceinline__ unsigned pk2(float lo, float hi) { unsigned r; asm("v_cvt_pk_bf16_f32 %0, %1, %2" : "=v"(r) : "v"(lo), "v"(hi)); return r; }
; __device__ __forceinline__ void transpose_item(const float* W, int K, int N, bf16* WT, int drow0, int kb, int n0, LAS float* scr, int lane) {
;     const int k0 = 64 * kb; const int c4 = 4 * (lane & 7); const bool ok = (n0 + c4) < N;
;     f32x4 v[8];
; #pragma unroll
;     for (int i = 0; i < 8; ++i) { const int kk = 8 * i + (lane >> 3); v[i] = ok ? *(const f32x4*)(W + (size_t)(k0 + kk) * N + n0 + c4) : (f32x4){0.f, 0.f, 0.f, 0.f}; }
; #pragma unroll
;     for (int i = 0; i < 8; ++i) { const int kk = 8 * i + (lane >> 3); LAS float* d = scr + kk * 33 + c4; d[0] = v[i][0]; d[1] = v[i][1]; d[2] = v[i][2]; d[3] = v[i][3]; }
;     LDS_WAIT(); asm volatile("" ::: "memory");
;     const int c = lane & 7;
; #pragma unroll
;     for (int j = 0; j < 4; ++j) { const int n = (lane >> 3) + 8 * j; const LAS float* s = scr + (8 * c) * 33 + n;
;         v4u o; o.x = pk2(s[0 * 33], s[1 * 33]); o.y = pk2(s[2 * 33], s[3 * 33]); o.z = pk2(s[4 * 33], s[5 * 33]); o.w = pk2(s[6 * 33], s[7 * 33]);
;         *(GAS v4u*)(WT + (size_t)(drow0 + n) * K + k0 + 8 * c) = o; }
;     LDS_WAIT(); asm volatile("" ::: "memory");
; }
; __device__ __forceinline__ void convert_item(const In& I, unsigned char* ws, int it, LAS float* scr, int lane) {
;     ...
;     if (r < 2 * I_SQ) { const int j = r / I_SQ; r -= j * I_SQ; const int kb = r / 32, nb = r % 32;
;         transpose_item(I.fox_w_out + (size_t)j * D * D, D, D, Wfout + (size_t)j * D * D, 32 * nb, kb, 32 * nb, scr, lane); return; }
.LBB0_550:
	s_andn2_b64 vcc, exec, s[2:3]
	s_cbranch_vccnz .LBB0_552
	s_add_i32 s2, s30, 0x800
	s_lshr_b32 s68, s2, 9
	v_readlane_b32 s40, v253, 16
	s_lshl_b64 s[2:3], s[68:69], 22
	v_readlane_b32 s52, v253, 28
	v_readlane_b32 s53, v253, 29
	s_add_u32 s4, s52, s2
	s_addc_u32 s5, s53, s3
	s_lshl_b64 s[2:3], s[68:69], 21
	s_add_u32 s6, s22, s2
	v_readlane_b32 s7, v253, 52
	s_addc_u32 s3, s23, s3
	s_add_i32 s7, s7, s15
	s_and_b32 s2, s33, 0x3e0
	s_addk_i32 s7, 0x1900
	s_and_b32 s7, s7, 0x3c0
	s_lshl_b32 s8, s2, 2
	s_add_u32 s4, s4, s8
	v_or_b32_e32 v6, s7, v37
	s_addc_u32 s5, s5, 0
	v_lshlrev_b32_e32 v2, 2, v36
	v_lshl_add_u64 v[4:5], s[4:5], 0, v[2:3]
	v_lshlrev_b32_e32 v2, 12, v6
	v_lshl_add_u64 v[32:33], v[4:5], 0, v[2:3]
	v_add_co_u32_e32 v8, vcc, s81, v32
	global_load_dwordx4 v[4:7], v[32:33], off nt
	s_nop 0
	v_addc_co_u32_e32 v9, vcc, 0, v33, vcc
	global_load_dwordx4 v[8:11], v[8:9], off nt
	v_add_co_u32_e32 v12, vcc, s79, v32
	v_add_u32_e32 v2, v39, v44
	s_nop 0
	v_addc_co_u32_e32 v13, vcc, 0, v33, vcc
	global_load_dwordx4 v[12:15], v[12:13], off nt
	v_add_co_u32_e32 v16, vcc, s80, v32
	s_lshl_b32 s4, s7, 1
	s_nop 0
	v_addc_co_u32_e32 v17, vcc, 0, v33, vcc
	global_load_dwordx4 v[16:19], v[16:17], off nt
	v_add_co_u32_e32 v20, vcc, s85, v32
	s_add_u32 s4, s6, s4
	s_nop 0
	v_addc_co_u32_e32 v21, vcc, 0, v33, vcc
	global_load_dwordx4 v[20:23], v[20:21], off nt
	v_add_co_u32_e32 v24, vcc, s86, v32
	s_addc_u32 s5, s3, 0
	s_nop 0
	v_addc_co_u32_e32 v25, vcc, 0, v33, vcc
	global_load_dwordx4 v[24:27], v[24:25], off nt
	v_add_co_u32_e32 v28, vcc, s87, v32
	v_readlane_b32 s41, v253, 17
	s_nop 0
	v_addc_co_u32_e32 v29, vcc, 0, v33, vcc
	global_load_dwordx4 v[28:31], v[28:29], off nt
	v_add_co_u32_e32 v32, vcc, s89, v32
	v_readlane_b32 s42, v253, 18
	s_nop 0
	v_addc_co_u32_e32 v33, vcc, 0, v33, vcc
	global_load_dwordx4 v[32:35], v[32:33], off nt
	v_readlane_b32 s43, v253, 19
	v_readlane_b32 s44, v253, 20
	v_readlane_b32 s45, v253, 21
	v_readlane_b32 s46, v253, 22
	v_readlane_b32 s47, v253, 23
	v_readlane_b32 s48, v253, 24
	v_readlane_b32 s49, v253, 25
	v_readlane_b32 s50, v253, 26
	v_readlane_b32 s51, v253, 27
	v_readlane_b32 s54, v253, 30
	v_readlane_b32 s55, v253, 31
	s_waitcnt vmcnt(0)
	ds_write2_b32 v2, v4, v5 offset1:1
	ds_write2_b32 v2, v6, v7 offset0:2 offset1:3
	v_add_u32_e32 v4, 0x420, v2
	ds_write2_b32 v4, v8, v9 offset1:1
	v_add_u32_e32 v4, 0x428, v2
	ds_write2_b32 v4, v10, v11 offset1:1
	v_add_u32_e32 v4, 0x840, v2
	ds_write2_b32 v4, v12, v13 offset1:1
	v_add_u32_e32 v4, 0x848, v2
	ds_write2_b32 v4, v14, v15 offset1:1
	v_add_u32_e32 v4, 0xc60, v2
	ds_write2_b32 v4, v16, v17 offset1:1
	v_add_u32_e32 v4, 0xc68, v2
	ds_write2_b32 v4, v18, v19 offset1:1
	v_add_u32_e32 v4, 0x1080, v2
	ds_write2_b32 v4, v20, v21 offset1:1
	v_add_u32_e32 v4, 0x1088, v2
	ds_write2_b32 v4, v22, v23 offset1:1
	v_add_u32_e32 v4, 0x14a0, v2
	ds_write2_b32 v4, v24, v25 offset1:1
	v_add_u32_e32 v4, 0x14a8, v2
	ds_write2_b32 v4, v26, v27 offset1:1
	v_add_u32_e32 v4, 0x18c0, v2
	ds_write2_b32 v4, v28, v29 offset1:1
	v_add_u32_e32 v4, 0x18c8, v2
	ds_write2_b32 v4, v30, v31 offset1:1
	v_add_u32_e32 v4, 0x1ce0, v2
	v_add_u32_e32 v2, 0x1ce8, v2
	ds_write2_b32 v4, v32, v33 offset1:1
	ds_write2_b32 v2, v34, v35 offset1:1
	s_waitcnt lgkmcnt(0)
	ds_read2_b32 v[10:11], v48 offset0:33 offset1:41
	ds_read2_b32 v[12:13], v48 offset1:8
	v_lshlrev_b32_e32 v2, 1, v38
	ds_read2_b32 v[14:15], v48 offset0:66 offset1:74
	ds_read2_b32 v[16:17], v48 offset0:99 offset1:107
	ds_read2_b32 v[18:19], v48 offset0:132 offset1:140
	ds_read2_b32 v[20:21], v48 offset0:165 offset1:173
	ds_read2_b32 v[22:23], v48 offset0:198 offset1:206
	ds_read2_b32 v[24:25], v48 offset0:231 offset1:239
	v_lshl_add_u64 v[8:9], s[4:5], 0, v[2:3]
	v_or_b32_e32 v2, s2, v37
	v_lshlrev_b32_e32 v2, 11, v2
	v_lshl_add_u64 v[26:27], v[8:9], 0, v[2:3]
	v_or_b32_e32 v2, s2, v45
	s_waitcnt lgkmcnt(0)
	v_cvt_pk_bf16_f32 v4, v12, v10
	v_lshlrev_b32_e32 v2, 11, v2
	v_cvt_pk_bf16_f32 v5, v14, v16
	v_cvt_pk_bf16_f32 v6, v18, v20
	v_cvt_pk_bf16_f32 v7, v22, v24
	global_store_dwordx4 v[26:27], v[4:7], off sc1 nt
	s_nop 1
	v_cvt_pk_bf16_f32 v4, v13, v11
	v_lshl_add_u64 v[10:11], v[8:9], 0, v[2:3]
	v_cvt_pk_bf16_f32 v5, v15, v17
	v_cvt_pk_bf16_f32 v6, v19, v21
	v_cvt_pk_bf16_f32 v7, v23, v25
	global_store_dwordx4 v[10:11], v[4:7], off sc1 nt
	ds_read2_b32 v[10:11], v48 offset0:16 offset1:24
	ds_read2_b32 v[12:13], v48 offset0:49 offset1:57
	ds_read2_b32 v[14:15], v48 offset0:82 offset1:90
	ds_read2_b32 v[16:17], v48 offset0:115 offset1:123
	ds_read2_b32 v[18:19], v48 offset0:148 offset1:156
	ds_read2_b32 v[20:21], v48 offset0:181 offset1:189
	ds_read2_b32 v[22:23], v48 offset0:214 offset1:222
	ds_read2_b32 v[24:25], v48 offset0:247 offset1:255
	v_or_b32_e32 v2, s2, v46
	v_lshlrev_b32_e32 v2, 11, v2
	v_lshl_add_u64 v[26:27], v[8:9], 0, v[2:3]
	v_or_b32_e32 v2, s2, v47
	v_lshlrev_b32_e32 v2, 11, v2
	s_waitcnt lgkmcnt(6)
	v_cvt_pk_bf16_f32 v4, v10, v12
	s_waitcnt lgkmcnt(4)
	v_cvt_pk_bf16_f32 v5, v14, v16
	s_waitcnt lgkmcnt(2)
	v_cvt_pk_bf16_f32 v6, v18, v20
	s_waitcnt lgkmcnt(0)
	v_cvt_pk_bf16_f32 v7, v22, v24
	v_lshl_add_u64 v[8:9], v[8:9], 0, v[2:3]
	global_store_dwordx4 v[26:27], v[4:7], off sc1 nt
	s_nop 1
	v_cvt_pk_bf16_f32 v4, v11, v13
	v_cvt_pk_bf16_f32 v5, v15, v17
	v_cvt_pk_bf16_f32 v6, v19, v21
	v_cvt_pk_bf16_f32 v7, v23, v25
	global_store_dwordx4 v[8:9], v[4:7], off sc1 nt
	s_waitcnt lgkmcnt(0)

; #define LAS __attribute__((address_space(3)))
; __device__ __forceinline__ void transpose_item(const float* W, int K, int N, bf16* WT, int drow0, int kb, int n0, LAS float* scr, int lane) {
;     const int k0 = 64 * kb; const int c4 = 4 * (lane & 7); const bool ok = (n0 + c4) < N;
;     f32x4 v[8];
; #pragma unroll
;     for (int i = 0; i < 8; ++i) { const int kk = 8 * i + (lane >> 3); v[i] = ok ? *(const f32x4*)(W + (size_t)(k0 + kk) * N + n0 + c4) : (f32x4){0.f, 0.f, 0.f, 0.f}; }
; __device__ __forceinline__ void convert_item(const In& I, unsigned char* ws, int it, LAS float* scr, int lane) {
;     ...
;     if (r < 2 * I_FIN) { const int j = r / I_FIN; r -= j * I_FIN; const int kb = r / 104, nb = r % 104;
;         transpose_item(I.fox_w_in + (size_t)j * D * FOX_IN, D, FOX_IN, Wfin + (size_t)j * FOX_IN_PAD * D, 32 * nb, kb, 32 * nb, scr, lane); return; }
.LBB0_553:
	s_andn2_b64 vcc, exec, s[2:3]
	s_cbranch_vccnz .LBB0_571
	s_add_i32 s2, s30, 0x1500
	s_cmpk_gt_u32 s2, 0x67f
	s_cselect_b64 s[8:9], -1, 0
	s_and_b64 s[2:3], s[8:9], exec
	s_cselect_b32 s2, 0xf980, 0
	s_cselect_b32 s3, 0xc10000, 0
	s_add_i32 s2, s14, s2
	s_add_i32 s2, s2, s16
	s_addk_i32 s2, 0x1500
	s_sext_i32_i16 s4, s2
	s_mulk_i32 s4, 0x4ec5
	s_lshr_b32 s5, s4, 31
	s_ashr_i32 s4, s4, 21
	s_add_i32 s5, s4, s5
	s_mul_i32 s4, s5, 0x68
	v_readlane_b32 s40, v253, 16
	s_sub_i32 s2, s2, s4
	v_readlane_b32 s48, v253, 24
	s_sext_i32_i16 s2, s2
	v_readlane_b32 s49, v253, 25
	s_add_u32 s7, s48, s3
	s_addc_u32 s35, s49, 0
	s_lshl_b32 s4, s2, 5
	s_lshl_b32 s6, s5, 6
	s_ashr_i32 s5, s4, 31
	s_lshl_b64 s[10:11], s[4:5], 2
	v_or_b32_e32 v2, s4, v36
	s_movk_i32 s2, 0xc10
	s_add_u32 s10, s7, s10
	v_cmp_gt_i32_e64 s[2:3], s2, v2
	s_addc_u32 s11, s35, s11
	v_lshlrev_b32_e32 v2, 2, v36
	v_or_b32_e32 v42, s6, v37
	v_lshl_add_u64 v[40:41], s[10:11], 0, v[2:3]
	v_mov_b32_e32 v8, 0
	v_mov_b32_e32 v4, 0
	v_mov_b32_e32 v5, 0
	v_mov_b32_e32 v6, 0
	v_mov_b32_e32 v7, 0
	v_readlane_b32 s41, v253, 17
	v_readlane_b32 s42, v253, 18
	v_readlane_b32 s43, v253, 19
	v_readlane_b32 s44, v253, 20
	v_readlane_b32 s45, v253, 21
	v_readlane_b32 s46, v253, 22
	v_readlane_b32 s47, v253, 23
	v_readlane_b32 s50, v253, 26
	v_readlane_b32 s51, v253, 27
	v_readlane_b32 s52, v253, 28
	v_readlane_b32 s53, v253, 29
	v_readlane_b32 s54, v253, 30
	v_readlane_b32 s55, v253, 31
	s_and_saveexec_b64 s[10:11], s[2:3]
	s_cbranch_execz .LBB0_556
	v_mul_i32_i24_e32 v4, 0x3040, v42
	v_ashrrev_i32_e32 v5, 31, v4
	v_lshl_add_u64 v[4:5], v[40:41], 0, v[4:5]
	global_load_dwordx4 v[4:7], v[4:5], off nt
.LBB0_556:
	s_or_b64 exec, exec, s[10:11]
	v_mov_b32_e32 v9, 0
	v_mov_b32_e32 v10, 0
	v_mov_b32_e32 v11, 0
	s_and_saveexec_b64 s[10:11], s[2:3]
	s_cbranch_execz .LBB0_558
	v_mul_i32_i24_e32 v8, 0x3040, v42
	v_ashrrev_i32_e32 v9, 31, v8
	v_lshl_add_u64 v[8:9], v[40:41], 0, v[8:9]
	v_add_co_u32_e32 v8, vcc, 0x18000, v8
	s_nop 1
	v_addc_co_u32_e32 v9, vcc, 0, v9, vcc
	global_load_dwordx4 v[8:11], v[8:9], off offset:512 nt
.LBB0_558:
	s_or_b64 exec, exec, s[10:11]
	v_mov_b32_e32 v12, 0
	v_mov_b32_e32 v16, 0
	v_mov_b32_e32 v17, 0
	v_mov_b32_e32 v18, 0
	v_mov_b32_e32 v19, 0
	s_and_saveexec_b64 s[10:11], s[2:3]
	s_cbranch_execz .LBB0_560
	v_mul_i32_i24_e32 v14, 0x3040, v42
	v_ashrrev_i32_e32 v15, 31, v14
	v_lshl_add_u64 v[14:15], v[40:41], 0, v[14:15]
	v_add_co_u32_e32 v14, vcc, 0x30000, v14
	s_nop 1
	v_addc_co_u32_e32 v15, vcc, 0, v15, vcc
	global_load_dwordx4 v[16:19], v[14:15], off offset:1024 nt
.LBB0_560:
	s_or_b64 exec, exec, s[10:11]
	v_mov_b32_e32 v13, 0
	v_mov_b32_e32 v14, 0
	v_mov_b32_e32 v15, 0
	s_and_saveexec_b64 s[10:11], s[2:3]
	s_cbranch_execz .LBB0_562
	v_mul_i32_i24_e32 v12, 0x3040, v42
	v_ashrrev_i32_e32 v13, 31, v12
	v_lshl_add_u64 v[12:13], v[40:41], 0, v[12:13]
	v_add_co_u32_e32 v12, vcc, 0x48000, v12
	s_nop 1
	v_addc_co_u32_e32 v13, vcc, 0, v13, vcc
	global_load_dwordx4 v[12:15], v[12:13], off offset:1536 nt
.LBB0_562:
	s_or_b64 exec, exec, s[10:11]
	v_mov_b32_e32 v20, 0
	v_mov_b32_e32 v24, 0
	v_mov_b32_e32 v25, 0
	v_mov_b32_e32 v26, 0
	v_mov_b32_e32 v27, 0
	s_and_saveexec_b64 s[10:11], s[2:3]
	s_cbranch_execz .LBB0_564
	v_mul_i32_i24_e32 v22, 0x3040, v42
	v_ashrrev_i32_e32 v23, 31, v22
	v_lshl_add_u64 v[22:23], v[40:41], 0, v[22:23]
	v_add_co_u32_e32 v22, vcc, 0x60000, v22
	s_nop 1
	v_addc_co_u32_e32 v23, vcc, 0, v23, vcc
	global_load_dwordx4 v[24:27], v[22:23], off offset:2048 nt
.LBB0_564:
	s_or_b64 exec, exec, s[10:11]
	v_mov_b32_e32 v21, 0
	v_mov_b32_e32 v22, 0
	v_mov_b32_e32 v23, 0
	s_and_saveexec_b64 s[10:11], s[2:3]
	s_cbranch_execz .LBB0_566
	v_mul_i32_i24_e32 v20, 0x3040, v42
	v_ashrrev_i32_e32 v21, 31, v20
	v_lshl_add_u64 v[20:21], v[40:41], 0, v[20:21]
	v_add_co_u32_e32 v20, vcc, 0x78000, v20
	s_nop 1
	v_addc_co_u32_e32 v21, vcc, 0, v21, vcc
	global_load_dwordx4 v[20:23], v[20:21], off offset:2560 nt
.LBB0_566:
	s_or_b64 exec, exec, s[10:11]
	v_mov_b32_e32 v28, 0
	v_mov_b32_e32 v32, 0
	v_mov_b32_e32 v33, 0
	v_mov_b32_e32 v34, 0
	v_mov_b32_e32 v35, 0
	s_and_saveexec_b64 s[10:11], s[2:3]
	s_cbranch_execz .LBB0_568
	v_mul_i32_i24_e32 v30, 0x3040, v42
	v_ashrrev_i32_e32 v31, 31, v30
	v_lshl_add_u64 v[30:31], v[40:41], 0, v[30:31]
	v_add_co_u32_e32 v30, vcc, 0x90000, v30
	s_nop 1
	v_addc_co_u32_e32 v31, vcc, 0, v31, vcc
	global_load_dwordx4 v[32:35], v[30:31], off offset:3072 nt
; #define GAS __attribute__((address_space(1)))
; #define LAS __attribute__((address_space(3)))
; #define LDS_WAIT() asm volatile("s_waitcnt lgkmcnt(0)" ::: "memory")
; __device__ __forceinline__ unsigned pk2(float lo, float hi) { unsigned r; asm("v_cvt_pk_bf16_f32 %0, %1, %2" : "=v"(r) : "v"(lo), "v"(hi)); return r; }
; __device__ __forceinline__ void transpose_item(const float* W, int K, int N, bf16* WT, int drow0, int kb, int n0, LAS float* scr, int lane) {
;     ...
;     for (int i = 0; i < 8; ++i) { const int kk = 8 * i + (lane >> 3); v[i] = ok ? *(const f32x4*)(W + (size_t)(k0 + kk) * N + n0 + c4) : (f32x4){0.f, 0.f, 0.f, 0.f}; }
; #pragma unroll
;     for (int i = 0; i < 8; ++i) { const int kk = 8 * i + (lane >> 3); LAS float* d = scr + kk * 33 + c4; d[0] = v[i][0]; d[1] = v[i][1]; d[2] = v[i][2]; d[3] = v[i][3]; }
;     LDS_WAIT(); asm volatile("" ::: "memory");
;     const int c = lane & 7;
; #pragma unroll
;     for (int j = 0; j < 4; ++j) { const int n = (lane >> 3) + 8 * j; const LAS float* s = scr + (8 * c) * 33 + n;
;         v4u o; o.x = pk2(s[0 * 33], s[1 * 33]); o.y = pk2(s[2 * 33], s[3 * 33]); o.z = pk2(s[4 * 33], s[5 * 33]); o.w = pk2(s[6 * 33], s[7 * 33]);
;         *(GAS v4u*)(WT + (size_t)(drow0 + n) * K + k0 + 8 * c) = o; }
; __device__ __forceinline__ void convert_item(const In& I, unsigned char* ws, int it, LAS float* scr, int lane) {
;     ...
;     if (r < 2 * I_FIN) { const int j = r / I_FIN; r -= j * I_FIN; const int kb = r / 104, nb = r % 104;
;         transpose_item(I.fox_w_in + (size_t)j * D * FOX_IN, D, FOX_IN, Wfin + (size_t)j * FOX_IN_PAD * D, 32 * nb, kb, 32 * nb, scr, lane); return; }
.LBB0_568:
	s_or_b64 exec, exec, s[10:11]
	v_mov_b32_e32 v29, 0
	v_mov_b32_e32 v30, 0
	v_mov_b32_e32 v31, 0
	s_and_saveexec_b64 s[10:11], s[2:3]
	s_cbranch_execz .LBB0_570
	v_mul_i32_i24_e32 v28, 0x3040, v42
	v_ashrrev_i32_e32 v29, 31, v28
	v_lshl_add_u64 v[28:29], v[40:41], 0, v[28:29]
	v_add_co_u32_e32 v28, vcc, 0xa8000, v28
	s_nop 1
	v_addc_co_u32_e32 v29, vcc, 0, v29, vcc
	global_load_dwordx4 v[28:31], v[28:29], off offset:3584 nt
.LBB0_570:
	s_or_b64 exec, exec, s[10:11]
	v_add_u32_e32 v2, v39, v44
	s_waitcnt vmcnt(0)
	ds_write2_b32 v2, v4, v5 offset1:1
	ds_write2_b32 v2, v6, v7 offset0:2 offset1:3
	v_add_u32_e32 v4, 0x420, v2
	ds_write2_b32 v4, v8, v9 offset1:1
	v_add_u32_e32 v4, 0x428, v2
	ds_write2_b32 v4, v10, v11 offset1:1
	v_add_u32_e32 v4, 0x840, v2
	ds_write2_b32 v4, v16, v17 offset1:1
	v_add_u32_e32 v4, 0x848, v2
	ds_write2_b32 v4, v18, v19 offset1:1
	v_add_u32_e32 v4, 0xc60, v2
	ds_write2_b32 v4, v12, v13 offset1:1
	v_add_u32_e32 v4, 0xc68, v2
	ds_write2_b32 v4, v14, v15 offset1:1
	v_add_u32_e32 v4, 0x1080, v2
	ds_write2_b32 v4, v24, v25 offset1:1
	v_add_u32_e32 v4, 0x1088, v2
	ds_write2_b32 v4, v26, v27 offset1:1
	v_add_u32_e32 v4, 0x14a0, v2
	ds_write2_b32 v4, v20, v21 offset1:1
	v_add_u32_e32 v4, 0x14a8, v2
	ds_write2_b32 v4, v22, v23 offset1:1
	v_add_u32_e32 v4, 0x18c0, v2
	ds_write2_b32 v4, v32, v33 offset1:1
	v_add_u32_e32 v4, 0x18c8, v2
	s_and_b64 s[2:3], s[8:9], exec
	ds_write2_b32 v4, v34, v35 offset1:1
	v_add_u32_e32 v4, 0x1ce0, v2
	v_add_u32_e32 v2, 0x1ce8, v2
	s_cselect_b32 s2, 0x680000, 0
	ds_write2_b32 v4, v28, v29 offset1:1
	ds_write2_b32 v2, v30, v31 offset1:1
	s_add_u32 s5, s20, s2
	s_waitcnt lgkmcnt(0)
	s_addc_u32 s8, s21, 0
	s_ashr_i32 s7, s6, 31
	s_lshl_b64 s[2:3], s[6:7], 1
	ds_read2_b32 v[8:9], v48 offset0:33 offset1:41
	ds_read2_b32 v[10:11], v48 offset1:8
	ds_read2_b32 v[12:13], v48 offset0:66 offset1:74
	ds_read2_b32 v[14:15], v48 offset0:99 offset1:107
	ds_read2_b32 v[16:17], v48 offset0:132 offset1:140
	ds_read2_b32 v[18:19], v48 offset0:165 offset1:173
	ds_read2_b32 v[20:21], v48 offset0:198 offset1:206
	ds_read2_b32 v[22:23], v48 offset0:231 offset1:239
	s_add_u32 s2, s5, s2
	v_or_b32_e32 v26, s4, v37
	s_addc_u32 s3, s8, s3
	v_lshlrev_b32_e32 v2, 1, v38
	v_ashrrev_i32_e32 v27, 31, v26
	v_lshl_add_u64 v[24:25], s[2:3], 0, v[2:3]
	v_lshlrev_b64 v[26:27], 11, v[26:27]
	s_waitcnt lgkmcnt(0)
	v_cvt_pk_bf16_f32 v4, v10, v8
	v_lshl_add_u64 v[26:27], v[24:25], 0, v[26:27]
	v_or_b32_e32 v8, s4, v45
	v_cvt_pk_bf16_f32 v5, v12, v14
	v_cvt_pk_bf16_f32 v6, v16, v18
	v_cvt_pk_bf16_f32 v7, v20, v22
	global_store_dwordx4 v[26:27], v[4:7], off sc1 nt
	s_nop 1
	v_cvt_pk_bf16_f32 v4, v11, v9
	v_ashrrev_i32_e32 v9, 31, v8
	v_lshlrev_b64 v[8:9], 11, v[8:9]
	v_cvt_pk_bf16_f32 v5, v13, v15
	v_cvt_pk_bf16_f32 v6, v17, v19
	v_cvt_pk_bf16_f32 v7, v21, v23
	v_lshl_add_u64 v[8:9], v[24:25], 0, v[8:9]
	ds_read2_b32 v[10:11], v48 offset0:16 offset1:24
	ds_read2_b32 v[12:13], v48 offset0:49 offset1:57
	ds_read2_b32 v[14:15], v48 offset0:82 offset1:90
	ds_read2_b32 v[16:17], v48 offset0:115 offset1:123
	ds_read2_b32 v[18:19], v48 offset0:148 offset1:156
	ds_read2_b32 v[20:21], v48 offset0:181 offset1:189
	ds_read2_b32 v[22:23], v48 offset0:214 offset1:222
	ds_read2_b32 v[26:27], v48 offset0:247 offset1:255
	global_store_dwordx4 v[8:9], v[4:7], off sc1 nt
	v_or_b32_e32 v8, s4, v46
	v_ashrrev_i32_e32 v9, 31, v8
	v_lshlrev_b64 v[8:9], 11, v[8:9]
	v_lshl_add_u64 v[8:9], v[24:25], 0, v[8:9]
	s_waitcnt lgkmcnt(6)
	v_cvt_pk_bf16_f32 v4, v10, v12
	s_waitcnt lgkmcnt(4)
	v_cvt_pk_bf16_f32 v5, v14, v16
	s_waitcnt lgkmcnt(2)
	v_cvt_pk_bf16_f32 v6, v18, v20
	s_waitcnt lgkmcnt(0)
	v_cvt_pk_bf16_f32 v7, v22, v26
	global_store_dwordx4 v[8:9], v[4:7], off sc1 nt
	v_or_b32_e32 v8, s4, v47
	v_ashrrev_i32_e32 v9, 31, v8
	v_lshlrev_b64 v[8:9], 11, v[8:9]
	v_lshl_add_u64 v[8:9], v[24:25], 0, v[8:9]
	v_cvt_pk_bf16_f32 v4, v11, v13
	v_cvt_pk_bf16_f32 v5, v15, v17
	v_cvt_pk_bf16_f32 v6, v19, v21
	v_cvt_pk_bf16_f32 v7, v23, v27
	global_store_dwordx4 v[8:9], v[4:7], off sc1 nt
	s_waitcnt lgkmcnt(0)

; #define GAS __attribute__((address_space(1)))
; #define LAS __attribute__((address_space(3)))
; #define LDS_WAIT() asm volatile("s_waitcnt lgkmcnt(0)" ::: "memory")
; __device__ __forceinline__ unsigned pk2(float lo, float hi) { unsigned r; asm("v_cvt_pk_bf16_f32 %0, %1, %2" : "=v"(r) : "v"(lo), "v"(hi)); return r; }
; __device__ __forceinline__ void transpose_item(const float* W, int K, int N, bf16* WT, int drow0, int kb, int n0, LAS float* scr, int lane) {
;     const int k0 = 64 * kb; const int c4 = 4 * (lane & 7); const bool ok = (n0 + c4) < N;
;     f32x4 v[8];
; #pragma unroll
;     for (int i = 0; i < 8; ++i) { const int kk = 8 * i + (lane >> 3); v[i] = ok ? *(const f32x4*)(W + (size_t)(k0 + kk) * N + n0 + c4) : (f32x4){0.f, 0.f, 0.f, 0.f}; }
; #pragma unroll
;     for (int i = 0; i < 8; ++i) { const int kk = 8 * i + (lane >> 3); LAS float* d = scr + kk * 33 + c4; d[0] = v[i][0]; d[1] = v[i][1]; d[2] = v[i][2]; d[3] = v[i][3]; }
;     LDS_WAIT(); asm volatile("" ::: "memory");
;     const int c = lane & 7;
; #pragma unroll
;     for (int j = 0; j < 4; ++j) { const int n = (lane >> 3) + 8 * j; const LAS float* s = scr + (8 * c) * 33 + n;
;         v4u o; o.x = pk2(s[0 * 33], s[1 * 33]); o.y = pk2(s[2 * 33], s[3 * 33]); o.z = pk2(s[4 * 33], s[5 * 33]); o.w = pk2(s[6 * 33], s[7 * 33]);
;         *(GAS v4u*)(WT + (size_t)(drow0 + n) * K + k0 + 8 * c) = o; }
;     LDS_WAIT(); asm volatile("" ::: "memory");
; }
.LBB0_572:
	s_andn2_b64 vcc, exec, s[2:3]
	s_cbranch_vccnz .LBB0_574
	s_add_i32 s2, s30, 0x1900
	s_lshr_b32 s68, s2, 9
	v_readlane_b32 s40, v253, 16
	s_lshl_b64 s[2:3], s[68:69], 22
	v_readlane_b32 s46, v253, 22
	v_readlane_b32 s47, v253, 23
	s_add_u32 s4, s46, s2
	s_addc_u32 s5, s47, s3
	s_lshl_b64 s[2:3], s[68:69], 21
	s_add_u32 s6, s18, s2
	v_readlane_b32 s7, v253, 52
	s_addc_u32 s3, s19, s3
	s_add_i32 s7, s7, s15
	s_and_b32 s2, s33, 0x3e0
	s_add_i32 s7, s7, 0xfffefb00
	s_and_b32 s7, s7, 0x3c0
	s_lshl_b32 s8, s2, 2
	s_add_u32 s4, s4, s8
	v_or_b32_e32 v6, s7, v37
	s_addc_u32 s5, s5, 0
	v_lshlrev_b32_e32 v2, 2, v36
	v_lshl_add_u64 v[4:5], s[4:5], 0, v[2:3]
	v_lshlrev_b32_e32 v2, 12, v6
	v_lshl_add_u64 v[32:33], v[4:5], 0, v[2:3]
	v_add_co_u32_e32 v8, vcc, s81, v32
	global_load_dwordx4 v[4:7], v[32:33], off nt
	s_nop 0
	v_addc_co_u32_e32 v9, vcc, 0, v33, vcc
	global_load_dwordx4 v[8:11], v[8:9], off nt
	v_add_co_u32_e32 v12, vcc, s79, v32
	v_add_u32_e32 v2, v39, v44
	s_nop 0
	v_addc_co_u32_e32 v13, vcc, 0, v33, vcc
	global_load_dwordx4 v[12:15], v[12:13], off nt
	v_add_co_u32_e32 v16, vcc, s80, v32
	s_lshl_b32 s4, s7, 1
	s_nop 0
	v_addc_co_u32_e32 v17, vcc, 0, v33, vcc
	global_load_dwordx4 v[16:19], v[16:17], off nt
	v_add_co_u32_e32 v20, vcc, s85, v32
	s_add_u32 s4, s6, s4
	s_nop 0
	v_addc_co_u32_e32 v21, vcc, 0, v33, vcc
	global_load_dwordx4 v[20:23], v[20:21], off nt
	v_add_co_u32_e32 v24, vcc, s86, v32
	s_addc_u32 s5, s3, 0
	s_nop 0
	v_addc_co_u32_e32 v25, vcc, 0, v33, vcc
	global_load_dwordx4 v[24:27], v[24:25], off nt
	v_add_co_u32_e32 v28, vcc, s87, v32
	v_readlane_b32 s41, v253, 17
	s_nop 0
	v_addc_co_u32_e32 v29, vcc, 0, v33, vcc
	global_load_dwordx4 v[28:31], v[28:29], off nt
	v_add_co_u32_e32 v32, vcc, s89, v32
	v_readlane_b32 s42, v253, 18
	s_nop 0
	v_addc_co_u32_e32 v33, vcc, 0, v33, vcc
	global_load_dwordx4 v[32:35], v[32:33], off nt
	v_readlane_b32 s43, v253, 19
	v_readlane_b32 s44, v253, 20
	v_readlane_b32 s45, v253, 21
	v_readlane_b32 s48, v253, 24
	v_readlane_b32 s49, v253, 25
	v_readlane_b32 s50, v253, 26
	v_readlane_b32 s51, v253, 27
	v_readlane_b32 s52, v253, 28
	v_readlane_b32 s53, v253, 29
	v_readlane_b32 s54, v253, 30
	v_readlane_b32 s55, v253, 31
	s_waitcnt vmcnt(0)
	ds_write2_b32 v2, v4, v5 offset1:1
	ds_write2_b32 v2, v6, v7 offset0:2 offset1:3
	v_add_u32_e32 v4, 0x420, v2
	ds_write2_b32 v4, v8, v9 offset1:1
	v_add_u32_e32 v4, 0x428, v2
	ds_write2_b32 v4, v10, v11 offset1:1
	v_add_u32_e32 v4, 0x840, v2
	ds_write2_b32 v4, v12, v13 offset1:1
	v_add_u32_e32 v4, 0x848, v2
	ds_write2_b32 v4, v14, v15 offset1:1
	v_add_u32_e32 v4, 0xc60, v2
	ds_write2_b32 v4, v16, v17 offset1:1
	v_add_u32_e32 v4, 0xc68, v2
	ds_write2_b32 v4, v18, v19 offset1:1
	v_add_u32_e32 v4, 0x1080, v2
	ds_write2_b32 v4, v20, v21 offset1:1
	v_add_u32_e32 v4, 0x1088, v2
	ds_write2_b32 v4, v22, v23 offset1:1
	v_add_u32_e32 v4, 0x14a0, v2
	ds_write2_b32 v4, v24, v25 offset1:1
	v_add_u32_e32 v4, 0x14a8, v2
	ds_write2_b32 v4, v26, v27 offset1:1
	v_add_u32_e32 v4, 0x18c0, v2
	ds_write2_b32 v4, v28, v29 offset1:1
	v_add_u32_e32 v4, 0x18c8, v2
	ds_write2_b32 v4, v30, v31 offset1:1
	v_add_u32_e32 v4, 0x1ce0, v2
	v_add_u32_e32 v2, 0x1ce8, v2
	ds_write2_b32 v4, v32, v33 offset1:1
	ds_write2_b32 v2, v34, v35 offset1:1
	s_waitcnt lgkmcnt(0)
	ds_read2_b32 v[10:11], v48 offset0:33 offset1:41
	ds_read2_b32 v[12:13], v48 offset1:8
	v_lshlrev_b32_e32 v2, 1, v38
	ds_read2_b32 v[14:15], v48 offset0:66 offset1:74
	ds_read2_b32 v[16:17], v48 offset0:99 offset1:107
	ds_read2_b32 v[18:19], v48 offset0:132 offset1:140
	ds_read2_b32 v[20:21], v48 offset0:165 offset1:173
	ds_read2_b32 v[22:23], v48 offset0:198 offset1:206
	ds_read2_b32 v[24:25], v48 offset0:231 offset1:239
	v_lshl_add_u64 v[8:9], s[4:5], 0, v[2:3]
	v_or_b32_e32 v2, s2, v37
	v_lshlrev_b32_e32 v2, 11, v2
	v_lshl_add_u64 v[26:27], v[8:9], 0, v[2:3]
	v_or_b32_e32 v2, s2, v45
	s_waitcnt lgkmcnt(0)
	v_cvt_pk_bf16_f32 v4, v12, v10
	v_lshlrev_b32_e32 v2, 11, v2
	v_cvt_pk_bf16_f32 v5, v14, v16
	v_cvt_pk_bf16_f32 v6, v18, v20
	v_cvt_pk_bf16_f32 v7, v22, v24
	global_store_dwordx4 v[26:27], v[4:7], off sc1 nt
	s_nop 1
	v_cvt_pk_bf16_f32 v4, v13, v11
	v_lshl_add_u64 v[10:11], v[8:9], 0, v[2:3]
	v_cvt_pk_bf16_f32 v5, v15, v17
	v_cvt_pk_bf16_f32 v6, v19, v21
	v_cvt_pk_bf16_f32 v7, v23, v25
	global_store_dwordx4 v[10:11], v[4:7], off sc1 nt
	ds_read2_b32 v[10:11], v48 offset0:16 offset1:24
	ds_read2_b32 v[12:13], v48 offset0:49 offset1:57
	ds_read2_b32 v[14:15], v48 offset0:82 offset1:90
	ds_read2_b32 v[16:17], v48 offset0:115 offset1:123
	ds_read2_b32 v[18:19], v48 offset0:148 offset1:156
	ds_read2_b32 v[20:21], v48 offset0:181 offset1:189
	ds_read2_b32 v[22:23], v48 offset0:214 offset1:222
	ds_read2_b32 v[24:25], v48 offset0:247 offset1:255
	v_or_b32_e32 v2, s2, v46
	v_lshlrev_b32_e32 v2, 11, v2
	v_lshl_add_u64 v[26:27], v[8:9], 0, v[2:3]
	v_or_b32_e32 v2, s2, v47
	v_lshlrev_b32_e32 v2, 11, v2
	s_waitcnt lgkmcnt(6)
	v_cvt_pk_bf16_f32 v4, v10, v12
	s_waitcnt lgkmcnt(4)
	v_cvt_pk_bf16_f32 v5, v14, v16
	s_waitcnt lgkmcnt(2)
	v_cvt_pk_bf16_f32 v6, v18, v20
	s_waitcnt lgkmcnt(0)
	v_cvt_pk_bf16_f32 v7, v22, v24
	v_lshl_add_u64 v[8:9], v[8:9], 0, v[2:3]
	global_store_dwordx4 v[26:27], v[4:7], off sc1 nt
	s_nop 1
	v_cvt_pk_bf16_f32 v4, v11, v13
	v_cvt_pk_bf16_f32 v5, v15, v17
	v_cvt_pk_bf16_f32 v6, v19, v21
	v_cvt_pk_bf16_f32 v7, v23, v25
	global_store_dwordx4 v[8:9], v[4:7], off sc1 nt
	s_waitcnt lgkmcnt(0)

; __device__ __forceinline__ void transpose_item(const float* W, int K, int N, bf16* WT, int drow0, int kb, int n0, LAS float* scr, int lane) {
;     const int k0 = 64 * kb; const int c4 = 4 * (lane & 7); const bool ok = (n0 + c4) < N;
;     f32x4 v[8];
; #pragma unroll
;     for (int i = 0; i < 8; ++i) { const int kk = 8 * i + (lane >> 3); v[i] = ok ? *(const f32x4*)(W + (size_t)(k0 + kk) * N + n0 + c4) : (f32x4){0.f, 0.f, 0.f, 0.f}; }
; __device__ __forceinline__ void convert_item(const In& I, unsigned char* ws, int it, LAS float* scr, int lane) {
;     ...
;     if (r < 2 * I_NIN) { const int j = r / I_NIN; r -= j * I_NIN; const int kb = r / 88, nb = r % 88;
;         transpose_item(I.nsa_w_in + (size_t)j * D * NSA_IN, D, NSA_IN, Wnin + (size_t)j * NSA_IN_PAD * D, 32 * nb, kb, 32 * nb, scr, lane); return; }
.LBB0_575:
	s_andn2_b64 vcc, exec, s[2:3]
	s_cbranch_vccnz .LBB0_593
	s_add_i32 s2, s30, 0x2400
	s_cmpk_gt_u32 s2, 0x57f
	s_cselect_b64 s[8:9], -1, 0
	s_and_b64 s[2:3], s[8:9], exec
	s_cselect_b32 s2, 0xfa80, 0
	s_cselect_b32 s3, 0xa30000, 0
	s_add_i32 s2, s14, s2
	s_add_i32 s2, s2, s16
	s_addk_i32 s2, 0x2400
	s_sext_i32_i16 s4, s2
	s_mulk_i32 s4, 0xba3
	s_lshr_b32 s5, s4, 31
	s_ashr_i32 s4, s4, 18
	s_add_i32 s5, s4, s5
	s_mul_i32 s4, s5, 0x58
	v_readlane_b32 s40, v253, 0
	s_sub_i32 s2, s2, s4
	v_readlane_b32 s52, v253, 12
	s_sext_i32_i16 s2, s2
	v_readlane_b32 s53, v253, 13
	s_add_u32 s7, s52, s3
	s_addc_u32 s35, s53, 0
	s_lshl_b32 s4, s2, 5
	s_lshl_b32 s6, s5, 6
	s_ashr_i32 s5, s4, 31
	s_lshl_b64 s[10:11], s[4:5], 2
	v_or_b32_e32 v2, s4, v36
	s_movk_i32 s2, 0xa30
	v_or_b32_e32 v5, s6, v37
	s_add_u32 s10, s7, s10
	v_cmp_gt_i32_e64 s[2:3], s2, v2
	s_addc_u32 s11, s35, s11
	v_lshlrev_b32_e32 v2, 2, v36
	v_mul_i32_i24_e32 v42, 0x28c0, v5
	v_lshl_add_u64 v[40:41], s[10:11], 0, v[2:3]
	v_mov_b32_e32 v4, 0
	v_ashrrev_i32_e32 v43, 31, v42
	v_mov_b32_e32 v8, 0
	v_mov_b32_e32 v9, 0
	v_mov_b32_e32 v10, 0
	v_mov_b32_e32 v11, 0
	v_readlane_b32 s41, v253, 1
	v_readlane_b32 s42, v253, 2
	v_readlane_b32 s43, v253, 3
	v_readlane_b32 s44, v253, 4
	v_readlane_b32 s45, v253, 5
	v_readlane_b32 s46, v253, 6
	v_readlane_b32 s47, v253, 7
	v_readlane_b32 s48, v253, 8
	v_readlane_b32 s49, v253, 9
	v_readlane_b32 s50, v253, 10
	v_readlane_b32 s51, v253, 11
	v_readlane_b32 s54, v253, 14
	v_readlane_b32 s55, v253, 15
	s_and_saveexec_b64 s[10:11], s[2:3]
	s_cbranch_execz .LBB0_578
	v_lshl_add_u64 v[6:7], v[40:41], 0, v[42:43]
	global_load_dwordx4 v[8:11], v[6:7], off nt
.LBB0_578:
	s_or_b64 exec, exec, s[10:11]
	v_mov_b32_e32 v5, 0
	v_mov_b32_e32 v6, 0
	v_mov_b32_e32 v7, 0
	s_and_saveexec_b64 s[10:11], s[2:3]
	s_cbranch_execz .LBB0_580
	v_lshl_add_u64 v[4:5], v[40:41], 0, v[42:43]
	v_add_co_u32_e32 v4, vcc, 0x14000, v4
	s_nop 1
	v_addc_co_u32_e32 v5, vcc, 0, v5, vcc
	global_load_dwordx4 v[4:7], v[4:5], off offset:1536 nt
.LBB0_580:
	s_or_b64 exec, exec, s[10:11]
	v_mov_b32_e32 v12, 0
	v_mov_b32_e32 v16, 0
	v_mov_b32_e32 v17, 0
	v_mov_b32_e32 v18, 0
	v_mov_b32_e32 v19, 0
	s_and_saveexec_b64 s[10:11], s[2:3]
	s_cbranch_execz .LBB0_582
	v_lshl_add_u64 v[14:15], v[40:41], 0, v[42:43]
	v_add_co_u32_e32 v14, vcc, 0x28000, v14
	s_nop 1
	v_addc_co_u32_e32 v15, vcc, 0, v15, vcc
	global_load_dwordx4 v[16:19], v[14:15], off offset:3072 nt
.LBB0_582:
	s_or_b64 exec, exec, s[10:11]
	v_mov_b32_e32 v13, 0
	v_mov_b32_e32 v14, 0
	v_mov_b32_e32 v15, 0
	s_and_saveexec_b64 s[10:11], s[2:3]
	s_cbranch_execz .LBB0_584
	v_lshl_add_u64 v[12:13], v[40:41], 0, v[42:43]
	v_add_co_u32_e32 v12, vcc, 0x3d000, v12
	s_nop 1
	v_addc_co_u32_e32 v13, vcc, 0, v13, vcc
	global_load_dwordx4 v[12:15], v[12:13], off offset:512 nt
.LBB0_584:
	s_or_b64 exec, exec, s[10:11]
	v_mov_b32_e32 v20, 0
	v_mov_b32_e32 v24, 0
	v_mov_b32_e32 v25, 0
	v_mov_b32_e32 v26, 0
	v_mov_b32_e32 v27, 0
	s_and_saveexec_b64 s[10:11], s[2:3]
	s_cbranch_execz .LBB0_586
	v_lshl_add_u64 v[22:23], v[40:41], 0, v[42:43]
	v_add_co_u32_e32 v22, vcc, 0x51000, v22
	s_nop 1
	v_addc_co_u32_e32 v23, vcc, 0, v23, vcc
	global_load_dwordx4 v[24:27], v[22:23], off offset:2048 nt
.LBB0_586:
	s_or_b64 exec, exec, s[10:11]
	v_mov_b32_e32 v21, 0
	v_mov_b32_e32 v22, 0
	v_mov_b32_e32 v23, 0
	s_and_saveexec_b64 s[10:11], s[2:3]
	s_cbranch_execz .LBB0_588
	v_lshl_add_u64 v[20:21], v[40:41], 0, v[42:43]
	v_add_co_u32_e32 v20, vcc, 0x65000, v20
	s_nop 1
	v_addc_co_u32_e32 v21, vcc, 0, v21, vcc
	global_load_dwordx4 v[20:23], v[20:21], off offset:3584 nt
.LBB0_588:
	s_or_b64 exec, exec, s[10:11]
	v_mov_b32_e32 v28, 0
	v_mov_b32_e32 v32, 0
	v_mov_b32_e32 v33, 0
	v_mov_b32_e32 v34, 0
	v_mov_b32_e32 v35, 0
	s_and_saveexec_b64 s[10:11], s[2:3]
	s_cbranch_execz .LBB0_590
	v_lshl_add_u64 v[30:31], v[40:41], 0, v[42:43]
	v_add_co_u32_e32 v30, vcc, 0x7a000, v30
	s_nop 1
	v_addc_co_u32_e32 v31, vcc, 0, v31, vcc
	global_load_dwordx4 v[32:35], v[30:31], off offset:1024 nt
; #define GAS __attribute__((address_space(1)))
; #define LAS __attribute__((address_space(3)))
; #define LDS_WAIT() asm volatile("s_waitcnt lgkmcnt(0)" ::: "memory")
; __device__ __forceinline__ unsigned pk2(float lo, float hi) { unsigned r; asm("v_cvt_pk_bf16_f32 %0, %1, %2" : "=v"(r) : "v"(lo), "v"(hi)); return r; }
; __device__ __forceinline__ void transpose_item(const float* W, int K, int N, bf16* WT, int drow0, int kb, int n0, LAS float* scr, int lane) {
;     const int k0 = 64 * kb; const int c4 = 4 * (lane & 7); const bool ok = (n0 + c4) < N;
;     f32x4 v[8];
; #pragma unroll
;     for (int i = 0; i < 8; ++i) { const int kk = 8 * i + (lane >> 3); v[i] = ok ? *(const f32x4*)(W + (size_t)(k0 + kk) * N + n0 + c4) : (f32x4){0.f, 0.f, 0.f, 0.f}; }
; #pragma unroll
;     for (int i = 0; i < 8; ++i) { const int kk = 8 * i + (lane >> 3); LAS float* d = scr + kk * 33 + c4; d[0] = v[i][0]; d[1] = v[i][1]; d[2] = v[i][2]; d[3] = v[i][3]; }
;     LDS_WAIT(); asm volatile("" ::: "memory");
;     const int c = lane & 7;
; #pragma unroll
;     for (int j = 0; j < 4; ++j) { const int n = (lane >> 3) + 8 * j; const LAS float* s = scr + (8 * c) * 33 + n;
;         v4u o; o.x = pk2(s[0 * 33], s[1 * 33]); o.y = pk2(s[2 * 33], s[3 * 33]); o.z = pk2(s[4 * 33], s[5 * 33]); o.w = pk2(s[6 * 33], s[7 * 33]);
;         *(GAS v4u*)(WT + (size_t)(drow0 + n) * K + k0 + 8 * c) = o; }
;     LDS_WAIT(); asm volatile("" ::: "memory");
.LBB0_590:
	s_or_b64 exec, exec, s[10:11]
	v_mov_b32_e32 v29, 0
	v_mov_b32_e32 v30, 0
	v_mov_b32_e32 v31, 0
	s_and_saveexec_b64 s[10:11], s[2:3]
	s_cbranch_execz .LBB0_592
	v_lshl_add_u64 v[28:29], v[40:41], 0, v[42:43]
	v_add_co_u32_e32 v28, vcc, 0x8e000, v28
	s_nop 1
	v_addc_co_u32_e32 v29, vcc, 0, v29, vcc
	global_load_dwordx4 v[28:31], v[28:29], off offset:2560 nt
.LBB0_592:
	s_or_b64 exec, exec, s[10:11]
	v_add_u32_e32 v2, v39, v44
	s_waitcnt vmcnt(0)
	ds_write2_b32 v2, v8, v9 offset1:1
	ds_write2_b32 v2, v10, v11 offset0:2 offset1:3
	v_add_u32_e32 v8, 0x420, v2
	ds_write2_b32 v8, v4, v5 offset1:1
	v_add_u32_e32 v4, 0x428, v2
	ds_write2_b32 v4, v6, v7 offset1:1
	v_add_u32_e32 v4, 0x840, v2
	ds_write2_b32 v4, v16, v17 offset1:1
	v_add_u32_e32 v4, 0x848, v2
	ds_write2_b32 v4, v18, v19 offset1:1
	v_add_u32_e32 v4, 0xc60, v2
	ds_write2_b32 v4, v12, v13 offset1:1
	v_add_u32_e32 v4, 0xc68, v2
	ds_write2_b32 v4, v14, v15 offset1:1
	v_add_u32_e32 v4, 0x1080, v2
	ds_write2_b32 v4, v24, v25 offset1:1
	v_add_u32_e32 v4, 0x1088, v2
	ds_write2_b32 v4, v26, v27 offset1:1
	v_add_u32_e32 v4, 0x14a0, v2
	ds_write2_b32 v4, v20, v21 offset1:1
	v_add_u32_e32 v4, 0x14a8, v2
	ds_write2_b32 v4, v22, v23 offset1:1
	v_add_u32_e32 v4, 0x18c0, v2
	ds_write2_b32 v4, v32, v33 offset1:1
	v_add_u32_e32 v4, 0x18c8, v2
	s_and_b64 s[2:3], s[8:9], exec
	ds_write2_b32 v4, v34, v35 offset1:1
	v_add_u32_e32 v4, 0x1ce0, v2
	v_add_u32_e32 v2, 0x1ce8, v2
	s_cselect_b32 s2, 0x580000, 0
	ds_write2_b32 v4, v28, v29 offset1:1
	ds_write2_b32 v2, v30, v31 offset1:1
	s_add_u32 s5, s13, s2
	s_waitcnt lgkmcnt(0)
	s_addc_u32 s8, s17, 0
	s_ashr_i32 s7, s6, 31
	s_lshl_b64 s[2:3], s[6:7], 1
	ds_read2_b32 v[8:9], v48 offset0:33 offset1:41
	ds_read2_b32 v[10:11], v48 offset1:8
	ds_read2_b32 v[12:13], v48 offset0:66 offset1:74
	ds_read2_b32 v[14:15], v48 offset0:99 offset1:107
	ds_read2_b32 v[16:17], v48 offset0:132 offset1:140
	ds_read2_b32 v[18:19], v48 offset0:165 offset1:173
	ds_read2_b32 v[20:21], v48 offset0:198 offset1:206
	ds_read2_b32 v[22:23], v48 offset0:231 offset1:239
	s_add_u32 s2, s5, s2
	v_or_b32_e32 v26, s4, v37
	s_addc_u32 s3, s8, s3
	v_lshlrev_b32_e32 v2, 1, v38
	v_ashrrev_i32_e32 v27, 31, v26
	v_lshl_add_u64 v[24:25], s[2:3], 0, v[2:3]
	v_lshlrev_b64 v[26:27], 11, v[26:27]
	s_waitcnt lgkmcnt(0)
	v_cvt_pk_bf16_f32 v4, v10, v8
	v_lshl_add_u64 v[26:27], v[24:25], 0, v[26:27]
	v_or_b32_e32 v8, s4, v45
	v_cvt_pk_bf16_f32 v5, v12, v14
	v_cvt_pk_bf16_f32 v6, v16, v18
	v_cvt_pk_bf16_f32 v7, v20, v22
	global_store_dwordx4 v[26:27], v[4:7], off sc1 nt
	s_nop 1
	v_cvt_pk_bf16_f32 v4, v11, v9
	v_ashrrev_i32_e32 v9, 31, v8
	v_lshlrev_b64 v[8:9], 11, v[8:9]
	v_cvt_pk_bf16_f32 v5, v13, v15
	v_cvt_pk_bf16_f32 v6, v17, v19
	v_cvt_pk_bf16_f32 v7, v21, v23
	v_lshl_add_u64 v[8:9], v[24:25], 0, v[8:9]
	ds_read2_b32 v[10:11], v48 offset0:16 offset1:24
	ds_read2_b32 v[12:13], v48 offset0:49 offset1:57
	ds_read2_b32 v[14:15], v48 offset0:82 offset1:90
	ds_read2_b32 v[16:17], v48 offset0:115 offset1:123
	ds_read2_b32 v[18:19], v48 offset0:148 offset1:156
	ds_read2_b32 v[20:21], v48 offset0:181 offset1:189
	ds_read2_b32 v[22:23], v48 offset0:214 offset1:222
	ds_read2_b32 v[26:27], v48 offset0:247 offset1:255
	global_store_dwordx4 v[8:9], v[4:7], off sc1 nt
	v_or_b32_e32 v8, s4, v46
	v_ashrrev_i32_e32 v9, 31, v8
	v_lshlrev_b64 v[8:9], 11, v[8:9]
	v_lshl_add_u64 v[8:9], v[24:25], 0, v[8:9]
	s_waitcnt lgkmcnt(6)
	v_cvt_pk_bf16_f32 v4, v10, v12
	s_waitcnt lgkmcnt(4)
	v_cvt_pk_bf16_f32 v5, v14, v16
	s_waitcnt lgkmcnt(2)
	v_cvt_pk_bf16_f32 v6, v18, v20
	s_waitcnt lgkmcnt(0)
	v_cvt_pk_bf16_f32 v7, v22, v26
	global_store_dwordx4 v[8:9], v[4:7], off sc1 nt
	v_or_b32_e32 v8, s4, v47
	v_ashrrev_i32_e32 v9, 31, v8
	v_lshlrev_b64 v[8:9], 11, v[8:9]
	v_lshl_add_u64 v[8:9], v[24:25], 0, v[8:9]
	v_cvt_pk_bf16_f32 v4, v11, v13
	v_cvt_pk_bf16_f32 v5, v15, v17
	v_cvt_pk_bf16_f32 v6, v19, v21
	v_cvt_pk_bf16_f32 v7, v23, v27
	global_store_dwordx4 v[8:9], v[4:7], off sc1 nt
	s_waitcnt lgkmcnt(0)

; #define GAS __attribute__((address_space(1)))
; #define LAS __attribute__((address_space(3)))
; #define LDS_WAIT() asm volatile("s_waitcnt lgkmcnt(0)" ::: "memory")
; __device__ __forceinline__ unsigned pk2(float lo, float hi) { unsigned r; asm("v_cvt_pk_bf16_f32 %0, %1, %2" : "=v"(r) : "v"(lo), "v"(hi)); return r; }
; __device__ __forceinline__ void transpose_item(const float* W, int K, int N, bf16* WT, int drow0, int kb, int n0, LAS float* scr, int lane) {
;     const int k0 = 64 * kb; const int c4 = 4 * (lane & 7); const bool ok = (n0 + c4) < N;
;     f32x4 v[8];
; #pragma unroll
;     for (int i = 0; i < 8; ++i) { const int kk = 8 * i + (lane >> 3); v[i] = ok ? *(const f32x4*)(W + (size_t)(k0 + kk) * N + n0 + c4) : (f32x4){0.f, 0.f, 0.f, 0.f}; }
; #pragma unroll
;     for (int i = 0; i < 8; ++i) { const int kk = 8 * i + (lane >> 3); LAS float* d = scr + kk * 33 + c4; d[0] = v[i][0]; d[1] = v[i][1]; d[2] = v[i][2]; d[3] = v[i][3]; }
;     LDS_WAIT(); asm volatile("" ::: "memory");
;     const int c = lane & 7;
; #pragma unroll
;     for (int j = 0; j < 4; ++j) { const int n = (lane >> 3) + 8 * j; const LAS float* s = scr + (8 * c) * 33 + n;
;         v4u o; o.x = pk2(s[0 * 33], s[1 * 33]); o.y = pk2(s[2 * 33], s[3 * 33]); o.z = pk2(s[4 * 33], s[5 * 33]); o.w = pk2(s[6 * 33], s[7 * 33]);
;         *(GAS v4u*)(WT + (size_t)(drow0 + n) * K + k0 + 8 * c) = o; }
;     LDS_WAIT(); asm volatile("" ::: "memory");
; }
; __device__ __forceinline__ void convert_item(const In& I, unsigned char* ws, int it, LAS float* scr, int lane) {
;     ...
;     if (r < T0) { const int f = r / I_FFN; r -= f * I_FFN;
;         if (r < 2 * I_G) { const int up = r >= I_G; r -= up * I_G; const int kb = r / 88, nb = r % 88;
;             transpose_item((up ? I.w_up : I.w_gate) + (size_t)f * D * FF, D, FF, Wgu + (size_t)f * NGU * D, 256 * (nb >> 2) + 32 * (nb & 3) + 128 * up, kb, 32 * nb, scr, lane); }
;         else { r -= 2 * I_G; const int kb = r / 32, nb = r % 32; transpose_item(I.w_down + (size_t)f * FF * D, FF, D, Wd + (size_t)f * D * FF, 32 * nb, kb, 32 * nb, scr, lane); }
.LBB0_594:
	s_andn2_b64 vcc, exec, s[2:3]
	s_cbranch_vccnz .LBB0_539
	s_mul_hi_i32 s2, s34, 0x3e0f83e1
	s_lshr_b32 s3, s2, 31
	s_ashr_i32 s6, s2, 10
	s_add_i32 s6, s6, s3
	s_mul_i32 s2, s6, 0xffffef80
	s_add_i32 s7, s30, s2
	s_add_i32 s7, s7, 0xa800
	v_add_u32_e32 v8, v39, v44
	s_mov_b64 s[2:3], -1
	s_cmpk_gt_i32 s7, 0xaff
	s_mul_hi_i32 s4, s6, 0xb00000
	s_mul_i32 s5, s6, 0xb00000
	v_lshlrev_b32_e32 v2, 2, v36
	v_add_u32_e32 v9, 0x420, v8
	v_add_u32_e32 v10, 0x428, v8
	v_add_u32_e32 v11, 0x840, v8
	v_add_u32_e32 v12, 0x848, v8
	v_add_u32_e32 v13, 0xc60, v8
	v_add_u32_e32 v14, 0xc68, v8
	v_add_u32_e32 v15, 0x1080, v8
	v_add_u32_e32 v16, 0x1088, v8
	v_add_u32_e32 v17, 0x14a0, v8
	v_add_u32_e32 v18, 0x14a8, v8
	v_add_u32_e32 v19, 0x18c0, v8
	v_add_u32_e32 v20, 0x18c8, v8
	v_add_u32_e32 v21, 0x1ce0, v8
	v_add_u32_e32 v22, 0x1ce8, v8
	v_lshlrev_b32_e32 v4, 1, v38
	s_cbranch_scc0 .LBB0_597
	v_readlane_b32 s40, v253, 0
	v_readlane_b32 s48, v253, 8
	v_readlane_b32 s49, v253, 9
	s_add_u32 s3, s48, s5
	s_addc_u32 s9, s49, s4
	s_mul_i32 s8, s6, 0x580000
	s_mul_hi_i32 s2, s6, 0x580000
	s_add_u32 s10, s1, s8
	v_readlane_b32 s34, v253, 52
	s_addc_u32 s11, s12, s2
	s_mul_i32 s8, s6, 0xffffdf00
	s_add_i32 s34, s34, s15
	s_add_i32 s8, s34, s8
	s_addk_i32 s8, 0x1900
	s_and_b32 s2, s33, 0x3e0
	s_andn2_b32 s8, s8, 63
	s_add_i32 s68, s8, 0xffffea00
	s_lshl_b32 s8, s2, 2
	v_or_b32_e32 v6, s68, v37
	s_add_u32 s8, s3, s8
	s_addc_u32 s9, s9, 0
	v_ashrrev_i32_e32 v7, 31, v6
	v_lshl_add_u64 v[62:63], s[8:9], 0, v[2:3]
	v_lshlrev_b64 v[24:25], 12, v[6:7]
	v_or_b32_e32 v28, 8, v6
	v_lshl_add_u64 v[24:25], v[62:63], 0, v[24:25]
	v_ashrrev_i32_e32 v29, 31, v28
	global_load_dwordx4 v[24:27], v[24:25], off nt
	v_lshlrev_b64 v[28:29], 12, v[28:29]
	v_or_b32_e32 v32, 16, v6
	v_lshl_add_u64 v[28:29], v[62:63], 0, v[28:29]
	v_ashrrev_i32_e32 v33, 31, v32
	global_load_dwordx4 v[28:31], v[28:29], off nt
	v_lshlrev_b64 v[32:33], 12, v[32:33]
	v_or_b32_e32 v40, 24, v6
	v_lshl_add_u64 v[32:33], v[62:63], 0, v[32:33]
	v_ashrrev_i32_e32 v41, 31, v40
	global_load_dwordx4 v[32:35], v[32:33], off nt
	v_lshlrev_b64 v[40:41], 12, v[40:41]
	v_or_b32_e32 v50, 32, v6
	v_lshl_add_u64 v[40:41], v[62:63], 0, v[40:41]
	v_ashrrev_i32_e32 v51, 31, v50
	global_load_dwordx4 v[40:43], v[40:41], off nt
	v_lshlrev_b64 v[50:51], 12, v[50:51]
	v_or_b32_e32 v54, 40, v6
	v_lshl_add_u64 v[50:51], v[62:63], 0, v[50:51]
	v_ashrrev_i32_e32 v55, 31, v54
	global_load_dwordx4 v[50:53], v[50:51], off nt
	v_lshlrev_b64 v[54:55], 12, v[54:55]
	v_or_b32_e32 v58, 48, v6
	v_lshl_add_u64 v[54:55], v[62:63], 0, v[54:55]
	v_ashrrev_i32_e32 v59, 31, v58
	global_load_dwordx4 v[54:57], v[54:55], off nt
	v_lshlrev_b64 v[58:59], 12, v[58:59]
	v_or_b32_e32 v6, 56, v6
	v_lshl_add_u64 v[58:59], v[62:63], 0, v[58:59]
	v_ashrrev_i32_e32 v7, 31, v6
	global_load_dwordx4 v[58:61], v[58:59], off nt
	v_lshlrev_b64 v[6:7], 12, v[6:7]
	v_lshl_add_u64 v[6:7], v[62:63], 0, v[6:7]
	global_load_dwordx4 v[62:65], v[6:7], off nt
	s_lshl_b64 s[8:9], s[68:69], 1
	s_add_u32 s8, s10, s8
	s_addc_u32 s9, s11, s9
	v_mov_b32_e32 v5, v3
	v_lshl_add_u64 v[6:7], s[8:9], 0, v[4:5]
	v_or_b32_e32 v5, s2, v37
	v_readlane_b32 s41, v253, 1
	v_readlane_b32 s42, v253, 2
	v_readlane_b32 s43, v253, 3
	v_readlane_b32 s44, v253, 4
	v_readlane_b32 s45, v253, 5
	v_readlane_b32 s46, v253, 6
	v_readlane_b32 s47, v253, 7
	v_readlane_b32 s50, v253, 10
	v_readlane_b32 s51, v253, 11
	v_readlane_b32 s52, v253, 12
	v_readlane_b32 s53, v253, 13
	v_readlane_b32 s54, v253, 14
	v_readlane_b32 s55, v253, 15
	s_waitcnt vmcnt(0)
	ds_write2_b32 v8, v24, v25 offset1:1
	ds_write2_b32 v8, v26, v27 offset0:2 offset1:3
	ds_write2_b32 v9, v28, v29 offset1:1
	ds_write2_b32 v10, v30, v31 offset1:1
	ds_write2_b32 v11, v32, v33 offset1:1
	ds_write2_b32 v12, v34, v35 offset1:1
	ds_write2_b32 v13, v40, v41 offset1:1
	ds_write2_b32 v14, v42, v43 offset1:1
	ds_write2_b32 v15, v50, v51 offset1:1
	ds_write2_b32 v16, v52, v53 offset1:1
	ds_write2_b32 v17, v54, v55 offset1:1
	ds_write2_b32 v18, v56, v57 offset1:1
	ds_write2_b32 v19, v58, v59 offset1:1
	ds_write2_b32 v20, v60, v61 offset1:1
	ds_write2_b32 v21, v62, v63 offset1:1
	ds_write2_b32 v22, v64, v65 offset1:1
	s_waitcnt lgkmcnt(0)
	ds_read2_b32 v[28:29], v48 offset0:33 offset1:41
	ds_read2_b32 v[30:31], v48 offset1:8
	ds_read2_b32 v[32:33], v48 offset0:66 offset1:74
	ds_read2_b32 v[34:35], v48 offset0:99 offset1:107
	ds_read2_b32 v[40:41], v48 offset0:132 offset1:140
	ds_read2_b32 v[42:43], v48 offset0:165 offset1:173
	ds_read2_b32 v[50:51], v48 offset0:198 offset1:206
	ds_read2_b32 v[52:53], v48 offset0:231 offset1:239
	v_mul_u32_u24_e32 v54, 0x1600, v5
	v_mov_b32_e32 v55, v3
	s_waitcnt lgkmcnt(0)
	v_cvt_pk_bf16_f32 v24, v30, v28
	v_lshl_add_u64 v[54:55], v[6:7], 0, v[54:55]
	v_or_b32_e32 v5, s2, v45
	v_cvt_pk_bf16_f32 v25, v32, v34
	v_cvt_pk_bf16_f32 v26, v40, v42
	v_cvt_pk_bf16_f32 v27, v50, v52
	global_store_dwordx4 v[54:55], v[24:27], off sc1 nt
	v_mul_u32_u24_e32 v28, 0x1600, v5
	v_or_b32_e32 v5, s2, v46
	v_cvt_pk_bf16_f32 v24, v31, v29
	v_mov_b32_e32 v29, v3
	v_lshl_add_u64 v[28:29], v[6:7], 0, v[28:29]
	v_cvt_pk_bf16_f32 v25, v33, v35
	v_cvt_pk_bf16_f32 v26, v41, v43
	v_cvt_pk_bf16_f32 v27, v51, v53
	global_store_dwordx4 v[28:29], v[24:27], off sc1 nt
	ds_read2_b32 v[28:29], v48 offset0:16 offset1:24
	ds_read2_b32 v[30:31], v48 offset0:49 offset1:57
	ds_read2_b32 v[32:33], v48 offset0:82 offset1:90
	ds_read2_b32 v[34:35], v48 offset0:115 offset1:123
	ds_read2_b32 v[40:41], v48 offset0:148 offset1:156
	ds_read2_b32 v[42:43], v48 offset0:181 offset1:189
	ds_read2_b32 v[50:51], v48 offset0:214 offset1:222
	ds_read2_b32 v[52:53], v48 offset0:247 offset1:255
	v_mul_u32_u24_e32 v54, 0x1600, v5
	v_mov_b32_e32 v55, v3
	s_waitcnt lgkmcnt(6)
	v_cvt_pk_bf16_f32 v24, v28, v30
	v_lshl_add_u64 v[54:55], v[6:7], 0, v[54:55]
	v_or_b32_e32 v5, s2, v47
	s_waitcnt lgkmcnt(4)
	v_cvt_pk_bf16_f32 v25, v32, v34
	s_waitcnt lgkmcnt(2)
	v_cvt_pk_bf16_f32 v26, v40, v42
	s_waitcnt lgkmcnt(0)
	v_cvt_pk_bf16_f32 v27, v50, v52
	global_store_dwordx4 v[54:55], v[24:27], off sc1 nt
	v_mul_u32_u24_e32 v28, 0x1600, v5
	s_mov_b64 s[2:3], 0
	v_cvt_pk_bf16_f32 v24, v29, v31
	v_mov_b32_e32 v29, v3
	v_lshl_add_u64 v[6:7], v[6:7], 0, v[28:29]
	v_cvt_pk_bf16_f32 v25, v33, v35
	v_cvt_pk_bf16_f32 v26, v41, v43
	v_cvt_pk_bf16_f32 v27, v51, v53
	global_store_dwordx4 v[6:7], v[24:27], off sc1 nt
	s_waitcnt lgkmcnt(0)
; #define GAS __attribute__((address_space(1)))
; #define LAS __attribute__((address_space(3)))
; #define LDS_WAIT() asm volatile("s_waitcnt lgkmcnt(0)" ::: "memory")
; __device__ __forceinline__ unsigned pk2(float lo, float hi) { unsigned r; asm("v_cvt_pk_bf16_f32 %0, %1, %2" : "=v"(r) : "v"(lo), "v"(hi)); return r; }
; __device__ __forceinline__ void transpose_item(const float* W, int K, int N, bf16* WT, int drow0, int kb, int n0, LAS float* scr, int lane) {
;     const int k0 = 64 * kb; const int c4 = 4 * (lane & 7); const bool ok = (n0 + c4) < N;
;     f32x4 v[8];
; #pragma unroll
;     for (int i = 0; i < 8; ++i) { const int kk = 8 * i + (lane >> 3); v[i] = ok ? *(const f32x4*)(W + (size_t)(k0 + kk) * N + n0 + c4) : (f32x4){0.f, 0.f, 0.f, 0.f}; }
; #pragma unroll
;     for (int i = 0; i < 8; ++i) { const int kk = 8 * i + (lane >> 3); LAS float* d = scr + kk * 33 + c4; d[0] = v[i][0]; d[1] = v[i][1]; d[2] = v[i][2]; d[3] = v[i][3]; }
;     LDS_WAIT(); asm volatile("" ::: "memory");
;     const int c = lane & 7;
; #pragma unroll
;     for (int j = 0; j < 4; ++j) { const int n = (lane >> 3) + 8 * j; const LAS float* s = scr + (8 * c) * 33 + n;
;         v4u o; o.x = pk2(s[0 * 33], s[1 * 33]); o.y = pk2(s[2 * 33], s[3 * 33]); o.z = pk2(s[4 * 33], s[5 * 33]); o.w = pk2(s[6 * 33], s[7 * 33]);
;         *(GAS v4u*)(WT + (size_t)(drow0 + n) * K + k0 + 8 * c) = o; }
;     LDS_WAIT(); asm volatile("" ::: "memory");
; }
; __device__ __forceinline__ void convert_item(const In& I, unsigned char* ws, int it, LAS float* scr, int lane) {
;     ...
;         if (r < 2 * I_G) { const int up = r >= I_G; r -= up * I_G; const int kb = r / 88, nb = r % 88;
;             transpose_item((up ? I.w_up : I.w_gate) + (size_t)f * D * FF, D, FF, Wgu + (size_t)f * NGU * D, 256 * (nb >> 2) + 32 * (nb & 3) + 128 * up, kb, 32 * nb, scr, lane); }
.LBB0_597:
	s_andn2_b64 vcc, exec, s[2:3]
	s_cbranch_vccnz .LBB0_539
	s_cmpk_gt_i32 s7, 0x57f
	v_readlane_b32 s40, v253, 0
	s_cselect_b32 s2, 0xfffffa80, 0
	s_mulk_i32 s6, 0x1080
	v_readlane_b32 s44, v253, 4
	v_readlane_b32 s45, v253, 5
	v_readlane_b32 s46, v253, 6
	v_readlane_b32 s47, v253, 7
	s_cselect_b32 s3, 0x80, 0
	s_cselect_b32 s7, s46, s44
	s_cselect_b32 s8, s47, s45
	s_sub_i32 s2, s2, s6
	s_add_i32 s2, s30, s2
	s_add_i32 s2, s2, 0xa800
	s_mul_hi_i32 s6, s2, 0x2e8ba2e9
	s_lshr_b32 s9, s6, 31
	s_ashr_i32 s6, s6, 4
	s_add_i32 s6, s6, s9
	s_mul_i32 s9, s6, 0x58
	s_sub_i32 s2, s2, s9
	s_add_u32 s7, s7, s5
	s_addc_u32 s8, s8, s4
	s_add_u32 s9, s28, s5
	s_addc_u32 s10, s29, s4
	s_lshl_b32 s4, s2, 6
	s_and_b32 s5, s4, 0xffffff00
	s_lshl_b32 s4, s2, 5
	s_and_b32 s2, s4, 0x60
	s_or_b32 s2, s2, s3
	s_or_b32 s2, s2, s5
	s_ashr_i32 s5, s4, 31
	s_lshl_b32 s6, s6, 6
	s_lshl_b64 s[4:5], s[4:5], 2
	s_add_u32 s4, s7, s4
	s_addc_u32 s5, s8, s5
	v_or_b32_e32 v5, s6, v37
	v_lshl_add_u64 v[6:7], s[4:5], 0, v[2:3]
	s_movk_i32 s3, 0x2c00
	v_mad_i64_i32 v[24:25], s[4:5], v5, s3, v[6:7]
	global_load_dwordx4 v[24:27], v[24:25], off nt
	v_or_b32_e32 v2, 8, v5
	v_mad_i64_i32 v[28:29], s[4:5], v2, s3, v[6:7]
	global_load_dwordx4 v[28:31], v[28:29], off nt
	v_or_b32_e32 v2, 16, v5
	v_mad_i64_i32 v[32:33], s[4:5], v2, s3, v[6:7]
	global_load_dwordx4 v[32:35], v[32:33], off nt
	v_or_b32_e32 v2, 24, v5
	v_mad_i64_i32 v[40:41], s[4:5], v2, s3, v[6:7]
	global_load_dwordx4 v[40:43], v[40:41], off nt
	v_or_b32_e32 v2, 32, v5
	v_mad_i64_i32 v[50:51], s[4:5], v2, s3, v[6:7]
	global_load_dwordx4 v[50:53], v[50:51], off nt
	v_or_b32_e32 v2, 40, v5
	v_mad_i64_i32 v[54:55], s[4:5], v2, s3, v[6:7]
	global_load_dwordx4 v[54:57], v[54:55], off nt
	v_or_b32_e32 v2, 48, v5
	v_mad_i64_i32 v[58:59], s[4:5], v2, s3, v[6:7]
	global_load_dwordx4 v[58:61], v[58:59], off nt
	v_or_b32_e32 v2, 56, v5
	v_mad_i64_i32 v[6:7], s[4:5], v2, s3, v[6:7]
	global_load_dwordx4 v[62:65], v[6:7], off nt
	s_ashr_i32 s7, s6, 31
	s_lshl_b64 s[4:5], s[6:7], 1
	s_add_u32 s4, s9, s4
	s_addc_u32 s5, s10, s5
	v_mov_b32_e32 v5, v3
	v_lshl_add_u64 v[4:5], s[4:5], 0, v[4:5]
	v_readlane_b32 s41, v253, 1
	v_readlane_b32 s42, v253, 2
	v_readlane_b32 s43, v253, 3
	v_readlane_b32 s48, v253, 8
	v_readlane_b32 s49, v253, 9
	v_readlane_b32 s50, v253, 10
	v_readlane_b32 s51, v253, 11
	v_readlane_b32 s52, v253, 12
	v_readlane_b32 s53, v253, 13
	v_readlane_b32 s54, v253, 14
	v_readlane_b32 s55, v253, 15
	s_waitcnt vmcnt(0)
	ds_write2_b32 v8, v24, v25 offset1:1
	ds_write2_b32 v8, v26, v27 offset0:2 offset1:3
	ds_write2_b32 v9, v28, v29 offset1:1
	ds_write2_b32 v10, v30, v31 offset1:1
	ds_write2_b32 v11, v32, v33 offset1:1
	ds_write2_b32 v12, v34, v35 offset1:1
	ds_write2_b32 v13, v40, v41 offset1:1
	ds_write2_b32 v14, v42, v43 offset1:1
	ds_write2_b32 v15, v50, v51 offset1:1
	ds_write2_b32 v16, v52, v53 offset1:1
	ds_write2_b32 v17, v54, v55 offset1:1
	ds_write2_b32 v18, v56, v57 offset1:1
	ds_write2_b32 v19, v58, v59 offset1:1
	ds_write2_b32 v20, v60, v61 offset1:1
	ds_write2_b32 v21, v62, v63 offset1:1
	ds_write2_b32 v22, v64, v65 offset1:1
	s_waitcnt lgkmcnt(0)
	ds_read2_b32 v[10:11], v48 offset0:33 offset1:41
	ds_read2_b32 v[12:13], v48 offset1:8
	ds_read2_b32 v[14:15], v48 offset0:66 offset1:74
	ds_read2_b32 v[16:17], v48 offset0:99 offset1:107
	ds_read2_b32 v[18:19], v48 offset0:132 offset1:140
	ds_read2_b32 v[20:21], v48 offset0:165 offset1:173
	ds_read2_b32 v[22:23], v48 offset0:198 offset1:206
	ds_read2_b32 v[24:25], v48 offset0:231 offset1:239
	v_or_b32_e32 v26, s2, v37
	v_ashrrev_i32_e32 v27, 31, v26
	v_lshlrev_b64 v[26:27], 11, v[26:27]
	s_waitcnt lgkmcnt(0)
	v_cvt_pk_bf16_f32 v6, v12, v10
	v_lshl_add_u64 v[26:27], v[4:5], 0, v[26:27]
	v_or_b32_e32 v10, s2, v45
	v_cvt_pk_bf16_f32 v7, v14, v16
	v_cvt_pk_bf16_f32 v8, v18, v20
	v_cvt_pk_bf16_f32 v9, v22, v24
	global_store_dwordx4 v[26:27], v[6:9], off sc1 nt
	v_or_b32_e32 v26, s2, v46
	v_ashrrev_i32_e32 v27, 31, v26
	v_cvt_pk_bf16_f32 v6, v13, v11
	v_ashrrev_i32_e32 v11, 31, v10
	v_lshlrev_b64 v[10:11], 11, v[10:11]
	v_lshl_add_u64 v[10:11], v[4:5], 0, v[10:11]
	v_cvt_pk_bf16_f32 v7, v15, v17
	v_cvt_pk_bf16_f32 v8, v19, v21
	v_cvt_pk_bf16_f32 v9, v23, v25
	global_store_dwordx4 v[10:11], v[6:9], off sc1 nt
	ds_read2_b32 v[10:11], v48 offset0:16 offset1:24
	ds_read2_b32 v[12:13], v48 offset0:49 offset1:57
	ds_read2_b32 v[14:15], v48 offset0:82 offset1:90
	ds_read2_b32 v[16:17], v48 offset0:115 offset1:123
	ds_read2_b32 v[18:19], v48 offset0:148 offset1:156
	ds_read2_b32 v[20:21], v48 offset0:181 offset1:189
	ds_read2_b32 v[22:23], v48 offset0:214 offset1:222
	ds_read2_b32 v[24:25], v48 offset0:247 offset1:255
	v_lshlrev_b64 v[26:27], 11, v[26:27]
	s_waitcnt lgkmcnt(6)
	v_cvt_pk_bf16_f32 v6, v10, v12
	v_lshl_add_u64 v[26:27], v[4:5], 0, v[26:27]
	v_or_b32_e32 v10, s2, v47
	s_waitcnt lgkmcnt(4)
	v_cvt_pk_bf16_f32 v7, v14, v16
	s_waitcnt lgkmcnt(2)
	v_cvt_pk_bf16_f32 v8, v18, v20
	s_waitcnt lgkmcnt(0)
	v_cvt_pk_bf16_f32 v9, v22, v24
	global_store_dwordx4 v[26:27], v[6:9], off sc1 nt
	s_nop 1
	v_cvt_pk_bf16_f32 v6, v11, v13
	v_ashrrev_i32_e32 v11, 31, v10
	v_lshlrev_b64 v[10:11], 11, v[10:11]
	v_lshl_add_u64 v[4:5], v[4:5], 0, v[10:11]
	v_cvt_pk_bf16_f32 v7, v15, v17
	v_cvt_pk_bf16_f32 v8, v19, v21
	v_cvt_pk_bf16_f32 v9, v23, v25
	global_store_dwordx4 v[4:5], v[6:9], off sc1 nt
	s_waitcnt lgkmcnt(0)
	s_branch .LBB0_539
